# indexer IQ LDS fill: 16 loads in flight instead of one per loop trip; weight-conversion write-out: 16 LDS reads batched instead of read-wait-store chain
# speedup vs baseline: 1.0123x; 1.0035x over previous
; #define LAS __attribute__((address_space(3)))
; #define CV_LOAD(v, kb) do { _Pragma("unroll") for (int j = 0; j < 16; ++j) v[j] = __builtin_nontemporal_load((const f32x2*)(src + (size_t)((kb) * 16 + j) * ldw)); } while (0)
; __device__ __forceinline__ void tr128_f8(const float* W, int ldw, int srccol, unsigned char* WT, size_t dstrow0, int K, int k0, LAS unsigned char* tile, int lane) {
;     const float* src = W + (size_t)k0 * ldw + srccol + 2 * lane;
;     f32x2 va[16], vb[16], vc[16], vd[16];
;     ...
;     CV_LOAD(va, 0); CV_LOAD(vb, 1); CV_LOAD(vc, 2);
;     CV_LOAD(vd, 3); CV_PUT(va, 0); CV_LOAD(va, 4); CV_PUT(vb, 1); CV_LOAD(vb, 5); CV_PUT(vc, 2); CV_LOAD(vc, 6); CV_PUT(vd, 3); CV_LOAD(vd, 7);
; __device__ __forceinline__ void cv_item(const Args& a, int it, LAS unsigned char* tile, int lane) {
;     if (it < CV_PA) { const int kt = it >> 4, nt = it & 15; tr128_f8(a.in[I_WPA], 2048, 128 * nt, (unsigned char*)(a.ws + WS_WA), (size_t)128 * nt, 2048, 128 * kt, tile, lane); return; } it -= CV_PA;
;     if (it < CV_PB) { const int kt = it >> 4, nt = it & 15; tr128_f8(a.in[I_WPB], 2048, 128 * nt, (unsigned char*)(a.ws + WS_WA + 1024), (size_t)128 * nt, 2048, 128 * kt, tile, lane); return; } it -= CV_PB;
;     if (it < CV_WO) { const int kt = it >> 4, nt = it & 15; tr128_f8(a.in[I_WOUT], 2048, 128 * nt, (unsigned char*)(a.ws + WS_WO), (size_t)128 * nt, 2048, 128 * kt, tile, lane); return; } it -= CV_WO;
;     if (it < CV_GU) { const int e = it / CV_GU1, q = it % CV_GU1, kt = q >> 5, nt = q & 31, d0 = 128 * nt, ct = d0 >> 8; const int src = (d0 & 128) ? (2048 + 128 * ct) : (128 * ct);
;         tr128_f8(a.in[I_WGU] + (size_t)e * 2048 * 4096, 4096, src, (unsigned char*)(a.ws + WS_WGU), (size_t)e * 4096 + d0, 2048, 128 * kt, tile, lane); }
;     else { const int r = it - CV_GU, e = r / CV_D1, q = r % CV_D1, kt = q >> 4, nt = q & 15;
;         tr128_f8(a.in[I_WD] + (size_t)e * 2048 * 2048, 2048, 128 * nt, (unsigned char*)(a.ws + WS_WD), (size_t)e * 2048 + 128 * nt, 2048, 128 * kt, tile, lane); }
.LBB0_497:
	s_or_b64 exec, exec, s[8:9]
	v_readfirstlane_b32 s10, v2
	s_cmpk_gt_i32 s10, 0x61ff
	s_mov_b64 s[8:9], -1
	s_cbranch_scc1 .LBB0_492
	s_cmpk_gt_i32 s10, 0x7f
	s_cbranch_scc0 .LBB0_512
	s_cmpk_gt_u32 s10, 0xff
	s_cbranch_scc0 .LBB0_509
	s_cmpk_gt_u32 s10, 0x1ff
	s_cbranch_scc0 .LBB0_506
	s_cmpk_gt_u32 s10, 0x41ff
	s_cbranch_scc0 .LBB0_503
	s_add_i32 s6, s10, 0xffffbe00
	s_lshr_b32 s6, s6, 8
	v_readlane_b32 s20, v250, 3
	s_lshl_b64 s[8:9], s[6:7], 11
	s_lshl_b64 s[12:13], s[6:7], 24
	v_readlane_b32 s24, v250, 7
	v_readlane_b32 s25, v250, 8
	s_add_u32 s11, s24, s12
	s_addc_u32 s12, s25, s13
	s_lshl_b32 s6, s10, 7
	s_and_b32 s13, s6, 0x780
	s_lshl_b32 s6, s10, 3
	s_and_b32 s6, s6, 0x780
	s_or_b32 s8, s8, s13
	s_lshl_b32 s33, s6, 13
	s_add_u32 s11, s11, s33
	s_addc_u32 s33, s12, 0
	s_lshl_b32 s12, s13, 2
	s_add_u32 s12, s11, s12
	s_addc_u32 s13, s33, 0
	v_lshlrev_b32_e32 v8, 2, v6
	s_movk_i32 s20, 0x2000
	v_lshl_add_u64 v[2:3], s[12:13], 0, v[8:9]
	v_readlane_b32 s21, v250, 4
	v_add_co_u32_e32 v50, vcc, s20, v2
	s_movk_i32 s21, 0x4000
	s_nop 0
	v_addc_co_u32_e32 v51, vcc, 0, v3, vcc
	v_readlane_b32 s22, v250, 5
	v_add_co_u32_e32 v52, vcc, s21, v2
	s_movk_i32 s22, 0x6000
	s_nop 0
	v_addc_co_u32_e32 v53, vcc, 0, v3, vcc
	v_readlane_b32 s23, v250, 6
	v_add_co_u32_e32 v54, vcc, s22, v2
	s_mov_b32 s23, 0x8000
	s_nop 0
	v_addc_co_u32_e32 v55, vcc, 0, v3, vcc
	v_add_co_u32_e32 v56, vcc, s23, v2
	s_mov_b32 s24, 0xa000
	s_nop 0
	v_addc_co_u32_e32 v57, vcc, 0, v3, vcc
	v_add_co_u32_e32 v58, vcc, s24, v2
	s_mov_b32 s25, 0xc000
	s_nop 0
	v_addc_co_u32_e32 v59, vcc, 0, v3, vcc
	v_readlane_b32 s26, v250, 9
	v_add_co_u32_e32 v60, vcc, s25, v2
	s_mov_b32 s26, 0xe000
	s_nop 0
	v_addc_co_u32_e32 v61, vcc, 0, v3, vcc
	v_readlane_b32 s27, v250, 10
	v_add_co_u32_e32 v62, vcc, s26, v2
	s_mov_b32 s27, 0x10000
	s_nop 0
	v_addc_co_u32_e32 v63, vcc, 0, v3, vcc
	v_add_co_u32_e32 v64, vcc, s27, v2
	s_mov_b32 s33, 0x12000
	s_nop 0
	v_addc_co_u32_e32 v65, vcc, 0, v3, vcc
	v_add_co_u32_e32 v66, vcc, s33, v2
	s_mov_b32 s11, 0x16000
	s_nop 0
	v_addc_co_u32_e32 v67, vcc, 0, v3, vcc
	v_add_co_u32_e32 v68, vcc, s34, v2
	global_load_dwordx2 v[4:5], v8, s[12:13] nt
	s_nop 0
	v_addc_co_u32_e32 v69, vcc, 0, v3, vcc
	global_load_dwordx2 v[50:51], v[50:51], off nt
	v_add_co_u32_e32 v70, vcc, s11, v2
	global_load_dwordx2 v[56:57], v[56:57], off nt
	s_nop 0
	v_addc_co_u32_e32 v71, vcc, 0, v3, vcc
	global_load_dwordx2 v[58:59], v[58:59], off nt
	v_add_co_u32_e32 v72, vcc, s58, v2
	s_mov_b32 s11, 0x1a000
	s_nop 0
	v_addc_co_u32_e32 v73, vcc, 0, v3, vcc
	global_load_dwordx2 v[52:53], v[52:53], off nt
	v_add_co_u32_e32 v74, vcc, s11, v2
	global_load_dwordx2 v[54:55], v[54:55], off nt
	s_nop 0
	v_addc_co_u32_e32 v75, vcc, 0, v3, vcc
	global_load_dwordx2 v[64:65], v[64:65], off nt
	v_add_co_u32_e32 v76, vcc, s62, v2
	global_load_dwordx2 v[66:67], v[66:67], off nt
	s_nop 0
	v_addc_co_u32_e32 v77, vcc, 0, v3, vcc
	global_load_dwordx2 v[60:61], v[60:61], off nt
	s_mov_b32 s11, 0x1e000
	global_load_dwordx2 v[62:63], v[62:63], off nt
	v_add_co_u32_e32 v78, vcc, s11, v2
	global_load_dwordx2 v[72:73], v[72:73], off nt
	s_nop 0
	v_addc_co_u32_e32 v79, vcc, 0, v3, vcc
	global_load_dwordx2 v[74:75], v[74:75], off nt
	v_add_co_u32_e32 v80, vcc, s29, v2
	global_load_dwordx2 v[68:69], v[68:69], off nt
	s_nop 0
	v_addc_co_u32_e32 v81, vcc, 0, v3, vcc
	global_load_dwordx2 v[70:71], v[70:71], off nt
	s_mov_b32 s11, 0x22000
	global_load_dwordx2 v[76:77], v[76:77], off nt
	v_add_co_u32_e32 v82, vcc, s11, v2
	global_load_dwordx2 v[78:79], v[78:79], off nt
	s_nop 0
	v_addc_co_u32_e32 v83, vcc, 0, v3, vcc
	v_add_co_u32_e32 v84, vcc, s31, v2
	s_mov_b32 s11, 0x26000
	s_nop 0
	v_addc_co_u32_e32 v85, vcc, 0, v3, vcc
	v_add_co_u32_e32 v86, vcc, s11, v2
	s_mov_b32 s11, 0x2a000
	s_nop 0
	v_addc_co_u32_e32 v87, vcc, 0, v3, vcc
	v_add_co_u32_e32 v88, vcc, s35, v2
	global_load_dwordx2 v[80:81], v[80:81], off nt
	s_nop 0
	v_addc_co_u32_e32 v89, vcc, 0, v3, vcc
	v_add_co_u32_e32 v90, vcc, s11, v2
	s_mov_b32 s11, 0x2e000
	s_nop 0
	v_addc_co_u32_e32 v91, vcc, 0, v3, vcc
	v_add_co_u32_e32 v92, vcc, s66, v2
	global_load_dwordx2 v[82:83], v[82:83], off nt
	s_nop 0
	v_addc_co_u32_e32 v93, vcc, 0, v3, vcc
	v_add_co_u32_e32 v94, vcc, s11, v2
	s_mov_b32 s11, 0x32000
	s_nop 0
	v_addc_co_u32_e32 v95, vcc, 0, v3, vcc
	v_add_co_u32_e32 v96, vcc, s70, v2
	global_load_dwordx2 v[86:87], v[86:87], off nt
	s_nop 0
	v_addc_co_u32_e32 v97, vcc, 0, v3, vcc
	v_add_co_u32_e32 v98, vcc, s11, v2
	s_mov_b32 s11, 0x36000
	s_nop 0
	v_addc_co_u32_e32 v99, vcc, 0, v3, vcc
	v_add_co_u32_e32 v100, vcc, s74, v2
	global_load_dwordx2 v[88:89], v[88:89], off nt
	s_nop 0
	v_addc_co_u32_e32 v101, vcc, 0, v3, vcc
	v_add_co_u32_e32 v102, vcc, s11, v2
	s_mov_b32 s11, 0x3a000
	s_nop 0
	v_addc_co_u32_e32 v103, vcc, 0, v3, vcc
	v_add_co_u32_e32 v104, vcc, s78, v2
	global_load_dwordx2 v[90:91], v[90:91], off nt
	s_nop 0
	v_addc_co_u32_e32 v105, vcc, 0, v3, vcc
	v_add_co_u32_e32 v106, vcc, s11, v2
	s_mov_b32 s11, 0x3e000
	s_nop 0
	v_addc_co_u32_e32 v107, vcc, 0, v3, vcc
	v_add_co_u32_e32 v108, vcc, s83, v2
	global_load_dwordx2 v[84:85], v[84:85], off nt
	s_nop 0
	v_addc_co_u32_e32 v109, vcc, 0, v3, vcc
	v_add_co_u32_e32 v110, vcc, s11, v2
	s_mov_b32 s11, 0x42000
	s_nop 0
	v_addc_co_u32_e32 v111, vcc, 0, v3, vcc
	v_add_co_u32_e32 v112, vcc, s87, v2
	global_load_dwordx2 v[94:95], v[94:95], off nt
	s_nop 0
	v_addc_co_u32_e32 v113, vcc, 0, v3, vcc
	v_add_co_u32_e32 v114, vcc, s11, v2
	s_mov_b32 s11, 0x46000
	s_nop 0
	v_addc_co_u32_e32 v115, vcc, 0, v3, vcc
	v_add_co_u32_e32 v116, vcc, s91, v2
	global_load_dwordx2 v[96:97], v[96:97], off nt
	s_nop 0
	v_addc_co_u32_e32 v117, vcc, 0, v3, vcc
	v_add_co_u32_e32 v118, vcc, s11, v2
	s_mov_b32 s11, 0x4a000
	s_nop 0
	v_addc_co_u32_e32 v119, vcc, 0, v3, vcc
	v_add_co_u32_e32 v120, vcc, s95, v2
	global_load_dwordx2 v[98:99], v[98:99], off nt
	s_nop 0
	v_addc_co_u32_e32 v121, vcc, 0, v3, vcc
	v_add_co_u32_e32 v122, vcc, s11, v2
	s_mov_b32 s11, 0x4e000
	s_nop 0
	v_addc_co_u32_e32 v123, vcc, 0, v3, vcc
	v_add_co_u32_e32 v124, vcc, s53, v2
	global_load_dwordx2 v[92:93], v[92:93], off nt
	s_nop 0
	v_addc_co_u32_e32 v125, vcc, 0, v3, vcc
	v_add_co_u32_e32 v126, vcc, s11, v2
	s_mov_b32 s11, 0x52000
	s_nop 0
	v_addc_co_u32_e32 v127, vcc, 0, v3, vcc
	v_add_co_u32_e32 v128, vcc, s55, v2
	global_load_dwordx2 v[102:103], v[102:103], off nt
	s_nop 0
	v_addc_co_u32_e32 v129, vcc, 0, v3, vcc
	v_add_co_u32_e32 v130, vcc, s11, v2
	s_mov_b32 s11, 0x56000
	s_nop 0
	v_addc_co_u32_e32 v131, vcc, 0, v3, vcc
	v_add_co_u32_e32 v132, vcc, s57, v2
	global_load_dwordx2 v[104:105], v[104:105], off nt
	s_nop 0
	v_addc_co_u32_e32 v133, vcc, 0, v3, vcc
	global_load_dwordx2 v[106:107], v[106:107], off nt
	v_add_co_u32_e32 v134, vcc, s11, v2
	global_load_dwordx2 v[100:101], v[100:101], off nt
	s_nop 0
	v_addc_co_u32_e32 v135, vcc, 0, v3, vcc
	v_add_co_u32_e32 v136, vcc, s59, v2
	s_waitcnt vmcnt(29)
; #define CV_LOAD(v, kb) do { _Pragma("unroll") for (int j = 0; j < 16; ++j) v[j] = __builtin_nontemporal_load((const f32x2*)(src + (size_t)((kb) * 16 + j) * ldw)); } while (0)
; __device__ __forceinline__ void tr128_f8(const float* W, int ldw, int srccol, unsigned char* WT, size_t dstrow0, int K, int k0, LAS unsigned char* tile, int lane) {
;     ...
;     CV_LOAD(va, 0); CV_LOAD(vb, 1); CV_LOAD(vc, 2);
;     CV_LOAD(vd, 3); CV_PUT(va, 0); CV_LOAD(va, 4); CV_PUT(vb, 1); CV_LOAD(vb, 5); CV_PUT(vc, 2); CV_LOAD(vc, 6); CV_PUT(vd, 3); CV_LOAD(vd, 7);
	v_mul_f32_e32 v4, 0x43800000, v4
	s_waitcnt vmcnt(28)
	v_mul_f32_e32 v8, 0x43800000, v50
	v_addc_co_u32_e32 v137, vcc, 0, v3, vcc
	s_mov_b32 s11, 0x5a000
	v_med3_f32 v4, v4, s79, v193
	v_med3_f32 v8, v8, s79, v193
	v_mov_b32_e32 v194, v9
	global_load_dwordx2 v[108:109], v[108:109], off nt
	v_add_co_u32_e32 v138, vcc, s11, v2
	global_load_dwordx2 v[110:111], v[110:111], off nt
	v_cvt_pk_fp8_f32 v194, v4, v8
	s_waitcnt vmcnt(29)
	v_mul_f32_e32 v4, 0x43800000, v56
	s_waitcnt vmcnt(28)
	v_mul_f32_e32 v8, 0x43800000, v58
	v_addc_co_u32_e32 v139, vcc, 0, v3, vcc
	v_med3_f32 v4, v4, s79, v193
	v_med3_f32 v8, v8, s79, v193
	v_mov_b32_e32 v195, v9
	v_add_co_u32_e32 v140, vcc, s61, v2
	s_waitcnt vmcnt(27)
	v_mul_f32_e32 v50, 0x43800000, v52
	s_waitcnt vmcnt(26)
	v_mul_f32_e32 v52, 0x43800000, v54
	v_cvt_pk_fp8_f32 v195, v4, v8
	s_waitcnt vmcnt(25)
	v_mul_f32_e32 v4, 0x43800000, v64
	s_waitcnt vmcnt(24)
	v_mul_f32_e32 v8, 0x43800000, v66
	v_addc_co_u32_e32 v141, vcc, 0, v3, vcc
	s_mov_b32 s11, 0x5e000
	v_med3_f32 v50, v50, s79, v193
	v_med3_f32 v52, v52, s79, v193
	v_med3_f32 v4, v4, s79, v193
	v_med3_f32 v8, v8, s79, v193
	v_mov_b32_e32 v196, v9
	v_add_co_u32_e32 v142, vcc, s11, v2
	v_cvt_pk_fp8_f32 v194, v50, v52 op_sel:[0,0,1]
	s_waitcnt vmcnt(23)
	v_mul_f32_e32 v50, 0x43800000, v60
	s_waitcnt vmcnt(22)
	v_mul_f32_e32 v52, 0x43800000, v62
	v_cvt_pk_fp8_f32 v196, v4, v8
	s_waitcnt vmcnt(21)
	v_mul_f32_e32 v4, 0x43800000, v72
	s_waitcnt vmcnt(20)
	v_mul_f32_e32 v8, 0x43800000, v74
	v_addc_co_u32_e32 v143, vcc, 0, v3, vcc
	v_med3_f32 v50, v50, s79, v193
	v_med3_f32 v52, v52, s79, v193
	v_med3_f32 v4, v4, s79, v193
	v_med3_f32 v8, v8, s79, v193
	v_mov_b32_e32 v197, v9
	v_add_co_u32_e32 v144, vcc, s63, v2
	v_cvt_pk_fp8_f32 v195, v50, v52 op_sel:[0,0,1]
	s_waitcnt vmcnt(19)
	v_mul_f32_e32 v50, 0x43800000, v68
	s_waitcnt vmcnt(18)
	v_mul_f32_e32 v52, 0x43800000, v70
	v_cvt_pk_fp8_f32 v197, v4, v8
	v_addc_co_u32_e32 v145, vcc, 0, v3, vcc
	s_mov_b32 s11, 0x62000
	v_med3_f32 v50, v50, s79, v193
	v_med3_f32 v52, v52, s79, v193
	v_add_co_u32_e32 v146, vcc, s11, v2
	v_cvt_pk_fp8_f32 v196, v50, v52 op_sel:[0,0,1]
	s_waitcnt vmcnt(17)
	v_mul_f32_e32 v50, 0x43800000, v76
	s_waitcnt vmcnt(16)
	v_mul_f32_e32 v52, 0x43800000, v78
	v_addc_co_u32_e32 v147, vcc, 0, v3, vcc
	v_med3_f32 v50, v50, s79, v193
	v_med3_f32 v52, v52, s79, v193
	v_add_co_u32_e32 v148, vcc, s65, v2
	v_cvt_pk_fp8_f32 v197, v50, v52 op_sel:[0,0,1]
	v_mul_f32_e32 v4, 0x43800000, v5
	v_mul_f32_e32 v5, 0x43800000, v51
	v_mul_f32_e32 v50, 0x43800000, v55
	v_addc_co_u32_e32 v149, vcc, 0, v3, vcc
	s_mov_b32 s11, 0x66000
	v_med3_f32 v4, v4, s79, v193
	v_med3_f32 v5, v5, s79, v193
	v_med3_f32 v51, v50, s79, v193
	v_mov_b32_e32 v50, v9
	v_add_co_u32_e32 v150, vcc, s11, v2
	v_cvt_pk_fp8_f32 v50, v4, v5
	s_nop 0
	v_addc_co_u32_e32 v151, vcc, 0, v3, vcc
	v_add_co_u32_e32 v152, vcc, s67, v2
	v_mul_f32_e32 v8, 0x43800000, v53
	s_nop 0
	v_addc_co_u32_e32 v153, vcc, 0, v3, vcc
	s_mov_b32 s11, 0x6a000
	v_med3_f32 v8, v8, s79, v193
	v_add_co_u32_e32 v154, vcc, s11, v2
	v_cvt_pk_fp8_f32 v50, v8, v51 op_sel:[0,0,1]
	v_mul_f32_e32 v4, 0x43800000, v57
	v_mul_f32_e32 v5, 0x43800000, v59
	v_mul_f32_e32 v51, 0x43800000, v63
	v_addc_co_u32_e32 v155, vcc, 0, v3, vcc
	v_med3_f32 v4, v4, s79, v193
	v_med3_f32 v5, v5, s79, v193
	v_med3_f32 v52, v51, s79, v193
	v_mov_b32_e32 v51, v9
	v_add_co_u32_e32 v156, vcc, s69, v2
	v_cvt_pk_fp8_f32 v51, v4, v5
	s_nop 0
	v_addc_co_u32_e32 v157, vcc, 0, v3, vcc
	s_mov_b32 s11, 0x6e000
	v_add_co_u32_e32 v158, vcc, s11, v2
	v_mul_f32_e32 v8, 0x43800000, v61
	s_nop 0
	v_addc_co_u32_e32 v159, vcc, 0, v3, vcc
	v_med3_f32 v8, v8, s79, v193
	v_add_co_u32_e32 v160, vcc, s71, v2
	v_cvt_pk_fp8_f32 v51, v8, v52 op_sel:[0,0,1]
	v_mul_f32_e32 v4, 0x43800000, v65
	v_mul_f32_e32 v5, 0x43800000, v67
	v_mul_f32_e32 v52, 0x43800000, v71
	v_addc_co_u32_e32 v161, vcc, 0, v3, vcc
	s_mov_b32 s11, 0x72000
	v_med3_f32 v4, v4, s79, v193
	v_med3_f32 v5, v5, s79, v193
	v_med3_f32 v53, v52, s79, v193
	v_mov_b32_e32 v52, v9
	v_add_co_u32_e32 v164, vcc, s11, v2
	v_cvt_pk_fp8_f32 v52, v4, v5
	s_nop 0
	v_addc_co_u32_e32 v165, vcc, 0, v3, vcc
	v_add_co_u32_e32 v166, vcc, s73, v2
	v_mul_f32_e32 v8, 0x43800000, v69
	s_nop 0
	v_addc_co_u32_e32 v167, vcc, 0, v3, vcc
	s_mov_b32 s11, 0x76000
	v_med3_f32 v8, v8, s79, v193
	v_add_co_u32_e32 v168, vcc, s11, v2
	v_cvt_pk_fp8_f32 v52, v8, v53 op_sel:[0,0,1]
	v_mul_f32_e32 v4, 0x43800000, v73
	v_mul_f32_e32 v5, 0x43800000, v75
	v_mul_f32_e32 v53, 0x43800000, v79
	v_addc_co_u32_e32 v169, vcc, 0, v3, vcc
	v_med3_f32 v4, v4, s79, v193
	v_med3_f32 v5, v5, s79, v193
	v_med3_f32 v54, v53, s79, v193
	v_mov_b32_e32 v53, v9
	v_add_co_u32_e32 v170, vcc, s75, v2
	v_cvt_pk_fp8_f32 v53, v4, v5
	s_nop 0
	v_addc_co_u32_e32 v171, vcc, 0, v3, vcc
	s_mov_b32 s11, 0x7a000
	v_add_co_u32_e32 v172, vcc, s11, v2
	v_mul_f32_e32 v8, 0x43800000, v77
	s_nop 0
	v_addc_co_u32_e32 v173, vcc, 0, v3, vcc
	v_med3_f32 v8, v8, s79, v193
	v_add_co_u32_e32 v174, vcc, s77, v2
	v_cvt_pk_fp8_f32 v53, v8, v54 op_sel:[0,0,1]
	s_nop 0
	v_addc_co_u32_e32 v175, vcc, 0, v3, vcc
	s_mov_b32 s11, 0x7e000
	v_add_co_u32_e32 v176, vcc, s11, v2
	v_add_u32_e32 v4, v13, v15
	s_nop 0
	v_addc_co_u32_e32 v177, vcc, 0, v3, vcc
	ds_write_b128 v4, v[50:53]
	v_add_co_u32_e32 v4, vcc, s80, v2
	s_mov_b32 s11, 0x82000
	s_nop 0
	v_addc_co_u32_e32 v5, vcc, 0, v3, vcc
	v_add_co_u32_e32 v50, vcc, s11, v2
	s_mov_b32 s11, 0x86000
	s_nop 0
	v_addc_co_u32_e32 v51, vcc, 0, v3, vcc
	v_add_co_u32_e32 v52, vcc, s82, v2
	global_load_dwordx2 v[112:113], v[112:113], off nt
	s_nop 0
	v_addc_co_u32_e32 v53, vcc, 0, v3, vcc
	v_add_co_u32_e32 v54, vcc, s11, v2
; #define CV_LOAD(v, kb) do { _Pragma("unroll") for (int j = 0; j < 16; ++j) v[j] = __builtin_nontemporal_load((const f32x2*)(src + (size_t)((kb) * 16 + j) * ldw)); } while (0)
; __device__ __forceinline__ void tr128_f8(const float* W, int ldw, int srccol, unsigned char* WT, size_t dstrow0, int K, int k0, LAS unsigned char* tile, int lane) {
;     ...
;     CV_LOAD(va, 0); CV_LOAD(vb, 1); CV_LOAD(vc, 2);
;     CV_LOAD(vd, 3); CV_PUT(va, 0); CV_LOAD(va, 4); CV_PUT(vb, 1); CV_LOAD(vb, 5); CV_PUT(vc, 2); CV_LOAD(vc, 6); CV_PUT(vd, 3); CV_LOAD(vd, 7);
	s_mov_b32 s11, 0x8a000
	s_nop 0
	v_addc_co_u32_e32 v55, vcc, 0, v3, vcc
	v_add_co_u32_e32 v56, vcc, s84, v2
	global_load_dwordx2 v[114:115], v[114:115], off nt
	s_nop 0
	v_addc_co_u32_e32 v57, vcc, 0, v3, vcc
	v_add_co_u32_e32 v58, vcc, s11, v2
	global_load_dwordx2 v[120:121], v[120:121], off nt
	s_nop 0
	v_addc_co_u32_e32 v59, vcc, 0, v3, vcc
	v_add_co_u32_e32 v60, vcc, s86, v2
	global_load_dwordx2 v[122:123], v[122:123], off nt
	s_nop 0
	v_addc_co_u32_e32 v61, vcc, 0, v3, vcc
	s_mov_b32 s11, 0x8e000
	v_add_co_u32_e32 v62, vcc, s11, v2
	global_load_dwordx2 v[116:117], v[116:117], off nt
	s_nop 0
	v_addc_co_u32_e32 v63, vcc, 0, v3, vcc
	global_load_dwordx2 v[118:119], v[118:119], off nt
	v_add_co_u32_e32 v64, vcc, s88, v2
	global_load_dwordx2 v[124:125], v[124:125], off nt
	s_nop 0
	v_addc_co_u32_e32 v65, vcc, 0, v3, vcc
	global_load_dwordx2 v[128:129], v[128:129], off nt
	s_mov_b32 s11, 0x92000
	global_load_dwordx2 v[130:131], v[130:131], off nt
	v_add_co_u32_e32 v66, vcc, s11, v2
	global_load_dwordx2 v[126:127], v[126:127], off nt
	s_nop 0
	v_addc_co_u32_e32 v67, vcc, 0, v3, vcc
	global_load_dwordx2 v[134:135], v[134:135], off nt
	v_add_co_u32_e32 v68, vcc, s90, v2
	global_load_dwordx2 v[136:137], v[136:137], off nt
	s_nop 0
	v_addc_co_u32_e32 v69, vcc, 0, v3, vcc
	global_load_dwordx2 v[138:139], v[138:139], off nt
	s_mov_b32 s11, 0x96000
	global_load_dwordx2 v[132:133], v[132:133], off nt
	v_add_co_u32_e32 v70, vcc, s11, v2
	global_load_dwordx2 v[140:141], v[140:141], off nt
	s_nop 0
	v_addc_co_u32_e32 v71, vcc, 0, v3, vcc
	global_load_dwordx2 v[142:143], v[142:143], off nt
	v_add_co_u32_e32 v72, vcc, s92, v2
	s_mov_b32 s11, 0x9a000
	s_nop 0
	v_addc_co_u32_e32 v73, vcc, 0, v3, vcc
	v_add_co_u32_e32 v74, vcc, s11, v2
	s_mov_b32 s11, 0x9e000
	s_nop 0
	v_addc_co_u32_e32 v75, vcc, 0, v3, vcc
	v_add_co_u32_e32 v76, vcc, s94, v2
	v_add_u32_e32 v8, v7, v11
	s_nop 0
	v_addc_co_u32_e32 v77, vcc, 0, v3, vcc
	v_add_co_u32_e32 v78, vcc, s11, v2
	s_waitcnt vmcnt(30)
	v_mul_f32_e32 v82, 0x43800000, v82
	v_addc_co_u32_e32 v79, vcc, 0, v3, vcc
	global_load_dwordx2 v[78:79], v[78:79], off nt
	v_mul_f32_e32 v80, 0x43800000, v80
	ds_write_b128 v8, v[194:197]
	v_med3_f32 v80, v80, s79, v193
	v_med3_f32 v82, v82, s79, v193
	v_mov_b32_e32 v194, v9
	v_cvt_pk_fp8_f32 v194, v80, v82
	s_waitcnt vmcnt(29)
	v_mul_f32_e32 v80, 0x43800000, v88
	s_waitcnt vmcnt(28)
	v_mul_f32_e32 v82, 0x43800000, v90
	v_med3_f32 v80, v80, s79, v193
	v_med3_f32 v82, v82, s79, v193
	v_mov_b32_e32 v195, v9
	s_waitcnt vmcnt(27)
	v_mul_f32_e32 v84, 0x43800000, v84
	v_mul_f32_e32 v86, 0x43800000, v86
	v_cvt_pk_fp8_f32 v195, v80, v82
	s_waitcnt vmcnt(25)
	v_mul_f32_e32 v80, 0x43800000, v96
	s_waitcnt vmcnt(24)
	v_mul_f32_e32 v82, 0x43800000, v98
	v_med3_f32 v84, v84, s79, v193
	v_med3_f32 v86, v86, s79, v193
	v_med3_f32 v80, v80, s79, v193
	v_med3_f32 v82, v82, s79, v193
	v_mov_b32_e32 v196, v9
	v_cvt_pk_fp8_f32 v194, v84, v86 op_sel:[0,0,1]
	s_waitcnt vmcnt(23)
	v_mul_f32_e32 v84, 0x43800000, v92
	v_mul_f32_e32 v86, 0x43800000, v94
	v_cvt_pk_fp8_f32 v196, v80, v82
	s_waitcnt vmcnt(21)
	v_mul_f32_e32 v80, 0x43800000, v104
	s_waitcnt vmcnt(20)
	v_mul_f32_e32 v82, 0x43800000, v106
	v_med3_f32 v84, v84, s79, v193
	v_med3_f32 v86, v86, s79, v193
	v_med3_f32 v80, v80, s79, v193
	v_med3_f32 v82, v82, s79, v193
	v_mov_b32_e32 v197, v9
	v_cvt_pk_fp8_f32 v195, v84, v86 op_sel:[0,0,1]
	s_waitcnt vmcnt(19)
	v_mul_f32_e32 v84, 0x43800000, v100
	v_mul_f32_e32 v86, 0x43800000, v102
	v_cvt_pk_fp8_f32 v197, v80, v82
	v_med3_f32 v84, v84, s79, v193
	v_med3_f32 v86, v86, s79, v193
	v_cvt_pk_fp8_f32 v196, v84, v86 op_sel:[0,0,1]
	s_waitcnt vmcnt(18)
	v_mul_f32_e32 v84, 0x43800000, v108
	s_waitcnt vmcnt(17)
	v_mul_f32_e32 v86, 0x43800000, v110
	v_med3_f32 v84, v84, s79, v193
	v_med3_f32 v86, v86, s79, v193
	v_mul_f32_e32 v80, 0x43800000, v81
	v_mul_f32_e32 v81, 0x43800000, v83
	v_cvt_pk_fp8_f32 v197, v84, v86 op_sel:[0,0,1]
	v_med3_f32 v84, v80, s79, v193
	v_med3_f32 v81, v81, s79, v193
	v_mov_b32_e32 v80, v9
	v_cvt_pk_fp8_f32 v80, v84, v81
	v_mul_f32_e32 v82, 0x43800000, v85
	v_mul_f32_e32 v83, 0x43800000, v87
	v_med3_f32 v82, v82, s79, v193
	v_med3_f32 v83, v83, s79, v193
	v_cvt_pk_fp8_f32 v80, v82, v83 op_sel:[0,0,1]
	v_mul_f32_e32 v81, 0x43800000, v89
	v_mul_f32_e32 v82, 0x43800000, v91
	v_med3_f32 v85, v81, s79, v193
	v_med3_f32 v82, v82, s79, v193
	v_mov_b32_e32 v81, v9
	v_cvt_pk_fp8_f32 v81, v85, v82
	v_mul_f32_e32 v83, 0x43800000, v93
	v_mul_f32_e32 v84, 0x43800000, v95
	v_med3_f32 v83, v83, s79, v193
	v_med3_f32 v84, v84, s79, v193
	v_cvt_pk_fp8_f32 v81, v83, v84 op_sel:[0,0,1]
	v_mul_f32_e32 v82, 0x43800000, v97
	v_mul_f32_e32 v83, 0x43800000, v99
	v_med3_f32 v86, v82, s79, v193
	v_med3_f32 v83, v83, s79, v193
	v_mov_b32_e32 v82, v9
	v_cvt_pk_fp8_f32 v82, v86, v83
	v_mul_f32_e32 v84, 0x43800000, v101
	v_mul_f32_e32 v85, 0x43800000, v103
	v_med3_f32 v84, v84, s79, v193
	v_med3_f32 v85, v85, s79, v193
	v_cvt_pk_fp8_f32 v82, v84, v85 op_sel:[0,0,1]
	v_mul_f32_e32 v83, 0x43800000, v105
	v_mul_f32_e32 v84, 0x43800000, v107
	v_med3_f32 v87, v83, s79, v193
	v_med3_f32 v84, v84, s79, v193
	v_mov_b32_e32 v83, v9
	v_cvt_pk_fp8_f32 v83, v87, v84
	v_mul_f32_e32 v85, 0x43800000, v109
	v_mul_f32_e32 v86, 0x43800000, v111
	v_med3_f32 v85, v85, s79, v193
	v_med3_f32 v86, v86, s79, v193
	v_cvt_pk_fp8_f32 v83, v85, v86 op_sel:[0,0,1]
	global_load_dwordx2 v[144:145], v[144:145], off nt
	ds_write_b128 v8, v[194:197] offset:16
	global_load_dwordx2 v[146:147], v[146:147], off nt
	v_add_u32_e32 v8, v13, v11
	global_load_dwordx2 v[152:153], v[152:153], off nt
	ds_write_b128 v8, v[80:83]
	global_load_dwordx2 v[154:155], v[154:155], off nt
; #define CV_LOAD(v, kb) do { _Pragma("unroll") for (int j = 0; j < 16; ++j) v[j] = __builtin_nontemporal_load((const f32x2*)(src + (size_t)((kb) * 16 + j) * ldw)); } while (0)
; __device__ __forceinline__ void tr128_f8(const float* W, int ldw, int srccol, unsigned char* WT, size_t dstrow0, int K, int k0, LAS unsigned char* tile, int lane) {
;     ...
;     CV_LOAD(va, 0); CV_LOAD(vb, 1); CV_LOAD(vc, 2);
;     CV_LOAD(vd, 3); CV_PUT(va, 0); CV_LOAD(va, 4); CV_PUT(vb, 1); CV_LOAD(vb, 5); CV_PUT(vc, 2); CV_LOAD(vc, 6); CV_PUT(vd, 3); CV_LOAD(vd, 7);
	v_add_co_u32_e32 v80, vcc, s96, v2
	s_mov_b32 s11, 0xa2000
	s_nop 0
	v_addc_co_u32_e32 v81, vcc, 0, v3, vcc
	global_load_dwordx2 v[148:149], v[148:149], off nt
	v_add_co_u32_e32 v82, vcc, s11, v2
	global_load_dwordx2 v[150:151], v[150:151], off nt
	s_nop 0
	v_addc_co_u32_e32 v83, vcc, 0, v3, vcc
	global_load_dwordx2 v[160:161], v[160:161], off nt
	v_add_co_u32_e32 v84, vcc, s4, v2
	global_load_dwordx2 v[164:165], v[164:165], off nt
	s_nop 0
	v_addc_co_u32_e32 v85, vcc, 0, v3, vcc
	global_load_dwordx2 v[156:157], v[156:157], off nt
	s_mov_b32 s11, 0xa6000
	global_load_dwordx2 v[158:159], v[158:159], off nt
	v_add_co_u32_e32 v86, vcc, s11, v2
	global_load_dwordx2 v[170:171], v[170:171], off nt
	s_nop 0
	v_addc_co_u32_e32 v87, vcc, 0, v3, vcc
	global_load_dwordx2 v[172:173], v[172:173], off nt
	v_add_co_u32_e32 v88, vcc, s14, v2
	global_load_dwordx2 v[166:167], v[166:167], off nt
	s_nop 0
	v_addc_co_u32_e32 v89, vcc, 0, v3, vcc
	global_load_dwordx2 v[168:169], v[168:169], off nt
	s_mov_b32 s11, 0xaa000
	global_load_dwordx2 v[174:175], v[174:175], off nt
	v_add_co_u32_e32 v90, vcc, s11, v2
	global_load_dwordx2 v[176:177], v[176:177], off nt
	s_nop 0
	v_addc_co_u32_e32 v91, vcc, 0, v3, vcc
	v_add_co_u32_e32 v92, vcc, s18, v2
	s_mov_b32 s11, 0xae000
	s_nop 0
	v_addc_co_u32_e32 v93, vcc, 0, v3, vcc
	global_load_dwordx2 v[88:89], v[88:89], off nt
	v_mov_b32_e32 v194, v9
	global_load_dwordx2 v[90:91], v[90:91], off nt
	v_mov_b32_e32 v195, v9
	global_load_dwordx2 v[94:95], v[92:93], off nt
	v_add_co_u32_e32 v92, vcc, s11, v2
	s_mov_b32 s11, 0xb2000
	s_nop 0
	v_addc_co_u32_e32 v93, vcc, 0, v3, vcc
	global_load_dwordx2 v[100:101], v[92:93], off nt
	v_add_co_u32_e32 v92, vcc, s5, v2
	s_waitcnt vmcnt(36)
	v_mul_f32_e32 v8, 0x43800000, v112
	v_addc_co_u32_e32 v93, vcc, 0, v3, vcc
	v_add_co_u32_e32 v96, vcc, s11, v2
	s_waitcnt vmcnt(35)
	v_mul_f32_e32 v112, 0x43800000, v114
	v_addc_co_u32_e32 v97, vcc, 0, v3, vcc
	v_add_co_u32_e32 v98, vcc, s54, v2
	s_mov_b32 s11, 0xb6000
	s_nop 0
	v_addc_co_u32_e32 v99, vcc, 0, v3, vcc
	v_med3_f32 v8, v8, s79, v193
	v_med3_f32 v112, v112, s79, v193
	global_load_dwordx2 v[92:93], v[92:93], off nt
	v_cvt_pk_fp8_f32 v194, v8, v112
	global_load_dwordx2 v[96:97], v[96:97], off nt
	s_waitcnt vmcnt(36)
	v_mul_f32_e32 v8, 0x43800000, v120
	global_load_dwordx2 v[102:103], v[98:99], off nt
	v_add_co_u32_e32 v98, vcc, s11, v2
	s_waitcnt vmcnt(36)
	v_mul_f32_e32 v112, 0x43800000, v122
	v_addc_co_u32_e32 v99, vcc, 0, v3, vcc
	v_med3_f32 v8, v8, s79, v193
	v_med3_f32 v112, v112, s79, v193
	global_load_dwordx2 v[106:107], v[98:99], off nt
	s_waitcnt vmcnt(36)
	v_mul_f32_e32 v114, 0x43800000, v116
	s_waitcnt vmcnt(35)
	v_mul_f32_e32 v116, 0x43800000, v118
	v_cvt_pk_fp8_f32 v195, v8, v112
	s_waitcnt vmcnt(33)
	v_mul_f32_e32 v8, 0x43800000, v128
	s_waitcnt vmcnt(32)
	v_mul_f32_e32 v112, 0x43800000, v130
	v_med3_f32 v114, v114, s79, v193
	v_med3_f32 v116, v116, s79, v193
	v_med3_f32 v8, v8, s79, v193
	v_med3_f32 v112, v112, s79, v193
	v_mov_b32_e32 v196, v9
	v_cvt_pk_fp8_f32 v194, v114, v116 op_sel:[0,0,1]
	v_mul_f32_e32 v114, 0x43800000, v124
	s_waitcnt vmcnt(31)
	v_mul_f32_e32 v116, 0x43800000, v126
	v_cvt_pk_fp8_f32 v196, v8, v112
	s_waitcnt vmcnt(29)
	v_mul_f32_e32 v8, 0x43800000, v136
	s_waitcnt vmcnt(28)
	v_mul_f32_e32 v112, 0x43800000, v138
	v_med3_f32 v114, v114, s79, v193
	v_med3_f32 v116, v116, s79, v193
	v_med3_f32 v8, v8, s79, v193
	v_med3_f32 v112, v112, s79, v193
	v_mov_b32_e32 v197, v9
	v_cvt_pk_fp8_f32 v195, v114, v116 op_sel:[0,0,1]
	s_waitcnt vmcnt(27)
	v_mul_f32_e32 v114, 0x43800000, v132
	v_mul_f32_e32 v116, 0x43800000, v134
	v_cvt_pk_fp8_f32 v197, v8, v112
	v_mul_f32_e32 v8, 0x43800000, v113
	v_mul_f32_e32 v112, 0x43800000, v115
	v_med3_f32 v114, v114, s79, v193
	v_med3_f32 v116, v116, s79, v193
	v_med3_f32 v8, v8, s79, v193
	v_med3_f32 v115, v112, s79, v193
	v_mov_b32_e32 v112, v9
	v_cvt_pk_fp8_f32 v196, v114, v116 op_sel:[0,0,1]
	s_waitcnt vmcnt(26)
	v_mul_f32_e32 v114, 0x43800000, v140
	s_waitcnt vmcnt(25)
	v_mul_f32_e32 v116, 0x43800000, v142
	v_cvt_pk_fp8_f32 v112, v8, v115
	v_med3_f32 v114, v114, s79, v193
	v_med3_f32 v116, v116, s79, v193
	v_cvt_pk_fp8_f32 v197, v114, v116 op_sel:[0,0,1]
	v_mul_f32_e32 v113, 0x43800000, v117
	v_mul_f32_e32 v114, 0x43800000, v119
	v_med3_f32 v113, v113, s79, v193
	v_med3_f32 v114, v114, s79, v193
	v_cvt_pk_fp8_f32 v112, v113, v114 op_sel:[0,0,1]
	v_mul_f32_e32 v8, 0x43800000, v121
	v_mul_f32_e32 v113, 0x43800000, v123
	v_med3_f32 v8, v8, s79, v193
	v_med3_f32 v116, v113, s79, v193
	v_mov_b32_e32 v113, v9
	v_cvt_pk_fp8_f32 v113, v8, v116
	v_mul_f32_e32 v114, 0x43800000, v125
	v_mul_f32_e32 v115, 0x43800000, v127
	v_med3_f32 v114, v114, s79, v193
	v_med3_f32 v115, v115, s79, v193
	v_cvt_pk_fp8_f32 v113, v114, v115 op_sel:[0,0,1]
	v_mul_f32_e32 v8, 0x43800000, v129
	v_mul_f32_e32 v114, 0x43800000, v131
	v_med3_f32 v8, v8, s79, v193
	v_med3_f32 v117, v114, s79, v193
	v_mov_b32_e32 v114, v9
	v_cvt_pk_fp8_f32 v114, v8, v117
	v_mul_f32_e32 v115, 0x43800000, v133
	v_mul_f32_e32 v116, 0x43800000, v135
	v_med3_f32 v115, v115, s79, v193
	v_med3_f32 v116, v116, s79, v193
	v_cvt_pk_fp8_f32 v114, v115, v116 op_sel:[0,0,1]
	v_mul_f32_e32 v8, 0x43800000, v137
	v_mul_f32_e32 v115, 0x43800000, v139
	v_med3_f32 v8, v8, s79, v193
	v_med3_f32 v118, v115, s79, v193
	v_mov_b32_e32 v115, v9
	v_add_co_u32_e32 v98, vcc, s30, v2
	v_cvt_pk_fp8_f32 v115, v8, v118
	s_nop 0
	v_addc_co_u32_e32 v99, vcc, 0, v3, vcc
	s_mov_b32 s11, 0xba000
	v_add_co_u32_e32 v104, vcc, s11, v2
	v_mul_f32_e32 v116, 0x43800000, v141
	v_mul_f32_e32 v117, 0x43800000, v143
	v_addc_co_u32_e32 v105, vcc, 0, v3, vcc
; #define CV_LOAD(v, kb) do { _Pragma("unroll") for (int j = 0; j < 16; ++j) v[j] = __builtin_nontemporal_load((const f32x2*)(src + (size_t)((kb) * 16 + j) * ldw)); } while (0)
; __device__ __forceinline__ void tr128_f8(const float* W, int ldw, int srccol, unsigned char* WT, size_t dstrow0, int K, int k0, LAS unsigned char* tile, int lane) {
;     ...
;     CV_LOAD(va, 0); CV_LOAD(vb, 1); CV_LOAD(vc, 2);
;     CV_LOAD(vd, 3); CV_PUT(va, 0); CV_LOAD(va, 4); CV_PUT(vb, 1); CV_LOAD(vb, 5); CV_PUT(vc, 2); CV_LOAD(vc, 6); CV_PUT(vd, 3); CV_LOAD(vd, 7);
;     CV_PUT(va, 4); CV_PUT(vb, 5); CV_PUT(vc, 6); CV_PUT(vd, 7);
	v_med3_f32 v116, v116, s79, v193
	v_med3_f32 v117, v117, s79, v193
	v_add_co_u32_e32 v108, vcc, s15, v2
	v_cvt_pk_fp8_f32 v115, v116, v117 op_sel:[0,0,1]
	s_nop 0
	v_addc_co_u32_e32 v109, vcc, 0, v3, vcc
	s_mov_b32 s11, 0xbe000
	v_add_co_u32_e32 v110, vcc, s11, v2
	v_add_u32_e32 v116, v13, v19
	s_nop 0
	v_addc_co_u32_e32 v111, vcc, 0, v3, vcc
	ds_write_b128 v116, v[112:115]
	v_add_co_u32_e32 v112, vcc, s17, v2
	s_mov_b32 s11, 0xc2000
	s_nop 0
	v_addc_co_u32_e32 v113, vcc, 0, v3, vcc
	v_add_co_u32_e32 v114, vcc, s11, v2
	s_mov_b32 s11, 0xc6000
	s_nop 0
	v_addc_co_u32_e32 v115, vcc, 0, v3, vcc
	v_add_co_u32_e32 v116, vcc, s19, v2
	global_load_dwordx2 v[112:113], v[112:113], off nt
	s_nop 0
	v_addc_co_u32_e32 v117, vcc, 0, v3, vcc
	global_load_dwordx2 v[114:115], v[114:115], off nt
	v_add_u32_e32 v8, v7, v17
	global_load_dwordx2 v[118:119], v[116:117], off nt
	v_add_co_u32_e32 v116, vcc, s11, v2
	s_mov_b32 s11, 0xca000
	s_nop 0
	v_addc_co_u32_e32 v117, vcc, 0, v3, vcc
	global_load_dwordx2 v[124:125], v[116:117], off nt
	v_add_co_u32_e32 v116, vcc, s28, v2
	global_load_dwordx2 v[4:5], v[4:5], off nt
	s_nop 0
	v_addc_co_u32_e32 v117, vcc, 0, v3, vcc
	v_add_co_u32_e32 v120, vcc, s11, v2
	global_load_dwordx2 v[50:51], v[50:51], off nt
	s_nop 0
	v_addc_co_u32_e32 v121, vcc, 0, v3, vcc
	v_add_co_u32_e32 v122, vcc, s52, v2
	s_mov_b32 s11, 0xce000
	s_nop 0
	v_addc_co_u32_e32 v123, vcc, 0, v3, vcc
	global_load_dwordx2 v[116:117], v[116:117], off nt
	s_waitcnt vmcnt(30)
	v_mul_f32_e32 v144, 0x43800000, v144
	global_load_dwordx2 v[120:121], v[120:121], off nt
	s_waitcnt vmcnt(30)
	v_mul_f32_e32 v146, 0x43800000, v146
	global_load_dwordx2 v[126:127], v[122:123], off nt
	v_add_co_u32_e32 v122, vcc, s11, v2
	global_load_dwordx2 v[54:55], v[54:55], off nt
	s_nop 0
	v_addc_co_u32_e32 v123, vcc, 0, v3, vcc
	global_load_dwordx2 v[56:57], v[56:57], off nt
	s_mov_b32 s11, 0xd2000
	global_load_dwordx2 v[58:59], v[58:59], off nt
	ds_write_b128 v8, v[194:197]
	global_load_dwordx2 v[132:133], v[122:123], off nt
	v_add_co_u32_e32 v122, vcc, s56, v2
	global_load_dwordx2 v[52:53], v[52:53], off nt
	s_nop 0
	v_addc_co_u32_e32 v123, vcc, 0, v3, vcc
	global_load_dwordx2 v[62:63], v[62:63], off nt
	v_add_co_u32_e32 v128, vcc, s11, v2
	global_load_dwordx2 v[64:65], v[64:65], off nt
	s_nop 0
	v_addc_co_u32_e32 v129, vcc, 0, v3, vcc
	global_load_dwordx2 v[66:67], v[66:67], off nt
	v_add_co_u32_e32 v130, vcc, s60, v2
	global_load_dwordx2 v[60:61], v[60:61], off nt
	s_nop 0
	v_addc_co_u32_e32 v131, vcc, 0, v3, vcc
	global_load_dwordx2 v[70:71], v[70:71], off nt
	s_mov_b32 s11, 0xd6000
	global_load_dwordx2 v[72:73], v[72:73], off nt
	v_med3_f32 v144, v144, s79, v193
	global_load_dwordx2 v[74:75], v[74:75], off nt
	v_med3_f32 v146, v146, s79, v193
	global_load_dwordx2 v[68:69], v[68:69], off nt
	v_mov_b32_e32 v194, v9
	global_load_dwordx2 v[122:123], v[122:123], off nt
	v_cvt_pk_fp8_f32 v194, v144, v146
	global_load_dwordx2 v[128:129], v[128:129], off nt
	v_mov_b32_e32 v195, v9
	global_load_dwordx2 v[134:135], v[130:131], off nt
	v_add_co_u32_e32 v130, vcc, s11, v2
	global_load_dwordx2 v[76:77], v[76:77], off nt
	s_nop 0
	v_addc_co_u32_e32 v131, vcc, 0, v3, vcc
	global_load_dwordx2 v[138:139], v[130:131], off nt
	s_waitcnt vmcnt(48)
	v_mul_f32_e32 v144, 0x43800000, v152
	s_waitcnt vmcnt(47)
	v_mul_f32_e32 v146, 0x43800000, v154
	v_med3_f32 v144, v144, s79, v193
	v_med3_f32 v146, v146, s79, v193
	s_waitcnt vmcnt(46)
	v_mul_f32_e32 v148, 0x43800000, v148
	s_waitcnt vmcnt(45)
	v_mul_f32_e32 v150, 0x43800000, v150
	v_cvt_pk_fp8_f32 v195, v144, v146
	s_waitcnt vmcnt(44)
	v_mul_f32_e32 v144, 0x43800000, v160
	s_waitcnt vmcnt(43)
	v_mul_f32_e32 v146, 0x43800000, v164
	v_med3_f32 v148, v148, s79, v193
	v_med3_f32 v150, v150, s79, v193
	v_med3_f32 v144, v144, s79, v193
	v_med3_f32 v146, v146, s79, v193
	v_mov_b32_e32 v196, v9
	v_cvt_pk_fp8_f32 v194, v148, v150 op_sel:[0,0,1]
	s_waitcnt vmcnt(42)
	v_mul_f32_e32 v148, 0x43800000, v156
	s_waitcnt vmcnt(41)
	v_mul_f32_e32 v150, 0x43800000, v158
	v_cvt_pk_fp8_f32 v196, v144, v146
	s_waitcnt vmcnt(40)
	v_mul_f32_e32 v144, 0x43800000, v170
	s_waitcnt vmcnt(39)
	v_mul_f32_e32 v146, 0x43800000, v172
	v_med3_f32 v148, v148, s79, v193
	v_med3_f32 v150, v150, s79, v193
	v_med3_f32 v144, v144, s79, v193
	v_med3_f32 v146, v146, s79, v193
	v_mov_b32_e32 v197, v9
	v_cvt_pk_fp8_f32 v195, v148, v150 op_sel:[0,0,1]
	s_waitcnt vmcnt(38)
	v_mul_f32_e32 v148, 0x43800000, v166
	s_waitcnt vmcnt(37)
	v_mul_f32_e32 v150, 0x43800000, v168
	v_cvt_pk_fp8_f32 v197, v144, v146
	v_med3_f32 v148, v148, s79, v193
	v_med3_f32 v150, v150, s79, v193
	v_cvt_pk_fp8_f32 v196, v148, v150 op_sel:[0,0,1]
	s_waitcnt vmcnt(36)
	v_mul_f32_e32 v148, 0x43800000, v174
	s_waitcnt vmcnt(35)
; #define CV_LOAD(v, kb) do { _Pragma("unroll") for (int j = 0; j < 16; ++j) v[j] = __builtin_nontemporal_load((const f32x2*)(src + (size_t)((kb) * 16 + j) * ldw)); } while (0)
; __device__ __forceinline__ void tr128_f8(const float* W, int ldw, int srccol, unsigned char* WT, size_t dstrow0, int K, int k0, LAS unsigned char* tile, int lane) {
;     ...
;     CV_LOAD(va, 0); CV_LOAD(vb, 1); CV_LOAD(vc, 2);
;     CV_LOAD(vd, 3); CV_PUT(va, 0); CV_LOAD(va, 4); CV_PUT(vb, 1); CV_LOAD(vb, 5); CV_PUT(vc, 2); CV_LOAD(vc, 6); CV_PUT(vd, 3); CV_LOAD(vd, 7);
;     CV_PUT(va, 4); CV_PUT(vb, 5); CV_PUT(vc, 6); CV_PUT(vd, 7);
	v_mul_f32_e32 v150, 0x43800000, v176
	v_med3_f32 v148, v148, s79, v193
	v_med3_f32 v150, v150, s79, v193
	v_mul_f32_e32 v144, 0x43800000, v145
	v_mul_f32_e32 v145, 0x43800000, v147
	v_cvt_pk_fp8_f32 v197, v148, v150 op_sel:[0,0,1]
	v_med3_f32 v148, v144, s79, v193
	v_med3_f32 v145, v145, s79, v193
	v_mov_b32_e32 v144, v9
	v_cvt_pk_fp8_f32 v144, v148, v145
	v_mul_f32_e32 v146, 0x43800000, v149
	v_mul_f32_e32 v147, 0x43800000, v151
	v_med3_f32 v146, v146, s79, v193
	v_med3_f32 v147, v147, s79, v193
	v_cvt_pk_fp8_f32 v144, v146, v147 op_sel:[0,0,1]
	v_mul_f32_e32 v145, 0x43800000, v153
	v_mul_f32_e32 v146, 0x43800000, v155
	v_med3_f32 v149, v145, s79, v193
	v_med3_f32 v146, v146, s79, v193
	v_mov_b32_e32 v145, v9
	v_cvt_pk_fp8_f32 v145, v149, v146
	v_mul_f32_e32 v147, 0x43800000, v157
	v_mul_f32_e32 v148, 0x43800000, v159
	v_med3_f32 v147, v147, s79, v193
	v_med3_f32 v148, v148, s79, v193
	v_cvt_pk_fp8_f32 v145, v147, v148 op_sel:[0,0,1]
	v_mul_f32_e32 v146, 0x43800000, v161
	v_mul_f32_e32 v147, 0x43800000, v165
	v_med3_f32 v150, v146, s79, v193
	v_med3_f32 v147, v147, s79, v193
	v_mov_b32_e32 v146, v9
	v_cvt_pk_fp8_f32 v146, v150, v147
	v_mul_f32_e32 v148, 0x43800000, v167
	v_mul_f32_e32 v149, 0x43800000, v169
	v_med3_f32 v148, v148, s79, v193
	v_med3_f32 v149, v149, s79, v193
	v_cvt_pk_fp8_f32 v146, v148, v149 op_sel:[0,0,1]
	v_mul_f32_e32 v147, 0x43800000, v171
	v_mul_f32_e32 v148, 0x43800000, v173
	v_med3_f32 v151, v147, s79, v193
	v_med3_f32 v148, v148, s79, v193
	v_mov_b32_e32 v147, v9
	global_load_dwordx2 v[80:81], v[80:81], off nt
	v_add_co_u32_e32 v130, vcc, s64, v2
	global_load_dwordx2 v[82:83], v[82:83], off nt
	v_cvt_pk_fp8_f32 v147, v151, v148
	global_load_dwordx2 v[84:85], v[84:85], off nt
	v_addc_co_u32_e32 v131, vcc, 0, v3, vcc
	s_mov_b32 s11, 0xda000
	v_add_co_u32_e32 v136, vcc, s11, v2
	v_mul_f32_e32 v149, 0x43800000, v175
	v_mul_f32_e32 v150, 0x43800000, v177
	v_addc_co_u32_e32 v137, vcc, 0, v3, vcc
	v_med3_f32 v149, v149, s79, v193
	v_med3_f32 v150, v150, s79, v193
	global_load_dwordx2 v[86:87], v[86:87], off nt
	v_add_co_u32_e32 v140, vcc, s68, v2
	v_cvt_pk_fp8_f32 v147, v149, v150 op_sel:[0,0,1]
	s_nop 0
	v_addc_co_u32_e32 v141, vcc, 0, v3, vcc
	s_mov_b32 s11, 0xde000
	v_add_co_u32_e32 v142, vcc, s11, v2
	ds_write_b128 v8, v[194:197] offset:16
	s_nop 0
	v_addc_co_u32_e32 v143, vcc, 0, v3, vcc
	v_add_u32_e32 v8, v13, v21
	ds_write_b128 v8, v[144:147]
	v_add_co_u32_e32 v144, vcc, s72, v2
	s_mov_b32 s11, 0xe2000
	s_nop 0
	v_addc_co_u32_e32 v145, vcc, 0, v3, vcc
	v_add_co_u32_e32 v146, vcc, s11, v2
	s_mov_b32 s11, 0xe6000
	s_nop 0
	v_addc_co_u32_e32 v147, vcc, 0, v3, vcc
	v_add_co_u32_e32 v148, vcc, s76, v2
	global_load_dwordx2 v[144:145], v[144:145], off nt
	s_nop 0
	v_addc_co_u32_e32 v149, vcc, 0, v3, vcc
	global_load_dwordx2 v[146:147], v[146:147], off nt
	s_waitcnt vmcnt(27)
	v_mul_f32_e32 v8, 0x43800000, v50
	global_load_dwordx2 v[150:151], v[148:149], off nt
	v_add_co_u32_e32 v148, vcc, s11, v2
	s_mov_b32 s11, 0xea000
	s_nop 0
	v_addc_co_u32_e32 v149, vcc, 0, v3, vcc
	global_load_dwordx2 v[156:157], v[148:149], off nt
	v_add_co_u32_e32 v148, vcc, s81, v2
	global_load_dwordx2 v[98:99], v[98:99], off nt
	s_nop 0
	v_addc_co_u32_e32 v149, vcc, 0, v3, vcc
	global_load_dwordx2 v[104:105], v[104:105], off nt
	v_add_co_u32_e32 v152, vcc, s11, v2
	global_load_dwordx2 v[108:109], v[108:109], off nt
	s_nop 0
	v_addc_co_u32_e32 v153, vcc, 0, v3, vcc
	v_add_co_u32_e32 v154, vcc, s85, v2
	s_mov_b32 s11, 0xee000
	s_nop 0
	v_addc_co_u32_e32 v155, vcc, 0, v3, vcc
	global_load_dwordx2 v[110:111], v[110:111], off nt
	v_med3_f32 v8, v8, s79, v193
	global_load_dwordx2 v[148:149], v[148:149], off nt
	v_mov_b32_e32 v194, v9
	global_load_dwordx2 v[152:153], v[152:153], off nt
	v_mov_b32_e32 v195, v9
	global_load_dwordx2 v[158:159], v[154:155], off nt
	v_add_co_u32_e32 v154, vcc, s11, v2
	s_mov_b32 s11, 0xf2000
	s_nop 0
	v_addc_co_u32_e32 v155, vcc, 0, v3, vcc
	global_load_dwordx2 v[166:167], v[154:155], off nt
	v_add_co_u32_e32 v154, vcc, s89, v2
	s_waitcnt vmcnt(29)
	v_mul_f32_e32 v50, 0x43800000, v52
	v_addc_co_u32_e32 v155, vcc, 0, v3, vcc
	v_add_co_u32_e32 v160, vcc, s11, v2
	s_mov_b32 s11, 0xf6000
	s_nop 0
	v_addc_co_u32_e32 v161, vcc, 0, v3, vcc
	v_add_co_u32_e32 v164, vcc, s93, v2
	global_load_dwordx2 v[154:155], v[154:155], off nt
	s_nop 0
	v_addc_co_u32_e32 v165, vcc, 0, v3, vcc
	global_load_dwordx2 v[160:161], v[160:161], off nt
	v_mul_f32_e32 v52, 0x43800000, v54
	global_load_dwordx2 v[168:169], v[164:165], off nt
	v_add_co_u32_e32 v164, vcc, s11, v2
	s_mov_b32 s11, 0xfa000
	s_nop 0
	v_addc_co_u32_e32 v165, vcc, 0, v3, vcc
	global_load_dwordx2 v[172:173], v[164:165], off nt
	v_add_co_u32_e32 v164, vcc, s97, v2
	v_med3_f32 v50, v50, s79, v193
	s_nop 0
	v_addc_co_u32_e32 v165, vcc, 0, v3, vcc
	v_add_co_u32_e32 v170, vcc, s11, v2
	s_mov_b32 s11, 0xfe000
	s_nop 0
	v_addc_co_u32_e32 v171, vcc, 0, v3, vcc
	v_add_co_u32_e32 v174, vcc, s16, v2
	v_med3_f32 v52, v52, s79, v193
	s_nop 0
	v_addc_co_u32_e32 v175, vcc, 0, v3, vcc
	v_add_co_u32_e32 v2, vcc, s11, v2
	v_mov_b32_e32 v196, v9
	s_nop 0
	v_addc_co_u32_e32 v3, vcc, 0, v3, vcc
	global_load_dwordx2 v[2:3], v[2:3], off nt
	v_mul_f32_e32 v4, 0x43800000, v4
	v_med3_f32 v4, v4, s79, v193
	v_cvt_pk_fp8_f32 v194, v4, v8
	v_mul_f32_e32 v4, 0x43800000, v56
	v_mul_f32_e32 v8, 0x43800000, v58
	v_med3_f32 v4, v4, s79, v193
	v_med3_f32 v8, v8, s79, v193
	v_cvt_pk_fp8_f32 v195, v4, v8
	s_waitcnt vmcnt(32)
	v_mul_f32_e32 v4, 0x43800000, v64
	s_waitcnt vmcnt(31)
	v_mul_f32_e32 v8, 0x43800000, v66
	v_med3_f32 v4, v4, s79, v193
	v_med3_f32 v8, v8, s79, v193
	v_cvt_pk_fp8_f32 v194, v50, v52 op_sel:[0,0,1]
	s_waitcnt vmcnt(30)
; #define CV_LOAD(v, kb) do { _Pragma("unroll") for (int j = 0; j < 16; ++j) v[j] = __builtin_nontemporal_load((const f32x2*)(src + (size_t)((kb) * 16 + j) * ldw)); } while (0)
; __device__ __forceinline__ void tr128_f8(const float* W, int ldw, int srccol, unsigned char* WT, size_t dstrow0, int K, int k0, LAS unsigned char* tile, int lane) {
;     ...
;     CV_LOAD(va, 0); CV_LOAD(vb, 1); CV_LOAD(vc, 2);
;     CV_LOAD(vd, 3); CV_PUT(va, 0); CV_LOAD(va, 4); CV_PUT(vb, 1); CV_LOAD(vb, 5); CV_PUT(vc, 2); CV_LOAD(vc, 6); CV_PUT(vd, 3); CV_LOAD(vd, 7);
;     CV_PUT(va, 4); CV_PUT(vb, 5); CV_PUT(vc, 6); CV_PUT(vd, 7);
	v_mul_f32_e32 v50, 0x43800000, v60
	v_mul_f32_e32 v52, 0x43800000, v62
	v_cvt_pk_fp8_f32 v196, v4, v8
	s_waitcnt vmcnt(28)
	v_mul_f32_e32 v4, 0x43800000, v72
	s_waitcnt vmcnt(27)
	v_mul_f32_e32 v8, 0x43800000, v74
	v_med3_f32 v50, v50, s79, v193
	v_med3_f32 v52, v52, s79, v193
	v_med3_f32 v4, v4, s79, v193
	v_med3_f32 v8, v8, s79, v193
	v_mov_b32_e32 v197, v9
	v_cvt_pk_fp8_f32 v195, v50, v52 op_sel:[0,0,1]
	s_waitcnt vmcnt(26)
	v_mul_f32_e32 v50, 0x43800000, v68
	v_mul_f32_e32 v52, 0x43800000, v70
	v_cvt_pk_fp8_f32 v197, v4, v8
	v_med3_f32 v50, v50, s79, v193
	v_med3_f32 v52, v52, s79, v193
	v_cvt_pk_fp8_f32 v196, v50, v52 op_sel:[0,0,1]
	s_waitcnt vmcnt(22)
	v_mul_f32_e32 v50, 0x43800000, v76
	v_mul_f32_e32 v52, 0x43800000, v78
	v_med3_f32 v50, v50, s79, v193
	v_med3_f32 v52, v52, s79, v193
	v_cvt_pk_fp8_f32 v197, v50, v52 op_sel:[0,0,1]
	v_mul_f32_e32 v4, 0x43800000, v5
	v_mul_f32_e32 v5, 0x43800000, v51
	v_mul_f32_e32 v50, 0x43800000, v55
	v_med3_f32 v4, v4, s79, v193
	v_med3_f32 v5, v5, s79, v193
	v_med3_f32 v51, v50, s79, v193
	v_mov_b32_e32 v50, v9
	v_cvt_pk_fp8_f32 v50, v4, v5
	v_mul_f32_e32 v8, 0x43800000, v53
	v_med3_f32 v8, v8, s79, v193
	v_mul_f32_e32 v4, 0x43800000, v57
	v_cvt_pk_fp8_f32 v50, v8, v51 op_sel:[0,0,1]
	v_mul_f32_e32 v5, 0x43800000, v59
	v_mul_f32_e32 v51, 0x43800000, v63
	v_med3_f32 v4, v4, s79, v193
	v_med3_f32 v5, v5, s79, v193
	v_med3_f32 v52, v51, s79, v193
	v_mov_b32_e32 v51, v9
	v_cvt_pk_fp8_f32 v51, v4, v5
	v_mul_f32_e32 v8, 0x43800000, v61
	v_med3_f32 v8, v8, s79, v193
	v_mul_f32_e32 v4, 0x43800000, v65
	v_cvt_pk_fp8_f32 v51, v8, v52 op_sel:[0,0,1]
	v_mul_f32_e32 v5, 0x43800000, v67
	v_mul_f32_e32 v52, 0x43800000, v71
	v_med3_f32 v4, v4, s79, v193
	v_med3_f32 v5, v5, s79, v193
	v_med3_f32 v53, v52, s79, v193
	v_mov_b32_e32 v52, v9
	v_cvt_pk_fp8_f32 v52, v4, v5
	v_mul_f32_e32 v8, 0x43800000, v69
	v_med3_f32 v8, v8, s79, v193
	global_load_dwordx2 v[130:131], v[130:131], off nt
	v_cvt_pk_fp8_f32 v52, v8, v53 op_sel:[0,0,1]
	global_load_dwordx2 v[136:137], v[136:137], off nt
	v_mul_f32_e32 v4, 0x43800000, v73
	global_load_dwordx2 v[140:141], v[140:141], off nt
	v_mul_f32_e32 v5, 0x43800000, v75
	global_load_dwordx2 v[142:143], v[142:143], off nt
	v_mul_f32_e32 v53, 0x43800000, v79
	v_med3_f32 v4, v4, s79, v193
	v_med3_f32 v5, v5, s79, v193
	v_med3_f32 v54, v53, s79, v193
	v_mov_b32_e32 v53, v9
	v_cvt_pk_fp8_f32 v53, v4, v5
	v_mul_f32_e32 v8, 0x43800000, v77
	v_med3_f32 v8, v8, s79, v193
	v_add_u32_e32 v5, v13, v25
	v_cvt_pk_fp8_f32 v53, v8, v54 op_sel:[0,0,1]
	s_waitcnt vmcnt(23)
	v_mul_f32_e32 v8, 0x43800000, v82
	v_med3_f32 v8, v8, s79, v193
	global_load_dwordx2 v[164:165], v[164:165], off nt
	ds_write_b128 v5, v[50:53]
	v_mul_f32_e32 v5, 0x43800000, v80
	s_waitcnt vmcnt(23)
	v_mul_f32_e32 v50, 0x43800000, v84
	v_med3_f32 v5, v5, s79, v193
	v_med3_f32 v52, v50, s79, v193
	v_mov_b32_e32 v50, v9
	v_cvt_pk_fp8_f32 v50, v5, v8
	s_waitcnt vmcnt(22)
	v_mul_f32_e32 v51, 0x43800000, v86
	v_med3_f32 v51, v51, s79, v193
	v_mul_f32_e32 v5, 0x43800000, v88
	v_cvt_pk_fp8_f32 v50, v52, v51 op_sel:[0,0,1]
	v_mul_f32_e32 v8, 0x43800000, v90
	v_mul_f32_e32 v51, 0x43800000, v94
	v_med3_f32 v5, v5, s79, v193
	v_med3_f32 v8, v8, s79, v193
	v_med3_f32 v53, v51, s79, v193
	v_mov_b32_e32 v51, v9
	v_cvt_pk_fp8_f32 v51, v5, v8
	v_mul_f32_e32 v52, 0x43800000, v100
	v_med3_f32 v52, v52, s79, v193
	v_mul_f32_e32 v5, 0x43800000, v92
	v_cvt_pk_fp8_f32 v51, v53, v52 op_sel:[0,0,1]
	v_mul_f32_e32 v8, 0x43800000, v96
	v_mul_f32_e32 v52, 0x43800000, v102
	v_med3_f32 v5, v5, s79, v193
	v_med3_f32 v8, v8, s79, v193
	v_med3_f32 v54, v52, s79, v193
	v_mov_b32_e32 v52, v9
	v_cvt_pk_fp8_f32 v52, v5, v8
	v_mul_f32_e32 v53, 0x43800000, v106
	v_med3_f32 v53, v53, s79, v193
	s_waitcnt vmcnt(17)
	v_mul_f32_e32 v5, 0x43800000, v98
	v_cvt_pk_fp8_f32 v52, v54, v53 op_sel:[0,0,1]
	s_waitcnt vmcnt(16)
	v_mul_f32_e32 v8, 0x43800000, v104
	s_waitcnt vmcnt(15)
	v_mul_f32_e32 v53, 0x43800000, v108
	v_med3_f32 v5, v5, s79, v193
	v_med3_f32 v8, v8, s79, v193
	v_med3_f32 v55, v53, s79, v193
	v_mov_b32_e32 v53, v9
	v_cvt_pk_fp8_f32 v53, v5, v8
	s_waitcnt vmcnt(14)
	v_mul_f32_e32 v54, 0x43800000, v110
	v_med3_f32 v54, v54, s79, v193
	v_mul_f32_e32 v5, 0x43800000, v81
	v_cvt_pk_fp8_f32 v53, v55, v54 op_sel:[0,0,1]
	v_mul_f32_e32 v8, 0x43800000, v83
	v_mul_f32_e32 v54, 0x43800000, v85
	v_med3_f32 v5, v5, s79, v193
	v_med3_f32 v8, v8, s79, v193
	v_med3_f32 v56, v54, s79, v193
	v_mov_b32_e32 v54, v9
	v_cvt_pk_fp8_f32 v54, v5, v8
	v_mul_f32_e32 v55, 0x43800000, v87
	v_med3_f32 v55, v55, s79, v193
	v_mul_f32_e32 v5, 0x43800000, v89
	v_cvt_pk_fp8_f32 v54, v56, v55 op_sel:[0,0,1]
	v_mul_f32_e32 v8, 0x43800000, v91
	v_mul_f32_e32 v55, 0x43800000, v95
	v_med3_f32 v5, v5, s79, v193
	v_med3_f32 v8, v8, s79, v193
	v_med3_f32 v57, v55, s79, v193
	v_mov_b32_e32 v55, v9
	v_cvt_pk_fp8_f32 v55, v5, v8
	v_mul_f32_e32 v56, 0x43800000, v101
	v_med3_f32 v56, v56, s79, v193
	v_mul_f32_e32 v5, 0x43800000, v93
	v_cvt_pk_fp8_f32 v55, v57, v56 op_sel:[0,0,1]
	v_mul_f32_e32 v8, 0x43800000, v97
	v_mul_f32_e32 v56, 0x43800000, v103
	v_med3_f32 v5, v5, s79, v193
	v_med3_f32 v8, v8, s79, v193
	v_med3_f32 v58, v56, s79, v193
	v_mov_b32_e32 v56, v9
	v_cvt_pk_fp8_f32 v56, v5, v8
	v_mul_f32_e32 v57, 0x43800000, v107
	v_med3_f32 v57, v57, s79, v193
	global_load_dwordx2 v[170:171], v[170:171], off nt
	v_cvt_pk_fp8_f32 v56, v58, v57 op_sel:[0,0,1]
	global_load_dwordx2 v[174:175], v[174:175], off nt
	v_mul_f32_e32 v5, 0x43800000, v99
	v_mul_f32_e32 v8, 0x43800000, v105
	v_mul_f32_e32 v57, 0x43800000, v109
	v_med3_f32 v5, v5, s79, v193
	v_med3_f32 v8, v8, s79, v193
	v_med3_f32 v59, v57, s79, v193
	v_mov_b32_e32 v57, v9
	v_cvt_pk_fp8_f32 v57, v5, v8
	v_mul_f32_e32 v58, 0x43800000, v111
	v_med3_f32 v58, v58, s79, v193
	v_add_u32_e32 v4, v7, v23
	v_cvt_pk_fp8_f32 v57, v59, v58 op_sel:[0,0,1]
	ds_write_b128 v4, v[194:197]
	ds_write_b128 v4, v[50:53] offset:16
	v_add_u32_e32 v4, v13, v27
	ds_write_b128 v4, v[54:57]
	v_mul_f32_e32 v4, 0x43800000, v112
	v_mul_f32_e32 v5, 0x43800000, v114
	v_mul_f32_e32 v50, 0x43800000, v124
	v_med3_f32 v4, v4, s79, v193
	v_med3_f32 v5, v5, s79, v193
	v_med3_f32 v51, v50, s79, v193
	v_mov_b32_e32 v50, v9
	v_cvt_pk_fp8_f32 v50, v4, v5
	v_mul_f32_e32 v8, 0x43800000, v118
	v_med3_f32 v8, v8, s79, v193
	v_mul_f32_e32 v4, 0x43800000, v116
	v_cvt_pk_fp8_f32 v50, v8, v51 op_sel:[0,0,1]
	v_mul_f32_e32 v5, 0x43800000, v120
	v_mul_f32_e32 v51, 0x43800000, v132
	v_med3_f32 v4, v4, s79, v193
	v_med3_f32 v5, v5, s79, v193
	v_med3_f32 v52, v51, s79, v193
	v_mov_b32_e32 v51, v9
	v_cvt_pk_fp8_f32 v51, v4, v5
	v_mul_f32_e32 v8, 0x43800000, v126
	v_med3_f32 v8, v8, s79, v193
	v_mul_f32_e32 v4, 0x43800000, v122
	v_cvt_pk_fp8_f32 v51, v8, v52 op_sel:[0,0,1]
	v_mul_f32_e32 v5, 0x43800000, v128
	v_mul_f32_e32 v52, 0x43800000, v138
	v_med3_f32 v4, v4, s79, v193
	v_med3_f32 v5, v5, s79, v193
	v_med3_f32 v53, v52, s79, v193
	v_mov_b32_e32 v52, v9
	v_cvt_pk_fp8_f32 v52, v4, v5
	v_mul_f32_e32 v8, 0x43800000, v134
	v_med3_f32 v8, v8, s79, v193
	s_waitcnt vmcnt(6)
; #define LDS_WAIT() asm volatile("s_waitcnt lgkmcnt(0)" ::: "memory")
; #define CV_LOAD(v, kb) do { _Pragma("unroll") for (int j = 0; j < 16; ++j) v[j] = __builtin_nontemporal_load((const f32x2*)(src + (size_t)((kb) * 16 + j) * ldw)); } while (0)
; __device__ __forceinline__ void tr128_f8(const float* W, int ldw, int srccol, unsigned char* WT, size_t dstrow0, int K, int k0, LAS unsigned char* tile, int lane) {
;     ...
;     CV_LOAD(va, 0); CV_LOAD(vb, 1); CV_LOAD(vc, 2);
;     CV_LOAD(vd, 3); CV_PUT(va, 0); CV_LOAD(va, 4); CV_PUT(vb, 1); CV_LOAD(vb, 5); CV_PUT(vc, 2); CV_LOAD(vc, 6); CV_PUT(vd, 3); CV_LOAD(vd, 7);
;     CV_PUT(va, 4); CV_PUT(vb, 5); CV_PUT(vc, 6); CV_PUT(vd, 7);
;     ...
;     LDS_WAIT(); asm volatile("" ::: "memory");
	v_mul_f32_e32 v4, 0x43800000, v130
	v_cvt_pk_fp8_f32 v52, v8, v53 op_sel:[0,0,1]
	s_waitcnt vmcnt(5)
	v_mul_f32_e32 v5, 0x43800000, v136
	s_waitcnt vmcnt(3)
	v_mul_f32_e32 v53, 0x43800000, v142
	v_med3_f32 v4, v4, s79, v193
	v_med3_f32 v5, v5, s79, v193
	v_med3_f32 v54, v53, s79, v193
	v_mov_b32_e32 v53, v9
	v_cvt_pk_fp8_f32 v53, v4, v5
	v_mul_f32_e32 v8, 0x43800000, v140
	v_med3_f32 v8, v8, s79, v193
	v_mul_f32_e32 v4, 0x43800000, v113
	v_cvt_pk_fp8_f32 v53, v8, v54 op_sel:[0,0,1]
	v_mul_f32_e32 v5, 0x43800000, v115
	v_mul_f32_e32 v54, 0x43800000, v125
	v_med3_f32 v4, v4, s79, v193
	v_med3_f32 v5, v5, s79, v193
	v_med3_f32 v55, v54, s79, v193
	v_mov_b32_e32 v54, v9
	v_cvt_pk_fp8_f32 v54, v4, v5
	v_mul_f32_e32 v8, 0x43800000, v119
	v_med3_f32 v8, v8, s79, v193
	v_mul_f32_e32 v4, 0x43800000, v117
	v_cvt_pk_fp8_f32 v54, v8, v55 op_sel:[0,0,1]
	v_mul_f32_e32 v5, 0x43800000, v121
	v_mul_f32_e32 v55, 0x43800000, v133
	v_med3_f32 v4, v4, s79, v193
	v_med3_f32 v5, v5, s79, v193
	v_med3_f32 v56, v55, s79, v193
	v_mov_b32_e32 v55, v9
	v_cvt_pk_fp8_f32 v55, v4, v5
	v_mul_f32_e32 v8, 0x43800000, v127
	v_med3_f32 v8, v8, s79, v193
	v_mul_f32_e32 v4, 0x43800000, v123
	v_cvt_pk_fp8_f32 v55, v8, v56 op_sel:[0,0,1]
	v_mul_f32_e32 v5, 0x43800000, v129
	v_mul_f32_e32 v56, 0x43800000, v139
	v_med3_f32 v4, v4, s79, v193
	v_med3_f32 v5, v5, s79, v193
	v_med3_f32 v57, v56, s79, v193
	v_mov_b32_e32 v56, v9
	v_cvt_pk_fp8_f32 v56, v4, v5
	v_mul_f32_e32 v8, 0x43800000, v135
	v_med3_f32 v8, v8, s79, v193
	v_mul_f32_e32 v4, 0x43800000, v131
	v_cvt_pk_fp8_f32 v56, v8, v57 op_sel:[0,0,1]
	v_mul_f32_e32 v5, 0x43800000, v137
	v_mul_f32_e32 v57, 0x43800000, v143
	v_med3_f32 v4, v4, s79, v193
	v_med3_f32 v5, v5, s79, v193
	v_med3_f32 v58, v57, s79, v193
	v_mov_b32_e32 v57, v9
	v_cvt_pk_fp8_f32 v57, v4, v5
	v_mul_f32_e32 v8, 0x43800000, v141
	v_med3_f32 v8, v8, s79, v193
	v_add_u32_e32 v4, v7, v29
	v_cvt_pk_fp8_f32 v57, v8, v58 op_sel:[0,0,1]
	v_add_u32_e32 v5, v13, v31
	ds_write_b128 v4, v[50:53]
	v_mul_f32_e32 v8, 0x43800000, v146
	ds_write_b128 v5, v[54:57]
	v_mul_f32_e32 v5, 0x43800000, v144
	v_mul_f32_e32 v50, 0x43800000, v150
	v_med3_f32 v5, v5, s79, v193
	v_med3_f32 v8, v8, s79, v193
	v_med3_f32 v52, v50, s79, v193
	v_mov_b32_e32 v50, v9
	v_cvt_pk_fp8_f32 v50, v5, v8
	v_mul_f32_e32 v51, 0x43800000, v156
	v_med3_f32 v51, v51, s79, v193
	v_mul_f32_e32 v5, 0x43800000, v148
	v_cvt_pk_fp8_f32 v50, v52, v51 op_sel:[0,0,1]
	v_mul_f32_e32 v8, 0x43800000, v152
	v_mul_f32_e32 v51, 0x43800000, v158
	v_med3_f32 v5, v5, s79, v193
	v_med3_f32 v8, v8, s79, v193
	v_med3_f32 v53, v51, s79, v193
	v_mov_b32_e32 v51, v9
	v_cvt_pk_fp8_f32 v51, v5, v8
	v_mul_f32_e32 v52, 0x43800000, v166
	v_med3_f32 v52, v52, s79, v193
	v_mul_f32_e32 v5, 0x43800000, v154
	v_cvt_pk_fp8_f32 v51, v53, v52 op_sel:[0,0,1]
	v_mul_f32_e32 v8, 0x43800000, v160
	v_mul_f32_e32 v52, 0x43800000, v168
	v_med3_f32 v5, v5, s79, v193
	v_med3_f32 v8, v8, s79, v193
	v_med3_f32 v54, v52, s79, v193
	v_mov_b32_e32 v52, v9
	v_cvt_pk_fp8_f32 v52, v5, v8
	v_mul_f32_e32 v53, 0x43800000, v172
	v_med3_f32 v53, v53, s79, v193
	s_waitcnt vmcnt(2)
	v_mul_f32_e32 v5, 0x43800000, v164
	v_cvt_pk_fp8_f32 v52, v54, v53 op_sel:[0,0,1]
	s_waitcnt vmcnt(1)
	v_mul_f32_e32 v8, 0x43800000, v170
	s_waitcnt vmcnt(0)
	v_mul_f32_e32 v53, 0x43800000, v174
	v_med3_f32 v5, v5, s79, v193
	v_med3_f32 v8, v8, s79, v193
	v_med3_f32 v54, v53, s79, v193
	v_mov_b32_e32 v53, v9
	v_cvt_pk_fp8_f32 v53, v5, v8
	v_mul_f32_e32 v2, 0x43800000, v2
	v_med3_f32 v2, v2, s79, v193
	v_mul_f32_e32 v5, 0x43800000, v147
	v_cvt_pk_fp8_f32 v53, v54, v2 op_sel:[0,0,1]
	v_mul_f32_e32 v2, 0x43800000, v145
	v_mul_f32_e32 v54, 0x43800000, v157
	v_med3_f32 v2, v2, s79, v193
	v_med3_f32 v5, v5, s79, v193
	v_med3_f32 v55, v54, s79, v193
	v_mov_b32_e32 v54, v9
	v_cvt_pk_fp8_f32 v54, v2, v5
	v_mul_f32_e32 v8, 0x43800000, v151
	v_med3_f32 v8, v8, s79, v193
	v_mul_f32_e32 v2, 0x43800000, v149
	v_cvt_pk_fp8_f32 v54, v8, v55 op_sel:[0,0,1]
	v_mul_f32_e32 v5, 0x43800000, v153
	v_mul_f32_e32 v55, 0x43800000, v167
	v_med3_f32 v2, v2, s79, v193
	v_med3_f32 v5, v5, s79, v193
	v_med3_f32 v56, v55, s79, v193
	v_mov_b32_e32 v55, v9
	v_cvt_pk_fp8_f32 v55, v2, v5
	v_mul_f32_e32 v8, 0x43800000, v159
	v_med3_f32 v8, v8, s79, v193
	v_mul_f32_e32 v2, 0x43800000, v155
	v_cvt_pk_fp8_f32 v55, v8, v56 op_sel:[0,0,1]
	v_mul_f32_e32 v5, 0x43800000, v161
	v_mul_f32_e32 v56, 0x43800000, v173
	v_med3_f32 v2, v2, s79, v193
	v_med3_f32 v5, v5, s79, v193
	v_med3_f32 v57, v56, s79, v193
	v_mov_b32_e32 v56, v9
	v_cvt_pk_fp8_f32 v56, v2, v5
	v_mul_f32_e32 v8, 0x43800000, v169
	v_med3_f32 v8, v8, s79, v193
	v_mul_f32_e32 v2, 0x43800000, v165
	v_mul_f32_e32 v5, 0x43800000, v171
	v_cvt_pk_fp8_f32 v56, v8, v57 op_sel:[0,0,1]
	v_med3_f32 v2, v2, s79, v193
	v_med3_f32 v5, v5, s79, v193
	v_mov_b32_e32 v57, v9
	v_cvt_pk_fp8_f32 v57, v2, v5
	v_mul_f32_e32 v8, 0x43800000, v175
	v_mul_f32_e32 v3, 0x43800000, v3
	v_med3_f32 v8, v8, s79, v193
	v_med3_f32 v3, v3, s79, v193
	v_cvt_pk_fp8_f32 v57, v8, v3 op_sel:[0,0,1]
	v_add_u32_e32 v2, v13, v33
	ds_write_b128 v4, v[50:53] offset:16
	v_mov_b32_e32 v53, s9
	ds_write_b128 v2, v[54:57]
	s_waitcnt lgkmcnt(0)
; #define LAS __attribute__((address_space(3)))
; #define LDS_WAIT() asm volatile("s_waitcnt lgkmcnt(0)" ::: "memory")
; __device__ __forceinline__ void tr128_f8(const float* W, int ldw, int srccol, unsigned char* WT, size_t dstrow0, int K, int k0, LAS unsigned char* tile, int lane) {
;     ...
;     const int c = lane & 7;
; #pragma unroll
;     for (int j = 0; j < 16; ++j) { const int n = (lane >> 3) + 8 * j; const v4u o = *(const LAS v4u*)(tile + n * 128 + ((c ^ (n & 7)) << 4));
;         __builtin_nontemporal_store(o, (v4u*)(WT + (dstrow0 + n) * K + k0 + 16 * c)); }
;     LDS_WAIT(); asm volatile("" ::: "memory");
	v_add_u32_e32 v56, v35, v37
	ds_read_b128 v[56:59], v56
	v_add_u32_e32 v60, v35, v39
	ds_read_b128 v[60:63], v60
	v_add_u32_e32 v64, v35, v179
	ds_read_b128 v[64:67], v64
	v_add_u32_e32 v68, v35, v180
	ds_read_b128 v[68:71], v68
	v_add_u32_e32 v72, v35, v181
	ds_read_b128 v[72:75], v72
	v_add_u32_e32 v76, v35, v182
	ds_read_b128 v[76:79], v76
	v_add_u32_e32 v80, v35, v183
	ds_read_b128 v[80:83], v80
	v_add_u32_e32 v84, v35, v184
	ds_read_b128 v[84:87], v84
	v_add_u32_e32 v88, v35, v185
	ds_read_b128 v[88:91], v88
	v_add_u32_e32 v92, v35, v186
	ds_read_b128 v[92:95], v92
	v_add_u32_e32 v96, v35, v187
	ds_read_b128 v[96:99], v96
	v_add_u32_e32 v100, v35, v188
	ds_read_b128 v[100:103], v100
	v_add_u32_e32 v104, v35, v189
	ds_read_b128 v[104:107], v104
	v_add_u32_e32 v108, v35, v190
	ds_read_b128 v[108:111], v108
	v_add_u32_e32 v112, v35, v191
	ds_read_b128 v[112:115], v112
	v_add_u32_e32 v116, v35, v192
	ds_read_b128 v[116:119], v116
	v_or_b32_e32 v52, s8, v162
	v_lshl_add_u64 v[50:51], v[40:41], 0, s[6:7]
	v_lshlrev_b64 v[52:53], 11, v[52:53]
	v_lshl_add_u64 v[52:53], v[50:51], 0, v[52:53]
	s_waitcnt lgkmcnt(15)
	global_store_dwordx4 v[52:53], v[56:59], off nt
	v_mov_b32_e32 v53, s9
	v_or_b32_e32 v52, s8, v10
	v_lshlrev_b64 v[52:53], 11, v[52:53]
	v_lshl_add_u64 v[52:53], v[50:51], 0, v[52:53]
	s_waitcnt lgkmcnt(14)
	global_store_dwordx4 v[52:53], v[60:63], off nt
	s_nop 1
	v_mov_b32_e32 v53, s9
	v_or_b32_e32 v52, s8, v12
	v_lshlrev_b64 v[52:53], 11, v[52:53]
	v_lshl_add_u64 v[52:53], v[50:51], 0, v[52:53]
	s_waitcnt lgkmcnt(13)
	global_store_dwordx4 v[52:53], v[64:67], off nt
	v_mov_b32_e32 v53, s9
	v_or_b32_e32 v52, s8, v14
	v_lshlrev_b64 v[52:53], 11, v[52:53]
	v_lshl_add_u64 v[52:53], v[50:51], 0, v[52:53]
	s_waitcnt lgkmcnt(12)
	global_store_dwordx4 v[52:53], v[68:71], off nt
	s_nop 1
	v_mov_b32_e32 v53, s9
	v_or_b32_e32 v52, s8, v16
	v_lshlrev_b64 v[52:53], 11, v[52:53]
	v_lshl_add_u64 v[52:53], v[50:51], 0, v[52:53]
	s_waitcnt lgkmcnt(11)
	global_store_dwordx4 v[52:53], v[72:75], off nt
	v_mov_b32_e32 v53, s9
	v_or_b32_e32 v52, s8, v18
	v_lshlrev_b64 v[52:53], 11, v[52:53]
	v_lshl_add_u64 v[52:53], v[50:51], 0, v[52:53]
	s_waitcnt lgkmcnt(10)
	global_store_dwordx4 v[52:53], v[76:79], off nt
	s_nop 1
	v_mov_b32_e32 v53, s9
	v_or_b32_e32 v52, s8, v20
	v_lshlrev_b64 v[52:53], 11, v[52:53]
	v_lshl_add_u64 v[52:53], v[50:51], 0, v[52:53]
	s_waitcnt lgkmcnt(9)
	global_store_dwordx4 v[52:53], v[80:83], off nt
	v_mov_b32_e32 v53, s9
	v_or_b32_e32 v52, s8, v22
	v_lshlrev_b64 v[52:53], 11, v[52:53]
	v_lshl_add_u64 v[52:53], v[50:51], 0, v[52:53]
	s_waitcnt lgkmcnt(8)
	global_store_dwordx4 v[52:53], v[84:87], off nt
	s_nop 1
	v_mov_b32_e32 v53, s9
	v_or_b32_e32 v52, s8, v24
	v_lshlrev_b64 v[52:53], 11, v[52:53]
	v_lshl_add_u64 v[52:53], v[50:51], 0, v[52:53]
	s_waitcnt lgkmcnt(7)
	global_store_dwordx4 v[52:53], v[88:91], off nt
	v_mov_b32_e32 v53, s9
	v_or_b32_e32 v52, s8, v26
	v_lshlrev_b64 v[52:53], 11, v[52:53]
	v_lshl_add_u64 v[52:53], v[50:51], 0, v[52:53]
	s_waitcnt lgkmcnt(6)
	global_store_dwordx4 v[52:53], v[92:95], off nt
	s_nop 1
	v_mov_b32_e32 v53, s9
	v_or_b32_e32 v52, s8, v28
	v_lshlrev_b64 v[52:53], 11, v[52:53]
	v_lshl_add_u64 v[52:53], v[50:51], 0, v[52:53]
	s_waitcnt lgkmcnt(5)
	global_store_dwordx4 v[52:53], v[96:99], off nt
	v_mov_b32_e32 v53, s9
	v_or_b32_e32 v52, s8, v30
	v_lshlrev_b64 v[52:53], 11, v[52:53]
	v_lshl_add_u64 v[52:53], v[50:51], 0, v[52:53]
	s_waitcnt lgkmcnt(4)
	global_store_dwordx4 v[52:53], v[100:103], off nt
	s_nop 1
	v_mov_b32_e32 v53, s9
	v_or_b32_e32 v52, s8, v32
	v_lshlrev_b64 v[52:53], 11, v[52:53]
	v_lshl_add_u64 v[52:53], v[50:51], 0, v[52:53]
	s_waitcnt lgkmcnt(3)
	global_store_dwordx4 v[52:53], v[104:107], off nt
	v_mov_b32_e32 v53, s9
	v_or_b32_e32 v52, s8, v34
	v_lshlrev_b64 v[52:53], 11, v[52:53]
	v_lshl_add_u64 v[52:53], v[50:51], 0, v[52:53]
	s_waitcnt lgkmcnt(2)
	global_store_dwordx4 v[52:53], v[108:111], off nt
	s_nop 1
	v_mov_b32_e32 v53, s9
	v_or_b32_e32 v52, s8, v36
	v_lshlrev_b64 v[52:53], 11, v[52:53]
	v_lshl_add_u64 v[52:53], v[50:51], 0, v[52:53]
	s_waitcnt lgkmcnt(1)
	global_store_dwordx4 v[52:53], v[112:115], off nt
	v_mov_b32_e32 v53, s9
	v_or_b32_e32 v52, s8, v38
	v_lshlrev_b64 v[52:53], 11, v[52:53]
	v_lshl_add_u64 v[50:51], v[50:51], 0, v[52:53]
	s_mov_b64 s[8:9], 0
	s_waitcnt lgkmcnt(0)
	global_store_dwordx4 v[50:51], v[116:119], off nt
	s_waitcnt lgkmcnt(0)
; #define LAS __attribute__((address_space(3)))
; #define CV_LOAD(v, kb) do { _Pragma("unroll") for (int j = 0; j < 16; ++j) v[j] = __builtin_nontemporal_load((const f32x2*)(src + (size_t)((kb) * 16 + j) * ldw)); } while (0)
; __device__ __forceinline__ void tr128_f8(const float* W, int ldw, int srccol, unsigned char* WT, size_t dstrow0, int K, int k0, LAS unsigned char* tile, int lane) {
;     const float* src = W + (size_t)k0 * ldw + srccol + 2 * lane;
;     f32x2 va[16], vb[16], vc[16], vd[16];
;     ...
;     CV_LOAD(va, 0); CV_LOAD(vb, 1); CV_LOAD(vc, 2);
;     CV_LOAD(vd, 3); CV_PUT(va, 0); CV_LOAD(va, 4); CV_PUT(vb, 1); CV_LOAD(vb, 5); CV_PUT(vc, 2); CV_LOAD(vc, 6); CV_PUT(vd, 3); CV_LOAD(vd, 7);
; __device__ __forceinline__ void cv_item(const Args& a, int it, LAS unsigned char* tile, int lane) {
;     ...
;     if (it < CV_GU) { const int e = it / CV_GU1, q = it % CV_GU1, kt = q >> 5, nt = q & 31, d0 = 128 * nt, ct = d0 >> 8; const int src = (d0 & 128) ? (2048 + 128 * ct) : (128 * ct);
;         tr128_f8(a.in[I_WGU] + (size_t)e * 2048 * 4096, 4096, src, (unsigned char*)(a.ws + WS_WGU), (size_t)e * 4096 + d0, 2048, 128 * kt, tile, lane); }
.LBB0_503:
	s_andn2_b64 vcc, exec, s[8:9]
	s_cbranch_vccnz .LBB0_505
	s_lshl_b32 s8, s10, 7
	s_add_i32 s6, s10, 0xfffffe00
	s_and_b32 s11, s8, 0xf80
	s_lshl_b32 s8, s10, 6
	s_lshl_b32 s9, s10, 11
	s_lshr_b32 s6, s6, 9
	s_and_b32 s8, s8, 0x780
	s_and_b32 s9, s9, 0x800
	s_or_b32 s12, s8, s9
	s_lshl_b64 s[8:9], s[6:7], 25
	v_readlane_b32 s20, v250, 3
	v_readlane_b32 s21, v250, 4
	s_add_u32 s13, s20, s8
	s_addc_u32 s33, s21, s9
	s_lshl_b64 s[8:9], s[6:7], 12
	s_lshl_b32 s6, s10, 2
	s_and_b32 s6, s6, 0x780
	s_or_b32 s8, s8, s11
	s_lshl_b32 s11, s6, 14
	s_add_u32 s11, s13, s11
	s_addc_u32 s13, s33, 0
	s_lshl_b32 s12, s12, 2
	s_add_u32 s12, s11, s12
	s_addc_u32 s13, s13, 0
	v_lshlrev_b32_e32 v8, 2, v6
	s_movk_i32 s21, 0x4000
	v_lshl_add_u64 v[82:83], s[12:13], 0, v[8:9]
	v_readlane_b32 s23, v250, 6
	v_add_co_u32_e32 v4, vcc, s21, v82
	s_mov_b32 s23, 0x8000
	s_nop 0
	v_addc_co_u32_e32 v5, vcc, 0, v83, vcc
	v_readlane_b32 s25, v250, 8
	v_add_co_u32_e32 v50, vcc, s23, v82
	s_mov_b32 s25, 0xc000
	s_nop 0
	v_addc_co_u32_e32 v51, vcc, 0, v83, vcc
	v_readlane_b32 s27, v250, 10
	v_add_co_u32_e32 v52, vcc, s25, v82
	s_mov_b32 s27, 0x10000
	s_nop 0
	v_addc_co_u32_e32 v53, vcc, 0, v83, vcc
	v_add_co_u32_e32 v54, vcc, s27, v82
	global_load_dwordx2 v[2:3], v8, s[12:13] nt
	s_nop 0
	v_addc_co_u32_e32 v55, vcc, 0, v83, vcc
	v_add_co_u32_e32 v56, vcc, s34, v82
	global_load_dwordx2 v[4:5], v[4:5], off nt
	s_nop 0
	v_addc_co_u32_e32 v57, vcc, 0, v83, vcc
	v_add_co_u32_e32 v58, vcc, s58, v82
	global_load_dwordx2 v[54:55], v[54:55], off nt
	s_nop 0
	v_addc_co_u32_e32 v59, vcc, 0, v83, vcc
	v_add_co_u32_e32 v60, vcc, s62, v82
	global_load_dwordx2 v[56:57], v[56:57], off nt
	s_nop 0
	v_addc_co_u32_e32 v61, vcc, 0, v83, vcc
	v_add_co_u32_e32 v62, vcc, s29, v82
	global_load_dwordx2 v[50:51], v[50:51], off nt
	s_nop 0
	v_addc_co_u32_e32 v63, vcc, 0, v83, vcc
	v_add_co_u32_e32 v64, vcc, s31, v82
	global_load_dwordx2 v[52:53], v[52:53], off nt
	s_nop 0
	v_addc_co_u32_e32 v65, vcc, 0, v83, vcc
	v_add_co_u32_e32 v66, vcc, s35, v82
	global_load_dwordx2 v[62:63], v[62:63], off nt
	s_nop 0
	v_addc_co_u32_e32 v67, vcc, 0, v83, vcc
	v_add_co_u32_e32 v68, vcc, s66, v82
	global_load_dwordx2 v[64:65], v[64:65], off nt
	s_nop 0
	v_addc_co_u32_e32 v69, vcc, 0, v83, vcc
	v_add_co_u32_e32 v70, vcc, s70, v82
	global_load_dwordx2 v[58:59], v[58:59], off nt
	s_nop 0
	v_addc_co_u32_e32 v71, vcc, 0, v83, vcc
	v_add_co_u32_e32 v72, vcc, s74, v82
	global_load_dwordx2 v[60:61], v[60:61], off nt
	s_nop 0
	v_addc_co_u32_e32 v73, vcc, 0, v83, vcc
	global_load_dwordx2 v[70:71], v[70:71], off nt
	v_add_co_u32_e32 v74, vcc, s78, v82
	global_load_dwordx2 v[72:73], v[72:73], off nt
	s_nop 0
	v_addc_co_u32_e32 v75, vcc, 0, v83, vcc
	global_load_dwordx2 v[66:67], v[66:67], off nt
	v_add_co_u32_e32 v76, vcc, s83, v82
	global_load_dwordx2 v[68:69], v[68:69], off nt
	s_nop 0
	v_addc_co_u32_e32 v77, vcc, 0, v83, vcc
	global_load_dwordx2 v[74:75], v[74:75], off nt
	v_add_co_u32_e32 v78, vcc, s87, v82
	global_load_dwordx2 v[76:77], v[76:77], off nt
	s_nop 0
	v_addc_co_u32_e32 v79, vcc, 0, v83, vcc
	v_add_co_u32_e32 v80, vcc, s91, v82
	global_load_dwordx2 v[78:79], v[78:79], off nt
	s_nop 0
	v_addc_co_u32_e32 v81, vcc, 0, v83, vcc
	v_add_co_u32_e32 v84, vcc, s95, v82
	global_load_dwordx2 v[80:81], v[80:81], off nt
	s_nop 0
	v_addc_co_u32_e32 v85, vcc, 0, v83, vcc
	v_add_co_u32_e32 v86, vcc, s53, v82
	global_load_dwordx2 v[84:85], v[84:85], off nt
	s_nop 0
	v_addc_co_u32_e32 v87, vcc, 0, v83, vcc
	v_add_co_u32_e32 v88, vcc, s55, v82
	global_load_dwordx2 v[86:87], v[86:87], off nt
	s_nop 0
	v_addc_co_u32_e32 v89, vcc, 0, v83, vcc
	v_add_co_u32_e32 v90, vcc, s57, v82
	global_load_dwordx2 v[88:89], v[88:89], off nt
	s_nop 0
	v_addc_co_u32_e32 v91, vcc, 0, v83, vcc
	v_add_co_u32_e32 v92, vcc, s59, v82
	global_load_dwordx2 v[90:91], v[90:91], off nt
	s_nop 0
	v_addc_co_u32_e32 v93, vcc, 0, v83, vcc
	v_add_co_u32_e32 v94, vcc, s61, v82
	global_load_dwordx2 v[92:93], v[92:93], off nt
	s_nop 0
	v_addc_co_u32_e32 v95, vcc, 0, v83, vcc
	v_add_co_u32_e32 v96, vcc, s63, v82
	global_load_dwordx2 v[94:95], v[94:95], off nt
	s_nop 0
	v_addc_co_u32_e32 v97, vcc, 0, v83, vcc
	v_add_co_u32_e32 v98, vcc, s65, v82
	global_load_dwordx2 v[96:97], v[96:97], off nt
	s_nop 0
	v_addc_co_u32_e32 v99, vcc, 0, v83, vcc
	v_add_co_u32_e32 v100, vcc, s67, v82
	global_load_dwordx2 v[98:99], v[98:99], off nt
	s_nop 0
	v_addc_co_u32_e32 v101, vcc, 0, v83, vcc
	v_add_co_u32_e32 v102, vcc, s69, v82
	global_load_dwordx2 v[100:101], v[100:101], off nt
	s_nop 0
	v_addc_co_u32_e32 v103, vcc, 0, v83, vcc
	v_add_co_u32_e32 v104, vcc, s71, v82
	global_load_dwordx2 v[102:103], v[102:103], off nt
	s_nop 0
	v_addc_co_u32_e32 v105, vcc, 0, v83, vcc
	v_add_co_u32_e32 v106, vcc, s73, v82
	global_load_dwordx2 v[104:105], v[104:105], off nt
	s_nop 0
	v_addc_co_u32_e32 v107, vcc, 0, v83, vcc
	v_add_co_u32_e32 v108, vcc, s75, v82
	global_load_dwordx2 v[106:107], v[106:107], off nt
	s_nop 0
	v_addc_co_u32_e32 v109, vcc, 0, v83, vcc
	v_add_co_u32_e32 v110, vcc, s77, v82
	global_load_dwordx2 v[108:109], v[108:109], off nt
	s_nop 0
	v_addc_co_u32_e32 v111, vcc, 0, v83, vcc
	v_add_co_u32_e32 v112, vcc, s80, v82
	global_load_dwordx2 v[110:111], v[110:111], off nt
	s_nop 0
	v_addc_co_u32_e32 v113, vcc, 0, v83, vcc
	v_add_co_u32_e32 v114, vcc, s82, v82
	s_waitcnt vmcnt(31)
	v_mul_f32_e32 v2, 0x43800000, v2
	v_addc_co_u32_e32 v115, vcc, 0, v83, vcc
	v_add_co_u32_e32 v116, vcc, s84, v82
	s_waitcnt vmcnt(30)
; #define CV_LOAD(v, kb) do { _Pragma("unroll") for (int j = 0; j < 16; ++j) v[j] = __builtin_nontemporal_load((const f32x2*)(src + (size_t)((kb) * 16 + j) * ldw)); } while (0)
; __device__ __forceinline__ void tr128_f8(const float* W, int ldw, int srccol, unsigned char* WT, size_t dstrow0, int K, int k0, LAS unsigned char* tile, int lane) {
;     ...
;     CV_LOAD(va, 0); CV_LOAD(vb, 1); CV_LOAD(vc, 2);
;     CV_LOAD(vd, 3); CV_PUT(va, 0); CV_LOAD(va, 4); CV_PUT(vb, 1); CV_LOAD(vb, 5); CV_PUT(vc, 2); CV_LOAD(vc, 6); CV_PUT(vd, 3); CV_LOAD(vd, 7);
	v_mul_f32_e32 v4, 0x43800000, v4
	v_addc_co_u32_e32 v117, vcc, 0, v83, vcc
	v_add_co_u32_e32 v118, vcc, s86, v82
	v_med3_f32 v2, v2, s79, v193
	s_nop 0
	v_addc_co_u32_e32 v119, vcc, 0, v83, vcc
	v_add_co_u32_e32 v120, vcc, s88, v82
	v_med3_f32 v4, v4, s79, v193
	s_nop 0
	v_addc_co_u32_e32 v121, vcc, 0, v83, vcc
	v_add_co_u32_e32 v122, vcc, s90, v82
	v_mov_b32_e32 v194, v9
	s_nop 0
	v_addc_co_u32_e32 v123, vcc, 0, v83, vcc
	v_add_co_u32_e32 v124, vcc, s92, v82
	v_cvt_pk_fp8_f32 v194, v2, v4
	s_nop 0
	v_addc_co_u32_e32 v125, vcc, 0, v83, vcc
	v_add_co_u32_e32 v126, vcc, s94, v82
	s_waitcnt vmcnt(29)
	v_mul_f32_e32 v2, 0x43800000, v54
	v_addc_co_u32_e32 v127, vcc, 0, v83, vcc
	v_add_co_u32_e32 v128, vcc, s96, v82
	s_waitcnt vmcnt(28)
	v_mul_f32_e32 v4, 0x43800000, v56
	v_addc_co_u32_e32 v129, vcc, 0, v83, vcc
	v_add_co_u32_e32 v130, vcc, s4, v82
	v_med3_f32 v2, v2, s79, v193
	s_nop 0
	v_addc_co_u32_e32 v131, vcc, 0, v83, vcc
	v_add_co_u32_e32 v132, vcc, s14, v82
	v_med3_f32 v4, v4, s79, v193
	s_nop 0
	v_addc_co_u32_e32 v133, vcc, 0, v83, vcc
	v_add_co_u32_e32 v134, vcc, s18, v82
	v_mov_b32_e32 v195, v9
	s_nop 0
	v_addc_co_u32_e32 v135, vcc, 0, v83, vcc
	v_add_co_u32_e32 v136, vcc, s5, v82
	s_waitcnt vmcnt(27)
	v_mul_f32_e32 v8, 0x43800000, v50
	v_addc_co_u32_e32 v137, vcc, 0, v83, vcc
	v_add_co_u32_e32 v138, vcc, s54, v82
	s_waitcnt vmcnt(26)
	v_mul_f32_e32 v50, 0x43800000, v52
	v_addc_co_u32_e32 v139, vcc, 0, v83, vcc
	v_add_co_u32_e32 v140, vcc, s30, v82
	v_cvt_pk_fp8_f32 v195, v2, v4
	s_nop 0
	v_addc_co_u32_e32 v141, vcc, 0, v83, vcc
	s_waitcnt vmcnt(25)
	v_mul_f32_e32 v2, 0x43800000, v62
	s_waitcnt vmcnt(24)
	v_mul_f32_e32 v4, 0x43800000, v64
	v_add_co_u32_e32 v142, vcc, s15, v82
	v_med3_f32 v8, v8, s79, v193
	v_med3_f32 v50, v50, s79, v193
	v_med3_f32 v2, v2, s79, v193
	v_med3_f32 v4, v4, s79, v193
	v_mov_b32_e32 v196, v9
	v_addc_co_u32_e32 v143, vcc, 0, v83, vcc
	v_cvt_pk_fp8_f32 v194, v8, v50 op_sel:[0,0,1]
	s_waitcnt vmcnt(23)
	v_mul_f32_e32 v8, 0x43800000, v58
	s_waitcnt vmcnt(22)
	v_mul_f32_e32 v50, 0x43800000, v60
	v_cvt_pk_fp8_f32 v196, v2, v4
	s_waitcnt vmcnt(21)
	v_mul_f32_e32 v2, 0x43800000, v70
	s_waitcnt vmcnt(20)
	v_mul_f32_e32 v4, 0x43800000, v72
	v_add_co_u32_e32 v144, vcc, s17, v82
	v_med3_f32 v8, v8, s79, v193
	v_med3_f32 v50, v50, s79, v193
	v_med3_f32 v2, v2, s79, v193
	v_med3_f32 v4, v4, s79, v193
	v_mov_b32_e32 v197, v9
	v_addc_co_u32_e32 v145, vcc, 0, v83, vcc
	v_cvt_pk_fp8_f32 v195, v8, v50 op_sel:[0,0,1]
	s_waitcnt vmcnt(19)
	v_mul_f32_e32 v8, 0x43800000, v66
	s_waitcnt vmcnt(18)
	v_mul_f32_e32 v50, 0x43800000, v68
	v_cvt_pk_fp8_f32 v197, v2, v4
	v_add_co_u32_e32 v146, vcc, s19, v82
	v_med3_f32 v8, v8, s79, v193
	v_med3_f32 v50, v50, s79, v193
	v_addc_co_u32_e32 v147, vcc, 0, v83, vcc
	v_cvt_pk_fp8_f32 v196, v8, v50 op_sel:[0,0,1]
	s_waitcnt vmcnt(17)
	v_mul_f32_e32 v8, 0x43800000, v74
	s_waitcnt vmcnt(16)
	v_mul_f32_e32 v50, 0x43800000, v76
	v_add_co_u32_e32 v148, vcc, s28, v82
	v_med3_f32 v8, v8, s79, v193
	v_med3_f32 v50, v50, s79, v193
	v_mul_f32_e32 v2, 0x43800000, v3
	v_mul_f32_e32 v3, 0x43800000, v5
	v_addc_co_u32_e32 v149, vcc, 0, v83, vcc
	v_cvt_pk_fp8_f32 v197, v8, v50 op_sel:[0,0,1]
	v_med3_f32 v8, v2, s79, v193
	v_med3_f32 v3, v3, s79, v193
	v_mov_b32_e32 v2, v9
	v_add_co_u32_e32 v150, vcc, s52, v82
	v_cvt_pk_fp8_f32 v2, v8, v3
	s_nop 0
	v_addc_co_u32_e32 v151, vcc, 0, v83, vcc
	v_add_co_u32_e32 v152, vcc, s56, v82
	v_mul_f32_e32 v4, 0x43800000, v51
	v_mul_f32_e32 v5, 0x43800000, v53
	v_addc_co_u32_e32 v153, vcc, 0, v83, vcc
	v_med3_f32 v4, v4, s79, v193
	v_med3_f32 v5, v5, s79, v193
	v_add_co_u32_e32 v154, vcc, s60, v82
	v_cvt_pk_fp8_f32 v2, v4, v5 op_sel:[0,0,1]
	v_mul_f32_e32 v3, 0x43800000, v55
	v_mul_f32_e32 v4, 0x43800000, v57
	v_addc_co_u32_e32 v155, vcc, 0, v83, vcc
	v_med3_f32 v50, v3, s79, v193
	v_med3_f32 v4, v4, s79, v193
	v_mov_b32_e32 v3, v9
	v_add_co_u32_e32 v156, vcc, s64, v82
	v_cvt_pk_fp8_f32 v3, v50, v4
	s_nop 0
	v_addc_co_u32_e32 v157, vcc, 0, v83, vcc
	v_add_co_u32_e32 v158, vcc, s68, v82
	v_mul_f32_e32 v5, 0x43800000, v59
	v_mul_f32_e32 v8, 0x43800000, v61
	v_addc_co_u32_e32 v159, vcc, 0, v83, vcc
	v_med3_f32 v5, v5, s79, v193
	v_med3_f32 v8, v8, s79, v193
	v_add_co_u32_e32 v160, vcc, s72, v82
	v_cvt_pk_fp8_f32 v3, v5, v8 op_sel:[0,0,1]
	v_mul_f32_e32 v4, 0x43800000, v63
	v_mul_f32_e32 v5, 0x43800000, v65
	v_addc_co_u32_e32 v161, vcc, 0, v83, vcc
	v_med3_f32 v51, v4, s79, v193
	v_med3_f32 v5, v5, s79, v193
	v_mov_b32_e32 v4, v9
	v_add_co_u32_e32 v164, vcc, s76, v82
	v_cvt_pk_fp8_f32 v4, v51, v5
	s_nop 0
	v_addc_co_u32_e32 v165, vcc, 0, v83, vcc
	v_add_co_u32_e32 v166, vcc, s81, v82
	v_mul_f32_e32 v8, 0x43800000, v67
	v_mul_f32_e32 v50, 0x43800000, v69
	v_addc_co_u32_e32 v167, vcc, 0, v83, vcc
	v_med3_f32 v8, v8, s79, v193
	v_med3_f32 v50, v50, s79, v193
	v_add_co_u32_e32 v168, vcc, s85, v82
	v_cvt_pk_fp8_f32 v4, v8, v50 op_sel:[0,0,1]
	v_mul_f32_e32 v5, 0x43800000, v71
	v_mul_f32_e32 v8, 0x43800000, v73
	global_load_dwordx2 v[112:113], v[112:113], off nt
	v_addc_co_u32_e32 v169, vcc, 0, v83, vcc
	global_load_dwordx2 v[114:115], v[114:115], off nt
	v_med3_f32 v52, v5, s79, v193
	v_med3_f32 v8, v8, s79, v193
	v_mov_b32_e32 v5, v9
	v_add_co_u32_e32 v170, vcc, s89, v82
	v_cvt_pk_fp8_f32 v5, v52, v8
	global_load_dwordx2 v[120:121], v[120:121], off nt
	v_addc_co_u32_e32 v171, vcc, 0, v83, vcc
	global_load_dwordx2 v[122:123], v[122:123], off nt
	v_add_co_u32_e32 v172, vcc, s93, v82
	v_mul_f32_e32 v50, 0x43800000, v75
	v_mul_f32_e32 v51, 0x43800000, v77
	global_load_dwordx2 v[116:117], v[116:117], off nt
	v_addc_co_u32_e32 v173, vcc, 0, v83, vcc
	global_load_dwordx2 v[118:119], v[118:119], off nt
	v_med3_f32 v50, v50, s79, v193
	global_load_dwordx2 v[128:129], v[128:129], off nt
	v_med3_f32 v51, v51, s79, v193
	global_load_dwordx2 v[130:131], v[130:131], off nt
	v_add_co_u32_e32 v174, vcc, s97, v82
	v_cvt_pk_fp8_f32 v5, v50, v51 op_sel:[0,0,1]
	global_load_dwordx2 v[124:125], v[124:125], off nt
	v_addc_co_u32_e32 v175, vcc, 0, v83, vcc
	global_load_dwordx2 v[126:127], v[126:127], off nt
	v_add_co_u32_e32 v176, vcc, s16, v82
	global_load_dwordx2 v[136:137], v[136:137], off nt
	s_nop 0
	v_addc_co_u32_e32 v177, vcc, 0, v83, vcc
	global_load_dwordx2 v[138:139], v[138:139], off nt
	v_add_u32_e32 v50, v13, v15
	global_load_dwordx2 v[132:133], v[132:133], off nt
	s_mov_b32 s11, 0x100000
	global_load_dwordx2 v[134:135], v[134:135], off nt
	ds_write_b128 v50, v[2:5]
	v_add_co_u32_e32 v2, vcc, s11, v82
	global_load_dwordx2 v[140:141], v[140:141], off nt
	s_nop 0
	v_addc_co_u32_e32 v3, vcc, 0, v83, vcc
	global_load_dwordx2 v[142:143], v[142:143], off nt
	s_mov_b32 s11, 0x104000
	global_load_dwordx2 v[152:153], v[152:153], off nt
	v_add_u32_e32 v8, v7, v11
	global_load_dwordx2 v[52:53], v[2:3], off nt
	v_add_co_u32_e32 v2, vcc, s11, v82
	s_mov_b32 s11, 0x108000
	s_nop 0
	v_addc_co_u32_e32 v3, vcc, 0, v83, vcc
	global_load_dwordx2 v[154:155], v[154:155], off nt
	s_waitcnt vmcnt(34)
; #define CV_LOAD(v, kb) do { _Pragma("unroll") for (int j = 0; j < 16; ++j) v[j] = __builtin_nontemporal_load((const f32x2*)(src + (size_t)((kb) * 16 + j) * ldw)); } while (0)
; __device__ __forceinline__ void tr128_f8(const float* W, int ldw, int srccol, unsigned char* WT, size_t dstrow0, int K, int k0, LAS unsigned char* tile, int lane) {
;     ...
;     CV_LOAD(va, 0); CV_LOAD(vb, 1); CV_LOAD(vc, 2);
;     CV_LOAD(vd, 3); CV_PUT(va, 0); CV_LOAD(va, 4); CV_PUT(vb, 1); CV_LOAD(vb, 5); CV_PUT(vc, 2); CV_LOAD(vc, 6); CV_PUT(vd, 3); CV_LOAD(vd, 7);
	v_mul_f32_e32 v78, 0x43800000, v78
	global_load_dwordx2 v[60:61], v[2:3], off nt
	v_add_co_u32_e32 v2, vcc, s11, v82
	s_mov_b32 s11, 0x10c000
	s_nop 0
	v_addc_co_u32_e32 v3, vcc, 0, v83, vcc
	global_load_dwordx2 v[156:157], v[156:157], off nt
	s_waitcnt vmcnt(35)
	v_mul_f32_e32 v80, 0x43800000, v80
	global_load_dwordx2 v[68:69], v[2:3], off nt
	v_add_co_u32_e32 v2, vcc, s11, v82
	s_mov_b32 s11, 0x110000
	s_nop 0
	v_addc_co_u32_e32 v3, vcc, 0, v83, vcc
	global_load_dwordx2 v[158:159], v[158:159], off nt
	ds_write_b128 v8, v[194:197]
	global_load_dwordx2 v[76:77], v[2:3], off nt
	v_add_co_u32_e32 v2, vcc, s11, v82
	s_mov_b32 s11, 0x114000
	s_nop 0
	v_addc_co_u32_e32 v3, vcc, 0, v83, vcc
	global_load_dwordx2 v[50:51], v[2:3], off nt
	v_add_co_u32_e32 v2, vcc, s11, v82
	s_mov_b32 s11, 0x118000
	s_nop 0
	v_addc_co_u32_e32 v3, vcc, 0, v83, vcc
	global_load_dwordx2 v[58:59], v[2:3], off nt
	v_add_co_u32_e32 v2, vcc, s11, v82
	s_mov_b32 s11, 0x11c000
	s_nop 0
	v_addc_co_u32_e32 v3, vcc, 0, v83, vcc
	global_load_dwordx2 v[66:67], v[2:3], off nt
	v_add_co_u32_e32 v2, vcc, s11, v82
	s_mov_b32 s11, 0x120000
	s_nop 0
	v_addc_co_u32_e32 v3, vcc, 0, v83, vcc
	global_load_dwordx2 v[74:75], v[2:3], off nt
	v_add_co_u32_e32 v2, vcc, s11, v82
	s_mov_b32 s11, 0x124000
	s_nop 0
	v_addc_co_u32_e32 v3, vcc, 0, v83, vcc
	v_med3_f32 v78, v78, s79, v193
	v_med3_f32 v80, v80, s79, v193
	v_mov_b32_e32 v194, v9
	global_load_dwordx2 v[144:145], v[144:145], off nt
	v_cvt_pk_fp8_f32 v194, v78, v80
	global_load_dwordx2 v[4:5], v[2:3], off nt
	v_add_co_u32_e32 v2, vcc, s11, v82
	s_waitcnt vmcnt(41)
	v_mul_f32_e32 v78, 0x43800000, v88
	s_waitcnt vmcnt(40)
	v_mul_f32_e32 v80, 0x43800000, v90
	v_addc_co_u32_e32 v3, vcc, 0, v83, vcc
	s_mov_b32 s11, 0x128000
	v_med3_f32 v78, v78, s79, v193
	v_med3_f32 v80, v80, s79, v193
	v_mov_b32_e32 v195, v9
	global_load_dwordx2 v[146:147], v[146:147], off nt
	v_mul_f32_e32 v84, 0x43800000, v84
	global_load_dwordx2 v[56:57], v[2:3], off nt
	v_add_co_u32_e32 v2, vcc, s11, v82
	v_mul_f32_e32 v86, 0x43800000, v86
	v_cvt_pk_fp8_f32 v195, v78, v80
	s_waitcnt vmcnt(39)
	v_mul_f32_e32 v78, 0x43800000, v96
	s_waitcnt vmcnt(38)
	v_mul_f32_e32 v80, 0x43800000, v98
	v_addc_co_u32_e32 v3, vcc, 0, v83, vcc
	s_mov_b32 s11, 0x12c000
	v_med3_f32 v84, v84, s79, v193
	v_med3_f32 v86, v86, s79, v193
	v_med3_f32 v78, v78, s79, v193
	v_med3_f32 v80, v80, s79, v193
	v_mov_b32_e32 v196, v9
	global_load_dwordx2 v[148:149], v[148:149], off nt
	v_cvt_pk_fp8_f32 v194, v84, v86 op_sel:[0,0,1]
	global_load_dwordx2 v[64:65], v[2:3], off nt
	v_add_co_u32_e32 v2, vcc, s11, v82
	v_mul_f32_e32 v84, 0x43800000, v92
	v_mul_f32_e32 v86, 0x43800000, v94
	v_cvt_pk_fp8_f32 v196, v78, v80
	s_waitcnt vmcnt(37)
	v_mul_f32_e32 v78, 0x43800000, v104
	s_waitcnt vmcnt(36)
	v_mul_f32_e32 v80, 0x43800000, v106
	v_addc_co_u32_e32 v3, vcc, 0, v83, vcc
	v_med3_f32 v84, v84, s79, v193
	v_med3_f32 v86, v86, s79, v193
	v_med3_f32 v78, v78, s79, v193
	v_med3_f32 v80, v80, s79, v193
	v_mov_b32_e32 v197, v9
	global_load_dwordx2 v[150:151], v[150:151], off nt
	v_cvt_pk_fp8_f32 v195, v84, v86 op_sel:[0,0,1]
	global_load_dwordx2 v[72:73], v[2:3], off nt
	v_mul_f32_e32 v84, 0x43800000, v100
	v_mul_f32_e32 v86, 0x43800000, v102
	v_cvt_pk_fp8_f32 v197, v78, v80
	v_med3_f32 v84, v84, s79, v193
	v_med3_f32 v86, v86, s79, v193
	v_cvt_pk_fp8_f32 v196, v84, v86 op_sel:[0,0,1]
	s_waitcnt vmcnt(37)
	v_mul_f32_e32 v84, 0x43800000, v108
	s_waitcnt vmcnt(36)
	v_mul_f32_e32 v86, 0x43800000, v110
	v_med3_f32 v84, v84, s79, v193
	v_med3_f32 v86, v86, s79, v193
	v_mul_f32_e32 v78, 0x43800000, v79
	v_mul_f32_e32 v79, 0x43800000, v81
	v_cvt_pk_fp8_f32 v197, v84, v86 op_sel:[0,0,1]
	v_med3_f32 v84, v78, s79, v193
	v_med3_f32 v79, v79, s79, v193
	v_mov_b32_e32 v78, v9
	v_cvt_pk_fp8_f32 v78, v84, v79
	v_mul_f32_e32 v80, 0x43800000, v85
	v_mul_f32_e32 v81, 0x43800000, v87
	v_med3_f32 v80, v80, s79, v193
	v_med3_f32 v81, v81, s79, v193
	v_cvt_pk_fp8_f32 v78, v80, v81 op_sel:[0,0,1]
	v_mul_f32_e32 v79, 0x43800000, v89
	v_mul_f32_e32 v80, 0x43800000, v91
	v_med3_f32 v85, v79, s79, v193
	v_med3_f32 v80, v80, s79, v193
	v_mov_b32_e32 v79, v9
	global_load_dwordx2 v[160:161], v[160:161], off nt
	v_cvt_pk_fp8_f32 v79, v85, v80
	global_load_dwordx2 v[164:165], v[164:165], off nt
	v_mul_f32_e32 v81, 0x43800000, v93
	global_load_dwordx2 v[170:171], v[170:171], off nt
	v_mul_f32_e32 v84, 0x43800000, v95
	global_load_dwordx2 v[172:173], v[172:173], off nt
	v_med3_f32 v81, v81, s79, v193
	v_med3_f32 v84, v84, s79, v193
	global_load_dwordx2 v[166:167], v[166:167], off nt
	v_cvt_pk_fp8_f32 v79, v81, v84 op_sel:[0,0,1]
	global_load_dwordx2 v[168:169], v[168:169], off nt
	v_mul_f32_e32 v80, 0x43800000, v97
	v_mul_f32_e32 v81, 0x43800000, v99
	v_med3_f32 v86, v80, s79, v193
	v_med3_f32 v81, v81, s79, v193
	v_mov_b32_e32 v80, v9
	global_load_dwordx2 v[174:175], v[174:175], off nt
	v_cvt_pk_fp8_f32 v80, v86, v81
	global_load_dwordx2 v[176:177], v[176:177], off nt
	v_mul_f32_e32 v84, 0x43800000, v101
	v_mul_f32_e32 v85, 0x43800000, v103
	v_med3_f32 v84, v84, s79, v193
	v_med3_f32 v85, v85, s79, v193
	v_cvt_pk_fp8_f32 v80, v84, v85 op_sel:[0,0,1]
	v_mul_f32_e32 v81, 0x43800000, v105
	v_mul_f32_e32 v84, 0x43800000, v107
	s_mov_b32 s11, 0x130000
	v_med3_f32 v87, v81, s79, v193
	v_med3_f32 v84, v84, s79, v193
	v_mov_b32_e32 v81, v9
	v_add_co_u32_e32 v2, vcc, s11, v82
	v_cvt_pk_fp8_f32 v81, v87, v84
	s_nop 0
	v_addc_co_u32_e32 v3, vcc, 0, v83, vcc
	s_mov_b32 s11, 0x134000
	v_add_co_u32_e32 v54, vcc, s11, v82
	v_mul_f32_e32 v85, 0x43800000, v109
	v_mul_f32_e32 v86, 0x43800000, v111
	v_addc_co_u32_e32 v55, vcc, 0, v83, vcc
	s_mov_b32 s11, 0x138000
; #define CV_LOAD(v, kb) do { _Pragma("unroll") for (int j = 0; j < 16; ++j) v[j] = __builtin_nontemporal_load((const f32x2*)(src + (size_t)((kb) * 16 + j) * ldw)); } while (0)
; __device__ __forceinline__ void tr128_f8(const float* W, int ldw, int srccol, unsigned char* WT, size_t dstrow0, int K, int k0, LAS unsigned char* tile, int lane) {
;     ...
;     CV_LOAD(va, 0); CV_LOAD(vb, 1); CV_LOAD(vc, 2);
;     CV_LOAD(vd, 3); CV_PUT(va, 0); CV_LOAD(va, 4); CV_PUT(vb, 1); CV_LOAD(vb, 5); CV_PUT(vc, 2); CV_LOAD(vc, 6); CV_PUT(vd, 3); CV_LOAD(vd, 7);
	v_med3_f32 v85, v85, s79, v193
	v_med3_f32 v86, v86, s79, v193
	v_add_co_u32_e32 v62, vcc, s11, v82
	v_cvt_pk_fp8_f32 v81, v85, v86 op_sel:[0,0,1]
	s_nop 0
	v_addc_co_u32_e32 v63, vcc, 0, v83, vcc
	s_mov_b32 s11, 0x13c000
	v_add_co_u32_e32 v70, vcc, s11, v82
	ds_write_b128 v8, v[194:197] offset:16
	s_nop 0
	v_addc_co_u32_e32 v71, vcc, 0, v83, vcc
	v_add_u32_e32 v8, v13, v11
	s_mov_b32 s11, 0x140000
	ds_write_b128 v8, v[78:81]
	v_add_co_u32_e32 v78, vcc, s11, v82
	s_mov_b32 s11, 0x144000
	s_nop 0
	v_addc_co_u32_e32 v79, vcc, 0, v83, vcc
	global_load_dwordx2 v[86:87], v[78:79], off nt
	v_add_co_u32_e32 v78, vcc, s11, v82
	s_mov_b32 s11, 0x148000
	s_nop 0
	v_addc_co_u32_e32 v79, vcc, 0, v83, vcc
	global_load_dwordx2 v[94:95], v[78:79], off nt
	v_add_co_u32_e32 v78, vcc, s11, v82
	s_mov_b32 s11, 0x14c000
	s_nop 0
	v_addc_co_u32_e32 v79, vcc, 0, v83, vcc
	global_load_dwordx2 v[102:103], v[78:79], off nt
	v_add_co_u32_e32 v78, vcc, s11, v82
	s_mov_b32 s11, 0x150000
	s_nop 0
	v_addc_co_u32_e32 v79, vcc, 0, v83, vcc
	global_load_dwordx2 v[110:111], v[78:79], off nt
	v_add_co_u32_e32 v78, vcc, s11, v82
	s_mov_b32 s11, 0x154000
	s_nop 0
	v_addc_co_u32_e32 v79, vcc, 0, v83, vcc
	global_load_dwordx2 v[84:85], v[78:79], off nt
	v_add_co_u32_e32 v78, vcc, s11, v82
	s_mov_b32 s11, 0x158000
	s_nop 0
	v_addc_co_u32_e32 v79, vcc, 0, v83, vcc
	global_load_dwordx2 v[92:93], v[78:79], off nt
	v_add_co_u32_e32 v78, vcc, s11, v82
	s_mov_b32 s11, 0x15c000
	s_nop 0
	v_addc_co_u32_e32 v79, vcc, 0, v83, vcc
	global_load_dwordx2 v[100:101], v[78:79], off nt
	v_add_co_u32_e32 v78, vcc, s11, v82
	s_mov_b32 s11, 0x160000
	s_nop 0
	v_addc_co_u32_e32 v79, vcc, 0, v83, vcc
	global_load_dwordx2 v[108:109], v[78:79], off nt
	v_add_co_u32_e32 v78, vcc, s11, v82
	s_waitcnt vmcnt(51)
	v_mul_f32_e32 v8, 0x43800000, v112
	s_waitcnt vmcnt(50)
	v_mul_f32_e32 v112, 0x43800000, v114
	v_addc_co_u32_e32 v79, vcc, 0, v83, vcc
	s_mov_b32 s11, 0x164000
	v_med3_f32 v8, v8, s79, v193
	v_med3_f32 v112, v112, s79, v193
	v_mov_b32_e32 v194, v9
	global_load_dwordx2 v[80:81], v[78:79], off nt
	v_add_co_u32_e32 v78, vcc, s11, v82
	v_cvt_pk_fp8_f32 v194, v8, v112
	s_waitcnt vmcnt(50)
	v_mul_f32_e32 v8, 0x43800000, v120
	s_waitcnt vmcnt(49)
	v_mul_f32_e32 v112, 0x43800000, v122
	v_addc_co_u32_e32 v79, vcc, 0, v83, vcc
	s_mov_b32 s11, 0x168000
	v_med3_f32 v8, v8, s79, v193
	v_med3_f32 v112, v112, s79, v193
	v_mov_b32_e32 v195, v9
	global_load_dwordx2 v[90:91], v[78:79], off nt
	v_add_co_u32_e32 v78, vcc, s11, v82
	s_waitcnt vmcnt(49)
	v_mul_f32_e32 v114, 0x43800000, v116
	s_waitcnt vmcnt(48)
	v_mul_f32_e32 v116, 0x43800000, v118
	v_cvt_pk_fp8_f32 v195, v8, v112
	s_waitcnt vmcnt(47)
	v_mul_f32_e32 v8, 0x43800000, v128
	s_waitcnt vmcnt(46)
	v_mul_f32_e32 v112, 0x43800000, v130
	global_load_dwordx2 v[2:3], v[2:3], off nt
	v_addc_co_u32_e32 v79, vcc, 0, v83, vcc
	global_load_dwordx2 v[54:55], v[54:55], off nt
	s_mov_b32 s11, 0x16c000
	v_med3_f32 v114, v114, s79, v193
	v_med3_f32 v116, v116, s79, v193
	v_med3_f32 v8, v8, s79, v193
	v_med3_f32 v112, v112, s79, v193
	v_mov_b32_e32 v196, v9
	global_load_dwordx2 v[98:99], v[78:79], off nt
	v_add_co_u32_e32 v78, vcc, s11, v82
	v_cvt_pk_fp8_f32 v194, v114, v116 op_sel:[0,0,1]
	s_waitcnt vmcnt(48)
	v_mul_f32_e32 v114, 0x43800000, v124
	s_waitcnt vmcnt(47)
	v_mul_f32_e32 v116, 0x43800000, v126
	v_cvt_pk_fp8_f32 v196, v8, v112
	s_waitcnt vmcnt(46)
	v_mul_f32_e32 v8, 0x43800000, v136
	s_waitcnt vmcnt(45)
	v_mul_f32_e32 v112, 0x43800000, v138
	v_addc_co_u32_e32 v79, vcc, 0, v83, vcc
	v_med3_f32 v114, v114, s79, v193
	v_med3_f32 v116, v116, s79, v193
	v_med3_f32 v8, v8, s79, v193
	v_med3_f32 v112, v112, s79, v193
	v_mov_b32_e32 v197, v9
	global_load_dwordx2 v[106:107], v[78:79], off nt
	v_cvt_pk_fp8_f32 v195, v114, v116 op_sel:[0,0,1]
	s_waitcnt vmcnt(45)
	v_mul_f32_e32 v114, 0x43800000, v132
	s_waitcnt vmcnt(44)
	v_mul_f32_e32 v116, 0x43800000, v134
	v_cvt_pk_fp8_f32 v197, v8, v112
	v_mul_f32_e32 v8, 0x43800000, v113
	v_mul_f32_e32 v112, 0x43800000, v115
	global_load_dwordx2 v[62:63], v[62:63], off nt
	v_med3_f32 v114, v114, s79, v193
	global_load_dwordx2 v[70:71], v[70:71], off nt
	v_med3_f32 v116, v116, s79, v193
	v_med3_f32 v8, v8, s79, v193
	v_med3_f32 v115, v112, s79, v193
	v_mov_b32_e32 v112, v9
	v_cvt_pk_fp8_f32 v196, v114, v116 op_sel:[0,0,1]
	s_waitcnt vmcnt(45)
	v_mul_f32_e32 v114, 0x43800000, v140
	s_waitcnt vmcnt(44)
; #define CV_LOAD(v, kb) do { _Pragma("unroll") for (int j = 0; j < 16; ++j) v[j] = __builtin_nontemporal_load((const f32x2*)(src + (size_t)((kb) * 16 + j) * ldw)); } while (0)
; __device__ __forceinline__ void tr128_f8(const float* W, int ldw, int srccol, unsigned char* WT, size_t dstrow0, int K, int k0, LAS unsigned char* tile, int lane) {
;     ...
;     CV_LOAD(va, 0); CV_LOAD(vb, 1); CV_LOAD(vc, 2);
;     CV_LOAD(vd, 3); CV_PUT(va, 0); CV_LOAD(va, 4); CV_PUT(vb, 1); CV_LOAD(vb, 5); CV_PUT(vc, 2); CV_LOAD(vc, 6); CV_PUT(vd, 3); CV_LOAD(vd, 7);
	v_mul_f32_e32 v116, 0x43800000, v142
	v_cvt_pk_fp8_f32 v112, v8, v115
	v_med3_f32 v114, v114, s79, v193
	v_med3_f32 v116, v116, s79, v193
	v_cvt_pk_fp8_f32 v197, v114, v116 op_sel:[0,0,1]
	v_mul_f32_e32 v113, 0x43800000, v117
	v_mul_f32_e32 v114, 0x43800000, v119
	v_med3_f32 v113, v113, s79, v193
	v_med3_f32 v114, v114, s79, v193
	v_cvt_pk_fp8_f32 v112, v113, v114 op_sel:[0,0,1]
	v_mul_f32_e32 v8, 0x43800000, v121
	v_mul_f32_e32 v113, 0x43800000, v123
	v_med3_f32 v8, v8, s79, v193
	v_med3_f32 v116, v113, s79, v193
	v_mov_b32_e32 v113, v9
	v_cvt_pk_fp8_f32 v113, v8, v116
	v_mul_f32_e32 v114, 0x43800000, v125
	v_mul_f32_e32 v115, 0x43800000, v127
	v_med3_f32 v114, v114, s79, v193
	v_med3_f32 v115, v115, s79, v193
	v_cvt_pk_fp8_f32 v113, v114, v115 op_sel:[0,0,1]
	v_mul_f32_e32 v8, 0x43800000, v129
	v_mul_f32_e32 v114, 0x43800000, v131
	v_med3_f32 v8, v8, s79, v193
	v_med3_f32 v117, v114, s79, v193
	v_mov_b32_e32 v114, v9
	v_cvt_pk_fp8_f32 v114, v8, v117
	v_mul_f32_e32 v115, 0x43800000, v133
	v_mul_f32_e32 v116, 0x43800000, v135
	v_med3_f32 v115, v115, s79, v193
	v_med3_f32 v116, v116, s79, v193
	v_cvt_pk_fp8_f32 v114, v115, v116 op_sel:[0,0,1]
	v_mul_f32_e32 v8, 0x43800000, v137
	v_mul_f32_e32 v115, 0x43800000, v139
	s_mov_b32 s11, 0x170000
	v_med3_f32 v8, v8, s79, v193
	v_med3_f32 v118, v115, s79, v193
	v_mov_b32_e32 v115, v9
	v_add_co_u32_e32 v78, vcc, s11, v82
	v_cvt_pk_fp8_f32 v115, v8, v118
	s_nop 0
	v_addc_co_u32_e32 v79, vcc, 0, v83, vcc
	s_mov_b32 s11, 0x174000
	v_add_co_u32_e32 v88, vcc, s11, v82
	v_mul_f32_e32 v116, 0x43800000, v141
	v_mul_f32_e32 v117, 0x43800000, v143
	v_addc_co_u32_e32 v89, vcc, 0, v83, vcc
	s_mov_b32 s11, 0x178000
	v_med3_f32 v116, v116, s79, v193
	v_med3_f32 v117, v117, s79, v193
	v_add_co_u32_e32 v96, vcc, s11, v82
	v_cvt_pk_fp8_f32 v115, v116, v117 op_sel:[0,0,1]
	s_nop 0
	v_addc_co_u32_e32 v97, vcc, 0, v83, vcc
	s_mov_b32 s11, 0x17c000
	v_add_co_u32_e32 v104, vcc, s11, v82
	v_add_u32_e32 v116, v13, v19
	s_nop 0
	v_addc_co_u32_e32 v105, vcc, 0, v83, vcc
	s_mov_b32 s11, 0x180000
	ds_write_b128 v116, v[112:115]
	v_add_co_u32_e32 v112, vcc, s11, v82
	s_mov_b32 s11, 0x184000
	s_nop 0
	v_addc_co_u32_e32 v113, vcc, 0, v83, vcc
	global_load_dwordx2 v[104:105], v[104:105], off nt
	v_add_u32_e32 v8, v7, v17
	global_load_dwordx2 v[118:119], v[112:113], off nt
	v_add_co_u32_e32 v112, vcc, s11, v82
	s_mov_b32 s11, 0x188000
	s_nop 0
	v_addc_co_u32_e32 v113, vcc, 0, v83, vcc
	global_load_dwordx2 v[126:127], v[112:113], off nt
	v_add_co_u32_e32 v112, vcc, s11, v82
	s_waitcnt vmcnt(34)
	v_mul_f32_e32 v144, 0x43800000, v144
	s_waitcnt vmcnt(32)
	v_mul_f32_e32 v146, 0x43800000, v146
	ds_write_b128 v8, v[194:197]
	v_addc_co_u32_e32 v113, vcc, 0, v83, vcc
	s_mov_b32 s11, 0x18c000
	v_med3_f32 v144, v144, s79, v193
	v_med3_f32 v146, v146, s79, v193
	v_mov_b32_e32 v194, v9
	global_load_dwordx2 v[134:135], v[112:113], off nt
	v_add_co_u32_e32 v112, vcc, s11, v82
	v_cvt_pk_fp8_f32 v194, v144, v146
	v_mul_f32_e32 v144, 0x43800000, v152
	v_mul_f32_e32 v146, 0x43800000, v154
	v_addc_co_u32_e32 v113, vcc, 0, v83, vcc
	s_mov_b32 s11, 0x190000
	v_med3_f32 v144, v144, s79, v193
	v_med3_f32 v146, v146, s79, v193
	v_mov_b32_e32 v195, v9
	global_load_dwordx2 v[142:143], v[112:113], off nt
	v_add_co_u32_e32 v112, vcc, s11, v82
	s_waitcnt vmcnt(32)
	v_mul_f32_e32 v148, 0x43800000, v148
	s_waitcnt vmcnt(30)
	v_mul_f32_e32 v150, 0x43800000, v150
	v_cvt_pk_fp8_f32 v195, v144, v146
	s_waitcnt vmcnt(28)
	v_mul_f32_e32 v144, 0x43800000, v160
	s_waitcnt vmcnt(27)
	v_mul_f32_e32 v146, 0x43800000, v164
	v_addc_co_u32_e32 v113, vcc, 0, v83, vcc
	s_mov_b32 s11, 0x194000
	v_med3_f32 v148, v148, s79, v193
	v_med3_f32 v150, v150, s79, v193
	v_med3_f32 v144, v144, s79, v193
	v_med3_f32 v146, v146, s79, v193
	v_mov_b32_e32 v196, v9
	global_load_dwordx2 v[116:117], v[112:113], off nt
	v_add_co_u32_e32 v112, vcc, s11, v82
	v_cvt_pk_fp8_f32 v194, v148, v150 op_sel:[0,0,1]
	v_mul_f32_e32 v148, 0x43800000, v156
	v_mul_f32_e32 v150, 0x43800000, v158
	v_cvt_pk_fp8_f32 v196, v144, v146
	s_waitcnt vmcnt(27)
	v_mul_f32_e32 v144, 0x43800000, v170
	s_waitcnt vmcnt(26)
	v_mul_f32_e32 v146, 0x43800000, v172
	v_addc_co_u32_e32 v113, vcc, 0, v83, vcc
	s_mov_b32 s11, 0x198000
	v_med3_f32 v148, v148, s79, v193
	v_med3_f32 v150, v150, s79, v193
	v_med3_f32 v144, v144, s79, v193
	v_med3_f32 v146, v146, s79, v193
	v_mov_b32_e32 v197, v9
	global_load_dwordx2 v[124:125], v[112:113], off nt
	v_add_co_u32_e32 v112, vcc, s11, v82
	v_cvt_pk_fp8_f32 v195, v148, v150 op_sel:[0,0,1]
	s_waitcnt vmcnt(26)
	v_mul_f32_e32 v148, 0x43800000, v166
	s_waitcnt vmcnt(25)
	v_mul_f32_e32 v150, 0x43800000, v168
	v_cvt_pk_fp8_f32 v197, v144, v146
	v_addc_co_u32_e32 v113, vcc, 0, v83, vcc
	v_med3_f32 v148, v148, s79, v193
	v_med3_f32 v150, v150, s79, v193
	global_load_dwordx2 v[132:133], v[112:113], off nt
	v_cvt_pk_fp8_f32 v196, v148, v150 op_sel:[0,0,1]
	s_waitcnt vmcnt(25)
	v_mul_f32_e32 v148, 0x43800000, v174
	s_waitcnt vmcnt(24)
; #define CV_LOAD(v, kb) do { _Pragma("unroll") for (int j = 0; j < 16; ++j) v[j] = __builtin_nontemporal_load((const f32x2*)(src + (size_t)((kb) * 16 + j) * ldw)); } while (0)
; __device__ __forceinline__ void tr128_f8(const float* W, int ldw, int srccol, unsigned char* WT, size_t dstrow0, int K, int k0, LAS unsigned char* tile, int lane) {
;     ...
;     CV_LOAD(va, 0); CV_LOAD(vb, 1); CV_LOAD(vc, 2);
;     CV_LOAD(vd, 3); CV_PUT(va, 0); CV_LOAD(va, 4); CV_PUT(vb, 1); CV_LOAD(vb, 5); CV_PUT(vc, 2); CV_LOAD(vc, 6); CV_PUT(vd, 3); CV_LOAD(vd, 7);
;     CV_PUT(va, 4); CV_PUT(vb, 5); CV_PUT(vc, 6); CV_PUT(vd, 7);
	v_mul_f32_e32 v150, 0x43800000, v176
	global_load_dwordx2 v[78:79], v[78:79], off nt
	v_med3_f32 v148, v148, s79, v193
	global_load_dwordx2 v[88:89], v[88:89], off nt
	v_med3_f32 v150, v150, s79, v193
	v_mul_f32_e32 v144, 0x43800000, v145
	v_mul_f32_e32 v145, 0x43800000, v147
	v_cvt_pk_fp8_f32 v197, v148, v150 op_sel:[0,0,1]
	v_med3_f32 v148, v144, s79, v193
	v_med3_f32 v145, v145, s79, v193
	v_mov_b32_e32 v144, v9
	v_cvt_pk_fp8_f32 v144, v148, v145
	global_load_dwordx2 v[96:97], v[96:97], off nt
	v_mul_f32_e32 v146, 0x43800000, v149
	v_mul_f32_e32 v147, 0x43800000, v151
	v_med3_f32 v146, v146, s79, v193
	v_med3_f32 v147, v147, s79, v193
	v_cvt_pk_fp8_f32 v144, v146, v147 op_sel:[0,0,1]
	v_mul_f32_e32 v145, 0x43800000, v153
	v_mul_f32_e32 v146, 0x43800000, v155
	v_med3_f32 v149, v145, s79, v193
	v_med3_f32 v146, v146, s79, v193
	v_mov_b32_e32 v145, v9
	v_cvt_pk_fp8_f32 v145, v149, v146
	v_mul_f32_e32 v147, 0x43800000, v157
	v_mul_f32_e32 v148, 0x43800000, v159
	v_med3_f32 v147, v147, s79, v193
	v_med3_f32 v148, v148, s79, v193
	v_cvt_pk_fp8_f32 v145, v147, v148 op_sel:[0,0,1]
	v_mul_f32_e32 v146, 0x43800000, v161
	v_mul_f32_e32 v147, 0x43800000, v165
	v_med3_f32 v150, v146, s79, v193
	v_med3_f32 v147, v147, s79, v193
	v_mov_b32_e32 v146, v9
	v_cvt_pk_fp8_f32 v146, v150, v147
	v_mul_f32_e32 v148, 0x43800000, v167
	v_mul_f32_e32 v149, 0x43800000, v169
	v_med3_f32 v148, v148, s79, v193
	v_med3_f32 v149, v149, s79, v193
	v_cvt_pk_fp8_f32 v146, v148, v149 op_sel:[0,0,1]
	v_mul_f32_e32 v147, 0x43800000, v171
	v_mul_f32_e32 v148, 0x43800000, v173
	v_med3_f32 v151, v147, s79, v193
	v_med3_f32 v148, v148, s79, v193
	v_mov_b32_e32 v147, v9
	v_cvt_pk_fp8_f32 v147, v151, v148
	v_mul_f32_e32 v149, 0x43800000, v175
	v_mul_f32_e32 v150, 0x43800000, v177
	v_med3_f32 v149, v149, s79, v193
	v_med3_f32 v150, v150, s79, v193
	v_cvt_pk_fp8_f32 v147, v149, v150 op_sel:[0,0,1]
	ds_write_b128 v8, v[194:197] offset:16
	v_add_u32_e32 v8, v13, v21
	s_mov_b32 s11, 0x19c000
	ds_write_b128 v8, v[144:147]
	v_mul_f32_e32 v8, 0x43800000, v52
	v_mul_f32_e32 v52, 0x43800000, v60
	v_med3_f32 v8, v8, s79, v193
	v_med3_f32 v52, v52, s79, v193
	v_mov_b32_e32 v194, v9
	v_add_co_u32_e32 v112, vcc, s11, v82
	v_cvt_pk_fp8_f32 v194, v8, v52
	v_mul_f32_e32 v8, 0x43800000, v50
	v_mul_f32_e32 v50, 0x43800000, v58
	v_addc_co_u32_e32 v113, vcc, 0, v83, vcc
	s_mov_b32 s11, 0x1a0000
	v_med3_f32 v8, v8, s79, v193
	v_med3_f32 v50, v50, s79, v193
	v_mov_b32_e32 v195, v9
	global_load_dwordx2 v[140:141], v[112:113], off nt
	v_add_co_u32_e32 v112, vcc, s11, v82
	v_cvt_pk_fp8_f32 v195, v8, v50
	v_mul_f32_e32 v4, 0x43800000, v4
	v_mul_f32_e32 v8, 0x43800000, v56
	v_addc_co_u32_e32 v113, vcc, 0, v83, vcc
	s_mov_b32 s11, 0x1a4000
	v_med3_f32 v4, v4, s79, v193
	v_med3_f32 v8, v8, s79, v193
	v_mov_b32_e32 v196, v9
	global_load_dwordx2 v[114:115], v[112:113], off nt
	v_add_co_u32_e32 v112, vcc, s11, v82
	v_mul_f32_e32 v52, 0x43800000, v66
	v_mul_f32_e32 v58, 0x43800000, v74
	v_cvt_pk_fp8_f32 v196, v4, v8
	s_waitcnt vmcnt(18)
	v_mul_f32_e32 v2, 0x43800000, v2
	s_waitcnt vmcnt(17)
	v_mul_f32_e32 v4, 0x43800000, v54
	v_addc_co_u32_e32 v113, vcc, 0, v83, vcc
	s_mov_b32 s11, 0x1a8000
	v_med3_f32 v52, v52, s79, v193
	v_med3_f32 v58, v58, s79, v193
	v_med3_f32 v2, v2, s79, v193
	v_med3_f32 v4, v4, s79, v193
	v_mov_b32_e32 v197, v9
	global_load_dwordx2 v[122:123], v[112:113], off nt
	v_add_co_u32_e32 v112, vcc, s11, v82
	v_cvt_pk_fp8_f32 v195, v52, v58 op_sel:[0,0,1]
	v_mul_f32_e32 v50, 0x43800000, v64
	v_mul_f32_e32 v52, 0x43800000, v72
	v_cvt_pk_fp8_f32 v197, v2, v4
	v_addc_co_u32_e32 v113, vcc, 0, v83, vcc
	s_mov_b32 s11, 0x1ac000
	v_med3_f32 v50, v50, s79, v193
	v_med3_f32 v52, v52, s79, v193
	global_load_dwordx2 v[130:131], v[112:113], off nt
	v_add_co_u32_e32 v112, vcc, s11, v82
	v_cvt_pk_fp8_f32 v196, v50, v52 op_sel:[0,0,1]
	s_waitcnt vmcnt(16)
	v_mul_f32_e32 v8, 0x43800000, v62
	s_waitcnt vmcnt(15)
	v_mul_f32_e32 v50, 0x43800000, v70
	v_addc_co_u32_e32 v113, vcc, 0, v83, vcc
	s_mov_b32 s11, 0x1b0000
	v_med3_f32 v8, v8, s79, v193
	v_med3_f32 v50, v50, s79, v193
	global_load_dwordx2 v[138:139], v[112:113], off nt
	v_add_co_u32_e32 v112, vcc, s11, v82
	v_cvt_pk_fp8_f32 v197, v8, v50 op_sel:[0,0,1]
	v_mul_f32_e32 v2, 0x43800000, v53
	v_mul_f32_e32 v4, 0x43800000, v61
	v_mul_f32_e32 v50, 0x43800000, v77
	v_addc_co_u32_e32 v113, vcc, 0, v83, vcc
	s_mov_b32 s11, 0x1b4000
	v_med3_f32 v2, v2, s79, v193
	v_med3_f32 v4, v4, s79, v193
	v_med3_f32 v52, v50, s79, v193
	v_mov_b32_e32 v50, v9
	v_add_co_u32_e32 v120, vcc, s11, v82
	v_cvt_pk_fp8_f32 v50, v2, v4
	s_nop 0
	v_addc_co_u32_e32 v121, vcc, 0, v83, vcc
	s_mov_b32 s11, 0x1b8000
	v_add_co_u32_e32 v128, vcc, s11, v82
	v_mul_f32_e32 v8, 0x43800000, v69
	s_nop 0
	v_addc_co_u32_e32 v129, vcc, 0, v83, vcc
	s_mov_b32 s11, 0x1bc000
	v_med3_f32 v8, v8, s79, v193
	v_mul_f32_e32 v2, 0x43800000, v51
	v_mul_f32_e32 v4, 0x43800000, v59
	v_mul_f32_e32 v51, 0x43800000, v75
	v_add_co_u32_e32 v136, vcc, s11, v82
	v_cvt_pk_fp8_f32 v50, v8, v52 op_sel:[0,0,1]
	v_med3_f32 v2, v2, s79, v193
	v_med3_f32 v4, v4, s79, v193
	v_med3_f32 v52, v51, s79, v193
	v_mov_b32_e32 v51, v9
	v_addc_co_u32_e32 v137, vcc, 0, v83, vcc
	s_mov_b32 s11, 0x1c0000
	v_cvt_pk_fp8_f32 v51, v2, v4
	v_add_co_u32_e32 v144, vcc, s11, v82
	s_mov_b32 s11, 0x1c4000
	s_nop 0
	v_addc_co_u32_e32 v145, vcc, 0, v83, vcc
	v_mul_f32_e32 v8, 0x43800000, v67
	global_load_dwordx2 v[150:151], v[144:145], off nt
	v_add_co_u32_e32 v144, vcc, s11, v82
	v_med3_f32 v8, v8, s79, v193
	v_mul_f32_e32 v2, 0x43800000, v5
	v_mul_f32_e32 v4, 0x43800000, v57
	v_addc_co_u32_e32 v145, vcc, 0, v83, vcc
	s_mov_b32 s11, 0x1c8000
; #define CV_LOAD(v, kb) do { _Pragma("unroll") for (int j = 0; j < 16; ++j) v[j] = __builtin_nontemporal_load((const f32x2*)(src + (size_t)((kb) * 16 + j) * ldw)); } while (0)
; __device__ __forceinline__ void tr128_f8(const float* W, int ldw, int srccol, unsigned char* WT, size_t dstrow0, int K, int k0, LAS unsigned char* tile, int lane) {
;     ...
;     CV_LOAD(va, 0); CV_LOAD(vb, 1); CV_LOAD(vc, 2);
;     CV_LOAD(vd, 3); CV_PUT(va, 0); CV_LOAD(va, 4); CV_PUT(vb, 1); CV_LOAD(vb, 5); CV_PUT(vc, 2); CV_LOAD(vc, 6); CV_PUT(vd, 3); CV_LOAD(vd, 7);
;     CV_PUT(va, 4); CV_PUT(vb, 5); CV_PUT(vc, 6); CV_PUT(vd, 7);
	v_cvt_pk_fp8_f32 v51, v8, v52 op_sel:[0,0,1]
	v_med3_f32 v2, v2, s79, v193
	v_med3_f32 v4, v4, s79, v193
	v_mov_b32_e32 v52, v9
	global_load_dwordx2 v[112:113], v[112:113], off nt
	v_cvt_pk_fp8_f32 v52, v2, v4
	global_load_dwordx2 v[120:121], v[120:121], off nt
	v_mul_f32_e32 v2, 0x43800000, v3
	global_load_dwordx2 v[156:157], v[144:145], off nt
	v_add_co_u32_e32 v144, vcc, s11, v82
	v_mul_f32_e32 v3, 0x43800000, v55
	s_nop 0
	v_addc_co_u32_e32 v145, vcc, 0, v83, vcc
	s_mov_b32 s11, 0x1cc000
	v_med3_f32 v2, v2, s79, v193
	v_med3_f32 v3, v3, s79, v193
	v_mov_b32_e32 v53, v9
	global_load_dwordx2 v[164:165], v[144:145], off nt
	v_add_co_u32_e32 v144, vcc, s11, v82
	v_mul_f32_e32 v5, 0x43800000, v65
	v_mul_f32_e32 v8, 0x43800000, v73
	v_cvt_pk_fp8_f32 v53, v2, v3
	v_addc_co_u32_e32 v145, vcc, 0, v83, vcc
	s_mov_b32 s11, 0x1d0000
	v_med3_f32 v5, v5, s79, v193
	v_med3_f32 v8, v8, s79, v193
	global_load_dwordx2 v[128:129], v[128:129], off nt
	v_cvt_pk_fp8_f32 v52, v5, v8 op_sel:[0,0,1]
	global_load_dwordx2 v[136:137], v[136:137], off nt
	v_mul_f32_e32 v4, 0x43800000, v63
	global_load_dwordx2 v[170:171], v[144:145], off nt
	v_add_co_u32_e32 v144, vcc, s11, v82
	v_mul_f32_e32 v5, 0x43800000, v71
	s_nop 0
	v_addc_co_u32_e32 v145, vcc, 0, v83, vcc
	s_mov_b32 s11, 0x1d4000
	v_med3_f32 v4, v4, s79, v193
	v_med3_f32 v5, v5, s79, v193
	global_load_dwordx2 v[148:149], v[144:145], off nt
	v_add_co_u32_e32 v144, vcc, s11, v82
	v_cvt_pk_fp8_f32 v53, v4, v5 op_sel:[0,0,1]
	s_nop 0
	v_addc_co_u32_e32 v145, vcc, 0, v83, vcc
	s_mov_b32 s11, 0x1d8000
	global_load_dwordx2 v[154:155], v[144:145], off nt
	v_add_co_u32_e32 v144, vcc, s11, v82
	s_mov_b32 s11, 0x1dc000
	s_nop 0
	v_addc_co_u32_e32 v145, vcc, 0, v83, vcc
	v_add_u32_e32 v2, v13, v25
	global_load_dwordx2 v[160:161], v[144:145], off nt
	v_add_co_u32_e32 v144, vcc, s11, v82
	ds_write_b128 v2, v[50:53]
	v_mul_f32_e32 v2, 0x43800000, v86
	v_mul_f32_e32 v3, 0x43800000, v94
	v_addc_co_u32_e32 v145, vcc, 0, v83, vcc
	s_mov_b32 s11, 0x1e0000
	v_med3_f32 v50, v2, s79, v193
	v_med3_f32 v3, v3, s79, v193
	v_mov_b32_e32 v2, v9
	global_load_dwordx2 v[168:169], v[144:145], off nt
	v_add_co_u32_e32 v144, vcc, s11, v82
	v_cvt_pk_fp8_f32 v2, v50, v3
	s_nop 0
	v_addc_co_u32_e32 v145, vcc, 0, v83, vcc
	s_mov_b32 s11, 0x1e4000
	global_load_dwordx2 v[146:147], v[144:145], off nt
	v_add_co_u32_e32 v144, vcc, s11, v82
	v_mul_f32_e32 v4, 0x43800000, v102
	v_mul_f32_e32 v5, 0x43800000, v110
	v_addc_co_u32_e32 v145, vcc, 0, v83, vcc
	s_mov_b32 s11, 0x1e8000
	v_med3_f32 v4, v4, s79, v193
	v_med3_f32 v5, v5, s79, v193
	global_load_dwordx2 v[152:153], v[144:145], off nt
	v_add_co_u32_e32 v144, vcc, s11, v82
	v_cvt_pk_fp8_f32 v2, v4, v5 op_sel:[0,0,1]
	v_mul_f32_e32 v3, 0x43800000, v84
	v_mul_f32_e32 v4, 0x43800000, v92
	v_addc_co_u32_e32 v145, vcc, 0, v83, vcc
	s_mov_b32 s11, 0x1ec000
	v_med3_f32 v51, v3, s79, v193
	v_med3_f32 v4, v4, s79, v193
	v_mov_b32_e32 v3, v9
	global_load_dwordx2 v[158:159], v[144:145], off nt
	v_add_co_u32_e32 v144, vcc, s11, v82
	v_cvt_pk_fp8_f32 v3, v51, v4
	s_nop 0
	v_addc_co_u32_e32 v145, vcc, 0, v83, vcc
	s_mov_b32 s11, 0x1f0000
	global_load_dwordx2 v[166:167], v[144:145], off nt
	v_add_co_u32_e32 v144, vcc, s11, v82
	v_mul_f32_e32 v5, 0x43800000, v100
	v_mul_f32_e32 v50, 0x43800000, v108
	v_addc_co_u32_e32 v145, vcc, 0, v83, vcc
	s_mov_b32 s11, 0x1f4000
	v_med3_f32 v5, v5, s79, v193
	v_med3_f32 v50, v50, s79, v193
	v_add_co_u32_e32 v172, vcc, s11, v82
	v_cvt_pk_fp8_f32 v3, v5, v50 op_sel:[0,0,1]
	v_mul_f32_e32 v4, 0x43800000, v80
	v_mul_f32_e32 v5, 0x43800000, v90
	v_addc_co_u32_e32 v173, vcc, 0, v83, vcc
	s_mov_b32 s11, 0x1f8000
	v_med3_f32 v52, v4, s79, v193
	v_med3_f32 v5, v5, s79, v193
	v_mov_b32_e32 v4, v9
	v_add_co_u32_e32 v174, vcc, s11, v82
	v_cvt_pk_fp8_f32 v4, v52, v5
	s_nop 0
	v_addc_co_u32_e32 v175, vcc, 0, v83, vcc
	s_mov_b32 s11, 0x1fc000
	v_add_co_u32_e32 v82, vcc, s11, v82
	v_mul_f32_e32 v50, 0x43800000, v98
	v_mul_f32_e32 v51, 0x43800000, v106
	v_addc_co_u32_e32 v83, vcc, 0, v83, vcc
	v_med3_f32 v50, v50, s79, v193
	v_med3_f32 v51, v51, s79, v193
	global_load_dwordx2 v[82:83], v[82:83], off nt
	v_cvt_pk_fp8_f32 v4, v50, v51 op_sel:[0,0,1]
	s_waitcnt vmcnt(24)
	v_mul_f32_e32 v5, 0x43800000, v78
	s_waitcnt vmcnt(23)
	v_mul_f32_e32 v50, 0x43800000, v88
	v_med3_f32 v53, v5, s79, v193
	v_med3_f32 v50, v50, s79, v193
	v_mov_b32_e32 v5, v9
	v_cvt_pk_fp8_f32 v5, v53, v50
	s_waitcnt vmcnt(22)
; #define CV_LOAD(v, kb) do { _Pragma("unroll") for (int j = 0; j < 16; ++j) v[j] = __builtin_nontemporal_load((const f32x2*)(src + (size_t)((kb) * 16 + j) * ldw)); } while (0)
; __device__ __forceinline__ void tr128_f8(const float* W, int ldw, int srccol, unsigned char* WT, size_t dstrow0, int K, int k0, LAS unsigned char* tile, int lane) {
;     ...
;     CV_LOAD(va, 0); CV_LOAD(vb, 1); CV_LOAD(vc, 2);
;     CV_LOAD(vd, 3); CV_PUT(va, 0); CV_LOAD(va, 4); CV_PUT(vb, 1); CV_LOAD(vb, 5); CV_PUT(vc, 2); CV_LOAD(vc, 6); CV_PUT(vd, 3); CV_LOAD(vd, 7);
;     CV_PUT(va, 4); CV_PUT(vb, 5); CV_PUT(vc, 6); CV_PUT(vd, 7);
	v_mul_f32_e32 v51, 0x43800000, v96
	v_mul_f32_e32 v52, 0x43800000, v104
	v_med3_f32 v51, v51, s79, v193
	v_med3_f32 v52, v52, s79, v193
	v_cvt_pk_fp8_f32 v5, v51, v52 op_sel:[0,0,1]
	v_mul_f32_e32 v50, 0x43800000, v87
	v_mul_f32_e32 v51, 0x43800000, v95
	v_med3_f32 v54, v50, s79, v193
	v_med3_f32 v51, v51, s79, v193
	v_mov_b32_e32 v50, v9
	v_cvt_pk_fp8_f32 v50, v54, v51
	v_mul_f32_e32 v52, 0x43800000, v103
	v_mul_f32_e32 v53, 0x43800000, v111
	v_med3_f32 v52, v52, s79, v193
	v_med3_f32 v53, v53, s79, v193
	v_cvt_pk_fp8_f32 v50, v52, v53 op_sel:[0,0,1]
	v_mul_f32_e32 v51, 0x43800000, v85
	v_mul_f32_e32 v52, 0x43800000, v93
	v_med3_f32 v55, v51, s79, v193
	v_med3_f32 v52, v52, s79, v193
	v_mov_b32_e32 v51, v9
	v_cvt_pk_fp8_f32 v51, v55, v52
	v_mul_f32_e32 v53, 0x43800000, v101
	v_mul_f32_e32 v54, 0x43800000, v109
	v_med3_f32 v53, v53, s79, v193
	v_med3_f32 v54, v54, s79, v193
	v_cvt_pk_fp8_f32 v51, v53, v54 op_sel:[0,0,1]
	v_mul_f32_e32 v52, 0x43800000, v81
	v_mul_f32_e32 v53, 0x43800000, v91
	v_med3_f32 v56, v52, s79, v193
	v_med3_f32 v53, v53, s79, v193
	v_mov_b32_e32 v52, v9
	v_cvt_pk_fp8_f32 v52, v56, v53
	v_mul_f32_e32 v54, 0x43800000, v99
	v_mul_f32_e32 v55, 0x43800000, v107
	v_med3_f32 v54, v54, s79, v193
	v_med3_f32 v55, v55, s79, v193
	global_load_dwordx2 v[144:145], v[144:145], off nt
	v_cvt_pk_fp8_f32 v52, v54, v55 op_sel:[0,0,1]
	global_load_dwordx2 v[172:173], v[172:173], off nt
	v_mul_f32_e32 v53, 0x43800000, v79
	v_mul_f32_e32 v54, 0x43800000, v89
	v_med3_f32 v57, v53, s79, v193
	v_med3_f32 v54, v54, s79, v193
	v_mov_b32_e32 v53, v9
	v_cvt_pk_fp8_f32 v53, v57, v54
	global_load_dwordx2 v[174:175], v[174:175], off nt
	v_mul_f32_e32 v55, 0x43800000, v97
	v_mul_f32_e32 v56, 0x43800000, v105
	v_mul_f32_e32 v60, 0x43800000, v68
	v_mul_f32_e32 v68, 0x43800000, v76
	v_med3_f32 v55, v55, s79, v193
	v_med3_f32 v56, v56, s79, v193
	v_med3_f32 v60, v60, s79, v193
	v_med3_f32 v68, v68, s79, v193
	v_cvt_pk_fp8_f32 v53, v55, v56 op_sel:[0,0,1]
	v_cvt_pk_fp8_f32 v194, v60, v68 op_sel:[0,0,1]
	v_add_u32_e32 v8, v7, v23
	ds_write_b128 v8, v[2:5] offset:16
	v_add_u32_e32 v2, v13, v27
	ds_write_b128 v2, v[50:53]
	v_mul_f32_e32 v2, 0x43800000, v118
	v_mul_f32_e32 v3, 0x43800000, v126
	ds_write_b128 v8, v[194:197]
	v_med3_f32 v8, v2, s79, v193
	v_med3_f32 v3, v3, s79, v193
	v_mov_b32_e32 v2, v9
	v_cvt_pk_fp8_f32 v2, v8, v3
	v_mul_f32_e32 v4, 0x43800000, v134
	v_mul_f32_e32 v5, 0x43800000, v142
	v_med3_f32 v4, v4, s79, v193
	v_med3_f32 v5, v5, s79, v193
	v_cvt_pk_fp8_f32 v2, v4, v5 op_sel:[0,0,1]
	v_mul_f32_e32 v3, 0x43800000, v116
	v_mul_f32_e32 v4, 0x43800000, v124
	v_med3_f32 v50, v3, s79, v193
	v_med3_f32 v4, v4, s79, v193
	v_mov_b32_e32 v3, v9
	v_cvt_pk_fp8_f32 v3, v50, v4
	v_mul_f32_e32 v5, 0x43800000, v132
	s_waitcnt vmcnt(24)
	v_mul_f32_e32 v8, 0x43800000, v140
	v_med3_f32 v5, v5, s79, v193
	v_med3_f32 v8, v8, s79, v193
	v_cvt_pk_fp8_f32 v3, v5, v8 op_sel:[0,0,1]
	s_waitcnt vmcnt(23)
	v_mul_f32_e32 v4, 0x43800000, v114
	s_waitcnt vmcnt(22)
	v_mul_f32_e32 v5, 0x43800000, v122
	v_med3_f32 v51, v4, s79, v193
	v_med3_f32 v5, v5, s79, v193
	v_mov_b32_e32 v4, v9
	v_cvt_pk_fp8_f32 v4, v51, v5
	s_waitcnt vmcnt(21)
	v_mul_f32_e32 v8, 0x43800000, v130
	s_waitcnt vmcnt(20)
	v_mul_f32_e32 v50, 0x43800000, v138
	v_med3_f32 v8, v8, s79, v193
	v_med3_f32 v50, v50, s79, v193
	v_cvt_pk_fp8_f32 v4, v8, v50 op_sel:[0,0,1]
	s_waitcnt vmcnt(18)
	v_mul_f32_e32 v5, 0x43800000, v112
	s_waitcnt vmcnt(17)
	v_mul_f32_e32 v8, 0x43800000, v120
	v_med3_f32 v52, v5, s79, v193
	v_med3_f32 v8, v8, s79, v193
	v_mov_b32_e32 v5, v9
	v_cvt_pk_fp8_f32 v5, v52, v8
	s_waitcnt vmcnt(14)
	v_mul_f32_e32 v50, 0x43800000, v128
	s_waitcnt vmcnt(13)
	v_mul_f32_e32 v51, 0x43800000, v136
	v_med3_f32 v50, v50, s79, v193
	v_med3_f32 v51, v51, s79, v193
	v_cvt_pk_fp8_f32 v5, v50, v51 op_sel:[0,0,1]
	v_mul_f32_e32 v8, 0x43800000, v119
	v_mul_f32_e32 v50, 0x43800000, v127
	v_med3_f32 v8, v8, s79, v193
	v_med3_f32 v53, v50, s79, v193
	v_mov_b32_e32 v50, v9
	v_cvt_pk_fp8_f32 v50, v8, v53
	v_mul_f32_e32 v51, 0x43800000, v135
	v_mul_f32_e32 v52, 0x43800000, v143
	v_med3_f32 v51, v51, s79, v193
	v_med3_f32 v52, v52, s79, v193
	v_cvt_pk_fp8_f32 v50, v51, v52 op_sel:[0,0,1]
	v_mul_f32_e32 v8, 0x43800000, v117
	v_mul_f32_e32 v51, 0x43800000, v125
	v_med3_f32 v8, v8, s79, v193
	v_med3_f32 v54, v51, s79, v193
	v_mov_b32_e32 v51, v9
	v_cvt_pk_fp8_f32 v51, v8, v54
	v_mul_f32_e32 v52, 0x43800000, v133
	v_mul_f32_e32 v53, 0x43800000, v141
	v_med3_f32 v52, v52, s79, v193
	v_med3_f32 v53, v53, s79, v193
	v_cvt_pk_fp8_f32 v51, v52, v53 op_sel:[0,0,1]
	v_mul_f32_e32 v8, 0x43800000, v115
	v_mul_f32_e32 v52, 0x43800000, v123
	v_med3_f32 v8, v8, s79, v193
	v_med3_f32 v55, v52, s79, v193
	v_mov_b32_e32 v52, v9
	v_cvt_pk_fp8_f32 v52, v8, v55
	v_mul_f32_e32 v53, 0x43800000, v131
	v_mul_f32_e32 v54, 0x43800000, v139
	v_med3_f32 v53, v53, s79, v193
	v_med3_f32 v54, v54, s79, v193
	v_cvt_pk_fp8_f32 v52, v53, v54 op_sel:[0,0,1]
	v_mul_f32_e32 v8, 0x43800000, v113
	v_mul_f32_e32 v53, 0x43800000, v121
	v_med3_f32 v8, v8, s79, v193
	v_med3_f32 v56, v53, s79, v193
	v_mov_b32_e32 v53, v9
	v_cvt_pk_fp8_f32 v53, v8, v56
	v_mul_f32_e32 v54, 0x43800000, v129
	v_mul_f32_e32 v55, 0x43800000, v137
	v_med3_f32 v54, v54, s79, v193
	v_med3_f32 v55, v55, s79, v193
	v_cvt_pk_fp8_f32 v53, v54, v55 op_sel:[0,0,1]
	v_add_u32_e32 v8, v7, v29
	ds_write_b128 v8, v[2:5]
	v_add_u32_e32 v2, v13, v31
	ds_write_b128 v2, v[50:53]
	v_mul_f32_e32 v2, 0x43800000, v150
	v_mul_f32_e32 v3, 0x43800000, v156
	v_med3_f32 v50, v2, s79, v193
	v_med3_f32 v3, v3, s79, v193
	v_mov_b32_e32 v2, v9
	v_cvt_pk_fp8_f32 v2, v50, v3
	v_mul_f32_e32 v4, 0x43800000, v164
	s_waitcnt vmcnt(12)
; #define LAS __attribute__((address_space(3)))
; #define LDS_WAIT() asm volatile("s_waitcnt lgkmcnt(0)" ::: "memory")
; __device__ __forceinline__ void tr128_f8(const float* W, int ldw, int srccol, unsigned char* WT, size_t dstrow0, int K, int k0, LAS unsigned char* tile, int lane) {
;     ...
;     LDS_WAIT(); asm volatile("" ::: "memory");
;     const int c = lane & 7;
; #pragma unroll
;     for (int j = 0; j < 16; ++j) { const int n = (lane >> 3) + 8 * j; const v4u o = *(const LAS v4u*)(tile + n * 128 + ((c ^ (n & 7)) << 4));
;         __builtin_nontemporal_store(o, (v4u*)(WT + (dstrow0 + n) * K + k0 + 16 * c)); }
	v_mul_f32_e32 v5, 0x43800000, v170
	v_med3_f32 v4, v4, s79, v193
	v_med3_f32 v5, v5, s79, v193
	v_cvt_pk_fp8_f32 v2, v4, v5 op_sel:[0,0,1]
	s_waitcnt vmcnt(11)
	v_mul_f32_e32 v3, 0x43800000, v148
	s_waitcnt vmcnt(10)
	v_mul_f32_e32 v4, 0x43800000, v154
	v_med3_f32 v51, v3, s79, v193
	v_med3_f32 v4, v4, s79, v193
	v_mov_b32_e32 v3, v9
	v_cvt_pk_fp8_f32 v3, v51, v4
	s_waitcnt vmcnt(9)
	v_mul_f32_e32 v5, 0x43800000, v160
	s_waitcnt vmcnt(8)
	v_mul_f32_e32 v50, 0x43800000, v168
	v_med3_f32 v5, v5, s79, v193
	v_med3_f32 v50, v50, s79, v193
	v_cvt_pk_fp8_f32 v3, v5, v50 op_sel:[0,0,1]
	s_waitcnt vmcnt(7)
	v_mul_f32_e32 v4, 0x43800000, v146
	s_waitcnt vmcnt(6)
	v_mul_f32_e32 v5, 0x43800000, v152
	v_med3_f32 v52, v4, s79, v193
	v_med3_f32 v5, v5, s79, v193
	v_mov_b32_e32 v4, v9
	v_cvt_pk_fp8_f32 v4, v52, v5
	s_waitcnt vmcnt(5)
	v_mul_f32_e32 v50, 0x43800000, v158
	s_waitcnt vmcnt(4)
	v_mul_f32_e32 v51, 0x43800000, v166
	v_med3_f32 v50, v50, s79, v193
	v_med3_f32 v51, v51, s79, v193
	v_cvt_pk_fp8_f32 v4, v50, v51 op_sel:[0,0,1]
	s_waitcnt vmcnt(2)
	v_mul_f32_e32 v5, 0x43800000, v144
	s_waitcnt vmcnt(1)
	v_mul_f32_e32 v50, 0x43800000, v172
	v_med3_f32 v53, v5, s79, v193
	v_med3_f32 v50, v50, s79, v193
	v_mov_b32_e32 v5, v9
	v_cvt_pk_fp8_f32 v5, v53, v50
	s_waitcnt vmcnt(0)
	v_mul_f32_e32 v51, 0x43800000, v174
	v_mul_f32_e32 v52, 0x43800000, v82
	v_med3_f32 v51, v51, s79, v193
	v_med3_f32 v52, v52, s79, v193
	v_cvt_pk_fp8_f32 v5, v51, v52 op_sel:[0,0,1]
	v_mul_f32_e32 v50, 0x43800000, v151
	v_mul_f32_e32 v51, 0x43800000, v157
	v_med3_f32 v54, v50, s79, v193
	v_med3_f32 v51, v51, s79, v193
	v_mov_b32_e32 v50, v9
	v_cvt_pk_fp8_f32 v50, v54, v51
	v_mul_f32_e32 v52, 0x43800000, v165
	v_mul_f32_e32 v53, 0x43800000, v171
	v_med3_f32 v52, v52, s79, v193
	v_med3_f32 v53, v53, s79, v193
	v_cvt_pk_fp8_f32 v50, v52, v53 op_sel:[0,0,1]
	v_mul_f32_e32 v51, 0x43800000, v149
	v_mul_f32_e32 v52, 0x43800000, v155
	v_med3_f32 v55, v51, s79, v193
	v_med3_f32 v52, v52, s79, v193
	v_mov_b32_e32 v51, v9
	v_cvt_pk_fp8_f32 v51, v55, v52
	v_mul_f32_e32 v53, 0x43800000, v161
	v_mul_f32_e32 v54, 0x43800000, v169
	v_med3_f32 v53, v53, s79, v193
	v_med3_f32 v54, v54, s79, v193
	v_cvt_pk_fp8_f32 v51, v53, v54 op_sel:[0,0,1]
	v_mul_f32_e32 v52, 0x43800000, v147
	v_mul_f32_e32 v53, 0x43800000, v153
	v_med3_f32 v56, v52, s79, v193
	v_med3_f32 v53, v53, s79, v193
	v_mov_b32_e32 v52, v9
	v_cvt_pk_fp8_f32 v52, v56, v53
	v_mul_f32_e32 v54, 0x43800000, v159
	v_mul_f32_e32 v55, 0x43800000, v167
	v_med3_f32 v54, v54, s79, v193
	v_med3_f32 v55, v55, s79, v193
	v_cvt_pk_fp8_f32 v52, v54, v55 op_sel:[0,0,1]
	v_mul_f32_e32 v53, 0x43800000, v145
	v_mul_f32_e32 v54, 0x43800000, v173
	v_med3_f32 v57, v53, s79, v193
	v_med3_f32 v54, v54, s79, v193
	v_mov_b32_e32 v53, v9
	v_cvt_pk_fp8_f32 v53, v57, v54
	v_mul_f32_e32 v55, 0x43800000, v175
	v_mul_f32_e32 v56, 0x43800000, v83
	v_med3_f32 v55, v55, s79, v193
	v_med3_f32 v56, v56, s79, v193
	v_cvt_pk_fp8_f32 v53, v55, v56 op_sel:[0,0,1]
	ds_write_b128 v8, v[2:5] offset:16
	v_add_u32_e32 v2, v13, v33
	v_readlane_b32 s22, v250, 5
	ds_write_b128 v2, v[50:53]
	s_waitcnt lgkmcnt(0)
	v_add_u32_e32 v56, v35, v37
	ds_read_b128 v[56:59], v56
	v_add_u32_e32 v60, v35, v39
	ds_read_b128 v[60:63], v60
	v_add_u32_e32 v64, v35, v179
	ds_read_b128 v[64:67], v64
	v_add_u32_e32 v68, v35, v180
	ds_read_b128 v[68:71], v68
	v_add_u32_e32 v72, v35, v181
	ds_read_b128 v[72:75], v72
	v_add_u32_e32 v76, v35, v182
	ds_read_b128 v[76:79], v76
	v_add_u32_e32 v80, v35, v183
	ds_read_b128 v[80:83], v80
	v_add_u32_e32 v84, v35, v184
	ds_read_b128 v[84:87], v84
	v_add_u32_e32 v88, v35, v185
	ds_read_b128 v[88:91], v88
	v_add_u32_e32 v92, v35, v186
	ds_read_b128 v[92:95], v92
	v_add_u32_e32 v96, v35, v187
	ds_read_b128 v[96:99], v96
	v_add_u32_e32 v100, v35, v188
	ds_read_b128 v[100:103], v100
	v_add_u32_e32 v104, v35, v189
	ds_read_b128 v[104:107], v104
	v_add_u32_e32 v108, v35, v190
	ds_read_b128 v[108:111], v108
	v_add_u32_e32 v112, v35, v191
	ds_read_b128 v[112:115], v112
	v_add_u32_e32 v116, v35, v192
	ds_read_b128 v[116:119], v116
	v_mov_b32_e32 v53, s9
	v_or_b32_e32 v52, s8, v162
	v_lshl_add_u64 v[50:51], v[42:43], 0, s[6:7]
	v_lshlrev_b64 v[52:53], 11, v[52:53]
	v_lshl_add_u64 v[52:53], v[50:51], 0, v[52:53]
	s_waitcnt lgkmcnt(15)
; #define LAS __attribute__((address_space(3)))
; #define LDS_WAIT() asm volatile("s_waitcnt lgkmcnt(0)" ::: "memory")
; __device__ __forceinline__ void tr128_f8(const float* W, int ldw, int srccol, unsigned char* WT, size_t dstrow0, int K, int k0, LAS unsigned char* tile, int lane) {
;     ...
;     LDS_WAIT(); asm volatile("" ::: "memory");
;     const int c = lane & 7;
; #pragma unroll
;     for (int j = 0; j < 16; ++j) { const int n = (lane >> 3) + 8 * j; const v4u o = *(const LAS v4u*)(tile + n * 128 + ((c ^ (n & 7)) << 4));
;         __builtin_nontemporal_store(o, (v4u*)(WT + (dstrow0 + n) * K + k0 + 16 * c)); }
;     LDS_WAIT(); asm volatile("" ::: "memory");
	global_store_dwordx4 v[52:53], v[56:59], off nt
	v_mov_b32_e32 v53, s9
	v_or_b32_e32 v52, s8, v10
	v_lshlrev_b64 v[52:53], 11, v[52:53]
	v_lshl_add_u64 v[52:53], v[50:51], 0, v[52:53]
	v_readlane_b32 s24, v250, 7
	v_readlane_b32 s26, v250, 9
	s_waitcnt lgkmcnt(14)
	global_store_dwordx4 v[52:53], v[60:63], off nt
	v_mov_b32_e32 v53, s9
	v_or_b32_e32 v52, s8, v12
	v_lshlrev_b64 v[52:53], 11, v[52:53]
	v_lshl_add_u64 v[52:53], v[50:51], 0, v[52:53]
	s_mov_b32 s26, 0xe000
	s_mov_b32 s24, 0xa000
	s_waitcnt lgkmcnt(13)
	global_store_dwordx4 v[52:53], v[64:67], off nt
	v_mov_b32_e32 v53, s9
	v_or_b32_e32 v52, s8, v14
	v_lshlrev_b64 v[52:53], 11, v[52:53]
	v_lshl_add_u64 v[52:53], v[50:51], 0, v[52:53]
	s_movk_i32 s22, 0x6000
	s_movk_i32 s20, 0x2000
	s_waitcnt lgkmcnt(12)
	global_store_dwordx4 v[52:53], v[68:71], off nt
	v_mov_b32_e32 v53, s9
	v_or_b32_e32 v52, s8, v16
	v_lshlrev_b64 v[52:53], 11, v[52:53]
	v_lshl_add_u64 v[52:53], v[50:51], 0, v[52:53]
	s_mov_b32 s33, 0x12000
	s_waitcnt lgkmcnt(11)
	global_store_dwordx4 v[52:53], v[72:75], off nt
	v_mov_b32_e32 v53, s9
	s_nop 0
	v_or_b32_e32 v52, s8, v18
	v_lshlrev_b64 v[52:53], 11, v[52:53]
	v_lshl_add_u64 v[52:53], v[50:51], 0, v[52:53]
	s_waitcnt lgkmcnt(10)
	global_store_dwordx4 v[52:53], v[76:79], off nt
	v_mov_b32_e32 v53, s9
	s_nop 0
	v_or_b32_e32 v52, s8, v20
	v_lshlrev_b64 v[52:53], 11, v[52:53]
	v_lshl_add_u64 v[52:53], v[50:51], 0, v[52:53]
	s_waitcnt lgkmcnt(9)
	global_store_dwordx4 v[52:53], v[80:83], off nt
	v_mov_b32_e32 v53, s9
	s_nop 0
	v_or_b32_e32 v52, s8, v22
	v_lshlrev_b64 v[52:53], 11, v[52:53]
	v_lshl_add_u64 v[52:53], v[50:51], 0, v[52:53]
	s_waitcnt lgkmcnt(8)
	global_store_dwordx4 v[52:53], v[84:87], off nt
	v_mov_b32_e32 v53, s9
	s_nop 0
	v_or_b32_e32 v52, s8, v24
	v_lshlrev_b64 v[52:53], 11, v[52:53]
	v_lshl_add_u64 v[52:53], v[50:51], 0, v[52:53]
	s_waitcnt lgkmcnt(7)
	global_store_dwordx4 v[52:53], v[88:91], off nt
	v_mov_b32_e32 v53, s9
	s_nop 0
	v_or_b32_e32 v52, s8, v26
	v_lshlrev_b64 v[52:53], 11, v[52:53]
	v_lshl_add_u64 v[52:53], v[50:51], 0, v[52:53]
	s_waitcnt lgkmcnt(6)
	global_store_dwordx4 v[52:53], v[92:95], off nt
	v_mov_b32_e32 v53, s9
	s_nop 0
	v_or_b32_e32 v52, s8, v28
	v_lshlrev_b64 v[52:53], 11, v[52:53]
	v_lshl_add_u64 v[52:53], v[50:51], 0, v[52:53]
	s_waitcnt lgkmcnt(5)
	global_store_dwordx4 v[52:53], v[96:99], off nt
	v_mov_b32_e32 v53, s9
	s_nop 0
	v_or_b32_e32 v52, s8, v30
	v_lshlrev_b64 v[52:53], 11, v[52:53]
	v_lshl_add_u64 v[52:53], v[50:51], 0, v[52:53]
	s_waitcnt lgkmcnt(4)
	global_store_dwordx4 v[52:53], v[100:103], off nt
	v_mov_b32_e32 v53, s9
	s_nop 0
	v_or_b32_e32 v52, s8, v32
	v_lshlrev_b64 v[52:53], 11, v[52:53]
	v_lshl_add_u64 v[52:53], v[50:51], 0, v[52:53]
	s_waitcnt lgkmcnt(3)
	global_store_dwordx4 v[52:53], v[104:107], off nt
	v_mov_b32_e32 v53, s9
	s_nop 0
	v_or_b32_e32 v52, s8, v34
	v_lshlrev_b64 v[52:53], 11, v[52:53]
	v_lshl_add_u64 v[52:53], v[50:51], 0, v[52:53]
	s_waitcnt lgkmcnt(2)
	global_store_dwordx4 v[52:53], v[108:111], off nt
	v_mov_b32_e32 v53, s9
	s_nop 0
	v_or_b32_e32 v52, s8, v36
	v_lshlrev_b64 v[52:53], 11, v[52:53]
	v_lshl_add_u64 v[52:53], v[50:51], 0, v[52:53]
	s_waitcnt lgkmcnt(1)
	global_store_dwordx4 v[52:53], v[112:115], off nt
	v_mov_b32_e32 v53, s9
	s_nop 0
	v_or_b32_e32 v52, s8, v38
	v_lshlrev_b64 v[52:53], 11, v[52:53]
	v_lshl_add_u64 v[50:51], v[50:51], 0, v[52:53]
	s_waitcnt lgkmcnt(0)
	global_store_dwordx4 v[50:51], v[116:119], off nt
	s_waitcnt lgkmcnt(0)

; #define CV_LOAD(v, kb) do { _Pragma("unroll") for (int j = 0; j < 16; ++j) v[j] = __builtin_nontemporal_load((const f32x2*)(src + (size_t)((kb) * 16 + j) * ldw)); } while (0)
; __device__ __forceinline__ void tr128_f8(const float* W, int ldw, int srccol, unsigned char* WT, size_t dstrow0, int K, int k0, LAS unsigned char* tile, int lane) {
;     const float* src = W + (size_t)k0 * ldw + srccol + 2 * lane;
;     f32x2 va[16], vb[16], vc[16], vd[16];
;     ...
;     CV_LOAD(va, 0); CV_LOAD(vb, 1); CV_LOAD(vc, 2);
;     CV_LOAD(vd, 3); CV_PUT(va, 0); CV_LOAD(va, 4); CV_PUT(vb, 1); CV_LOAD(vb, 5); CV_PUT(vc, 2); CV_LOAD(vc, 6); CV_PUT(vd, 3); CV_LOAD(vd, 7);
; __device__ __forceinline__ void cv_item(const Args& a, int it, LAS unsigned char* tile, int lane) {
;     ...
;     if (it < CV_WO) { const int kt = it >> 4, nt = it & 15; tr128_f8(a.in[I_WOUT], 2048, 128 * nt, (unsigned char*)(a.ws + WS_WO), (size_t)128 * nt, 2048, 128 * kt, tile, lane); return; } it -= CV_WO;
.LBB0_506:
	s_andn2_b64 vcc, exec, s[8:9]
	s_cbranch_vccnz .LBB0_508
	s_lshl_b32 s6, s10, 7
	s_and_b32 s8, s6, 0x780
	s_lshl_b32 s6, s10, 3
	s_and_b32 s6, s6, 0xf80
	s_addk_i32 s6, 0xf800
	v_readlane_b32 s36, v250, 60
	s_lshl_b64 s[12:13], s[6:7], 13
	v_readlane_b32 s44, v251, 4
	v_readlane_b32 s45, v251, 5
	s_add_u32 s9, s44, s12
	s_addc_u32 s11, s45, s13
	s_lshl_b32 s12, s8, 2
	s_add_u32 s12, s9, s12
	s_addc_u32 s13, s11, 0
	v_lshlrev_b32_e32 v8, 2, v6
	v_lshl_add_u64 v[2:3], s[12:13], 0, v[8:9]
	v_add_co_u32_e32 v50, vcc, s20, v2
	s_mov_b32 s9, 0x16000
	s_nop 0
	v_addc_co_u32_e32 v51, vcc, 0, v3, vcc
	v_add_co_u32_e32 v52, vcc, s21, v2
	global_load_dwordx2 v[4:5], v8, s[12:13] nt
	s_nop 0
	v_addc_co_u32_e32 v53, vcc, 0, v3, vcc
	v_add_co_u32_e32 v54, vcc, s22, v2
	global_load_dwordx2 v[50:51], v[50:51], off nt
	s_nop 0
	v_addc_co_u32_e32 v55, vcc, 0, v3, vcc
	v_add_co_u32_e32 v56, vcc, s23, v2
	global_load_dwordx2 v[52:53], v[52:53], off nt
	s_nop 0
	v_addc_co_u32_e32 v57, vcc, 0, v3, vcc
	v_add_co_u32_e32 v58, vcc, s24, v2
	global_load_dwordx2 v[56:57], v[56:57], off nt
	s_nop 0
	v_addc_co_u32_e32 v59, vcc, 0, v3, vcc
	v_add_co_u32_e32 v60, vcc, s25, v2
	global_load_dwordx2 v[58:59], v[58:59], off nt
	s_nop 0
	v_addc_co_u32_e32 v61, vcc, 0, v3, vcc
	v_add_co_u32_e32 v62, vcc, s26, v2
	global_load_dwordx2 v[54:55], v[54:55], off nt
	s_nop 0
	v_addc_co_u32_e32 v63, vcc, 0, v3, vcc
	v_add_co_u32_e32 v64, vcc, s27, v2
	global_load_dwordx2 v[60:61], v[60:61], off nt
	s_nop 0
	v_addc_co_u32_e32 v65, vcc, 0, v3, vcc
	v_add_co_u32_e32 v66, vcc, s33, v2
	global_load_dwordx2 v[64:65], v[64:65], off nt
	s_nop 0
	v_addc_co_u32_e32 v67, vcc, 0, v3, vcc
	v_add_co_u32_e32 v68, vcc, s34, v2
	global_load_dwordx2 v[66:67], v[66:67], off nt
	s_nop 0
	v_addc_co_u32_e32 v69, vcc, 0, v3, vcc
	v_add_co_u32_e32 v70, vcc, s9, v2
	s_mov_b32 s9, 0x1a000
	s_nop 0
	v_addc_co_u32_e32 v71, vcc, 0, v3, vcc
	v_add_co_u32_e32 v72, vcc, s58, v2
	global_load_dwordx2 v[62:63], v[62:63], off nt
	s_nop 0
	v_addc_co_u32_e32 v73, vcc, 0, v3, vcc
	v_add_co_u32_e32 v74, vcc, s9, v2
	global_load_dwordx2 v[72:73], v[72:73], off nt
	s_nop 0
	v_addc_co_u32_e32 v75, vcc, 0, v3, vcc
	global_load_dwordx2 v[74:75], v[74:75], off nt
	v_add_co_u32_e32 v76, vcc, s62, v2
	s_mov_b32 s9, 0x1e000
	s_nop 0
	v_addc_co_u32_e32 v77, vcc, 0, v3, vcc
	global_load_dwordx2 v[68:69], v[68:69], off nt
	v_add_co_u32_e32 v78, vcc, s9, v2
	global_load_dwordx2 v[70:71], v[70:71], off nt
	s_nop 0
	v_addc_co_u32_e32 v79, vcc, 0, v3, vcc
	global_load_dwordx2 v[76:77], v[76:77], off nt
	v_add_co_u32_e32 v80, vcc, s29, v2
	global_load_dwordx2 v[78:79], v[78:79], off nt
	s_nop 0
	v_addc_co_u32_e32 v81, vcc, 0, v3, vcc
	s_mov_b32 s9, 0x22000
	v_add_co_u32_e32 v82, vcc, s9, v2
	s_mov_b32 s9, 0x26000
	s_nop 0
	v_addc_co_u32_e32 v83, vcc, 0, v3, vcc
	v_add_co_u32_e32 v84, vcc, s31, v2
	global_load_dwordx2 v[80:81], v[80:81], off nt
	s_nop 0
	v_addc_co_u32_e32 v85, vcc, 0, v3, vcc
	v_add_co_u32_e32 v86, vcc, s9, v2
	s_mov_b32 s9, 0x2a000
	s_nop 0
	v_addc_co_u32_e32 v87, vcc, 0, v3, vcc
	v_add_co_u32_e32 v88, vcc, s35, v2
	global_load_dwordx2 v[82:83], v[82:83], off nt
	s_nop 0
	v_addc_co_u32_e32 v89, vcc, 0, v3, vcc
	v_add_co_u32_e32 v90, vcc, s9, v2
	s_mov_b32 s9, 0x2e000
	s_nop 0
	v_addc_co_u32_e32 v91, vcc, 0, v3, vcc
	v_add_co_u32_e32 v92, vcc, s66, v2
	global_load_dwordx2 v[86:87], v[86:87], off nt
	s_nop 0
	v_addc_co_u32_e32 v93, vcc, 0, v3, vcc
	v_add_co_u32_e32 v94, vcc, s9, v2
	s_mov_b32 s9, 0x32000
	s_nop 0
	v_addc_co_u32_e32 v95, vcc, 0, v3, vcc
	v_add_co_u32_e32 v96, vcc, s70, v2
	global_load_dwordx2 v[88:89], v[88:89], off nt
	s_nop 0
	v_addc_co_u32_e32 v97, vcc, 0, v3, vcc
	v_add_co_u32_e32 v98, vcc, s9, v2
	s_mov_b32 s9, 0x36000
	s_nop 0
	v_addc_co_u32_e32 v99, vcc, 0, v3, vcc
	v_add_co_u32_e32 v100, vcc, s74, v2
	global_load_dwordx2 v[90:91], v[90:91], off nt
	s_nop 0
	v_addc_co_u32_e32 v101, vcc, 0, v3, vcc
	v_add_co_u32_e32 v102, vcc, s9, v2
	s_mov_b32 s9, 0x3a000
	s_nop 0
	v_addc_co_u32_e32 v103, vcc, 0, v3, vcc
	v_add_co_u32_e32 v104, vcc, s78, v2
	global_load_dwordx2 v[84:85], v[84:85], off nt
	s_nop 0
	v_addc_co_u32_e32 v105, vcc, 0, v3, vcc
	v_add_co_u32_e32 v106, vcc, s9, v2
	s_mov_b32 s9, 0x3e000
	s_nop 0
	v_addc_co_u32_e32 v107, vcc, 0, v3, vcc
	v_add_co_u32_e32 v108, vcc, s83, v2
	global_load_dwordx2 v[94:95], v[94:95], off nt
	s_nop 0
	v_addc_co_u32_e32 v109, vcc, 0, v3, vcc
	v_add_co_u32_e32 v110, vcc, s9, v2
	s_mov_b32 s9, 0x42000
	s_nop 0
	v_addc_co_u32_e32 v111, vcc, 0, v3, vcc
	v_add_co_u32_e32 v112, vcc, s87, v2
	global_load_dwordx2 v[96:97], v[96:97], off nt
	s_nop 0
	v_addc_co_u32_e32 v113, vcc, 0, v3, vcc
	v_add_co_u32_e32 v114, vcc, s9, v2
	s_mov_b32 s9, 0x46000
	s_nop 0
	v_addc_co_u32_e32 v115, vcc, 0, v3, vcc
	v_add_co_u32_e32 v116, vcc, s91, v2
	global_load_dwordx2 v[98:99], v[98:99], off nt
	s_nop 0
	v_addc_co_u32_e32 v117, vcc, 0, v3, vcc
	v_add_co_u32_e32 v118, vcc, s9, v2
	s_mov_b32 s9, 0x4a000
	s_nop 0
	v_addc_co_u32_e32 v119, vcc, 0, v3, vcc
	v_add_co_u32_e32 v120, vcc, s95, v2
	global_load_dwordx2 v[92:93], v[92:93], off nt
	s_nop 0
	v_addc_co_u32_e32 v121, vcc, 0, v3, vcc
	v_add_co_u32_e32 v122, vcc, s9, v2
	s_mov_b32 s9, 0x4e000
	s_nop 0
	v_addc_co_u32_e32 v123, vcc, 0, v3, vcc
	v_add_co_u32_e32 v124, vcc, s53, v2
	global_load_dwordx2 v[102:103], v[102:103], off nt
	s_nop 0
	v_addc_co_u32_e32 v125, vcc, 0, v3, vcc
	v_add_co_u32_e32 v126, vcc, s9, v2
	s_mov_b32 s9, 0x52000
	s_nop 0
	v_addc_co_u32_e32 v127, vcc, 0, v3, vcc
	v_add_co_u32_e32 v128, vcc, s55, v2
	global_load_dwordx2 v[104:105], v[104:105], off nt
	s_nop 0
	v_addc_co_u32_e32 v129, vcc, 0, v3, vcc
	v_add_co_u32_e32 v130, vcc, s9, v2
	s_mov_b32 s9, 0x56000
	s_nop 0
	v_addc_co_u32_e32 v131, vcc, 0, v3, vcc
	v_add_co_u32_e32 v132, vcc, s57, v2
	global_load_dwordx2 v[106:107], v[106:107], off nt
	s_nop 0
	v_addc_co_u32_e32 v133, vcc, 0, v3, vcc
	v_add_co_u32_e32 v134, vcc, s9, v2
	global_load_dwordx2 v[100:101], v[100:101], off nt
	s_nop 0
	v_addc_co_u32_e32 v135, vcc, 0, v3, vcc
	v_add_co_u32_e32 v136, vcc, s59, v2
	s_waitcnt vmcnt(29)
; #define CV_LOAD(v, kb) do { _Pragma("unroll") for (int j = 0; j < 16; ++j) v[j] = __builtin_nontemporal_load((const f32x2*)(src + (size_t)((kb) * 16 + j) * ldw)); } while (0)
; __device__ __forceinline__ void tr128_f8(const float* W, int ldw, int srccol, unsigned char* WT, size_t dstrow0, int K, int k0, LAS unsigned char* tile, int lane) {
;     ...
;     CV_LOAD(va, 0); CV_LOAD(vb, 1); CV_LOAD(vc, 2);
;     CV_LOAD(vd, 3); CV_PUT(va, 0); CV_LOAD(va, 4); CV_PUT(vb, 1); CV_LOAD(vb, 5); CV_PUT(vc, 2); CV_LOAD(vc, 6); CV_PUT(vd, 3); CV_LOAD(vd, 7);
;     CV_PUT(va, 4); CV_PUT(vb, 5); CV_PUT(vc, 6); CV_PUT(vd, 7);
	v_mul_f32_e32 v4, 0x43800000, v4
	s_waitcnt vmcnt(28)
	v_mul_f32_e32 v8, 0x43800000, v50
	v_addc_co_u32_e32 v137, vcc, 0, v3, vcc
	s_mov_b32 s9, 0x5a000
	v_med3_f32 v4, v4, s79, v193
	v_med3_f32 v8, v8, s79, v193
	v_mov_b32_e32 v194, v9
	global_load_dwordx2 v[108:109], v[108:109], off nt
	v_add_co_u32_e32 v138, vcc, s9, v2
	global_load_dwordx2 v[110:111], v[110:111], off nt
	v_cvt_pk_fp8_f32 v194, v4, v8
	s_waitcnt vmcnt(28)
	v_mul_f32_e32 v4, 0x43800000, v56
	s_waitcnt vmcnt(27)
	v_mul_f32_e32 v8, 0x43800000, v58
	v_addc_co_u32_e32 v139, vcc, 0, v3, vcc
	v_med3_f32 v4, v4, s79, v193
	v_med3_f32 v8, v8, s79, v193
	v_mov_b32_e32 v195, v9
	v_add_co_u32_e32 v140, vcc, s61, v2
	v_mul_f32_e32 v50, 0x43800000, v52
	s_waitcnt vmcnt(26)
	v_mul_f32_e32 v52, 0x43800000, v54
	v_cvt_pk_fp8_f32 v195, v4, v8
	s_waitcnt vmcnt(24)
	v_mul_f32_e32 v4, 0x43800000, v64
	s_waitcnt vmcnt(23)
	v_mul_f32_e32 v8, 0x43800000, v66
	v_addc_co_u32_e32 v141, vcc, 0, v3, vcc
	s_mov_b32 s9, 0x5e000
	v_med3_f32 v50, v50, s79, v193
	v_med3_f32 v52, v52, s79, v193
	v_med3_f32 v4, v4, s79, v193
	v_med3_f32 v8, v8, s79, v193
	v_mov_b32_e32 v196, v9
	v_add_co_u32_e32 v142, vcc, s9, v2
	v_cvt_pk_fp8_f32 v194, v50, v52 op_sel:[0,0,1]
	v_mul_f32_e32 v50, 0x43800000, v60
	s_waitcnt vmcnt(22)
	v_mul_f32_e32 v52, 0x43800000, v62
	v_cvt_pk_fp8_f32 v196, v4, v8
	s_waitcnt vmcnt(21)
	v_mul_f32_e32 v4, 0x43800000, v72
	s_waitcnt vmcnt(20)
	v_mul_f32_e32 v8, 0x43800000, v74
	v_addc_co_u32_e32 v143, vcc, 0, v3, vcc
	v_med3_f32 v50, v50, s79, v193
	v_med3_f32 v52, v52, s79, v193
	v_med3_f32 v4, v4, s79, v193
	v_med3_f32 v8, v8, s79, v193
	v_mov_b32_e32 v197, v9
	v_add_co_u32_e32 v144, vcc, s63, v2
	v_cvt_pk_fp8_f32 v195, v50, v52 op_sel:[0,0,1]
	s_waitcnt vmcnt(19)
	v_mul_f32_e32 v50, 0x43800000, v68
	s_waitcnt vmcnt(18)
	v_mul_f32_e32 v52, 0x43800000, v70
	v_cvt_pk_fp8_f32 v197, v4, v8
	v_addc_co_u32_e32 v145, vcc, 0, v3, vcc
	s_mov_b32 s9, 0x62000
	v_med3_f32 v50, v50, s79, v193
	v_med3_f32 v52, v52, s79, v193
	v_add_co_u32_e32 v146, vcc, s9, v2
	v_cvt_pk_fp8_f32 v196, v50, v52 op_sel:[0,0,1]
	s_waitcnt vmcnt(17)
	v_mul_f32_e32 v50, 0x43800000, v76
	s_waitcnt vmcnt(16)
	v_mul_f32_e32 v52, 0x43800000, v78
	v_addc_co_u32_e32 v147, vcc, 0, v3, vcc
	v_med3_f32 v50, v50, s79, v193
	v_med3_f32 v52, v52, s79, v193
	v_add_co_u32_e32 v148, vcc, s65, v2
	v_cvt_pk_fp8_f32 v197, v50, v52 op_sel:[0,0,1]
	v_mul_f32_e32 v4, 0x43800000, v5
	v_mul_f32_e32 v5, 0x43800000, v51
	v_mul_f32_e32 v50, 0x43800000, v55
	v_addc_co_u32_e32 v149, vcc, 0, v3, vcc
	s_mov_b32 s9, 0x66000
	v_med3_f32 v4, v4, s79, v193
	v_med3_f32 v5, v5, s79, v193
	v_med3_f32 v51, v50, s79, v193
	v_mov_b32_e32 v50, v9
	v_add_co_u32_e32 v150, vcc, s9, v2
	v_cvt_pk_fp8_f32 v50, v4, v5
	s_nop 0
	v_addc_co_u32_e32 v151, vcc, 0, v3, vcc
	v_add_co_u32_e32 v152, vcc, s67, v2
	v_mul_f32_e32 v8, 0x43800000, v53
	s_nop 0
	v_addc_co_u32_e32 v153, vcc, 0, v3, vcc
	s_mov_b32 s9, 0x6a000
	v_med3_f32 v8, v8, s79, v193
	v_add_co_u32_e32 v154, vcc, s9, v2
	v_cvt_pk_fp8_f32 v50, v8, v51 op_sel:[0,0,1]
	v_mul_f32_e32 v4, 0x43800000, v57
	v_mul_f32_e32 v5, 0x43800000, v59
	v_mul_f32_e32 v51, 0x43800000, v63
	v_addc_co_u32_e32 v155, vcc, 0, v3, vcc
	v_med3_f32 v4, v4, s79, v193
	v_med3_f32 v5, v5, s79, v193
	v_med3_f32 v52, v51, s79, v193
	v_mov_b32_e32 v51, v9
	v_add_co_u32_e32 v156, vcc, s69, v2
	v_cvt_pk_fp8_f32 v51, v4, v5
	s_nop 0
	v_addc_co_u32_e32 v157, vcc, 0, v3, vcc
	s_mov_b32 s9, 0x6e000
	v_add_co_u32_e32 v158, vcc, s9, v2
	v_mul_f32_e32 v8, 0x43800000, v61
	s_nop 0
	v_addc_co_u32_e32 v159, vcc, 0, v3, vcc
	v_med3_f32 v8, v8, s79, v193
	v_add_co_u32_e32 v160, vcc, s71, v2
	v_cvt_pk_fp8_f32 v51, v8, v52 op_sel:[0,0,1]
	v_mul_f32_e32 v4, 0x43800000, v65
	v_mul_f32_e32 v5, 0x43800000, v67
	v_mul_f32_e32 v52, 0x43800000, v71
	v_addc_co_u32_e32 v161, vcc, 0, v3, vcc
	s_mov_b32 s9, 0x72000
	v_med3_f32 v4, v4, s79, v193
	v_med3_f32 v5, v5, s79, v193
	v_med3_f32 v53, v52, s79, v193
	v_mov_b32_e32 v52, v9
	v_add_co_u32_e32 v164, vcc, s9, v2
	v_cvt_pk_fp8_f32 v52, v4, v5
	s_nop 0
	v_addc_co_u32_e32 v165, vcc, 0, v3, vcc
	v_add_co_u32_e32 v166, vcc, s73, v2
	v_mul_f32_e32 v8, 0x43800000, v69
	s_nop 0
	v_addc_co_u32_e32 v167, vcc, 0, v3, vcc
	s_mov_b32 s9, 0x76000
	v_med3_f32 v8, v8, s79, v193
	v_add_co_u32_e32 v168, vcc, s9, v2
	v_cvt_pk_fp8_f32 v52, v8, v53 op_sel:[0,0,1]
	v_mul_f32_e32 v4, 0x43800000, v73
	v_mul_f32_e32 v5, 0x43800000, v75
	v_mul_f32_e32 v53, 0x43800000, v79
	v_addc_co_u32_e32 v169, vcc, 0, v3, vcc
	v_med3_f32 v4, v4, s79, v193
	v_med3_f32 v5, v5, s79, v193
	v_med3_f32 v54, v53, s79, v193
	v_mov_b32_e32 v53, v9
	v_add_co_u32_e32 v170, vcc, s75, v2
	v_cvt_pk_fp8_f32 v53, v4, v5
	s_nop 0
	v_addc_co_u32_e32 v171, vcc, 0, v3, vcc
	s_mov_b32 s9, 0x7a000
	v_add_co_u32_e32 v172, vcc, s9, v2
	v_mul_f32_e32 v8, 0x43800000, v77
	s_nop 0
	v_addc_co_u32_e32 v173, vcc, 0, v3, vcc
	v_med3_f32 v8, v8, s79, v193
	v_add_co_u32_e32 v174, vcc, s77, v2
	v_cvt_pk_fp8_f32 v53, v8, v54 op_sel:[0,0,1]
	s_nop 0
	v_addc_co_u32_e32 v175, vcc, 0, v3, vcc
	s_mov_b32 s9, 0x7e000
	v_add_co_u32_e32 v176, vcc, s9, v2
	v_add_u32_e32 v4, v13, v15
	s_nop 0
	v_addc_co_u32_e32 v177, vcc, 0, v3, vcc
	ds_write_b128 v4, v[50:53]
	v_add_co_u32_e32 v4, vcc, s80, v2
	s_mov_b32 s9, 0x82000
	s_nop 0
	v_addc_co_u32_e32 v5, vcc, 0, v3, vcc
	v_add_co_u32_e32 v50, vcc, s9, v2
	s_mov_b32 s9, 0x86000
	s_nop 0
	v_addc_co_u32_e32 v51, vcc, 0, v3, vcc
	v_add_co_u32_e32 v52, vcc, s82, v2
	global_load_dwordx2 v[112:113], v[112:113], off nt
	s_nop 0
	v_addc_co_u32_e32 v53, vcc, 0, v3, vcc
	v_add_co_u32_e32 v54, vcc, s9, v2
	s_mov_b32 s9, 0x8a000
	s_nop 0
	v_addc_co_u32_e32 v55, vcc, 0, v3, vcc
; #define CV_LOAD(v, kb) do { _Pragma("unroll") for (int j = 0; j < 16; ++j) v[j] = __builtin_nontemporal_load((const f32x2*)(src + (size_t)((kb) * 16 + j) * ldw)); } while (0)
; __device__ __forceinline__ void tr128_f8(const float* W, int ldw, int srccol, unsigned char* WT, size_t dstrow0, int K, int k0, LAS unsigned char* tile, int lane) {
;     ...
;     CV_LOAD(va, 0); CV_LOAD(vb, 1); CV_LOAD(vc, 2);
;     CV_LOAD(vd, 3); CV_PUT(va, 0); CV_LOAD(va, 4); CV_PUT(vb, 1); CV_LOAD(vb, 5); CV_PUT(vc, 2); CV_LOAD(vc, 6); CV_PUT(vd, 3); CV_LOAD(vd, 7);
;     CV_PUT(va, 4); CV_PUT(vb, 5); CV_PUT(vc, 6); CV_PUT(vd, 7);
	v_add_co_u32_e32 v56, vcc, s84, v2
	global_load_dwordx2 v[114:115], v[114:115], off nt
	s_nop 0
	v_addc_co_u32_e32 v57, vcc, 0, v3, vcc
	v_add_co_u32_e32 v58, vcc, s9, v2
	global_load_dwordx2 v[120:121], v[120:121], off nt
	s_nop 0
	v_addc_co_u32_e32 v59, vcc, 0, v3, vcc
	v_add_co_u32_e32 v60, vcc, s86, v2
	global_load_dwordx2 v[122:123], v[122:123], off nt
	s_nop 0
	v_addc_co_u32_e32 v61, vcc, 0, v3, vcc
	s_mov_b32 s9, 0x8e000
	v_add_co_u32_e32 v62, vcc, s9, v2
	global_load_dwordx2 v[116:117], v[116:117], off nt
	s_nop 0
	v_addc_co_u32_e32 v63, vcc, 0, v3, vcc
	global_load_dwordx2 v[118:119], v[118:119], off nt
	v_add_co_u32_e32 v64, vcc, s88, v2
	global_load_dwordx2 v[124:125], v[124:125], off nt
	s_nop 0
	v_addc_co_u32_e32 v65, vcc, 0, v3, vcc
	global_load_dwordx2 v[128:129], v[128:129], off nt
	s_mov_b32 s9, 0x92000
	global_load_dwordx2 v[130:131], v[130:131], off nt
	v_add_co_u32_e32 v66, vcc, s9, v2
	global_load_dwordx2 v[126:127], v[126:127], off nt
	s_nop 0
	v_addc_co_u32_e32 v67, vcc, 0, v3, vcc
	global_load_dwordx2 v[134:135], v[134:135], off nt
	v_add_co_u32_e32 v68, vcc, s90, v2
	global_load_dwordx2 v[136:137], v[136:137], off nt
	s_nop 0
	v_addc_co_u32_e32 v69, vcc, 0, v3, vcc
	global_load_dwordx2 v[138:139], v[138:139], off nt
	s_mov_b32 s9, 0x96000
	global_load_dwordx2 v[132:133], v[132:133], off nt
	v_add_co_u32_e32 v70, vcc, s9, v2
	global_load_dwordx2 v[140:141], v[140:141], off nt
	s_nop 0
	v_addc_co_u32_e32 v71, vcc, 0, v3, vcc
	global_load_dwordx2 v[142:143], v[142:143], off nt
	v_add_co_u32_e32 v72, vcc, s92, v2
	s_mov_b32 s9, 0x9a000
	s_nop 0
	v_addc_co_u32_e32 v73, vcc, 0, v3, vcc
	v_add_co_u32_e32 v74, vcc, s9, v2
	s_mov_b32 s9, 0x9e000
	s_nop 0
	v_addc_co_u32_e32 v75, vcc, 0, v3, vcc
	v_add_co_u32_e32 v76, vcc, s94, v2
	v_add_u32_e32 v8, v7, v11
	s_nop 0
	v_addc_co_u32_e32 v77, vcc, 0, v3, vcc
	v_add_co_u32_e32 v78, vcc, s9, v2
	s_waitcnt vmcnt(30)
	v_mul_f32_e32 v82, 0x43800000, v82
	v_addc_co_u32_e32 v79, vcc, 0, v3, vcc
	global_load_dwordx2 v[78:79], v[78:79], off nt
	v_mul_f32_e32 v80, 0x43800000, v80
	ds_write_b128 v8, v[194:197]
	v_med3_f32 v80, v80, s79, v193
	v_med3_f32 v82, v82, s79, v193
	v_mov_b32_e32 v194, v9
	v_cvt_pk_fp8_f32 v194, v80, v82
	s_waitcnt vmcnt(29)
	v_mul_f32_e32 v80, 0x43800000, v88
	s_waitcnt vmcnt(28)
	v_mul_f32_e32 v82, 0x43800000, v90
	v_med3_f32 v80, v80, s79, v193
	v_med3_f32 v82, v82, s79, v193
	v_mov_b32_e32 v195, v9
	s_waitcnt vmcnt(27)
	v_mul_f32_e32 v84, 0x43800000, v84
	v_mul_f32_e32 v86, 0x43800000, v86
	v_cvt_pk_fp8_f32 v195, v80, v82
	s_waitcnt vmcnt(25)
	v_mul_f32_e32 v80, 0x43800000, v96
	s_waitcnt vmcnt(24)
	v_mul_f32_e32 v82, 0x43800000, v98
	v_med3_f32 v84, v84, s79, v193
	v_med3_f32 v86, v86, s79, v193
	v_med3_f32 v80, v80, s79, v193
	v_med3_f32 v82, v82, s79, v193
	v_mov_b32_e32 v196, v9
	v_cvt_pk_fp8_f32 v194, v84, v86 op_sel:[0,0,1]
	s_waitcnt vmcnt(23)
	v_mul_f32_e32 v84, 0x43800000, v92
	v_mul_f32_e32 v86, 0x43800000, v94
	v_cvt_pk_fp8_f32 v196, v80, v82
	s_waitcnt vmcnt(21)
	v_mul_f32_e32 v80, 0x43800000, v104
	s_waitcnt vmcnt(20)
	v_mul_f32_e32 v82, 0x43800000, v106
	v_med3_f32 v84, v84, s79, v193
	v_med3_f32 v86, v86, s79, v193
	v_med3_f32 v80, v80, s79, v193
	v_med3_f32 v82, v82, s79, v193
	v_mov_b32_e32 v197, v9
	v_cvt_pk_fp8_f32 v195, v84, v86 op_sel:[0,0,1]
	s_waitcnt vmcnt(19)
	v_mul_f32_e32 v84, 0x43800000, v100
	v_mul_f32_e32 v86, 0x43800000, v102
	v_cvt_pk_fp8_f32 v197, v80, v82
	v_med3_f32 v84, v84, s79, v193
	v_med3_f32 v86, v86, s79, v193
	v_cvt_pk_fp8_f32 v196, v84, v86 op_sel:[0,0,1]
	s_waitcnt vmcnt(18)
	v_mul_f32_e32 v84, 0x43800000, v108
	s_waitcnt vmcnt(17)
	v_mul_f32_e32 v86, 0x43800000, v110
	v_med3_f32 v84, v84, s79, v193
	v_med3_f32 v86, v86, s79, v193
	v_mul_f32_e32 v80, 0x43800000, v81
	v_mul_f32_e32 v81, 0x43800000, v83
	v_cvt_pk_fp8_f32 v197, v84, v86 op_sel:[0,0,1]
	v_med3_f32 v84, v80, s79, v193
	v_med3_f32 v81, v81, s79, v193
	v_mov_b32_e32 v80, v9
	v_cvt_pk_fp8_f32 v80, v84, v81
	v_mul_f32_e32 v82, 0x43800000, v85
	v_mul_f32_e32 v83, 0x43800000, v87
	v_med3_f32 v82, v82, s79, v193
	v_med3_f32 v83, v83, s79, v193
	v_cvt_pk_fp8_f32 v80, v82, v83 op_sel:[0,0,1]
	v_mul_f32_e32 v81, 0x43800000, v89
	v_mul_f32_e32 v82, 0x43800000, v91
	v_med3_f32 v85, v81, s79, v193
	v_med3_f32 v82, v82, s79, v193
	v_mov_b32_e32 v81, v9
	v_cvt_pk_fp8_f32 v81, v85, v82
	v_mul_f32_e32 v83, 0x43800000, v93
	v_mul_f32_e32 v84, 0x43800000, v95
	v_med3_f32 v83, v83, s79, v193
	v_med3_f32 v84, v84, s79, v193
	v_cvt_pk_fp8_f32 v81, v83, v84 op_sel:[0,0,1]
	v_mul_f32_e32 v82, 0x43800000, v97
	v_mul_f32_e32 v83, 0x43800000, v99
	v_med3_f32 v86, v82, s79, v193
	v_med3_f32 v83, v83, s79, v193
	v_mov_b32_e32 v82, v9
	v_cvt_pk_fp8_f32 v82, v86, v83
	v_mul_f32_e32 v84, 0x43800000, v101
	v_mul_f32_e32 v85, 0x43800000, v103
	v_med3_f32 v84, v84, s79, v193
	v_med3_f32 v85, v85, s79, v193
	v_cvt_pk_fp8_f32 v82, v84, v85 op_sel:[0,0,1]
	v_mul_f32_e32 v83, 0x43800000, v105
	v_mul_f32_e32 v84, 0x43800000, v107
	v_med3_f32 v87, v83, s79, v193
	v_med3_f32 v84, v84, s79, v193
	v_mov_b32_e32 v83, v9
	v_cvt_pk_fp8_f32 v83, v87, v84
	v_mul_f32_e32 v85, 0x43800000, v109
	v_mul_f32_e32 v86, 0x43800000, v111
	v_med3_f32 v85, v85, s79, v193
	v_med3_f32 v86, v86, s79, v193
	v_cvt_pk_fp8_f32 v83, v85, v86 op_sel:[0,0,1]
	global_load_dwordx2 v[144:145], v[144:145], off nt
	ds_write_b128 v8, v[194:197] offset:16
	global_load_dwordx2 v[146:147], v[146:147], off nt
	v_add_u32_e32 v8, v13, v11
	global_load_dwordx2 v[152:153], v[152:153], off nt
	ds_write_b128 v8, v[80:83]
	global_load_dwordx2 v[154:155], v[154:155], off nt
	v_add_co_u32_e32 v80, vcc, s96, v2
	s_mov_b32 s9, 0xa2000
; #define CV_LOAD(v, kb) do { _Pragma("unroll") for (int j = 0; j < 16; ++j) v[j] = __builtin_nontemporal_load((const f32x2*)(src + (size_t)((kb) * 16 + j) * ldw)); } while (0)
; __device__ __forceinline__ void tr128_f8(const float* W, int ldw, int srccol, unsigned char* WT, size_t dstrow0, int K, int k0, LAS unsigned char* tile, int lane) {
;     ...
;     CV_LOAD(va, 0); CV_LOAD(vb, 1); CV_LOAD(vc, 2);
;     CV_LOAD(vd, 3); CV_PUT(va, 0); CV_LOAD(va, 4); CV_PUT(vb, 1); CV_LOAD(vb, 5); CV_PUT(vc, 2); CV_LOAD(vc, 6); CV_PUT(vd, 3); CV_LOAD(vd, 7);
;     CV_PUT(va, 4); CV_PUT(vb, 5); CV_PUT(vc, 6); CV_PUT(vd, 7);
	s_nop 0
	v_addc_co_u32_e32 v81, vcc, 0, v3, vcc
	global_load_dwordx2 v[148:149], v[148:149], off nt
	v_add_co_u32_e32 v82, vcc, s9, v2
	global_load_dwordx2 v[150:151], v[150:151], off nt
	s_nop 0
	v_addc_co_u32_e32 v83, vcc, 0, v3, vcc
	global_load_dwordx2 v[160:161], v[160:161], off nt
	v_add_co_u32_e32 v84, vcc, s4, v2
	global_load_dwordx2 v[164:165], v[164:165], off nt
	s_nop 0
	v_addc_co_u32_e32 v85, vcc, 0, v3, vcc
	global_load_dwordx2 v[156:157], v[156:157], off nt
	s_mov_b32 s9, 0xa6000
	global_load_dwordx2 v[158:159], v[158:159], off nt
	v_add_co_u32_e32 v86, vcc, s9, v2
	global_load_dwordx2 v[170:171], v[170:171], off nt
	s_nop 0
	v_addc_co_u32_e32 v87, vcc, 0, v3, vcc
	global_load_dwordx2 v[172:173], v[172:173], off nt
	v_add_co_u32_e32 v88, vcc, s14, v2
	global_load_dwordx2 v[166:167], v[166:167], off nt
	s_nop 0
	v_addc_co_u32_e32 v89, vcc, 0, v3, vcc
	global_load_dwordx2 v[168:169], v[168:169], off nt
	s_mov_b32 s9, 0xaa000
	global_load_dwordx2 v[174:175], v[174:175], off nt
	v_add_co_u32_e32 v90, vcc, s9, v2
	global_load_dwordx2 v[176:177], v[176:177], off nt
	s_nop 0
	v_addc_co_u32_e32 v91, vcc, 0, v3, vcc
	v_add_co_u32_e32 v92, vcc, s18, v2
	s_mov_b32 s9, 0xae000
	s_nop 0
	v_addc_co_u32_e32 v93, vcc, 0, v3, vcc
	global_load_dwordx2 v[88:89], v[88:89], off nt
	v_mov_b32_e32 v194, v9
	global_load_dwordx2 v[90:91], v[90:91], off nt
	v_mov_b32_e32 v195, v9
	global_load_dwordx2 v[94:95], v[92:93], off nt
	v_add_co_u32_e32 v92, vcc, s9, v2
	s_mov_b32 s9, 0xb2000
	s_nop 0
	v_addc_co_u32_e32 v93, vcc, 0, v3, vcc
	global_load_dwordx2 v[100:101], v[92:93], off nt
	v_add_co_u32_e32 v92, vcc, s5, v2
	s_waitcnt vmcnt(36)
	v_mul_f32_e32 v8, 0x43800000, v112
	v_addc_co_u32_e32 v93, vcc, 0, v3, vcc
	v_add_co_u32_e32 v96, vcc, s9, v2
	s_waitcnt vmcnt(35)
	v_mul_f32_e32 v112, 0x43800000, v114
	v_addc_co_u32_e32 v97, vcc, 0, v3, vcc
	v_add_co_u32_e32 v98, vcc, s54, v2
	s_mov_b32 s9, 0xb6000
	s_nop 0
	v_addc_co_u32_e32 v99, vcc, 0, v3, vcc
	v_med3_f32 v8, v8, s79, v193
	v_med3_f32 v112, v112, s79, v193
	global_load_dwordx2 v[92:93], v[92:93], off nt
	v_cvt_pk_fp8_f32 v194, v8, v112
	global_load_dwordx2 v[96:97], v[96:97], off nt
	s_waitcnt vmcnt(36)
	v_mul_f32_e32 v8, 0x43800000, v120
	global_load_dwordx2 v[102:103], v[98:99], off nt
	v_add_co_u32_e32 v98, vcc, s9, v2
	s_waitcnt vmcnt(36)
	v_mul_f32_e32 v112, 0x43800000, v122
	v_addc_co_u32_e32 v99, vcc, 0, v3, vcc
	v_med3_f32 v8, v8, s79, v193
	v_med3_f32 v112, v112, s79, v193
	global_load_dwordx2 v[106:107], v[98:99], off nt
	s_waitcnt vmcnt(36)
	v_mul_f32_e32 v114, 0x43800000, v116
	s_waitcnt vmcnt(35)
	v_mul_f32_e32 v116, 0x43800000, v118
	v_cvt_pk_fp8_f32 v195, v8, v112
	s_waitcnt vmcnt(33)
	v_mul_f32_e32 v8, 0x43800000, v128
	s_waitcnt vmcnt(32)
	v_mul_f32_e32 v112, 0x43800000, v130
	v_med3_f32 v114, v114, s79, v193
	v_med3_f32 v116, v116, s79, v193
	v_med3_f32 v8, v8, s79, v193
	v_med3_f32 v112, v112, s79, v193
	v_mov_b32_e32 v196, v9
	v_cvt_pk_fp8_f32 v194, v114, v116 op_sel:[0,0,1]
	v_mul_f32_e32 v114, 0x43800000, v124
	s_waitcnt vmcnt(31)
	v_mul_f32_e32 v116, 0x43800000, v126
	v_cvt_pk_fp8_f32 v196, v8, v112
	s_waitcnt vmcnt(29)
	v_mul_f32_e32 v8, 0x43800000, v136
	s_waitcnt vmcnt(28)
	v_mul_f32_e32 v112, 0x43800000, v138
	v_med3_f32 v114, v114, s79, v193
	v_med3_f32 v116, v116, s79, v193
	v_med3_f32 v8, v8, s79, v193
	v_med3_f32 v112, v112, s79, v193
	v_mov_b32_e32 v197, v9
	v_cvt_pk_fp8_f32 v195, v114, v116 op_sel:[0,0,1]
	s_waitcnt vmcnt(27)
	v_mul_f32_e32 v114, 0x43800000, v132
	v_mul_f32_e32 v116, 0x43800000, v134
	v_cvt_pk_fp8_f32 v197, v8, v112
	v_mul_f32_e32 v8, 0x43800000, v113
	v_mul_f32_e32 v112, 0x43800000, v115
	v_med3_f32 v114, v114, s79, v193
	v_med3_f32 v116, v116, s79, v193
	v_med3_f32 v8, v8, s79, v193
	v_med3_f32 v115, v112, s79, v193
	v_mov_b32_e32 v112, v9
	v_cvt_pk_fp8_f32 v196, v114, v116 op_sel:[0,0,1]
	s_waitcnt vmcnt(26)
	v_mul_f32_e32 v114, 0x43800000, v140
	s_waitcnt vmcnt(25)
	v_mul_f32_e32 v116, 0x43800000, v142
	v_cvt_pk_fp8_f32 v112, v8, v115
	v_med3_f32 v114, v114, s79, v193
	v_med3_f32 v116, v116, s79, v193
	v_cvt_pk_fp8_f32 v197, v114, v116 op_sel:[0,0,1]
	v_mul_f32_e32 v113, 0x43800000, v117
	v_mul_f32_e32 v114, 0x43800000, v119
	v_med3_f32 v113, v113, s79, v193
	v_med3_f32 v114, v114, s79, v193
	v_cvt_pk_fp8_f32 v112, v113, v114 op_sel:[0,0,1]
	v_mul_f32_e32 v8, 0x43800000, v121
	v_mul_f32_e32 v113, 0x43800000, v123
	v_med3_f32 v8, v8, s79, v193
	v_med3_f32 v116, v113, s79, v193
	v_mov_b32_e32 v113, v9
	v_cvt_pk_fp8_f32 v113, v8, v116
	v_mul_f32_e32 v114, 0x43800000, v125
	v_mul_f32_e32 v115, 0x43800000, v127
	v_med3_f32 v114, v114, s79, v193
	v_med3_f32 v115, v115, s79, v193
	v_cvt_pk_fp8_f32 v113, v114, v115 op_sel:[0,0,1]
	v_mul_f32_e32 v8, 0x43800000, v129
	v_mul_f32_e32 v114, 0x43800000, v131
	v_med3_f32 v8, v8, s79, v193
	v_med3_f32 v117, v114, s79, v193
	v_mov_b32_e32 v114, v9
	v_cvt_pk_fp8_f32 v114, v8, v117
	v_mul_f32_e32 v115, 0x43800000, v133
	v_mul_f32_e32 v116, 0x43800000, v135
	v_med3_f32 v115, v115, s79, v193
	v_med3_f32 v116, v116, s79, v193
	v_cvt_pk_fp8_f32 v114, v115, v116 op_sel:[0,0,1]
	v_mul_f32_e32 v8, 0x43800000, v137
	v_mul_f32_e32 v115, 0x43800000, v139
	v_med3_f32 v8, v8, s79, v193
	v_med3_f32 v118, v115, s79, v193
	v_mov_b32_e32 v115, v9
	v_add_co_u32_e32 v98, vcc, s30, v2
	v_cvt_pk_fp8_f32 v115, v8, v118
	s_nop 0
	v_addc_co_u32_e32 v99, vcc, 0, v3, vcc
	s_mov_b32 s9, 0xba000
	v_add_co_u32_e32 v104, vcc, s9, v2
	v_mul_f32_e32 v116, 0x43800000, v141
	v_mul_f32_e32 v117, 0x43800000, v143
	v_addc_co_u32_e32 v105, vcc, 0, v3, vcc
	v_med3_f32 v116, v116, s79, v193
	v_med3_f32 v117, v117, s79, v193
	v_add_co_u32_e32 v108, vcc, s15, v2
	v_cvt_pk_fp8_f32 v115, v116, v117 op_sel:[0,0,1]
	s_nop 0
	v_addc_co_u32_e32 v109, vcc, 0, v3, vcc
	s_mov_b32 s9, 0xbe000
	v_add_co_u32_e32 v110, vcc, s9, v2
	v_add_u32_e32 v116, v13, v19
	s_nop 0
	v_addc_co_u32_e32 v111, vcc, 0, v3, vcc
	ds_write_b128 v116, v[112:115]
	v_add_co_u32_e32 v112, vcc, s17, v2
	s_mov_b32 s9, 0xc2000
	s_nop 0
	v_addc_co_u32_e32 v113, vcc, 0, v3, vcc
	v_add_co_u32_e32 v114, vcc, s9, v2
	s_mov_b32 s9, 0xc6000
	s_nop 0
	v_addc_co_u32_e32 v115, vcc, 0, v3, vcc
	v_add_co_u32_e32 v116, vcc, s19, v2
	global_load_dwordx2 v[112:113], v[112:113], off nt
	s_nop 0
	v_addc_co_u32_e32 v117, vcc, 0, v3, vcc
	global_load_dwordx2 v[114:115], v[114:115], off nt
	v_add_u32_e32 v8, v7, v17
	global_load_dwordx2 v[118:119], v[116:117], off nt
	v_add_co_u32_e32 v116, vcc, s9, v2
	s_mov_b32 s9, 0xca000
	s_nop 0
	v_addc_co_u32_e32 v117, vcc, 0, v3, vcc
	global_load_dwordx2 v[124:125], v[116:117], off nt
	v_add_co_u32_e32 v116, vcc, s28, v2
	global_load_dwordx2 v[4:5], v[4:5], off nt
	s_nop 0
	v_addc_co_u32_e32 v117, vcc, 0, v3, vcc
	v_add_co_u32_e32 v120, vcc, s9, v2
	global_load_dwordx2 v[50:51], v[50:51], off nt
	s_nop 0
	v_addc_co_u32_e32 v121, vcc, 0, v3, vcc
	v_add_co_u32_e32 v122, vcc, s52, v2
	s_mov_b32 s9, 0xce000
	s_nop 0
	v_addc_co_u32_e32 v123, vcc, 0, v3, vcc
	global_load_dwordx2 v[116:117], v[116:117], off nt
	s_waitcnt vmcnt(30)
; #define CV_LOAD(v, kb) do { _Pragma("unroll") for (int j = 0; j < 16; ++j) v[j] = __builtin_nontemporal_load((const f32x2*)(src + (size_t)((kb) * 16 + j) * ldw)); } while (0)
; __device__ __forceinline__ void tr128_f8(const float* W, int ldw, int srccol, unsigned char* WT, size_t dstrow0, int K, int k0, LAS unsigned char* tile, int lane) {
;     ...
;     CV_LOAD(va, 0); CV_LOAD(vb, 1); CV_LOAD(vc, 2);
;     CV_LOAD(vd, 3); CV_PUT(va, 0); CV_LOAD(va, 4); CV_PUT(vb, 1); CV_LOAD(vb, 5); CV_PUT(vc, 2); CV_LOAD(vc, 6); CV_PUT(vd, 3); CV_LOAD(vd, 7);
;     CV_PUT(va, 4); CV_PUT(vb, 5); CV_PUT(vc, 6); CV_PUT(vd, 7);
	v_mul_f32_e32 v144, 0x43800000, v144
	global_load_dwordx2 v[120:121], v[120:121], off nt
	s_waitcnt vmcnt(30)
	v_mul_f32_e32 v146, 0x43800000, v146
	global_load_dwordx2 v[126:127], v[122:123], off nt
	v_add_co_u32_e32 v122, vcc, s9, v2
	global_load_dwordx2 v[54:55], v[54:55], off nt
	s_nop 0
	v_addc_co_u32_e32 v123, vcc, 0, v3, vcc
	global_load_dwordx2 v[56:57], v[56:57], off nt
	s_mov_b32 s9, 0xd2000
	global_load_dwordx2 v[58:59], v[58:59], off nt
	ds_write_b128 v8, v[194:197]
	global_load_dwordx2 v[132:133], v[122:123], off nt
	v_add_co_u32_e32 v122, vcc, s56, v2
	global_load_dwordx2 v[52:53], v[52:53], off nt
	s_nop 0
	v_addc_co_u32_e32 v123, vcc, 0, v3, vcc
	global_load_dwordx2 v[62:63], v[62:63], off nt
	v_add_co_u32_e32 v128, vcc, s9, v2
	global_load_dwordx2 v[64:65], v[64:65], off nt
	s_nop 0
	v_addc_co_u32_e32 v129, vcc, 0, v3, vcc
	global_load_dwordx2 v[66:67], v[66:67], off nt
	v_add_co_u32_e32 v130, vcc, s60, v2
	global_load_dwordx2 v[60:61], v[60:61], off nt
	s_nop 0
	v_addc_co_u32_e32 v131, vcc, 0, v3, vcc
	global_load_dwordx2 v[70:71], v[70:71], off nt
	s_mov_b32 s9, 0xd6000
	global_load_dwordx2 v[72:73], v[72:73], off nt
	v_med3_f32 v144, v144, s79, v193
	global_load_dwordx2 v[74:75], v[74:75], off nt
	v_med3_f32 v146, v146, s79, v193
	global_load_dwordx2 v[68:69], v[68:69], off nt
	v_mov_b32_e32 v194, v9
	global_load_dwordx2 v[122:123], v[122:123], off nt
	v_cvt_pk_fp8_f32 v194, v144, v146
	global_load_dwordx2 v[128:129], v[128:129], off nt
	v_mov_b32_e32 v195, v9
	global_load_dwordx2 v[134:135], v[130:131], off nt
	v_add_co_u32_e32 v130, vcc, s9, v2
	global_load_dwordx2 v[76:77], v[76:77], off nt
	s_nop 0
	v_addc_co_u32_e32 v131, vcc, 0, v3, vcc
	global_load_dwordx2 v[138:139], v[130:131], off nt
	s_waitcnt vmcnt(48)
	v_mul_f32_e32 v144, 0x43800000, v152
	s_waitcnt vmcnt(47)
	v_mul_f32_e32 v146, 0x43800000, v154
	v_med3_f32 v144, v144, s79, v193
	v_med3_f32 v146, v146, s79, v193
	s_waitcnt vmcnt(46)
	v_mul_f32_e32 v148, 0x43800000, v148
	s_waitcnt vmcnt(45)
	v_mul_f32_e32 v150, 0x43800000, v150
	v_cvt_pk_fp8_f32 v195, v144, v146
	s_waitcnt vmcnt(44)
	v_mul_f32_e32 v144, 0x43800000, v160
	s_waitcnt vmcnt(43)
	v_mul_f32_e32 v146, 0x43800000, v164
	v_med3_f32 v148, v148, s79, v193
	v_med3_f32 v150, v150, s79, v193
	v_med3_f32 v144, v144, s79, v193
	v_med3_f32 v146, v146, s79, v193
	v_mov_b32_e32 v196, v9
	v_cvt_pk_fp8_f32 v194, v148, v150 op_sel:[0,0,1]
	s_waitcnt vmcnt(42)
	v_mul_f32_e32 v148, 0x43800000, v156
	s_waitcnt vmcnt(41)
	v_mul_f32_e32 v150, 0x43800000, v158
	v_cvt_pk_fp8_f32 v196, v144, v146
	s_waitcnt vmcnt(40)
	v_mul_f32_e32 v144, 0x43800000, v170
	s_waitcnt vmcnt(39)
	v_mul_f32_e32 v146, 0x43800000, v172
	v_med3_f32 v148, v148, s79, v193
	v_med3_f32 v150, v150, s79, v193
	v_med3_f32 v144, v144, s79, v193
	v_med3_f32 v146, v146, s79, v193
	v_mov_b32_e32 v197, v9
	v_cvt_pk_fp8_f32 v195, v148, v150 op_sel:[0,0,1]
	s_waitcnt vmcnt(38)
	v_mul_f32_e32 v148, 0x43800000, v166
	s_waitcnt vmcnt(37)
	v_mul_f32_e32 v150, 0x43800000, v168
	v_cvt_pk_fp8_f32 v197, v144, v146
	v_med3_f32 v148, v148, s79, v193
	v_med3_f32 v150, v150, s79, v193
	v_cvt_pk_fp8_f32 v196, v148, v150 op_sel:[0,0,1]
	s_waitcnt vmcnt(36)
	v_mul_f32_e32 v148, 0x43800000, v174
	s_waitcnt vmcnt(35)
	v_mul_f32_e32 v150, 0x43800000, v176
	v_med3_f32 v148, v148, s79, v193
	v_med3_f32 v150, v150, s79, v193
	v_mul_f32_e32 v144, 0x43800000, v145
	v_mul_f32_e32 v145, 0x43800000, v147
	v_cvt_pk_fp8_f32 v197, v148, v150 op_sel:[0,0,1]
	v_med3_f32 v148, v144, s79, v193
	v_med3_f32 v145, v145, s79, v193
	v_mov_b32_e32 v144, v9
	v_cvt_pk_fp8_f32 v144, v148, v145
	v_mul_f32_e32 v146, 0x43800000, v149
	v_mul_f32_e32 v147, 0x43800000, v151
	v_med3_f32 v146, v146, s79, v193
	v_med3_f32 v147, v147, s79, v193
	v_cvt_pk_fp8_f32 v144, v146, v147 op_sel:[0,0,1]
	v_mul_f32_e32 v145, 0x43800000, v153
	v_mul_f32_e32 v146, 0x43800000, v155
	v_med3_f32 v149, v145, s79, v193
	v_med3_f32 v146, v146, s79, v193
	v_mov_b32_e32 v145, v9
	v_cvt_pk_fp8_f32 v145, v149, v146
	v_mul_f32_e32 v147, 0x43800000, v157
	v_mul_f32_e32 v148, 0x43800000, v159
	v_med3_f32 v147, v147, s79, v193
	v_med3_f32 v148, v148, s79, v193
	v_cvt_pk_fp8_f32 v145, v147, v148 op_sel:[0,0,1]
	v_mul_f32_e32 v146, 0x43800000, v161
	v_mul_f32_e32 v147, 0x43800000, v165
	v_med3_f32 v150, v146, s79, v193
	v_med3_f32 v147, v147, s79, v193
	v_mov_b32_e32 v146, v9
	v_cvt_pk_fp8_f32 v146, v150, v147
	v_mul_f32_e32 v148, 0x43800000, v167
	v_mul_f32_e32 v149, 0x43800000, v169
	v_med3_f32 v148, v148, s79, v193
	v_med3_f32 v149, v149, s79, v193
	v_cvt_pk_fp8_f32 v146, v148, v149 op_sel:[0,0,1]
	v_mul_f32_e32 v147, 0x43800000, v171
	v_mul_f32_e32 v148, 0x43800000, v173
	v_med3_f32 v151, v147, s79, v193
	v_med3_f32 v148, v148, s79, v193
	v_mov_b32_e32 v147, v9
	global_load_dwordx2 v[80:81], v[80:81], off nt
	v_add_co_u32_e32 v130, vcc, s64, v2
	global_load_dwordx2 v[82:83], v[82:83], off nt
	v_cvt_pk_fp8_f32 v147, v151, v148
	global_load_dwordx2 v[84:85], v[84:85], off nt
	v_addc_co_u32_e32 v131, vcc, 0, v3, vcc
	s_mov_b32 s9, 0xda000
	v_add_co_u32_e32 v136, vcc, s9, v2
	v_mul_f32_e32 v149, 0x43800000, v175
	v_mul_f32_e32 v150, 0x43800000, v177
	v_addc_co_u32_e32 v137, vcc, 0, v3, vcc
	v_med3_f32 v149, v149, s79, v193
	v_med3_f32 v150, v150, s79, v193
	global_load_dwordx2 v[86:87], v[86:87], off nt
	v_add_co_u32_e32 v140, vcc, s68, v2
	v_cvt_pk_fp8_f32 v147, v149, v150 op_sel:[0,0,1]
	s_nop 0
	v_addc_co_u32_e32 v141, vcc, 0, v3, vcc
	s_mov_b32 s9, 0xde000
	v_add_co_u32_e32 v142, vcc, s9, v2
	ds_write_b128 v8, v[194:197] offset:16
	s_nop 0
	v_addc_co_u32_e32 v143, vcc, 0, v3, vcc
	v_add_u32_e32 v8, v13, v21
	ds_write_b128 v8, v[144:147]
	v_add_co_u32_e32 v144, vcc, s72, v2
	s_mov_b32 s9, 0xe2000
	s_nop 0
	v_addc_co_u32_e32 v145, vcc, 0, v3, vcc
	v_add_co_u32_e32 v146, vcc, s9, v2
	s_mov_b32 s9, 0xe6000
	s_nop 0
	v_addc_co_u32_e32 v147, vcc, 0, v3, vcc
	v_add_co_u32_e32 v148, vcc, s76, v2
	global_load_dwordx2 v[144:145], v[144:145], off nt
	s_nop 0
	v_addc_co_u32_e32 v149, vcc, 0, v3, vcc
	global_load_dwordx2 v[146:147], v[146:147], off nt
	s_waitcnt vmcnt(27)
; #define CV_LOAD(v, kb) do { _Pragma("unroll") for (int j = 0; j < 16; ++j) v[j] = __builtin_nontemporal_load((const f32x2*)(src + (size_t)((kb) * 16 + j) * ldw)); } while (0)
; __device__ __forceinline__ void tr128_f8(const float* W, int ldw, int srccol, unsigned char* WT, size_t dstrow0, int K, int k0, LAS unsigned char* tile, int lane) {
;     ...
;     CV_LOAD(va, 0); CV_LOAD(vb, 1); CV_LOAD(vc, 2);
;     CV_LOAD(vd, 3); CV_PUT(va, 0); CV_LOAD(va, 4); CV_PUT(vb, 1); CV_LOAD(vb, 5); CV_PUT(vc, 2); CV_LOAD(vc, 6); CV_PUT(vd, 3); CV_LOAD(vd, 7);
;     CV_PUT(va, 4); CV_PUT(vb, 5); CV_PUT(vc, 6); CV_PUT(vd, 7);
	v_mul_f32_e32 v8, 0x43800000, v50
	global_load_dwordx2 v[150:151], v[148:149], off nt
	v_add_co_u32_e32 v148, vcc, s9, v2
	s_mov_b32 s9, 0xea000
	s_nop 0
	v_addc_co_u32_e32 v149, vcc, 0, v3, vcc
	global_load_dwordx2 v[156:157], v[148:149], off nt
	v_add_co_u32_e32 v148, vcc, s81, v2
	global_load_dwordx2 v[98:99], v[98:99], off nt
	s_nop 0
	v_addc_co_u32_e32 v149, vcc, 0, v3, vcc
	global_load_dwordx2 v[104:105], v[104:105], off nt
	v_add_co_u32_e32 v152, vcc, s9, v2
	global_load_dwordx2 v[108:109], v[108:109], off nt
	s_nop 0
	v_addc_co_u32_e32 v153, vcc, 0, v3, vcc
	v_add_co_u32_e32 v154, vcc, s85, v2
	s_mov_b32 s9, 0xee000
	s_nop 0
	v_addc_co_u32_e32 v155, vcc, 0, v3, vcc
	global_load_dwordx2 v[110:111], v[110:111], off nt
	v_med3_f32 v8, v8, s79, v193
	global_load_dwordx2 v[148:149], v[148:149], off nt
	v_mov_b32_e32 v194, v9
	global_load_dwordx2 v[152:153], v[152:153], off nt
	v_mov_b32_e32 v195, v9
	global_load_dwordx2 v[158:159], v[154:155], off nt
	v_add_co_u32_e32 v154, vcc, s9, v2
	s_mov_b32 s9, 0xf2000
	s_nop 0
	v_addc_co_u32_e32 v155, vcc, 0, v3, vcc
	global_load_dwordx2 v[166:167], v[154:155], off nt
	v_add_co_u32_e32 v154, vcc, s89, v2
	s_waitcnt vmcnt(29)
	v_mul_f32_e32 v50, 0x43800000, v52
	v_addc_co_u32_e32 v155, vcc, 0, v3, vcc
	v_add_co_u32_e32 v160, vcc, s9, v2
	s_mov_b32 s9, 0xf6000
	s_nop 0
	v_addc_co_u32_e32 v161, vcc, 0, v3, vcc
	v_add_co_u32_e32 v164, vcc, s93, v2
	global_load_dwordx2 v[154:155], v[154:155], off nt
	s_nop 0
	v_addc_co_u32_e32 v165, vcc, 0, v3, vcc
	global_load_dwordx2 v[160:161], v[160:161], off nt
	v_mul_f32_e32 v52, 0x43800000, v54
	global_load_dwordx2 v[168:169], v[164:165], off nt
	v_add_co_u32_e32 v164, vcc, s9, v2
	s_mov_b32 s9, 0xfa000
	s_nop 0
	v_addc_co_u32_e32 v165, vcc, 0, v3, vcc
	global_load_dwordx2 v[172:173], v[164:165], off nt
	v_add_co_u32_e32 v164, vcc, s97, v2
	v_med3_f32 v50, v50, s79, v193
	s_nop 0
	v_addc_co_u32_e32 v165, vcc, 0, v3, vcc
	v_add_co_u32_e32 v170, vcc, s9, v2
	s_mov_b32 s9, 0xfe000
	s_nop 0
	v_addc_co_u32_e32 v171, vcc, 0, v3, vcc
	v_add_co_u32_e32 v174, vcc, s16, v2
	v_med3_f32 v52, v52, s79, v193
	s_nop 0
	v_addc_co_u32_e32 v175, vcc, 0, v3, vcc
	v_add_co_u32_e32 v2, vcc, s9, v2
	v_mov_b32_e32 v196, v9
	s_nop 0
	v_addc_co_u32_e32 v3, vcc, 0, v3, vcc
	global_load_dwordx2 v[2:3], v[2:3], off nt
	v_mul_f32_e32 v4, 0x43800000, v4
	v_med3_f32 v4, v4, s79, v193
	v_cvt_pk_fp8_f32 v194, v4, v8
	v_mul_f32_e32 v4, 0x43800000, v56
	v_mul_f32_e32 v8, 0x43800000, v58
	v_med3_f32 v4, v4, s79, v193
	v_med3_f32 v8, v8, s79, v193
	v_cvt_pk_fp8_f32 v195, v4, v8
	s_waitcnt vmcnt(32)
	v_mul_f32_e32 v4, 0x43800000, v64
	s_waitcnt vmcnt(31)
	v_mul_f32_e32 v8, 0x43800000, v66
	v_med3_f32 v4, v4, s79, v193
	v_med3_f32 v8, v8, s79, v193
	v_cvt_pk_fp8_f32 v194, v50, v52 op_sel:[0,0,1]
	s_waitcnt vmcnt(30)
	v_mul_f32_e32 v50, 0x43800000, v60
	v_mul_f32_e32 v52, 0x43800000, v62
	v_cvt_pk_fp8_f32 v196, v4, v8
	s_waitcnt vmcnt(28)
	v_mul_f32_e32 v4, 0x43800000, v72
	s_waitcnt vmcnt(27)
	v_mul_f32_e32 v8, 0x43800000, v74
	v_med3_f32 v50, v50, s79, v193
	v_med3_f32 v52, v52, s79, v193
	v_med3_f32 v4, v4, s79, v193
	v_med3_f32 v8, v8, s79, v193
	v_mov_b32_e32 v197, v9
	v_cvt_pk_fp8_f32 v195, v50, v52 op_sel:[0,0,1]
	s_waitcnt vmcnt(26)
	v_mul_f32_e32 v50, 0x43800000, v68
	v_mul_f32_e32 v52, 0x43800000, v70
	v_cvt_pk_fp8_f32 v197, v4, v8
	v_med3_f32 v50, v50, s79, v193
	v_med3_f32 v52, v52, s79, v193
	v_cvt_pk_fp8_f32 v196, v50, v52 op_sel:[0,0,1]
	s_waitcnt vmcnt(22)
	v_mul_f32_e32 v50, 0x43800000, v76
	v_mul_f32_e32 v52, 0x43800000, v78
	v_med3_f32 v50, v50, s79, v193
	v_med3_f32 v52, v52, s79, v193
	v_cvt_pk_fp8_f32 v197, v50, v52 op_sel:[0,0,1]
	v_mul_f32_e32 v4, 0x43800000, v5
	v_mul_f32_e32 v5, 0x43800000, v51
	v_mul_f32_e32 v50, 0x43800000, v55
	v_med3_f32 v4, v4, s79, v193
	v_med3_f32 v5, v5, s79, v193
	v_med3_f32 v51, v50, s79, v193
	v_mov_b32_e32 v50, v9
	v_cvt_pk_fp8_f32 v50, v4, v5
	v_mul_f32_e32 v8, 0x43800000, v53
	v_med3_f32 v8, v8, s79, v193
	v_mul_f32_e32 v4, 0x43800000, v57
	v_cvt_pk_fp8_f32 v50, v8, v51 op_sel:[0,0,1]
	v_mul_f32_e32 v5, 0x43800000, v59
	v_mul_f32_e32 v51, 0x43800000, v63
	v_med3_f32 v4, v4, s79, v193
	v_med3_f32 v5, v5, s79, v193
	v_med3_f32 v52, v51, s79, v193
	v_mov_b32_e32 v51, v9
	v_cvt_pk_fp8_f32 v51, v4, v5
	v_mul_f32_e32 v8, 0x43800000, v61
	v_med3_f32 v8, v8, s79, v193
	v_mul_f32_e32 v4, 0x43800000, v65
	v_cvt_pk_fp8_f32 v51, v8, v52 op_sel:[0,0,1]
	v_mul_f32_e32 v5, 0x43800000, v67
	v_mul_f32_e32 v52, 0x43800000, v71
	v_med3_f32 v4, v4, s79, v193
	v_med3_f32 v5, v5, s79, v193
	v_med3_f32 v53, v52, s79, v193
	v_mov_b32_e32 v52, v9
	v_cvt_pk_fp8_f32 v52, v4, v5
	v_mul_f32_e32 v8, 0x43800000, v69
	v_med3_f32 v8, v8, s79, v193
	global_load_dwordx2 v[130:131], v[130:131], off nt
	v_cvt_pk_fp8_f32 v52, v8, v53 op_sel:[0,0,1]
	global_load_dwordx2 v[136:137], v[136:137], off nt
	v_mul_f32_e32 v4, 0x43800000, v73
	global_load_dwordx2 v[140:141], v[140:141], off nt
	v_mul_f32_e32 v5, 0x43800000, v75
	global_load_dwordx2 v[142:143], v[142:143], off nt
	v_mul_f32_e32 v53, 0x43800000, v79
	v_med3_f32 v4, v4, s79, v193
	v_med3_f32 v5, v5, s79, v193
	v_med3_f32 v54, v53, s79, v193
	v_mov_b32_e32 v53, v9
	v_cvt_pk_fp8_f32 v53, v4, v5
	v_mul_f32_e32 v8, 0x43800000, v77
	v_med3_f32 v8, v8, s79, v193
	v_add_u32_e32 v5, v13, v25
	v_cvt_pk_fp8_f32 v53, v8, v54 op_sel:[0,0,1]
	s_waitcnt vmcnt(23)
	v_mul_f32_e32 v8, 0x43800000, v82
	v_med3_f32 v8, v8, s79, v193
	global_load_dwordx2 v[164:165], v[164:165], off nt
	ds_write_b128 v5, v[50:53]
	v_mul_f32_e32 v5, 0x43800000, v80
	s_waitcnt vmcnt(23)
; #define CV_LOAD(v, kb) do { _Pragma("unroll") for (int j = 0; j < 16; ++j) v[j] = __builtin_nontemporal_load((const f32x2*)(src + (size_t)((kb) * 16 + j) * ldw)); } while (0)
; __device__ __forceinline__ void tr128_f8(const float* W, int ldw, int srccol, unsigned char* WT, size_t dstrow0, int K, int k0, LAS unsigned char* tile, int lane) {
;     ...
;     CV_LOAD(va, 0); CV_LOAD(vb, 1); CV_LOAD(vc, 2);
;     CV_LOAD(vd, 3); CV_PUT(va, 0); CV_LOAD(va, 4); CV_PUT(vb, 1); CV_LOAD(vb, 5); CV_PUT(vc, 2); CV_LOAD(vc, 6); CV_PUT(vd, 3); CV_LOAD(vd, 7);
;     CV_PUT(va, 4); CV_PUT(vb, 5); CV_PUT(vc, 6); CV_PUT(vd, 7);
	v_mul_f32_e32 v50, 0x43800000, v84
	v_med3_f32 v5, v5, s79, v193
	v_med3_f32 v52, v50, s79, v193
	v_mov_b32_e32 v50, v9
	v_cvt_pk_fp8_f32 v50, v5, v8
	s_waitcnt vmcnt(22)
	v_mul_f32_e32 v51, 0x43800000, v86
	v_med3_f32 v51, v51, s79, v193
	v_mul_f32_e32 v5, 0x43800000, v88
	v_cvt_pk_fp8_f32 v50, v52, v51 op_sel:[0,0,1]
	v_mul_f32_e32 v8, 0x43800000, v90
	v_mul_f32_e32 v51, 0x43800000, v94
	v_med3_f32 v5, v5, s79, v193
	v_med3_f32 v8, v8, s79, v193
	v_med3_f32 v53, v51, s79, v193
	v_mov_b32_e32 v51, v9
	v_cvt_pk_fp8_f32 v51, v5, v8
	v_mul_f32_e32 v52, 0x43800000, v100
	v_med3_f32 v52, v52, s79, v193
	v_mul_f32_e32 v5, 0x43800000, v92
	v_cvt_pk_fp8_f32 v51, v53, v52 op_sel:[0,0,1]
	v_mul_f32_e32 v8, 0x43800000, v96
	v_mul_f32_e32 v52, 0x43800000, v102
	v_med3_f32 v5, v5, s79, v193
	v_med3_f32 v8, v8, s79, v193
	v_med3_f32 v54, v52, s79, v193
	v_mov_b32_e32 v52, v9
	v_cvt_pk_fp8_f32 v52, v5, v8
	v_mul_f32_e32 v53, 0x43800000, v106
	v_med3_f32 v53, v53, s79, v193
	s_waitcnt vmcnt(17)
	v_mul_f32_e32 v5, 0x43800000, v98
	v_cvt_pk_fp8_f32 v52, v54, v53 op_sel:[0,0,1]
	s_waitcnt vmcnt(16)
	v_mul_f32_e32 v8, 0x43800000, v104
	s_waitcnt vmcnt(15)
	v_mul_f32_e32 v53, 0x43800000, v108
	v_med3_f32 v5, v5, s79, v193
	v_med3_f32 v8, v8, s79, v193
	v_med3_f32 v55, v53, s79, v193
	v_mov_b32_e32 v53, v9
	v_cvt_pk_fp8_f32 v53, v5, v8
	s_waitcnt vmcnt(14)
	v_mul_f32_e32 v54, 0x43800000, v110
	v_med3_f32 v54, v54, s79, v193
	v_mul_f32_e32 v5, 0x43800000, v81
	v_cvt_pk_fp8_f32 v53, v55, v54 op_sel:[0,0,1]
	v_mul_f32_e32 v8, 0x43800000, v83
	v_mul_f32_e32 v54, 0x43800000, v85
	v_med3_f32 v5, v5, s79, v193
	v_med3_f32 v8, v8, s79, v193
	v_med3_f32 v56, v54, s79, v193
	v_mov_b32_e32 v54, v9
	v_cvt_pk_fp8_f32 v54, v5, v8
	v_mul_f32_e32 v55, 0x43800000, v87
	v_med3_f32 v55, v55, s79, v193
	v_mul_f32_e32 v5, 0x43800000, v89
	v_cvt_pk_fp8_f32 v54, v56, v55 op_sel:[0,0,1]
	v_mul_f32_e32 v8, 0x43800000, v91
	v_mul_f32_e32 v55, 0x43800000, v95
	v_med3_f32 v5, v5, s79, v193
	v_med3_f32 v8, v8, s79, v193
	v_med3_f32 v57, v55, s79, v193
	v_mov_b32_e32 v55, v9
	v_cvt_pk_fp8_f32 v55, v5, v8
	v_mul_f32_e32 v56, 0x43800000, v101
	v_med3_f32 v56, v56, s79, v193
	v_mul_f32_e32 v5, 0x43800000, v93
	v_cvt_pk_fp8_f32 v55, v57, v56 op_sel:[0,0,1]
	v_mul_f32_e32 v8, 0x43800000, v97
	v_mul_f32_e32 v56, 0x43800000, v103
	v_med3_f32 v5, v5, s79, v193
	v_med3_f32 v8, v8, s79, v193
	v_med3_f32 v58, v56, s79, v193
	v_mov_b32_e32 v56, v9
	v_cvt_pk_fp8_f32 v56, v5, v8
	v_mul_f32_e32 v57, 0x43800000, v107
	v_med3_f32 v57, v57, s79, v193
	global_load_dwordx2 v[170:171], v[170:171], off nt
	v_cvt_pk_fp8_f32 v56, v58, v57 op_sel:[0,0,1]
	global_load_dwordx2 v[174:175], v[174:175], off nt
	v_mul_f32_e32 v5, 0x43800000, v99
	v_mul_f32_e32 v8, 0x43800000, v105
	v_mul_f32_e32 v57, 0x43800000, v109
	v_med3_f32 v5, v5, s79, v193
	v_med3_f32 v8, v8, s79, v193
	v_med3_f32 v59, v57, s79, v193
	v_mov_b32_e32 v57, v9
	v_cvt_pk_fp8_f32 v57, v5, v8
	v_mul_f32_e32 v58, 0x43800000, v111
	v_med3_f32 v58, v58, s79, v193
	v_add_u32_e32 v4, v7, v23
	v_cvt_pk_fp8_f32 v57, v59, v58 op_sel:[0,0,1]
	ds_write_b128 v4, v[194:197]
	ds_write_b128 v4, v[50:53] offset:16
	v_add_u32_e32 v4, v13, v27
	ds_write_b128 v4, v[54:57]
	v_mul_f32_e32 v4, 0x43800000, v112
	v_mul_f32_e32 v5, 0x43800000, v114
	v_mul_f32_e32 v50, 0x43800000, v124
	v_med3_f32 v4, v4, s79, v193
	v_med3_f32 v5, v5, s79, v193
	v_med3_f32 v51, v50, s79, v193
	v_mov_b32_e32 v50, v9
	v_cvt_pk_fp8_f32 v50, v4, v5
	v_mul_f32_e32 v8, 0x43800000, v118
	v_med3_f32 v8, v8, s79, v193
	v_mul_f32_e32 v4, 0x43800000, v116
	v_cvt_pk_fp8_f32 v50, v8, v51 op_sel:[0,0,1]
	v_mul_f32_e32 v5, 0x43800000, v120
	v_mul_f32_e32 v51, 0x43800000, v132
	v_med3_f32 v4, v4, s79, v193
	v_med3_f32 v5, v5, s79, v193
	v_med3_f32 v52, v51, s79, v193
	v_mov_b32_e32 v51, v9
	v_cvt_pk_fp8_f32 v51, v4, v5
	v_mul_f32_e32 v8, 0x43800000, v126
	v_med3_f32 v8, v8, s79, v193
	v_mul_f32_e32 v4, 0x43800000, v122
	v_cvt_pk_fp8_f32 v51, v8, v52 op_sel:[0,0,1]
	v_mul_f32_e32 v5, 0x43800000, v128
	v_mul_f32_e32 v52, 0x43800000, v138
	v_med3_f32 v4, v4, s79, v193
	v_med3_f32 v5, v5, s79, v193
	v_med3_f32 v53, v52, s79, v193
	v_mov_b32_e32 v52, v9
	v_cvt_pk_fp8_f32 v52, v4, v5
	v_mul_f32_e32 v8, 0x43800000, v134
	v_med3_f32 v8, v8, s79, v193
	s_waitcnt vmcnt(6)
	v_mul_f32_e32 v4, 0x43800000, v130
	v_cvt_pk_fp8_f32 v52, v8, v53 op_sel:[0,0,1]
	s_waitcnt vmcnt(5)
	v_mul_f32_e32 v5, 0x43800000, v136
	s_waitcnt vmcnt(3)
; #define CV_LOAD(v, kb) do { _Pragma("unroll") for (int j = 0; j < 16; ++j) v[j] = __builtin_nontemporal_load((const f32x2*)(src + (size_t)((kb) * 16 + j) * ldw)); } while (0)
; __device__ __forceinline__ void tr128_f8(const float* W, int ldw, int srccol, unsigned char* WT, size_t dstrow0, int K, int k0, LAS unsigned char* tile, int lane) {
;     ...
;     CV_LOAD(va, 0); CV_LOAD(vb, 1); CV_LOAD(vc, 2);
;     CV_LOAD(vd, 3); CV_PUT(va, 0); CV_LOAD(va, 4); CV_PUT(vb, 1); CV_LOAD(vb, 5); CV_PUT(vc, 2); CV_LOAD(vc, 6); CV_PUT(vd, 3); CV_LOAD(vd, 7);
;     CV_PUT(va, 4); CV_PUT(vb, 5); CV_PUT(vc, 6); CV_PUT(vd, 7);
	v_mul_f32_e32 v53, 0x43800000, v142
	v_med3_f32 v4, v4, s79, v193
	v_med3_f32 v5, v5, s79, v193
	v_med3_f32 v54, v53, s79, v193
	v_mov_b32_e32 v53, v9
	v_cvt_pk_fp8_f32 v53, v4, v5
	v_mul_f32_e32 v8, 0x43800000, v140
	v_med3_f32 v8, v8, s79, v193
	v_mul_f32_e32 v4, 0x43800000, v113
	v_cvt_pk_fp8_f32 v53, v8, v54 op_sel:[0,0,1]
	v_mul_f32_e32 v5, 0x43800000, v115
	v_mul_f32_e32 v54, 0x43800000, v125
	v_med3_f32 v4, v4, s79, v193
	v_med3_f32 v5, v5, s79, v193
	v_med3_f32 v55, v54, s79, v193
	v_mov_b32_e32 v54, v9
	v_cvt_pk_fp8_f32 v54, v4, v5
	v_mul_f32_e32 v8, 0x43800000, v119
	v_med3_f32 v8, v8, s79, v193
	v_mul_f32_e32 v4, 0x43800000, v117
	v_cvt_pk_fp8_f32 v54, v8, v55 op_sel:[0,0,1]
	v_mul_f32_e32 v5, 0x43800000, v121
	v_mul_f32_e32 v55, 0x43800000, v133
	v_med3_f32 v4, v4, s79, v193
	v_med3_f32 v5, v5, s79, v193
	v_med3_f32 v56, v55, s79, v193
	v_mov_b32_e32 v55, v9
	v_cvt_pk_fp8_f32 v55, v4, v5
	v_mul_f32_e32 v8, 0x43800000, v127
	v_med3_f32 v8, v8, s79, v193
	v_mul_f32_e32 v4, 0x43800000, v123
	v_cvt_pk_fp8_f32 v55, v8, v56 op_sel:[0,0,1]
	v_mul_f32_e32 v5, 0x43800000, v129
	v_mul_f32_e32 v56, 0x43800000, v139
	v_med3_f32 v4, v4, s79, v193
	v_med3_f32 v5, v5, s79, v193
	v_med3_f32 v57, v56, s79, v193
	v_mov_b32_e32 v56, v9
	v_cvt_pk_fp8_f32 v56, v4, v5
	v_mul_f32_e32 v8, 0x43800000, v135
	v_med3_f32 v8, v8, s79, v193
	v_mul_f32_e32 v4, 0x43800000, v131
	v_cvt_pk_fp8_f32 v56, v8, v57 op_sel:[0,0,1]
	v_mul_f32_e32 v5, 0x43800000, v137
	v_mul_f32_e32 v57, 0x43800000, v143
	v_med3_f32 v4, v4, s79, v193
	v_med3_f32 v5, v5, s79, v193
	v_med3_f32 v58, v57, s79, v193
	v_mov_b32_e32 v57, v9
	v_cvt_pk_fp8_f32 v57, v4, v5
	v_mul_f32_e32 v8, 0x43800000, v141
	v_med3_f32 v8, v8, s79, v193
	v_add_u32_e32 v4, v7, v29
	v_cvt_pk_fp8_f32 v57, v8, v58 op_sel:[0,0,1]
	v_add_u32_e32 v5, v13, v31
	ds_write_b128 v4, v[50:53]
	v_mul_f32_e32 v8, 0x43800000, v146
	ds_write_b128 v5, v[54:57]
	v_mul_f32_e32 v5, 0x43800000, v144
	v_mul_f32_e32 v50, 0x43800000, v150
	v_med3_f32 v5, v5, s79, v193
	v_med3_f32 v8, v8, s79, v193
	v_med3_f32 v52, v50, s79, v193
	v_mov_b32_e32 v50, v9
	v_cvt_pk_fp8_f32 v50, v5, v8
	v_mul_f32_e32 v51, 0x43800000, v156
	v_med3_f32 v51, v51, s79, v193
	v_mul_f32_e32 v5, 0x43800000, v148
	v_cvt_pk_fp8_f32 v50, v52, v51 op_sel:[0,0,1]
	v_mul_f32_e32 v8, 0x43800000, v152
	v_mul_f32_e32 v51, 0x43800000, v158
	v_med3_f32 v5, v5, s79, v193
	v_med3_f32 v8, v8, s79, v193
	v_med3_f32 v53, v51, s79, v193
	v_mov_b32_e32 v51, v9
	v_cvt_pk_fp8_f32 v51, v5, v8
	v_mul_f32_e32 v52, 0x43800000, v166
	v_med3_f32 v52, v52, s79, v193
	v_mul_f32_e32 v5, 0x43800000, v154
	v_cvt_pk_fp8_f32 v51, v53, v52 op_sel:[0,0,1]
	v_mul_f32_e32 v8, 0x43800000, v160
	v_mul_f32_e32 v52, 0x43800000, v168
	v_med3_f32 v5, v5, s79, v193
	v_med3_f32 v8, v8, s79, v193
	v_med3_f32 v54, v52, s79, v193
	v_mov_b32_e32 v52, v9
	v_cvt_pk_fp8_f32 v52, v5, v8
	v_mul_f32_e32 v53, 0x43800000, v172
	v_med3_f32 v53, v53, s79, v193
	s_waitcnt vmcnt(2)
	v_mul_f32_e32 v5, 0x43800000, v164
	v_cvt_pk_fp8_f32 v52, v54, v53 op_sel:[0,0,1]
	s_waitcnt vmcnt(1)
	v_mul_f32_e32 v8, 0x43800000, v170
	s_waitcnt vmcnt(0)
	v_mul_f32_e32 v53, 0x43800000, v174
	v_med3_f32 v5, v5, s79, v193
	v_med3_f32 v8, v8, s79, v193
	v_med3_f32 v54, v53, s79, v193
	v_mov_b32_e32 v53, v9
	v_cvt_pk_fp8_f32 v53, v5, v8
	v_mul_f32_e32 v2, 0x43800000, v2
	v_med3_f32 v2, v2, s79, v193
	v_mul_f32_e32 v5, 0x43800000, v147
	v_cvt_pk_fp8_f32 v53, v54, v2 op_sel:[0,0,1]
	v_mul_f32_e32 v2, 0x43800000, v145
	v_mul_f32_e32 v54, 0x43800000, v157
	v_med3_f32 v2, v2, s79, v193
	v_med3_f32 v5, v5, s79, v193
	v_med3_f32 v55, v54, s79, v193
	v_mov_b32_e32 v54, v9
	v_cvt_pk_fp8_f32 v54, v2, v5
	v_mul_f32_e32 v8, 0x43800000, v151
	v_med3_f32 v8, v8, s79, v193
	v_mul_f32_e32 v2, 0x43800000, v149
	v_cvt_pk_fp8_f32 v54, v8, v55 op_sel:[0,0,1]
	v_mul_f32_e32 v5, 0x43800000, v153
	v_mul_f32_e32 v55, 0x43800000, v167
	v_med3_f32 v2, v2, s79, v193
	v_med3_f32 v5, v5, s79, v193
	v_med3_f32 v56, v55, s79, v193
	v_mov_b32_e32 v55, v9
	v_cvt_pk_fp8_f32 v55, v2, v5
	v_mul_f32_e32 v8, 0x43800000, v159
	v_med3_f32 v8, v8, s79, v193
	v_mul_f32_e32 v2, 0x43800000, v155
	v_cvt_pk_fp8_f32 v55, v8, v56 op_sel:[0,0,1]
	v_mul_f32_e32 v5, 0x43800000, v161
	v_mul_f32_e32 v56, 0x43800000, v173
	v_med3_f32 v2, v2, s79, v193
	v_med3_f32 v5, v5, s79, v193
	v_med3_f32 v57, v56, s79, v193
	v_mov_b32_e32 v56, v9
	v_cvt_pk_fp8_f32 v56, v2, v5
	v_mul_f32_e32 v8, 0x43800000, v169
	v_med3_f32 v8, v8, s79, v193
	v_mul_f32_e32 v2, 0x43800000, v165
	v_mul_f32_e32 v5, 0x43800000, v171
	v_cvt_pk_fp8_f32 v56, v8, v57 op_sel:[0,0,1]
	v_med3_f32 v2, v2, s79, v193
	v_med3_f32 v5, v5, s79, v193
	v_mov_b32_e32 v57, v9
	v_cvt_pk_fp8_f32 v57, v2, v5
	v_mul_f32_e32 v8, 0x43800000, v175
	v_mul_f32_e32 v3, 0x43800000, v3
	v_med3_f32 v8, v8, s79, v193
	v_med3_f32 v3, v3, s79, v193
	v_cvt_pk_fp8_f32 v57, v8, v3 op_sel:[0,0,1]
	v_add_u32_e32 v2, v13, v33
	ds_write_b128 v4, v[50:53] offset:16
	v_or_b32_e32 v8, s8, v162
	ds_write_b128 v2, v[54:57]
	s_waitcnt lgkmcnt(0)
; #define LAS __attribute__((address_space(3)))
; #define LDS_WAIT() asm volatile("s_waitcnt lgkmcnt(0)" ::: "memory")
; __device__ __forceinline__ void tr128_f8(const float* W, int ldw, int srccol, unsigned char* WT, size_t dstrow0, int K, int k0, LAS unsigned char* tile, int lane) {
;     ...
;     LDS_WAIT(); asm volatile("" ::: "memory");
;     const int c = lane & 7;
; #pragma unroll
;     for (int j = 0; j < 16; ++j) { const int n = (lane >> 3) + 8 * j; const v4u o = *(const LAS v4u*)(tile + n * 128 + ((c ^ (n & 7)) << 4));
;         __builtin_nontemporal_store(o, (v4u*)(WT + (dstrow0 + n) * K + k0 + 16 * c)); }
;     LDS_WAIT(); asm volatile("" ::: "memory");
	v_add_u32_e32 v56, v35, v37
	ds_read_b128 v[56:59], v56
	v_add_u32_e32 v60, v35, v39
	ds_read_b128 v[60:63], v60
	v_add_u32_e32 v64, v35, v179
	ds_read_b128 v[64:67], v64
	v_add_u32_e32 v68, v35, v180
	ds_read_b128 v[68:71], v68
	v_add_u32_e32 v72, v35, v181
	ds_read_b128 v[72:75], v72
	v_add_u32_e32 v76, v35, v182
	ds_read_b128 v[76:79], v76
	v_add_u32_e32 v80, v35, v183
	ds_read_b128 v[80:83], v80
	v_add_u32_e32 v84, v35, v184
	ds_read_b128 v[84:87], v84
	v_add_u32_e32 v88, v35, v185
	ds_read_b128 v[88:91], v88
	v_add_u32_e32 v92, v35, v186
	ds_read_b128 v[92:95], v92
	v_add_u32_e32 v96, v35, v187
	ds_read_b128 v[96:99], v96
	v_add_u32_e32 v100, v35, v188
	ds_read_b128 v[100:103], v100
	v_add_u32_e32 v104, v35, v189
	ds_read_b128 v[104:107], v104
	v_add_u32_e32 v108, v35, v190
	ds_read_b128 v[108:111], v108
	v_add_u32_e32 v112, v35, v191
	ds_read_b128 v[112:115], v112
	v_add_u32_e32 v116, v35, v192
	ds_read_b128 v[116:119], v116
	v_lshl_add_u64 v[50:51], v[44:45], 0, s[6:7]
	v_lshlrev_b32_e32 v8, 11, v8
	v_lshl_add_u64 v[52:53], v[50:51], 0, v[8:9]
	v_or_b32_e32 v8, s8, v10
	s_waitcnt lgkmcnt(15)
	global_store_dwordx4 v[52:53], v[56:59], off nt
	v_lshlrev_b32_e32 v8, 11, v8
	v_lshl_add_u64 v[52:53], v[50:51], 0, v[8:9]
	v_or_b32_e32 v8, s8, v12
	v_lshlrev_b32_e32 v8, 11, v8
	v_readlane_b32 s37, v250, 61
	v_readlane_b32 s38, v250, 62
	s_waitcnt lgkmcnt(14)
	global_store_dwordx4 v[52:53], v[60:63], off nt
	v_lshl_add_u64 v[52:53], v[50:51], 0, v[8:9]
	v_or_b32_e32 v8, s8, v14
	v_lshlrev_b32_e32 v8, 11, v8
	v_readlane_b32 s39, v250, 63
	v_readlane_b32 s40, v251, 0
	v_readlane_b32 s41, v251, 1
	s_waitcnt lgkmcnt(13)
	global_store_dwordx4 v[52:53], v[64:67], off nt
	v_lshl_add_u64 v[52:53], v[50:51], 0, v[8:9]
	v_or_b32_e32 v8, s8, v16
	v_lshlrev_b32_e32 v8, 11, v8
	v_readlane_b32 s42, v251, 2
	v_readlane_b32 s43, v251, 3
	v_readlane_b32 s46, v251, 6
	s_waitcnt lgkmcnt(12)
	global_store_dwordx4 v[52:53], v[68:71], off nt
	v_lshl_add_u64 v[52:53], v[50:51], 0, v[8:9]
	v_or_b32_e32 v8, s8, v18
	v_lshlrev_b32_e32 v8, 11, v8
	v_readlane_b32 s47, v251, 7
	v_readlane_b32 s48, v251, 8
	v_readlane_b32 s49, v251, 9
	s_waitcnt lgkmcnt(11)
	global_store_dwordx4 v[52:53], v[72:75], off nt
	v_lshl_add_u64 v[52:53], v[50:51], 0, v[8:9]
	v_or_b32_e32 v8, s8, v20
	v_lshlrev_b32_e32 v8, 11, v8
	v_readlane_b32 s50, v251, 10
	v_readlane_b32 s51, v251, 11
	s_waitcnt lgkmcnt(10)
	global_store_dwordx4 v[52:53], v[76:79], off nt
	v_lshl_add_u64 v[52:53], v[50:51], 0, v[8:9]
	s_nop 0
	v_or_b32_e32 v8, s8, v22
	v_lshlrev_b32_e32 v8, 11, v8
	s_waitcnt lgkmcnt(9)
	global_store_dwordx4 v[52:53], v[80:83], off nt
	s_nop 1
	v_lshl_add_u64 v[52:53], v[50:51], 0, v[8:9]
	v_or_b32_e32 v8, s8, v24
	v_lshlrev_b32_e32 v8, 11, v8
	s_waitcnt lgkmcnt(8)
	global_store_dwordx4 v[52:53], v[84:87], off nt
	v_lshl_add_u64 v[52:53], v[50:51], 0, v[8:9]
	s_nop 0
	v_or_b32_e32 v8, s8, v26
	v_lshlrev_b32_e32 v8, 11, v8
	s_waitcnt lgkmcnt(7)
	global_store_dwordx4 v[52:53], v[88:91], off nt
	s_nop 1
	v_lshl_add_u64 v[52:53], v[50:51], 0, v[8:9]
	v_or_b32_e32 v8, s8, v28
	v_lshlrev_b32_e32 v8, 11, v8
	s_waitcnt lgkmcnt(6)
	global_store_dwordx4 v[52:53], v[92:95], off nt
	v_lshl_add_u64 v[52:53], v[50:51], 0, v[8:9]
	s_nop 0
	v_or_b32_e32 v8, s8, v30
	v_lshlrev_b32_e32 v8, 11, v8
	s_waitcnt lgkmcnt(5)
	global_store_dwordx4 v[52:53], v[96:99], off nt
	s_nop 1
	v_lshl_add_u64 v[52:53], v[50:51], 0, v[8:9]
	v_or_b32_e32 v8, s8, v32
	v_lshlrev_b32_e32 v8, 11, v8
	s_waitcnt lgkmcnt(4)
	global_store_dwordx4 v[52:53], v[100:103], off nt
	v_lshl_add_u64 v[52:53], v[50:51], 0, v[8:9]
	s_nop 0
	v_or_b32_e32 v8, s8, v34
	v_lshlrev_b32_e32 v8, 11, v8
	s_waitcnt lgkmcnt(3)
	global_store_dwordx4 v[52:53], v[104:107], off nt
	s_nop 1
	v_lshl_add_u64 v[52:53], v[50:51], 0, v[8:9]
	v_or_b32_e32 v8, s8, v36
	v_lshlrev_b32_e32 v8, 11, v8
	s_waitcnt lgkmcnt(2)
	global_store_dwordx4 v[52:53], v[108:111], off nt
	v_lshl_add_u64 v[52:53], v[50:51], 0, v[8:9]
	s_nop 0
	v_or_b32_e32 v8, s8, v38
	v_lshlrev_b32_e32 v8, 11, v8
	v_lshl_add_u64 v[50:51], v[50:51], 0, v[8:9]
	s_waitcnt lgkmcnt(1)
	global_store_dwordx4 v[52:53], v[112:115], off nt
	s_nop 1
	s_waitcnt lgkmcnt(0)
	global_store_dwordx4 v[50:51], v[116:119], off nt
	s_waitcnt lgkmcnt(0)

; #define CV_LOAD(v, kb) do { _Pragma("unroll") for (int j = 0; j < 16; ++j) v[j] = __builtin_nontemporal_load((const f32x2*)(src + (size_t)((kb) * 16 + j) * ldw)); } while (0)
; __device__ __forceinline__ void tr128_f8(const float* W, int ldw, int srccol, unsigned char* WT, size_t dstrow0, int K, int k0, LAS unsigned char* tile, int lane) {
;     const float* src = W + (size_t)k0 * ldw + srccol + 2 * lane;
;     f32x2 va[16], vb[16], vc[16], vd[16];
;     ...
;     CV_LOAD(va, 0); CV_LOAD(vb, 1); CV_LOAD(vc, 2);
;     CV_LOAD(vd, 3); CV_PUT(va, 0); CV_LOAD(va, 4); CV_PUT(vb, 1); CV_LOAD(vb, 5); CV_PUT(vc, 2); CV_LOAD(vc, 6); CV_PUT(vd, 3); CV_LOAD(vd, 7);
; __device__ __forceinline__ void cv_item(const Args& a, int it, LAS unsigned char* tile, int lane) {
;     ...
;     if (it < CV_PB) { const int kt = it >> 4, nt = it & 15; tr128_f8(a.in[I_WPB], 2048, 128 * nt, (unsigned char*)(a.ws + WS_WA + 1024), (size_t)128 * nt, 2048, 128 * kt, tile, lane); return; } it -= CV_PB;
.LBB0_509:
	s_andn2_b64 vcc, exec, s[8:9]
	s_cbranch_vccnz .LBB0_511
	s_lshl_b32 s6, s10, 7
	s_and_b32 s8, s6, 0x780
	s_lshl_b32 s6, s10, 3
	s_and_b32 s6, s6, 0x780
	s_addk_i32 s6, 0xfc00
	v_readlane_b32 s36, v250, 60
	s_lshl_b64 s[12:13], s[6:7], 13
	v_readlane_b32 s42, v251, 2
	v_readlane_b32 s43, v251, 3
	s_add_u32 s9, s42, s12
	s_addc_u32 s11, s43, s13
	s_lshl_b32 s12, s8, 2
	s_add_u32 s12, s9, s12
	s_addc_u32 s13, s11, 0
	v_lshlrev_b32_e32 v8, 2, v6
	v_lshl_add_u64 v[2:3], s[12:13], 0, v[8:9]
	v_add_co_u32_e32 v50, vcc, s20, v2
	s_mov_b32 s9, 0x16000
	s_nop 0
	v_addc_co_u32_e32 v51, vcc, 0, v3, vcc
	v_add_co_u32_e32 v52, vcc, s21, v2
	global_load_dwordx2 v[4:5], v8, s[12:13] nt
	s_nop 0
	v_addc_co_u32_e32 v53, vcc, 0, v3, vcc
	v_add_co_u32_e32 v54, vcc, s22, v2
	global_load_dwordx2 v[50:51], v[50:51], off nt
	s_nop 0
	v_addc_co_u32_e32 v55, vcc, 0, v3, vcc
	v_add_co_u32_e32 v56, vcc, s23, v2
	global_load_dwordx2 v[52:53], v[52:53], off nt
	s_nop 0
	v_addc_co_u32_e32 v57, vcc, 0, v3, vcc
	v_add_co_u32_e32 v58, vcc, s24, v2
	global_load_dwordx2 v[56:57], v[56:57], off nt
	s_nop 0
	v_addc_co_u32_e32 v59, vcc, 0, v3, vcc
	v_add_co_u32_e32 v60, vcc, s25, v2
	global_load_dwordx2 v[58:59], v[58:59], off nt
	s_nop 0
	v_addc_co_u32_e32 v61, vcc, 0, v3, vcc
	v_add_co_u32_e32 v62, vcc, s26, v2
	global_load_dwordx2 v[54:55], v[54:55], off nt
	s_nop 0
	v_addc_co_u32_e32 v63, vcc, 0, v3, vcc
	v_add_co_u32_e32 v64, vcc, s27, v2
	global_load_dwordx2 v[60:61], v[60:61], off nt
	s_nop 0
	v_addc_co_u32_e32 v65, vcc, 0, v3, vcc
	v_add_co_u32_e32 v66, vcc, s33, v2
	global_load_dwordx2 v[64:65], v[64:65], off nt
	s_nop 0
	v_addc_co_u32_e32 v67, vcc, 0, v3, vcc
	v_add_co_u32_e32 v68, vcc, s34, v2
	global_load_dwordx2 v[66:67], v[66:67], off nt
	s_nop 0
	v_addc_co_u32_e32 v69, vcc, 0, v3, vcc
	v_add_co_u32_e32 v70, vcc, s9, v2
	s_mov_b32 s9, 0x1a000
	s_nop 0
	v_addc_co_u32_e32 v71, vcc, 0, v3, vcc
	v_add_co_u32_e32 v72, vcc, s58, v2
	global_load_dwordx2 v[62:63], v[62:63], off nt
	s_nop 0
	v_addc_co_u32_e32 v73, vcc, 0, v3, vcc
	v_add_co_u32_e32 v74, vcc, s9, v2
	global_load_dwordx2 v[72:73], v[72:73], off nt
	s_nop 0
	v_addc_co_u32_e32 v75, vcc, 0, v3, vcc
	global_load_dwordx2 v[74:75], v[74:75], off nt
	v_add_co_u32_e32 v76, vcc, s62, v2
	s_mov_b32 s9, 0x1e000
	s_nop 0
	v_addc_co_u32_e32 v77, vcc, 0, v3, vcc
	global_load_dwordx2 v[68:69], v[68:69], off nt
	v_add_co_u32_e32 v78, vcc, s9, v2
	global_load_dwordx2 v[70:71], v[70:71], off nt
	s_nop 0
	v_addc_co_u32_e32 v79, vcc, 0, v3, vcc
	global_load_dwordx2 v[76:77], v[76:77], off nt
	v_add_co_u32_e32 v80, vcc, s29, v2
	global_load_dwordx2 v[78:79], v[78:79], off nt
	s_nop 0
	v_addc_co_u32_e32 v81, vcc, 0, v3, vcc
	s_mov_b32 s9, 0x22000
	v_add_co_u32_e32 v82, vcc, s9, v2
	s_mov_b32 s9, 0x26000
	s_nop 0
	v_addc_co_u32_e32 v83, vcc, 0, v3, vcc
	v_add_co_u32_e32 v84, vcc, s31, v2
	global_load_dwordx2 v[80:81], v[80:81], off nt
	s_nop 0
	v_addc_co_u32_e32 v85, vcc, 0, v3, vcc
	v_add_co_u32_e32 v86, vcc, s9, v2
	s_mov_b32 s9, 0x2a000
	s_nop 0
	v_addc_co_u32_e32 v87, vcc, 0, v3, vcc
	v_add_co_u32_e32 v88, vcc, s35, v2
	global_load_dwordx2 v[82:83], v[82:83], off nt
	s_nop 0
	v_addc_co_u32_e32 v89, vcc, 0, v3, vcc
	v_add_co_u32_e32 v90, vcc, s9, v2
	s_mov_b32 s9, 0x2e000
	s_nop 0
	v_addc_co_u32_e32 v91, vcc, 0, v3, vcc
	v_add_co_u32_e32 v92, vcc, s66, v2
	global_load_dwordx2 v[86:87], v[86:87], off nt
	s_nop 0
	v_addc_co_u32_e32 v93, vcc, 0, v3, vcc
	v_add_co_u32_e32 v94, vcc, s9, v2
	s_mov_b32 s9, 0x32000
	s_nop 0
	v_addc_co_u32_e32 v95, vcc, 0, v3, vcc
	v_add_co_u32_e32 v96, vcc, s70, v2
	global_load_dwordx2 v[88:89], v[88:89], off nt
	s_nop 0
	v_addc_co_u32_e32 v97, vcc, 0, v3, vcc
	v_add_co_u32_e32 v98, vcc, s9, v2
	s_mov_b32 s9, 0x36000
	s_nop 0
	v_addc_co_u32_e32 v99, vcc, 0, v3, vcc
	v_add_co_u32_e32 v100, vcc, s74, v2
	global_load_dwordx2 v[90:91], v[90:91], off nt
	s_nop 0
	v_addc_co_u32_e32 v101, vcc, 0, v3, vcc
	v_add_co_u32_e32 v102, vcc, s9, v2
	s_mov_b32 s9, 0x3a000
	s_nop 0
	v_addc_co_u32_e32 v103, vcc, 0, v3, vcc
	v_add_co_u32_e32 v104, vcc, s78, v2
	global_load_dwordx2 v[84:85], v[84:85], off nt
	s_nop 0
	v_addc_co_u32_e32 v105, vcc, 0, v3, vcc
	v_add_co_u32_e32 v106, vcc, s9, v2
	s_mov_b32 s9, 0x3e000
	s_nop 0
	v_addc_co_u32_e32 v107, vcc, 0, v3, vcc
	v_add_co_u32_e32 v108, vcc, s83, v2
	global_load_dwordx2 v[94:95], v[94:95], off nt
	s_nop 0
	v_addc_co_u32_e32 v109, vcc, 0, v3, vcc
	v_add_co_u32_e32 v110, vcc, s9, v2
	s_mov_b32 s9, 0x42000
	s_nop 0
	v_addc_co_u32_e32 v111, vcc, 0, v3, vcc
	v_add_co_u32_e32 v112, vcc, s87, v2
	global_load_dwordx2 v[96:97], v[96:97], off nt
	s_nop 0
	v_addc_co_u32_e32 v113, vcc, 0, v3, vcc
	v_add_co_u32_e32 v114, vcc, s9, v2
	s_mov_b32 s9, 0x46000
	s_nop 0
	v_addc_co_u32_e32 v115, vcc, 0, v3, vcc
	v_add_co_u32_e32 v116, vcc, s91, v2
	global_load_dwordx2 v[98:99], v[98:99], off nt
	s_nop 0
	v_addc_co_u32_e32 v117, vcc, 0, v3, vcc
	v_add_co_u32_e32 v118, vcc, s9, v2
	s_mov_b32 s9, 0x4a000
	s_nop 0
	v_addc_co_u32_e32 v119, vcc, 0, v3, vcc
	v_add_co_u32_e32 v120, vcc, s95, v2
	global_load_dwordx2 v[92:93], v[92:93], off nt
	s_nop 0
	v_addc_co_u32_e32 v121, vcc, 0, v3, vcc
	v_add_co_u32_e32 v122, vcc, s9, v2
	s_mov_b32 s9, 0x4e000
	s_nop 0
	v_addc_co_u32_e32 v123, vcc, 0, v3, vcc
	v_add_co_u32_e32 v124, vcc, s53, v2
	global_load_dwordx2 v[102:103], v[102:103], off nt
	s_nop 0
	v_addc_co_u32_e32 v125, vcc, 0, v3, vcc
	v_add_co_u32_e32 v126, vcc, s9, v2
	s_mov_b32 s9, 0x52000
	s_nop 0
	v_addc_co_u32_e32 v127, vcc, 0, v3, vcc
	v_add_co_u32_e32 v128, vcc, s55, v2
	global_load_dwordx2 v[104:105], v[104:105], off nt
	s_nop 0
	v_addc_co_u32_e32 v129, vcc, 0, v3, vcc
	v_add_co_u32_e32 v130, vcc, s9, v2
	s_mov_b32 s9, 0x56000
	s_nop 0
	v_addc_co_u32_e32 v131, vcc, 0, v3, vcc
	v_add_co_u32_e32 v132, vcc, s57, v2
	global_load_dwordx2 v[106:107], v[106:107], off nt
	s_nop 0
	v_addc_co_u32_e32 v133, vcc, 0, v3, vcc
	v_add_co_u32_e32 v134, vcc, s9, v2
	global_load_dwordx2 v[100:101], v[100:101], off nt
	s_nop 0
	v_addc_co_u32_e32 v135, vcc, 0, v3, vcc
	v_add_co_u32_e32 v136, vcc, s59, v2
	s_waitcnt vmcnt(29)
; #define CV_LOAD(v, kb) do { _Pragma("unroll") for (int j = 0; j < 16; ++j) v[j] = __builtin_nontemporal_load((const f32x2*)(src + (size_t)((kb) * 16 + j) * ldw)); } while (0)
; __device__ __forceinline__ void tr128_f8(const float* W, int ldw, int srccol, unsigned char* WT, size_t dstrow0, int K, int k0, LAS unsigned char* tile, int lane) {
;     ...
;     CV_LOAD(va, 0); CV_LOAD(vb, 1); CV_LOAD(vc, 2);
;     CV_LOAD(vd, 3); CV_PUT(va, 0); CV_LOAD(va, 4); CV_PUT(vb, 1); CV_LOAD(vb, 5); CV_PUT(vc, 2); CV_LOAD(vc, 6); CV_PUT(vd, 3); CV_LOAD(vd, 7);
;     CV_PUT(va, 4); CV_PUT(vb, 5); CV_PUT(vc, 6); CV_PUT(vd, 7);
	v_mul_f32_e32 v4, 0x43800000, v4
	s_waitcnt vmcnt(28)
	v_mul_f32_e32 v8, 0x43800000, v50
	v_addc_co_u32_e32 v137, vcc, 0, v3, vcc
	s_mov_b32 s9, 0x5a000
	v_med3_f32 v4, v4, s79, v193
	v_med3_f32 v8, v8, s79, v193
	v_mov_b32_e32 v194, v9
	global_load_dwordx2 v[108:109], v[108:109], off nt
	v_add_co_u32_e32 v138, vcc, s9, v2
	global_load_dwordx2 v[110:111], v[110:111], off nt
	v_cvt_pk_fp8_f32 v194, v4, v8
	s_waitcnt vmcnt(28)
	v_mul_f32_e32 v4, 0x43800000, v56
	s_waitcnt vmcnt(27)
	v_mul_f32_e32 v8, 0x43800000, v58
	v_addc_co_u32_e32 v139, vcc, 0, v3, vcc
	v_med3_f32 v4, v4, s79, v193
	v_med3_f32 v8, v8, s79, v193
	v_mov_b32_e32 v195, v9
	v_add_co_u32_e32 v140, vcc, s61, v2
	v_mul_f32_e32 v50, 0x43800000, v52
	s_waitcnt vmcnt(26)
	v_mul_f32_e32 v52, 0x43800000, v54
	v_cvt_pk_fp8_f32 v195, v4, v8
	s_waitcnt vmcnt(24)
	v_mul_f32_e32 v4, 0x43800000, v64
	s_waitcnt vmcnt(23)
	v_mul_f32_e32 v8, 0x43800000, v66
	v_addc_co_u32_e32 v141, vcc, 0, v3, vcc
	s_mov_b32 s9, 0x5e000
	v_med3_f32 v50, v50, s79, v193
	v_med3_f32 v52, v52, s79, v193
	v_med3_f32 v4, v4, s79, v193
	v_med3_f32 v8, v8, s79, v193
	v_mov_b32_e32 v196, v9
	v_add_co_u32_e32 v142, vcc, s9, v2
	v_cvt_pk_fp8_f32 v194, v50, v52 op_sel:[0,0,1]
	v_mul_f32_e32 v50, 0x43800000, v60
	s_waitcnt vmcnt(22)
	v_mul_f32_e32 v52, 0x43800000, v62
	v_cvt_pk_fp8_f32 v196, v4, v8
	s_waitcnt vmcnt(21)
	v_mul_f32_e32 v4, 0x43800000, v72
	s_waitcnt vmcnt(20)
	v_mul_f32_e32 v8, 0x43800000, v74
	v_addc_co_u32_e32 v143, vcc, 0, v3, vcc
	v_med3_f32 v50, v50, s79, v193
	v_med3_f32 v52, v52, s79, v193
	v_med3_f32 v4, v4, s79, v193
	v_med3_f32 v8, v8, s79, v193
	v_mov_b32_e32 v197, v9
	v_add_co_u32_e32 v144, vcc, s63, v2
	v_cvt_pk_fp8_f32 v195, v50, v52 op_sel:[0,0,1]
	s_waitcnt vmcnt(19)
	v_mul_f32_e32 v50, 0x43800000, v68
	s_waitcnt vmcnt(18)
	v_mul_f32_e32 v52, 0x43800000, v70
	v_cvt_pk_fp8_f32 v197, v4, v8
	v_addc_co_u32_e32 v145, vcc, 0, v3, vcc
	s_mov_b32 s9, 0x62000
	v_med3_f32 v50, v50, s79, v193
	v_med3_f32 v52, v52, s79, v193
	v_add_co_u32_e32 v146, vcc, s9, v2
	v_cvt_pk_fp8_f32 v196, v50, v52 op_sel:[0,0,1]
	s_waitcnt vmcnt(17)
	v_mul_f32_e32 v50, 0x43800000, v76
	s_waitcnt vmcnt(16)
	v_mul_f32_e32 v52, 0x43800000, v78
	v_addc_co_u32_e32 v147, vcc, 0, v3, vcc
	v_med3_f32 v50, v50, s79, v193
	v_med3_f32 v52, v52, s79, v193
	v_add_co_u32_e32 v148, vcc, s65, v2
	v_cvt_pk_fp8_f32 v197, v50, v52 op_sel:[0,0,1]
	v_mul_f32_e32 v4, 0x43800000, v5
	v_mul_f32_e32 v5, 0x43800000, v51
	v_mul_f32_e32 v50, 0x43800000, v55
	v_addc_co_u32_e32 v149, vcc, 0, v3, vcc
	s_mov_b32 s9, 0x66000
	v_med3_f32 v4, v4, s79, v193
	v_med3_f32 v5, v5, s79, v193
	v_med3_f32 v51, v50, s79, v193
	v_mov_b32_e32 v50, v9
	v_add_co_u32_e32 v150, vcc, s9, v2
	v_cvt_pk_fp8_f32 v50, v4, v5
	s_nop 0
	v_addc_co_u32_e32 v151, vcc, 0, v3, vcc
	v_add_co_u32_e32 v152, vcc, s67, v2
	v_mul_f32_e32 v8, 0x43800000, v53
	s_nop 0
	v_addc_co_u32_e32 v153, vcc, 0, v3, vcc
	s_mov_b32 s9, 0x6a000
	v_med3_f32 v8, v8, s79, v193
	v_add_co_u32_e32 v154, vcc, s9, v2
	v_cvt_pk_fp8_f32 v50, v8, v51 op_sel:[0,0,1]
	v_mul_f32_e32 v4, 0x43800000, v57
	v_mul_f32_e32 v5, 0x43800000, v59
	v_mul_f32_e32 v51, 0x43800000, v63
	v_addc_co_u32_e32 v155, vcc, 0, v3, vcc
	v_med3_f32 v4, v4, s79, v193
	v_med3_f32 v5, v5, s79, v193
	v_med3_f32 v52, v51, s79, v193
	v_mov_b32_e32 v51, v9
	v_add_co_u32_e32 v156, vcc, s69, v2
	v_cvt_pk_fp8_f32 v51, v4, v5
	s_nop 0
	v_addc_co_u32_e32 v157, vcc, 0, v3, vcc
	s_mov_b32 s9, 0x6e000
	v_add_co_u32_e32 v158, vcc, s9, v2
	v_mul_f32_e32 v8, 0x43800000, v61
	s_nop 0
	v_addc_co_u32_e32 v159, vcc, 0, v3, vcc
	v_med3_f32 v8, v8, s79, v193
	v_add_co_u32_e32 v160, vcc, s71, v2
	v_cvt_pk_fp8_f32 v51, v8, v52 op_sel:[0,0,1]
	v_mul_f32_e32 v4, 0x43800000, v65
	v_mul_f32_e32 v5, 0x43800000, v67
	v_mul_f32_e32 v52, 0x43800000, v71
	v_addc_co_u32_e32 v161, vcc, 0, v3, vcc
	s_mov_b32 s9, 0x72000
	v_med3_f32 v4, v4, s79, v193
	v_med3_f32 v5, v5, s79, v193
	v_med3_f32 v53, v52, s79, v193
	v_mov_b32_e32 v52, v9
	v_add_co_u32_e32 v164, vcc, s9, v2
	v_cvt_pk_fp8_f32 v52, v4, v5
	s_nop 0
	v_addc_co_u32_e32 v165, vcc, 0, v3, vcc
	v_add_co_u32_e32 v166, vcc, s73, v2
	v_mul_f32_e32 v8, 0x43800000, v69
	s_nop 0
	v_addc_co_u32_e32 v167, vcc, 0, v3, vcc
	s_mov_b32 s9, 0x76000
	v_med3_f32 v8, v8, s79, v193
	v_add_co_u32_e32 v168, vcc, s9, v2
	v_cvt_pk_fp8_f32 v52, v8, v53 op_sel:[0,0,1]
	v_mul_f32_e32 v4, 0x43800000, v73
	v_mul_f32_e32 v5, 0x43800000, v75
	v_mul_f32_e32 v53, 0x43800000, v79
	v_addc_co_u32_e32 v169, vcc, 0, v3, vcc
	v_med3_f32 v4, v4, s79, v193
	v_med3_f32 v5, v5, s79, v193
	v_med3_f32 v54, v53, s79, v193
	v_mov_b32_e32 v53, v9
	v_add_co_u32_e32 v170, vcc, s75, v2
	v_cvt_pk_fp8_f32 v53, v4, v5
	s_nop 0
	v_addc_co_u32_e32 v171, vcc, 0, v3, vcc
	s_mov_b32 s9, 0x7a000
	v_add_co_u32_e32 v172, vcc, s9, v2
	v_mul_f32_e32 v8, 0x43800000, v77
	s_nop 0
	v_addc_co_u32_e32 v173, vcc, 0, v3, vcc
	v_med3_f32 v8, v8, s79, v193
	v_add_co_u32_e32 v174, vcc, s77, v2
	v_cvt_pk_fp8_f32 v53, v8, v54 op_sel:[0,0,1]
	s_nop 0
	v_addc_co_u32_e32 v175, vcc, 0, v3, vcc
	s_mov_b32 s9, 0x7e000
	v_add_co_u32_e32 v176, vcc, s9, v2
	v_add_u32_e32 v4, v13, v15
	s_nop 0
	v_addc_co_u32_e32 v177, vcc, 0, v3, vcc
	ds_write_b128 v4, v[50:53]
	v_add_co_u32_e32 v4, vcc, s80, v2
	s_mov_b32 s9, 0x82000
	s_nop 0
	v_addc_co_u32_e32 v5, vcc, 0, v3, vcc
	v_add_co_u32_e32 v50, vcc, s9, v2
	s_mov_b32 s9, 0x86000
	s_nop 0
	v_addc_co_u32_e32 v51, vcc, 0, v3, vcc
	v_add_co_u32_e32 v52, vcc, s82, v2
	global_load_dwordx2 v[112:113], v[112:113], off nt
	s_nop 0
	v_addc_co_u32_e32 v53, vcc, 0, v3, vcc
	v_add_co_u32_e32 v54, vcc, s9, v2
	s_mov_b32 s9, 0x8a000
	s_nop 0
	v_addc_co_u32_e32 v55, vcc, 0, v3, vcc
; #define CV_LOAD(v, kb) do { _Pragma("unroll") for (int j = 0; j < 16; ++j) v[j] = __builtin_nontemporal_load((const f32x2*)(src + (size_t)((kb) * 16 + j) * ldw)); } while (0)
; __device__ __forceinline__ void tr128_f8(const float* W, int ldw, int srccol, unsigned char* WT, size_t dstrow0, int K, int k0, LAS unsigned char* tile, int lane) {
;     ...
;     CV_LOAD(va, 0); CV_LOAD(vb, 1); CV_LOAD(vc, 2);
;     CV_LOAD(vd, 3); CV_PUT(va, 0); CV_LOAD(va, 4); CV_PUT(vb, 1); CV_LOAD(vb, 5); CV_PUT(vc, 2); CV_LOAD(vc, 6); CV_PUT(vd, 3); CV_LOAD(vd, 7);
;     CV_PUT(va, 4); CV_PUT(vb, 5); CV_PUT(vc, 6); CV_PUT(vd, 7);
	v_add_co_u32_e32 v56, vcc, s84, v2
	global_load_dwordx2 v[114:115], v[114:115], off nt
	s_nop 0
	v_addc_co_u32_e32 v57, vcc, 0, v3, vcc
	v_add_co_u32_e32 v58, vcc, s9, v2
	global_load_dwordx2 v[120:121], v[120:121], off nt
	s_nop 0
	v_addc_co_u32_e32 v59, vcc, 0, v3, vcc
	v_add_co_u32_e32 v60, vcc, s86, v2
	global_load_dwordx2 v[122:123], v[122:123], off nt
	s_nop 0
	v_addc_co_u32_e32 v61, vcc, 0, v3, vcc
	s_mov_b32 s9, 0x8e000
	v_add_co_u32_e32 v62, vcc, s9, v2
	global_load_dwordx2 v[116:117], v[116:117], off nt
	s_nop 0
	v_addc_co_u32_e32 v63, vcc, 0, v3, vcc
	global_load_dwordx2 v[118:119], v[118:119], off nt
	v_add_co_u32_e32 v64, vcc, s88, v2
	global_load_dwordx2 v[124:125], v[124:125], off nt
	s_nop 0
	v_addc_co_u32_e32 v65, vcc, 0, v3, vcc
	global_load_dwordx2 v[128:129], v[128:129], off nt
	s_mov_b32 s9, 0x92000
	global_load_dwordx2 v[130:131], v[130:131], off nt
	v_add_co_u32_e32 v66, vcc, s9, v2
	global_load_dwordx2 v[126:127], v[126:127], off nt
	s_nop 0
	v_addc_co_u32_e32 v67, vcc, 0, v3, vcc
	global_load_dwordx2 v[134:135], v[134:135], off nt
	v_add_co_u32_e32 v68, vcc, s90, v2
	global_load_dwordx2 v[136:137], v[136:137], off nt
	s_nop 0
	v_addc_co_u32_e32 v69, vcc, 0, v3, vcc
	global_load_dwordx2 v[138:139], v[138:139], off nt
	s_mov_b32 s9, 0x96000
	global_load_dwordx2 v[132:133], v[132:133], off nt
	v_add_co_u32_e32 v70, vcc, s9, v2
	global_load_dwordx2 v[140:141], v[140:141], off nt
	s_nop 0
	v_addc_co_u32_e32 v71, vcc, 0, v3, vcc
	global_load_dwordx2 v[142:143], v[142:143], off nt
	v_add_co_u32_e32 v72, vcc, s92, v2
	s_mov_b32 s9, 0x9a000
	s_nop 0
	v_addc_co_u32_e32 v73, vcc, 0, v3, vcc
	v_add_co_u32_e32 v74, vcc, s9, v2
	s_mov_b32 s9, 0x9e000
	s_nop 0
	v_addc_co_u32_e32 v75, vcc, 0, v3, vcc
	v_add_co_u32_e32 v76, vcc, s94, v2
	v_add_u32_e32 v8, v7, v11
	s_nop 0
	v_addc_co_u32_e32 v77, vcc, 0, v3, vcc
	v_add_co_u32_e32 v78, vcc, s9, v2
	s_waitcnt vmcnt(30)
	v_mul_f32_e32 v82, 0x43800000, v82
	v_addc_co_u32_e32 v79, vcc, 0, v3, vcc
	global_load_dwordx2 v[78:79], v[78:79], off nt
	v_mul_f32_e32 v80, 0x43800000, v80
	ds_write_b128 v8, v[194:197]
	v_med3_f32 v80, v80, s79, v193
	v_med3_f32 v82, v82, s79, v193
	v_mov_b32_e32 v194, v9
	v_cvt_pk_fp8_f32 v194, v80, v82
	s_waitcnt vmcnt(29)
	v_mul_f32_e32 v80, 0x43800000, v88
	s_waitcnt vmcnt(28)
	v_mul_f32_e32 v82, 0x43800000, v90
	v_med3_f32 v80, v80, s79, v193
	v_med3_f32 v82, v82, s79, v193
	v_mov_b32_e32 v195, v9
	s_waitcnt vmcnt(27)
	v_mul_f32_e32 v84, 0x43800000, v84
	v_mul_f32_e32 v86, 0x43800000, v86
	v_cvt_pk_fp8_f32 v195, v80, v82
	s_waitcnt vmcnt(25)
	v_mul_f32_e32 v80, 0x43800000, v96
	s_waitcnt vmcnt(24)
	v_mul_f32_e32 v82, 0x43800000, v98
	v_med3_f32 v84, v84, s79, v193
	v_med3_f32 v86, v86, s79, v193
	v_med3_f32 v80, v80, s79, v193
	v_med3_f32 v82, v82, s79, v193
	v_mov_b32_e32 v196, v9
	v_cvt_pk_fp8_f32 v194, v84, v86 op_sel:[0,0,1]
	s_waitcnt vmcnt(23)
	v_mul_f32_e32 v84, 0x43800000, v92
	v_mul_f32_e32 v86, 0x43800000, v94
	v_cvt_pk_fp8_f32 v196, v80, v82
	s_waitcnt vmcnt(21)
	v_mul_f32_e32 v80, 0x43800000, v104
	s_waitcnt vmcnt(20)
	v_mul_f32_e32 v82, 0x43800000, v106
	v_med3_f32 v84, v84, s79, v193
	v_med3_f32 v86, v86, s79, v193
	v_med3_f32 v80, v80, s79, v193
	v_med3_f32 v82, v82, s79, v193
	v_mov_b32_e32 v197, v9
	v_cvt_pk_fp8_f32 v195, v84, v86 op_sel:[0,0,1]
	s_waitcnt vmcnt(19)
	v_mul_f32_e32 v84, 0x43800000, v100
	v_mul_f32_e32 v86, 0x43800000, v102
	v_cvt_pk_fp8_f32 v197, v80, v82
	v_med3_f32 v84, v84, s79, v193
	v_med3_f32 v86, v86, s79, v193
	v_cvt_pk_fp8_f32 v196, v84, v86 op_sel:[0,0,1]
	s_waitcnt vmcnt(18)
	v_mul_f32_e32 v84, 0x43800000, v108
	s_waitcnt vmcnt(17)
	v_mul_f32_e32 v86, 0x43800000, v110
	v_med3_f32 v84, v84, s79, v193
	v_med3_f32 v86, v86, s79, v193
	v_mul_f32_e32 v80, 0x43800000, v81
	v_mul_f32_e32 v81, 0x43800000, v83
	v_cvt_pk_fp8_f32 v197, v84, v86 op_sel:[0,0,1]
	v_med3_f32 v84, v80, s79, v193
	v_med3_f32 v81, v81, s79, v193
	v_mov_b32_e32 v80, v9
	v_cvt_pk_fp8_f32 v80, v84, v81
	v_mul_f32_e32 v82, 0x43800000, v85
	v_mul_f32_e32 v83, 0x43800000, v87
	v_med3_f32 v82, v82, s79, v193
	v_med3_f32 v83, v83, s79, v193
	v_cvt_pk_fp8_f32 v80, v82, v83 op_sel:[0,0,1]
	v_mul_f32_e32 v81, 0x43800000, v89
	v_mul_f32_e32 v82, 0x43800000, v91
	v_med3_f32 v85, v81, s79, v193
	v_med3_f32 v82, v82, s79, v193
	v_mov_b32_e32 v81, v9
	v_cvt_pk_fp8_f32 v81, v85, v82
	v_mul_f32_e32 v83, 0x43800000, v93
	v_mul_f32_e32 v84, 0x43800000, v95
	v_med3_f32 v83, v83, s79, v193
	v_med3_f32 v84, v84, s79, v193
	v_cvt_pk_fp8_f32 v81, v83, v84 op_sel:[0,0,1]
	v_mul_f32_e32 v82, 0x43800000, v97
	v_mul_f32_e32 v83, 0x43800000, v99
	v_med3_f32 v86, v82, s79, v193
	v_med3_f32 v83, v83, s79, v193
	v_mov_b32_e32 v82, v9
	v_cvt_pk_fp8_f32 v82, v86, v83
	v_mul_f32_e32 v84, 0x43800000, v101
	v_mul_f32_e32 v85, 0x43800000, v103
	v_med3_f32 v84, v84, s79, v193
	v_med3_f32 v85, v85, s79, v193
	v_cvt_pk_fp8_f32 v82, v84, v85 op_sel:[0,0,1]
	v_mul_f32_e32 v83, 0x43800000, v105
	v_mul_f32_e32 v84, 0x43800000, v107
	v_med3_f32 v87, v83, s79, v193
	v_med3_f32 v84, v84, s79, v193
	v_mov_b32_e32 v83, v9
	v_cvt_pk_fp8_f32 v83, v87, v84
	v_mul_f32_e32 v85, 0x43800000, v109
	v_mul_f32_e32 v86, 0x43800000, v111
	v_med3_f32 v85, v85, s79, v193
	v_med3_f32 v86, v86, s79, v193
	v_cvt_pk_fp8_f32 v83, v85, v86 op_sel:[0,0,1]
	global_load_dwordx2 v[144:145], v[144:145], off nt
	ds_write_b128 v8, v[194:197] offset:16
	global_load_dwordx2 v[146:147], v[146:147], off nt
	v_add_u32_e32 v8, v13, v11
	global_load_dwordx2 v[152:153], v[152:153], off nt
	ds_write_b128 v8, v[80:83]
	global_load_dwordx2 v[154:155], v[154:155], off nt
	v_add_co_u32_e32 v80, vcc, s96, v2
	s_mov_b32 s9, 0xa2000
; #define CV_LOAD(v, kb) do { _Pragma("unroll") for (int j = 0; j < 16; ++j) v[j] = __builtin_nontemporal_load((const f32x2*)(src + (size_t)((kb) * 16 + j) * ldw)); } while (0)
; __device__ __forceinline__ void tr128_f8(const float* W, int ldw, int srccol, unsigned char* WT, size_t dstrow0, int K, int k0, LAS unsigned char* tile, int lane) {
;     ...
;     CV_LOAD(va, 0); CV_LOAD(vb, 1); CV_LOAD(vc, 2);
;     CV_LOAD(vd, 3); CV_PUT(va, 0); CV_LOAD(va, 4); CV_PUT(vb, 1); CV_LOAD(vb, 5); CV_PUT(vc, 2); CV_LOAD(vc, 6); CV_PUT(vd, 3); CV_LOAD(vd, 7);
;     CV_PUT(va, 4); CV_PUT(vb, 5); CV_PUT(vc, 6); CV_PUT(vd, 7);
	s_nop 0
	v_addc_co_u32_e32 v81, vcc, 0, v3, vcc
	global_load_dwordx2 v[148:149], v[148:149], off nt
	v_add_co_u32_e32 v82, vcc, s9, v2
	global_load_dwordx2 v[150:151], v[150:151], off nt
	s_nop 0
	v_addc_co_u32_e32 v83, vcc, 0, v3, vcc
	global_load_dwordx2 v[160:161], v[160:161], off nt
	v_add_co_u32_e32 v84, vcc, s4, v2
	global_load_dwordx2 v[164:165], v[164:165], off nt
	s_nop 0
	v_addc_co_u32_e32 v85, vcc, 0, v3, vcc
	global_load_dwordx2 v[156:157], v[156:157], off nt
	s_mov_b32 s9, 0xa6000
	global_load_dwordx2 v[158:159], v[158:159], off nt
	v_add_co_u32_e32 v86, vcc, s9, v2
	global_load_dwordx2 v[170:171], v[170:171], off nt
	s_nop 0
	v_addc_co_u32_e32 v87, vcc, 0, v3, vcc
	global_load_dwordx2 v[172:173], v[172:173], off nt
	v_add_co_u32_e32 v88, vcc, s14, v2
	global_load_dwordx2 v[166:167], v[166:167], off nt
	s_nop 0
	v_addc_co_u32_e32 v89, vcc, 0, v3, vcc
	global_load_dwordx2 v[168:169], v[168:169], off nt
	s_mov_b32 s9, 0xaa000
	global_load_dwordx2 v[174:175], v[174:175], off nt
	v_add_co_u32_e32 v90, vcc, s9, v2
	global_load_dwordx2 v[176:177], v[176:177], off nt
	s_nop 0
	v_addc_co_u32_e32 v91, vcc, 0, v3, vcc
	v_add_co_u32_e32 v92, vcc, s18, v2
	s_mov_b32 s9, 0xae000
	s_nop 0
	v_addc_co_u32_e32 v93, vcc, 0, v3, vcc
	global_load_dwordx2 v[88:89], v[88:89], off nt
	v_mov_b32_e32 v194, v9
	global_load_dwordx2 v[90:91], v[90:91], off nt
	v_mov_b32_e32 v195, v9
	global_load_dwordx2 v[94:95], v[92:93], off nt
	v_add_co_u32_e32 v92, vcc, s9, v2
	s_mov_b32 s9, 0xb2000
	s_nop 0
	v_addc_co_u32_e32 v93, vcc, 0, v3, vcc
	global_load_dwordx2 v[100:101], v[92:93], off nt
	v_add_co_u32_e32 v92, vcc, s5, v2
	s_waitcnt vmcnt(36)
	v_mul_f32_e32 v8, 0x43800000, v112
	v_addc_co_u32_e32 v93, vcc, 0, v3, vcc
	v_add_co_u32_e32 v96, vcc, s9, v2
	s_waitcnt vmcnt(35)
	v_mul_f32_e32 v112, 0x43800000, v114
	v_addc_co_u32_e32 v97, vcc, 0, v3, vcc
	v_add_co_u32_e32 v98, vcc, s54, v2
	s_mov_b32 s9, 0xb6000
	s_nop 0
	v_addc_co_u32_e32 v99, vcc, 0, v3, vcc
	v_med3_f32 v8, v8, s79, v193
	v_med3_f32 v112, v112, s79, v193
	global_load_dwordx2 v[92:93], v[92:93], off nt
	v_cvt_pk_fp8_f32 v194, v8, v112
	global_load_dwordx2 v[96:97], v[96:97], off nt
	s_waitcnt vmcnt(36)
	v_mul_f32_e32 v8, 0x43800000, v120
	global_load_dwordx2 v[102:103], v[98:99], off nt
	v_add_co_u32_e32 v98, vcc, s9, v2
	s_waitcnt vmcnt(36)
	v_mul_f32_e32 v112, 0x43800000, v122
	v_addc_co_u32_e32 v99, vcc, 0, v3, vcc
	v_med3_f32 v8, v8, s79, v193
	v_med3_f32 v112, v112, s79, v193
	global_load_dwordx2 v[106:107], v[98:99], off nt
	s_waitcnt vmcnt(36)
	v_mul_f32_e32 v114, 0x43800000, v116
	s_waitcnt vmcnt(35)
	v_mul_f32_e32 v116, 0x43800000, v118
	v_cvt_pk_fp8_f32 v195, v8, v112
	s_waitcnt vmcnt(33)
	v_mul_f32_e32 v8, 0x43800000, v128
	s_waitcnt vmcnt(32)
	v_mul_f32_e32 v112, 0x43800000, v130
	v_med3_f32 v114, v114, s79, v193
	v_med3_f32 v116, v116, s79, v193
	v_med3_f32 v8, v8, s79, v193
	v_med3_f32 v112, v112, s79, v193
	v_mov_b32_e32 v196, v9
	v_cvt_pk_fp8_f32 v194, v114, v116 op_sel:[0,0,1]
	v_mul_f32_e32 v114, 0x43800000, v124
	s_waitcnt vmcnt(31)
	v_mul_f32_e32 v116, 0x43800000, v126
	v_cvt_pk_fp8_f32 v196, v8, v112
	s_waitcnt vmcnt(29)
	v_mul_f32_e32 v8, 0x43800000, v136
	s_waitcnt vmcnt(28)
	v_mul_f32_e32 v112, 0x43800000, v138
	v_med3_f32 v114, v114, s79, v193
	v_med3_f32 v116, v116, s79, v193
	v_med3_f32 v8, v8, s79, v193
	v_med3_f32 v112, v112, s79, v193
	v_mov_b32_e32 v197, v9
	v_cvt_pk_fp8_f32 v195, v114, v116 op_sel:[0,0,1]
	s_waitcnt vmcnt(27)
	v_mul_f32_e32 v114, 0x43800000, v132
	v_mul_f32_e32 v116, 0x43800000, v134
	v_cvt_pk_fp8_f32 v197, v8, v112
	v_mul_f32_e32 v8, 0x43800000, v113
	v_mul_f32_e32 v112, 0x43800000, v115
	v_med3_f32 v114, v114, s79, v193
	v_med3_f32 v116, v116, s79, v193
	v_med3_f32 v8, v8, s79, v193
	v_med3_f32 v115, v112, s79, v193
	v_mov_b32_e32 v112, v9
	v_cvt_pk_fp8_f32 v196, v114, v116 op_sel:[0,0,1]
	s_waitcnt vmcnt(26)
	v_mul_f32_e32 v114, 0x43800000, v140
	s_waitcnt vmcnt(25)
	v_mul_f32_e32 v116, 0x43800000, v142
	v_cvt_pk_fp8_f32 v112, v8, v115
	v_med3_f32 v114, v114, s79, v193
	v_med3_f32 v116, v116, s79, v193
	v_cvt_pk_fp8_f32 v197, v114, v116 op_sel:[0,0,1]
	v_mul_f32_e32 v113, 0x43800000, v117
	v_mul_f32_e32 v114, 0x43800000, v119
	v_med3_f32 v113, v113, s79, v193
	v_med3_f32 v114, v114, s79, v193
	v_cvt_pk_fp8_f32 v112, v113, v114 op_sel:[0,0,1]
	v_mul_f32_e32 v8, 0x43800000, v121
	v_mul_f32_e32 v113, 0x43800000, v123
	v_med3_f32 v8, v8, s79, v193
	v_med3_f32 v116, v113, s79, v193
	v_mov_b32_e32 v113, v9
	v_cvt_pk_fp8_f32 v113, v8, v116
	v_mul_f32_e32 v114, 0x43800000, v125
	v_mul_f32_e32 v115, 0x43800000, v127
	v_med3_f32 v114, v114, s79, v193
	v_med3_f32 v115, v115, s79, v193
	v_cvt_pk_fp8_f32 v113, v114, v115 op_sel:[0,0,1]
	v_mul_f32_e32 v8, 0x43800000, v129
	v_mul_f32_e32 v114, 0x43800000, v131
	v_med3_f32 v8, v8, s79, v193
	v_med3_f32 v117, v114, s79, v193
	v_mov_b32_e32 v114, v9
	v_cvt_pk_fp8_f32 v114, v8, v117
	v_mul_f32_e32 v115, 0x43800000, v133
	v_mul_f32_e32 v116, 0x43800000, v135
	v_med3_f32 v115, v115, s79, v193
	v_med3_f32 v116, v116, s79, v193
	v_cvt_pk_fp8_f32 v114, v115, v116 op_sel:[0,0,1]
	v_mul_f32_e32 v8, 0x43800000, v137
	v_mul_f32_e32 v115, 0x43800000, v139
	v_med3_f32 v8, v8, s79, v193
	v_med3_f32 v118, v115, s79, v193
	v_mov_b32_e32 v115, v9
	v_add_co_u32_e32 v98, vcc, s30, v2
	v_cvt_pk_fp8_f32 v115, v8, v118
	s_nop 0
	v_addc_co_u32_e32 v99, vcc, 0, v3, vcc
	s_mov_b32 s9, 0xba000
	v_add_co_u32_e32 v104, vcc, s9, v2
	v_mul_f32_e32 v116, 0x43800000, v141
	v_mul_f32_e32 v117, 0x43800000, v143
	v_addc_co_u32_e32 v105, vcc, 0, v3, vcc
	v_med3_f32 v116, v116, s79, v193
	v_med3_f32 v117, v117, s79, v193
	v_add_co_u32_e32 v108, vcc, s15, v2
	v_cvt_pk_fp8_f32 v115, v116, v117 op_sel:[0,0,1]
	s_nop 0
	v_addc_co_u32_e32 v109, vcc, 0, v3, vcc
	s_mov_b32 s9, 0xbe000
	v_add_co_u32_e32 v110, vcc, s9, v2
	v_add_u32_e32 v116, v13, v19
	s_nop 0
	v_addc_co_u32_e32 v111, vcc, 0, v3, vcc
	ds_write_b128 v116, v[112:115]
	v_add_co_u32_e32 v112, vcc, s17, v2
	s_mov_b32 s9, 0xc2000
	s_nop 0
	v_addc_co_u32_e32 v113, vcc, 0, v3, vcc
	v_add_co_u32_e32 v114, vcc, s9, v2
	s_mov_b32 s9, 0xc6000
	s_nop 0
	v_addc_co_u32_e32 v115, vcc, 0, v3, vcc
	v_add_co_u32_e32 v116, vcc, s19, v2
	global_load_dwordx2 v[112:113], v[112:113], off nt
	s_nop 0
	v_addc_co_u32_e32 v117, vcc, 0, v3, vcc
	global_load_dwordx2 v[114:115], v[114:115], off nt
	v_add_u32_e32 v8, v7, v17
	global_load_dwordx2 v[118:119], v[116:117], off nt
	v_add_co_u32_e32 v116, vcc, s9, v2
	s_mov_b32 s9, 0xca000
	s_nop 0
	v_addc_co_u32_e32 v117, vcc, 0, v3, vcc
	global_load_dwordx2 v[124:125], v[116:117], off nt
	v_add_co_u32_e32 v116, vcc, s28, v2
	global_load_dwordx2 v[4:5], v[4:5], off nt
	s_nop 0
	v_addc_co_u32_e32 v117, vcc, 0, v3, vcc
	v_add_co_u32_e32 v120, vcc, s9, v2
	global_load_dwordx2 v[50:51], v[50:51], off nt
	s_nop 0
	v_addc_co_u32_e32 v121, vcc, 0, v3, vcc
	v_add_co_u32_e32 v122, vcc, s52, v2
	s_mov_b32 s9, 0xce000
	s_nop 0
	v_addc_co_u32_e32 v123, vcc, 0, v3, vcc
	global_load_dwordx2 v[116:117], v[116:117], off nt
	s_waitcnt vmcnt(30)
; #define CV_LOAD(v, kb) do { _Pragma("unroll") for (int j = 0; j < 16; ++j) v[j] = __builtin_nontemporal_load((const f32x2*)(src + (size_t)((kb) * 16 + j) * ldw)); } while (0)
; __device__ __forceinline__ void tr128_f8(const float* W, int ldw, int srccol, unsigned char* WT, size_t dstrow0, int K, int k0, LAS unsigned char* tile, int lane) {
;     ...
;     CV_LOAD(va, 0); CV_LOAD(vb, 1); CV_LOAD(vc, 2);
;     CV_LOAD(vd, 3); CV_PUT(va, 0); CV_LOAD(va, 4); CV_PUT(vb, 1); CV_LOAD(vb, 5); CV_PUT(vc, 2); CV_LOAD(vc, 6); CV_PUT(vd, 3); CV_LOAD(vd, 7);
;     CV_PUT(va, 4); CV_PUT(vb, 5); CV_PUT(vc, 6); CV_PUT(vd, 7);
	v_mul_f32_e32 v144, 0x43800000, v144
	global_load_dwordx2 v[120:121], v[120:121], off nt
	s_waitcnt vmcnt(30)
	v_mul_f32_e32 v146, 0x43800000, v146
	global_load_dwordx2 v[126:127], v[122:123], off nt
	v_add_co_u32_e32 v122, vcc, s9, v2
	global_load_dwordx2 v[54:55], v[54:55], off nt
	s_nop 0
	v_addc_co_u32_e32 v123, vcc, 0, v3, vcc
	global_load_dwordx2 v[56:57], v[56:57], off nt
	s_mov_b32 s9, 0xd2000
	global_load_dwordx2 v[58:59], v[58:59], off nt
	ds_write_b128 v8, v[194:197]
	global_load_dwordx2 v[132:133], v[122:123], off nt
	v_add_co_u32_e32 v122, vcc, s56, v2
	global_load_dwordx2 v[52:53], v[52:53], off nt
	s_nop 0
	v_addc_co_u32_e32 v123, vcc, 0, v3, vcc
	global_load_dwordx2 v[62:63], v[62:63], off nt
	v_add_co_u32_e32 v128, vcc, s9, v2
	global_load_dwordx2 v[64:65], v[64:65], off nt
	s_nop 0
	v_addc_co_u32_e32 v129, vcc, 0, v3, vcc
	global_load_dwordx2 v[66:67], v[66:67], off nt
	v_add_co_u32_e32 v130, vcc, s60, v2
	global_load_dwordx2 v[60:61], v[60:61], off nt
	s_nop 0
	v_addc_co_u32_e32 v131, vcc, 0, v3, vcc
	global_load_dwordx2 v[70:71], v[70:71], off nt
	s_mov_b32 s9, 0xd6000
	global_load_dwordx2 v[72:73], v[72:73], off nt
	v_med3_f32 v144, v144, s79, v193
	global_load_dwordx2 v[74:75], v[74:75], off nt
	v_med3_f32 v146, v146, s79, v193
	global_load_dwordx2 v[68:69], v[68:69], off nt
	v_mov_b32_e32 v194, v9
	global_load_dwordx2 v[122:123], v[122:123], off nt
	v_cvt_pk_fp8_f32 v194, v144, v146
	global_load_dwordx2 v[128:129], v[128:129], off nt
	v_mov_b32_e32 v195, v9
	global_load_dwordx2 v[134:135], v[130:131], off nt
	v_add_co_u32_e32 v130, vcc, s9, v2
	global_load_dwordx2 v[76:77], v[76:77], off nt
	s_nop 0
	v_addc_co_u32_e32 v131, vcc, 0, v3, vcc
	global_load_dwordx2 v[138:139], v[130:131], off nt
	s_waitcnt vmcnt(48)
	v_mul_f32_e32 v144, 0x43800000, v152
	s_waitcnt vmcnt(47)
	v_mul_f32_e32 v146, 0x43800000, v154
	v_med3_f32 v144, v144, s79, v193
	v_med3_f32 v146, v146, s79, v193
	s_waitcnt vmcnt(46)
	v_mul_f32_e32 v148, 0x43800000, v148
	s_waitcnt vmcnt(45)
	v_mul_f32_e32 v150, 0x43800000, v150
	v_cvt_pk_fp8_f32 v195, v144, v146
	s_waitcnt vmcnt(44)
	v_mul_f32_e32 v144, 0x43800000, v160
	s_waitcnt vmcnt(43)
	v_mul_f32_e32 v146, 0x43800000, v164
	v_med3_f32 v148, v148, s79, v193
	v_med3_f32 v150, v150, s79, v193
	v_med3_f32 v144, v144, s79, v193
	v_med3_f32 v146, v146, s79, v193
	v_mov_b32_e32 v196, v9
	v_cvt_pk_fp8_f32 v194, v148, v150 op_sel:[0,0,1]
	s_waitcnt vmcnt(42)
	v_mul_f32_e32 v148, 0x43800000, v156
	s_waitcnt vmcnt(41)
	v_mul_f32_e32 v150, 0x43800000, v158
	v_cvt_pk_fp8_f32 v196, v144, v146
	s_waitcnt vmcnt(40)
	v_mul_f32_e32 v144, 0x43800000, v170
	s_waitcnt vmcnt(39)
	v_mul_f32_e32 v146, 0x43800000, v172
	v_med3_f32 v148, v148, s79, v193
	v_med3_f32 v150, v150, s79, v193
	v_med3_f32 v144, v144, s79, v193
	v_med3_f32 v146, v146, s79, v193
	v_mov_b32_e32 v197, v9
	v_cvt_pk_fp8_f32 v195, v148, v150 op_sel:[0,0,1]
	s_waitcnt vmcnt(38)
	v_mul_f32_e32 v148, 0x43800000, v166
	s_waitcnt vmcnt(37)
	v_mul_f32_e32 v150, 0x43800000, v168
	v_cvt_pk_fp8_f32 v197, v144, v146
	v_med3_f32 v148, v148, s79, v193
	v_med3_f32 v150, v150, s79, v193
	v_cvt_pk_fp8_f32 v196, v148, v150 op_sel:[0,0,1]
	s_waitcnt vmcnt(36)
	v_mul_f32_e32 v148, 0x43800000, v174
	s_waitcnt vmcnt(35)
	v_mul_f32_e32 v150, 0x43800000, v176
	v_med3_f32 v148, v148, s79, v193
	v_med3_f32 v150, v150, s79, v193
	v_mul_f32_e32 v144, 0x43800000, v145
	v_mul_f32_e32 v145, 0x43800000, v147
	v_cvt_pk_fp8_f32 v197, v148, v150 op_sel:[0,0,1]
	v_med3_f32 v148, v144, s79, v193
	v_med3_f32 v145, v145, s79, v193
	v_mov_b32_e32 v144, v9
	v_cvt_pk_fp8_f32 v144, v148, v145
	v_mul_f32_e32 v146, 0x43800000, v149
	v_mul_f32_e32 v147, 0x43800000, v151
	v_med3_f32 v146, v146, s79, v193
	v_med3_f32 v147, v147, s79, v193
	v_cvt_pk_fp8_f32 v144, v146, v147 op_sel:[0,0,1]
	v_mul_f32_e32 v145, 0x43800000, v153
	v_mul_f32_e32 v146, 0x43800000, v155
	v_med3_f32 v149, v145, s79, v193
	v_med3_f32 v146, v146, s79, v193
	v_mov_b32_e32 v145, v9
	v_cvt_pk_fp8_f32 v145, v149, v146
	v_mul_f32_e32 v147, 0x43800000, v157
	v_mul_f32_e32 v148, 0x43800000, v159
	v_med3_f32 v147, v147, s79, v193
	v_med3_f32 v148, v148, s79, v193
	v_cvt_pk_fp8_f32 v145, v147, v148 op_sel:[0,0,1]
	v_mul_f32_e32 v146, 0x43800000, v161
	v_mul_f32_e32 v147, 0x43800000, v165
	v_med3_f32 v150, v146, s79, v193
	v_med3_f32 v147, v147, s79, v193
	v_mov_b32_e32 v146, v9
	v_cvt_pk_fp8_f32 v146, v150, v147
	v_mul_f32_e32 v148, 0x43800000, v167
	v_mul_f32_e32 v149, 0x43800000, v169
	v_med3_f32 v148, v148, s79, v193
	v_med3_f32 v149, v149, s79, v193
	v_cvt_pk_fp8_f32 v146, v148, v149 op_sel:[0,0,1]
	v_mul_f32_e32 v147, 0x43800000, v171
	v_mul_f32_e32 v148, 0x43800000, v173
	v_med3_f32 v151, v147, s79, v193
	v_med3_f32 v148, v148, s79, v193
	v_mov_b32_e32 v147, v9
	global_load_dwordx2 v[80:81], v[80:81], off nt
	v_add_co_u32_e32 v130, vcc, s64, v2
	global_load_dwordx2 v[82:83], v[82:83], off nt
	v_cvt_pk_fp8_f32 v147, v151, v148
	global_load_dwordx2 v[84:85], v[84:85], off nt
	v_addc_co_u32_e32 v131, vcc, 0, v3, vcc
	s_mov_b32 s9, 0xda000
	v_add_co_u32_e32 v136, vcc, s9, v2
	v_mul_f32_e32 v149, 0x43800000, v175
	v_mul_f32_e32 v150, 0x43800000, v177
	v_addc_co_u32_e32 v137, vcc, 0, v3, vcc
	v_med3_f32 v149, v149, s79, v193
	v_med3_f32 v150, v150, s79, v193
	global_load_dwordx2 v[86:87], v[86:87], off nt
	v_add_co_u32_e32 v140, vcc, s68, v2
	v_cvt_pk_fp8_f32 v147, v149, v150 op_sel:[0,0,1]
	s_nop 0
	v_addc_co_u32_e32 v141, vcc, 0, v3, vcc
	s_mov_b32 s9, 0xde000
	v_add_co_u32_e32 v142, vcc, s9, v2
	ds_write_b128 v8, v[194:197] offset:16
	s_nop 0
	v_addc_co_u32_e32 v143, vcc, 0, v3, vcc
	v_add_u32_e32 v8, v13, v21
	ds_write_b128 v8, v[144:147]
	v_add_co_u32_e32 v144, vcc, s72, v2
	s_mov_b32 s9, 0xe2000
	s_nop 0
	v_addc_co_u32_e32 v145, vcc, 0, v3, vcc
	v_add_co_u32_e32 v146, vcc, s9, v2
	s_mov_b32 s9, 0xe6000
	s_nop 0
	v_addc_co_u32_e32 v147, vcc, 0, v3, vcc
	v_add_co_u32_e32 v148, vcc, s76, v2
	global_load_dwordx2 v[144:145], v[144:145], off nt
	s_nop 0
	v_addc_co_u32_e32 v149, vcc, 0, v3, vcc
	global_load_dwordx2 v[146:147], v[146:147], off nt
	s_waitcnt vmcnt(27)
; #define CV_LOAD(v, kb) do { _Pragma("unroll") for (int j = 0; j < 16; ++j) v[j] = __builtin_nontemporal_load((const f32x2*)(src + (size_t)((kb) * 16 + j) * ldw)); } while (0)
; __device__ __forceinline__ void tr128_f8(const float* W, int ldw, int srccol, unsigned char* WT, size_t dstrow0, int K, int k0, LAS unsigned char* tile, int lane) {
;     ...
;     CV_LOAD(va, 0); CV_LOAD(vb, 1); CV_LOAD(vc, 2);
;     CV_LOAD(vd, 3); CV_PUT(va, 0); CV_LOAD(va, 4); CV_PUT(vb, 1); CV_LOAD(vb, 5); CV_PUT(vc, 2); CV_LOAD(vc, 6); CV_PUT(vd, 3); CV_LOAD(vd, 7);
;     CV_PUT(va, 4); CV_PUT(vb, 5); CV_PUT(vc, 6); CV_PUT(vd, 7);
	v_mul_f32_e32 v8, 0x43800000, v50
	global_load_dwordx2 v[150:151], v[148:149], off nt
	v_add_co_u32_e32 v148, vcc, s9, v2
	s_mov_b32 s9, 0xea000
	s_nop 0
	v_addc_co_u32_e32 v149, vcc, 0, v3, vcc
	global_load_dwordx2 v[156:157], v[148:149], off nt
	v_add_co_u32_e32 v148, vcc, s81, v2
	global_load_dwordx2 v[98:99], v[98:99], off nt
	s_nop 0
	v_addc_co_u32_e32 v149, vcc, 0, v3, vcc
	global_load_dwordx2 v[104:105], v[104:105], off nt
	v_add_co_u32_e32 v152, vcc, s9, v2
	global_load_dwordx2 v[108:109], v[108:109], off nt
	s_nop 0
	v_addc_co_u32_e32 v153, vcc, 0, v3, vcc
	v_add_co_u32_e32 v154, vcc, s85, v2
	s_mov_b32 s9, 0xee000
	s_nop 0
	v_addc_co_u32_e32 v155, vcc, 0, v3, vcc
	global_load_dwordx2 v[110:111], v[110:111], off nt
	v_med3_f32 v8, v8, s79, v193
	global_load_dwordx2 v[148:149], v[148:149], off nt
	v_mov_b32_e32 v194, v9
	global_load_dwordx2 v[152:153], v[152:153], off nt
	v_mov_b32_e32 v195, v9
	global_load_dwordx2 v[158:159], v[154:155], off nt
	v_add_co_u32_e32 v154, vcc, s9, v2
	s_mov_b32 s9, 0xf2000
	s_nop 0
	v_addc_co_u32_e32 v155, vcc, 0, v3, vcc
	global_load_dwordx2 v[166:167], v[154:155], off nt
	v_add_co_u32_e32 v154, vcc, s89, v2
	s_waitcnt vmcnt(29)
	v_mul_f32_e32 v50, 0x43800000, v52
	v_addc_co_u32_e32 v155, vcc, 0, v3, vcc
	v_add_co_u32_e32 v160, vcc, s9, v2
	s_mov_b32 s9, 0xf6000
	s_nop 0
	v_addc_co_u32_e32 v161, vcc, 0, v3, vcc
	v_add_co_u32_e32 v164, vcc, s93, v2
	global_load_dwordx2 v[154:155], v[154:155], off nt
	s_nop 0
	v_addc_co_u32_e32 v165, vcc, 0, v3, vcc
	global_load_dwordx2 v[160:161], v[160:161], off nt
	v_mul_f32_e32 v52, 0x43800000, v54
	global_load_dwordx2 v[168:169], v[164:165], off nt
	v_add_co_u32_e32 v164, vcc, s9, v2
	s_mov_b32 s9, 0xfa000
	s_nop 0
	v_addc_co_u32_e32 v165, vcc, 0, v3, vcc
	global_load_dwordx2 v[172:173], v[164:165], off nt
	v_add_co_u32_e32 v164, vcc, s97, v2
	v_med3_f32 v50, v50, s79, v193
	s_nop 0
	v_addc_co_u32_e32 v165, vcc, 0, v3, vcc
	v_add_co_u32_e32 v170, vcc, s9, v2
	s_mov_b32 s9, 0xfe000
	s_nop 0
	v_addc_co_u32_e32 v171, vcc, 0, v3, vcc
	v_add_co_u32_e32 v174, vcc, s16, v2
	v_med3_f32 v52, v52, s79, v193
	s_nop 0
	v_addc_co_u32_e32 v175, vcc, 0, v3, vcc
	v_add_co_u32_e32 v2, vcc, s9, v2
	v_mov_b32_e32 v196, v9
	s_nop 0
	v_addc_co_u32_e32 v3, vcc, 0, v3, vcc
	global_load_dwordx2 v[2:3], v[2:3], off nt
	v_mul_f32_e32 v4, 0x43800000, v4
	v_med3_f32 v4, v4, s79, v193
	v_cvt_pk_fp8_f32 v194, v4, v8
	v_mul_f32_e32 v4, 0x43800000, v56
	v_mul_f32_e32 v8, 0x43800000, v58
	v_med3_f32 v4, v4, s79, v193
	v_med3_f32 v8, v8, s79, v193
	v_cvt_pk_fp8_f32 v195, v4, v8
	s_waitcnt vmcnt(32)
	v_mul_f32_e32 v4, 0x43800000, v64
	s_waitcnt vmcnt(31)
	v_mul_f32_e32 v8, 0x43800000, v66
	v_med3_f32 v4, v4, s79, v193
	v_med3_f32 v8, v8, s79, v193
	v_cvt_pk_fp8_f32 v194, v50, v52 op_sel:[0,0,1]
	s_waitcnt vmcnt(30)
	v_mul_f32_e32 v50, 0x43800000, v60
	v_mul_f32_e32 v52, 0x43800000, v62
	v_cvt_pk_fp8_f32 v196, v4, v8
	s_waitcnt vmcnt(28)
	v_mul_f32_e32 v4, 0x43800000, v72
	s_waitcnt vmcnt(27)
	v_mul_f32_e32 v8, 0x43800000, v74
	v_med3_f32 v50, v50, s79, v193
	v_med3_f32 v52, v52, s79, v193
	v_med3_f32 v4, v4, s79, v193
	v_med3_f32 v8, v8, s79, v193
	v_mov_b32_e32 v197, v9
	v_cvt_pk_fp8_f32 v195, v50, v52 op_sel:[0,0,1]
	s_waitcnt vmcnt(26)
	v_mul_f32_e32 v50, 0x43800000, v68
	v_mul_f32_e32 v52, 0x43800000, v70
	v_cvt_pk_fp8_f32 v197, v4, v8
	v_med3_f32 v50, v50, s79, v193
	v_med3_f32 v52, v52, s79, v193
	v_cvt_pk_fp8_f32 v196, v50, v52 op_sel:[0,0,1]
	s_waitcnt vmcnt(22)
	v_mul_f32_e32 v50, 0x43800000, v76
	v_mul_f32_e32 v52, 0x43800000, v78
	v_med3_f32 v50, v50, s79, v193
	v_med3_f32 v52, v52, s79, v193
	v_cvt_pk_fp8_f32 v197, v50, v52 op_sel:[0,0,1]
	v_mul_f32_e32 v4, 0x43800000, v5
	v_mul_f32_e32 v5, 0x43800000, v51
	v_mul_f32_e32 v50, 0x43800000, v55
	v_med3_f32 v4, v4, s79, v193
	v_med3_f32 v5, v5, s79, v193
	v_med3_f32 v51, v50, s79, v193
	v_mov_b32_e32 v50, v9
	v_cvt_pk_fp8_f32 v50, v4, v5
	v_mul_f32_e32 v8, 0x43800000, v53
	v_med3_f32 v8, v8, s79, v193
	v_mul_f32_e32 v4, 0x43800000, v57
	v_cvt_pk_fp8_f32 v50, v8, v51 op_sel:[0,0,1]
	v_mul_f32_e32 v5, 0x43800000, v59
	v_mul_f32_e32 v51, 0x43800000, v63
	v_med3_f32 v4, v4, s79, v193
	v_med3_f32 v5, v5, s79, v193
	v_med3_f32 v52, v51, s79, v193
	v_mov_b32_e32 v51, v9
	v_cvt_pk_fp8_f32 v51, v4, v5
	v_mul_f32_e32 v8, 0x43800000, v61
	v_med3_f32 v8, v8, s79, v193
	v_mul_f32_e32 v4, 0x43800000, v65
	v_cvt_pk_fp8_f32 v51, v8, v52 op_sel:[0,0,1]
	v_mul_f32_e32 v5, 0x43800000, v67
	v_mul_f32_e32 v52, 0x43800000, v71
	v_med3_f32 v4, v4, s79, v193
	v_med3_f32 v5, v5, s79, v193
	v_med3_f32 v53, v52, s79, v193
	v_mov_b32_e32 v52, v9
	v_cvt_pk_fp8_f32 v52, v4, v5
	v_mul_f32_e32 v8, 0x43800000, v69
	v_med3_f32 v8, v8, s79, v193
	global_load_dwordx2 v[130:131], v[130:131], off nt
	v_cvt_pk_fp8_f32 v52, v8, v53 op_sel:[0,0,1]
	global_load_dwordx2 v[136:137], v[136:137], off nt
	v_mul_f32_e32 v4, 0x43800000, v73
	global_load_dwordx2 v[140:141], v[140:141], off nt
	v_mul_f32_e32 v5, 0x43800000, v75
	global_load_dwordx2 v[142:143], v[142:143], off nt
	v_mul_f32_e32 v53, 0x43800000, v79
	v_med3_f32 v4, v4, s79, v193
	v_med3_f32 v5, v5, s79, v193
	v_med3_f32 v54, v53, s79, v193
	v_mov_b32_e32 v53, v9
	v_cvt_pk_fp8_f32 v53, v4, v5
	v_mul_f32_e32 v8, 0x43800000, v77
	v_med3_f32 v8, v8, s79, v193
	v_add_u32_e32 v5, v13, v25
	v_cvt_pk_fp8_f32 v53, v8, v54 op_sel:[0,0,1]
	s_waitcnt vmcnt(23)
	v_mul_f32_e32 v8, 0x43800000, v82
	v_med3_f32 v8, v8, s79, v193
	global_load_dwordx2 v[164:165], v[164:165], off nt
	ds_write_b128 v5, v[50:53]
	v_mul_f32_e32 v5, 0x43800000, v80
	s_waitcnt vmcnt(23)
; #define CV_LOAD(v, kb) do { _Pragma("unroll") for (int j = 0; j < 16; ++j) v[j] = __builtin_nontemporal_load((const f32x2*)(src + (size_t)((kb) * 16 + j) * ldw)); } while (0)
; __device__ __forceinline__ void tr128_f8(const float* W, int ldw, int srccol, unsigned char* WT, size_t dstrow0, int K, int k0, LAS unsigned char* tile, int lane) {
;     ...
;     CV_LOAD(va, 0); CV_LOAD(vb, 1); CV_LOAD(vc, 2);
;     CV_LOAD(vd, 3); CV_PUT(va, 0); CV_LOAD(va, 4); CV_PUT(vb, 1); CV_LOAD(vb, 5); CV_PUT(vc, 2); CV_LOAD(vc, 6); CV_PUT(vd, 3); CV_LOAD(vd, 7);
;     CV_PUT(va, 4); CV_PUT(vb, 5); CV_PUT(vc, 6); CV_PUT(vd, 7);
	v_mul_f32_e32 v50, 0x43800000, v84
	v_med3_f32 v5, v5, s79, v193
	v_med3_f32 v52, v50, s79, v193
	v_mov_b32_e32 v50, v9
	v_cvt_pk_fp8_f32 v50, v5, v8
	s_waitcnt vmcnt(22)
	v_mul_f32_e32 v51, 0x43800000, v86
	v_med3_f32 v51, v51, s79, v193
	v_mul_f32_e32 v5, 0x43800000, v88
	v_cvt_pk_fp8_f32 v50, v52, v51 op_sel:[0,0,1]
	v_mul_f32_e32 v8, 0x43800000, v90
	v_mul_f32_e32 v51, 0x43800000, v94
	v_med3_f32 v5, v5, s79, v193
	v_med3_f32 v8, v8, s79, v193
	v_med3_f32 v53, v51, s79, v193
	v_mov_b32_e32 v51, v9
	v_cvt_pk_fp8_f32 v51, v5, v8
	v_mul_f32_e32 v52, 0x43800000, v100
	v_med3_f32 v52, v52, s79, v193
	v_mul_f32_e32 v5, 0x43800000, v92
	v_cvt_pk_fp8_f32 v51, v53, v52 op_sel:[0,0,1]
	v_mul_f32_e32 v8, 0x43800000, v96
	v_mul_f32_e32 v52, 0x43800000, v102
	v_med3_f32 v5, v5, s79, v193
	v_med3_f32 v8, v8, s79, v193
	v_med3_f32 v54, v52, s79, v193
	v_mov_b32_e32 v52, v9
	v_cvt_pk_fp8_f32 v52, v5, v8
	v_mul_f32_e32 v53, 0x43800000, v106
	v_med3_f32 v53, v53, s79, v193
	s_waitcnt vmcnt(17)
	v_mul_f32_e32 v5, 0x43800000, v98
	v_cvt_pk_fp8_f32 v52, v54, v53 op_sel:[0,0,1]
	s_waitcnt vmcnt(16)
	v_mul_f32_e32 v8, 0x43800000, v104
	s_waitcnt vmcnt(15)
	v_mul_f32_e32 v53, 0x43800000, v108
	v_med3_f32 v5, v5, s79, v193
	v_med3_f32 v8, v8, s79, v193
	v_med3_f32 v55, v53, s79, v193
	v_mov_b32_e32 v53, v9
	v_cvt_pk_fp8_f32 v53, v5, v8
	s_waitcnt vmcnt(14)
	v_mul_f32_e32 v54, 0x43800000, v110
	v_med3_f32 v54, v54, s79, v193
	v_mul_f32_e32 v5, 0x43800000, v81
	v_cvt_pk_fp8_f32 v53, v55, v54 op_sel:[0,0,1]
	v_mul_f32_e32 v8, 0x43800000, v83
	v_mul_f32_e32 v54, 0x43800000, v85
	v_med3_f32 v5, v5, s79, v193
	v_med3_f32 v8, v8, s79, v193
	v_med3_f32 v56, v54, s79, v193
	v_mov_b32_e32 v54, v9
	v_cvt_pk_fp8_f32 v54, v5, v8
	v_mul_f32_e32 v55, 0x43800000, v87
	v_med3_f32 v55, v55, s79, v193
	v_mul_f32_e32 v5, 0x43800000, v89
	v_cvt_pk_fp8_f32 v54, v56, v55 op_sel:[0,0,1]
	v_mul_f32_e32 v8, 0x43800000, v91
	v_mul_f32_e32 v55, 0x43800000, v95
	v_med3_f32 v5, v5, s79, v193
	v_med3_f32 v8, v8, s79, v193
	v_med3_f32 v57, v55, s79, v193
	v_mov_b32_e32 v55, v9
	v_cvt_pk_fp8_f32 v55, v5, v8
	v_mul_f32_e32 v56, 0x43800000, v101
	v_med3_f32 v56, v56, s79, v193
	v_mul_f32_e32 v5, 0x43800000, v93
	v_cvt_pk_fp8_f32 v55, v57, v56 op_sel:[0,0,1]
	v_mul_f32_e32 v8, 0x43800000, v97
	v_mul_f32_e32 v56, 0x43800000, v103
	v_med3_f32 v5, v5, s79, v193
	v_med3_f32 v8, v8, s79, v193
	v_med3_f32 v58, v56, s79, v193
	v_mov_b32_e32 v56, v9
	v_cvt_pk_fp8_f32 v56, v5, v8
	v_mul_f32_e32 v57, 0x43800000, v107
	v_med3_f32 v57, v57, s79, v193
	global_load_dwordx2 v[170:171], v[170:171], off nt
	v_cvt_pk_fp8_f32 v56, v58, v57 op_sel:[0,0,1]
	global_load_dwordx2 v[174:175], v[174:175], off nt
	v_mul_f32_e32 v5, 0x43800000, v99
	v_mul_f32_e32 v8, 0x43800000, v105
	v_mul_f32_e32 v57, 0x43800000, v109
	v_med3_f32 v5, v5, s79, v193
	v_med3_f32 v8, v8, s79, v193
	v_med3_f32 v59, v57, s79, v193
	v_mov_b32_e32 v57, v9
	v_cvt_pk_fp8_f32 v57, v5, v8
	v_mul_f32_e32 v58, 0x43800000, v111
	v_med3_f32 v58, v58, s79, v193
	v_add_u32_e32 v4, v7, v23
	v_cvt_pk_fp8_f32 v57, v59, v58 op_sel:[0,0,1]
	ds_write_b128 v4, v[194:197]
	ds_write_b128 v4, v[50:53] offset:16
	v_add_u32_e32 v4, v13, v27
	ds_write_b128 v4, v[54:57]
	v_mul_f32_e32 v4, 0x43800000, v112
	v_mul_f32_e32 v5, 0x43800000, v114
	v_mul_f32_e32 v50, 0x43800000, v124
	v_med3_f32 v4, v4, s79, v193
	v_med3_f32 v5, v5, s79, v193
	v_med3_f32 v51, v50, s79, v193
	v_mov_b32_e32 v50, v9
	v_cvt_pk_fp8_f32 v50, v4, v5
	v_mul_f32_e32 v8, 0x43800000, v118
	v_med3_f32 v8, v8, s79, v193
	v_mul_f32_e32 v4, 0x43800000, v116
	v_cvt_pk_fp8_f32 v50, v8, v51 op_sel:[0,0,1]
	v_mul_f32_e32 v5, 0x43800000, v120
	v_mul_f32_e32 v51, 0x43800000, v132
	v_med3_f32 v4, v4, s79, v193
	v_med3_f32 v5, v5, s79, v193
	v_med3_f32 v52, v51, s79, v193
	v_mov_b32_e32 v51, v9
	v_cvt_pk_fp8_f32 v51, v4, v5
	v_mul_f32_e32 v8, 0x43800000, v126
	v_med3_f32 v8, v8, s79, v193
	v_mul_f32_e32 v4, 0x43800000, v122
	v_cvt_pk_fp8_f32 v51, v8, v52 op_sel:[0,0,1]
	v_mul_f32_e32 v5, 0x43800000, v128
	v_mul_f32_e32 v52, 0x43800000, v138
	v_med3_f32 v4, v4, s79, v193
	v_med3_f32 v5, v5, s79, v193
	v_med3_f32 v53, v52, s79, v193
	v_mov_b32_e32 v52, v9
	v_cvt_pk_fp8_f32 v52, v4, v5
	v_mul_f32_e32 v8, 0x43800000, v134
	v_med3_f32 v8, v8, s79, v193
	s_waitcnt vmcnt(6)
	v_mul_f32_e32 v4, 0x43800000, v130
	v_cvt_pk_fp8_f32 v52, v8, v53 op_sel:[0,0,1]
	s_waitcnt vmcnt(5)
	v_mul_f32_e32 v5, 0x43800000, v136
	s_waitcnt vmcnt(3)
; #define CV_LOAD(v, kb) do { _Pragma("unroll") for (int j = 0; j < 16; ++j) v[j] = __builtin_nontemporal_load((const f32x2*)(src + (size_t)((kb) * 16 + j) * ldw)); } while (0)
; __device__ __forceinline__ void tr128_f8(const float* W, int ldw, int srccol, unsigned char* WT, size_t dstrow0, int K, int k0, LAS unsigned char* tile, int lane) {
;     ...
;     CV_LOAD(va, 0); CV_LOAD(vb, 1); CV_LOAD(vc, 2);
;     CV_LOAD(vd, 3); CV_PUT(va, 0); CV_LOAD(va, 4); CV_PUT(vb, 1); CV_LOAD(vb, 5); CV_PUT(vc, 2); CV_LOAD(vc, 6); CV_PUT(vd, 3); CV_LOAD(vd, 7);
;     CV_PUT(va, 4); CV_PUT(vb, 5); CV_PUT(vc, 6); CV_PUT(vd, 7);
	v_mul_f32_e32 v53, 0x43800000, v142
	v_med3_f32 v4, v4, s79, v193
	v_med3_f32 v5, v5, s79, v193
	v_med3_f32 v54, v53, s79, v193
	v_mov_b32_e32 v53, v9
	v_cvt_pk_fp8_f32 v53, v4, v5
	v_mul_f32_e32 v8, 0x43800000, v140
	v_med3_f32 v8, v8, s79, v193
	v_mul_f32_e32 v4, 0x43800000, v113
	v_cvt_pk_fp8_f32 v53, v8, v54 op_sel:[0,0,1]
	v_mul_f32_e32 v5, 0x43800000, v115
	v_mul_f32_e32 v54, 0x43800000, v125
	v_med3_f32 v4, v4, s79, v193
	v_med3_f32 v5, v5, s79, v193
	v_med3_f32 v55, v54, s79, v193
	v_mov_b32_e32 v54, v9
	v_cvt_pk_fp8_f32 v54, v4, v5
	v_mul_f32_e32 v8, 0x43800000, v119
	v_med3_f32 v8, v8, s79, v193
	v_mul_f32_e32 v4, 0x43800000, v117
	v_cvt_pk_fp8_f32 v54, v8, v55 op_sel:[0,0,1]
	v_mul_f32_e32 v5, 0x43800000, v121
	v_mul_f32_e32 v55, 0x43800000, v133
	v_med3_f32 v4, v4, s79, v193
	v_med3_f32 v5, v5, s79, v193
	v_med3_f32 v56, v55, s79, v193
	v_mov_b32_e32 v55, v9
	v_cvt_pk_fp8_f32 v55, v4, v5
	v_mul_f32_e32 v8, 0x43800000, v127
	v_med3_f32 v8, v8, s79, v193
	v_mul_f32_e32 v4, 0x43800000, v123
	v_cvt_pk_fp8_f32 v55, v8, v56 op_sel:[0,0,1]
	v_mul_f32_e32 v5, 0x43800000, v129
	v_mul_f32_e32 v56, 0x43800000, v139
	v_med3_f32 v4, v4, s79, v193
	v_med3_f32 v5, v5, s79, v193
	v_med3_f32 v57, v56, s79, v193
	v_mov_b32_e32 v56, v9
	v_cvt_pk_fp8_f32 v56, v4, v5
	v_mul_f32_e32 v8, 0x43800000, v135
	v_med3_f32 v8, v8, s79, v193
	v_mul_f32_e32 v4, 0x43800000, v131
	v_cvt_pk_fp8_f32 v56, v8, v57 op_sel:[0,0,1]
	v_mul_f32_e32 v5, 0x43800000, v137
	v_mul_f32_e32 v57, 0x43800000, v143
	v_med3_f32 v4, v4, s79, v193
	v_med3_f32 v5, v5, s79, v193
	v_med3_f32 v58, v57, s79, v193
	v_mov_b32_e32 v57, v9
	v_cvt_pk_fp8_f32 v57, v4, v5
	v_mul_f32_e32 v8, 0x43800000, v141
	v_med3_f32 v8, v8, s79, v193
	v_add_u32_e32 v4, v7, v29
	v_cvt_pk_fp8_f32 v57, v8, v58 op_sel:[0,0,1]
	v_add_u32_e32 v5, v13, v31
	ds_write_b128 v4, v[50:53]
	v_mul_f32_e32 v8, 0x43800000, v146
	ds_write_b128 v5, v[54:57]
	v_mul_f32_e32 v5, 0x43800000, v144
	v_mul_f32_e32 v50, 0x43800000, v150
	v_med3_f32 v5, v5, s79, v193
	v_med3_f32 v8, v8, s79, v193
	v_med3_f32 v52, v50, s79, v193
	v_mov_b32_e32 v50, v9
	v_cvt_pk_fp8_f32 v50, v5, v8
	v_mul_f32_e32 v51, 0x43800000, v156
	v_med3_f32 v51, v51, s79, v193
	v_mul_f32_e32 v5, 0x43800000, v148
	v_cvt_pk_fp8_f32 v50, v52, v51 op_sel:[0,0,1]
	v_mul_f32_e32 v8, 0x43800000, v152
	v_mul_f32_e32 v51, 0x43800000, v158
	v_med3_f32 v5, v5, s79, v193
	v_med3_f32 v8, v8, s79, v193
	v_med3_f32 v53, v51, s79, v193
	v_mov_b32_e32 v51, v9
	v_cvt_pk_fp8_f32 v51, v5, v8
	v_mul_f32_e32 v52, 0x43800000, v166
	v_med3_f32 v52, v52, s79, v193
	v_mul_f32_e32 v5, 0x43800000, v154
	v_cvt_pk_fp8_f32 v51, v53, v52 op_sel:[0,0,1]
	v_mul_f32_e32 v8, 0x43800000, v160
	v_mul_f32_e32 v52, 0x43800000, v168
	v_med3_f32 v5, v5, s79, v193
	v_med3_f32 v8, v8, s79, v193
	v_med3_f32 v54, v52, s79, v193
	v_mov_b32_e32 v52, v9
	v_cvt_pk_fp8_f32 v52, v5, v8
	v_mul_f32_e32 v53, 0x43800000, v172
	v_med3_f32 v53, v53, s79, v193
	s_waitcnt vmcnt(2)
	v_mul_f32_e32 v5, 0x43800000, v164
	v_cvt_pk_fp8_f32 v52, v54, v53 op_sel:[0,0,1]
	s_waitcnt vmcnt(1)
	v_mul_f32_e32 v8, 0x43800000, v170
	s_waitcnt vmcnt(0)
	v_mul_f32_e32 v53, 0x43800000, v174
	v_med3_f32 v5, v5, s79, v193
	v_med3_f32 v8, v8, s79, v193
	v_med3_f32 v54, v53, s79, v193
	v_mov_b32_e32 v53, v9
	v_cvt_pk_fp8_f32 v53, v5, v8
	v_mul_f32_e32 v2, 0x43800000, v2
	v_med3_f32 v2, v2, s79, v193
	v_mul_f32_e32 v5, 0x43800000, v147
	v_cvt_pk_fp8_f32 v53, v54, v2 op_sel:[0,0,1]
	v_mul_f32_e32 v2, 0x43800000, v145
	v_mul_f32_e32 v54, 0x43800000, v157
	v_med3_f32 v2, v2, s79, v193
	v_med3_f32 v5, v5, s79, v193
	v_med3_f32 v55, v54, s79, v193
	v_mov_b32_e32 v54, v9
	v_cvt_pk_fp8_f32 v54, v2, v5
	v_mul_f32_e32 v8, 0x43800000, v151
	v_med3_f32 v8, v8, s79, v193
	v_mul_f32_e32 v2, 0x43800000, v149
	v_cvt_pk_fp8_f32 v54, v8, v55 op_sel:[0,0,1]
	v_mul_f32_e32 v5, 0x43800000, v153
	v_mul_f32_e32 v55, 0x43800000, v167
	v_med3_f32 v2, v2, s79, v193
	v_med3_f32 v5, v5, s79, v193
	v_med3_f32 v56, v55, s79, v193
	v_mov_b32_e32 v55, v9
	v_cvt_pk_fp8_f32 v55, v2, v5
	v_mul_f32_e32 v8, 0x43800000, v159
	v_med3_f32 v8, v8, s79, v193
	v_mul_f32_e32 v2, 0x43800000, v155
	v_cvt_pk_fp8_f32 v55, v8, v56 op_sel:[0,0,1]
	v_mul_f32_e32 v5, 0x43800000, v161
	v_mul_f32_e32 v56, 0x43800000, v173
	v_med3_f32 v2, v2, s79, v193
	v_med3_f32 v5, v5, s79, v193
	v_med3_f32 v57, v56, s79, v193
	v_mov_b32_e32 v56, v9
	v_cvt_pk_fp8_f32 v56, v2, v5
	v_mul_f32_e32 v8, 0x43800000, v169
	v_med3_f32 v8, v8, s79, v193
	v_mul_f32_e32 v2, 0x43800000, v165
	v_mul_f32_e32 v5, 0x43800000, v171
	v_cvt_pk_fp8_f32 v56, v8, v57 op_sel:[0,0,1]
	v_med3_f32 v2, v2, s79, v193
	v_med3_f32 v5, v5, s79, v193
	v_mov_b32_e32 v57, v9
	v_cvt_pk_fp8_f32 v57, v2, v5
	v_mul_f32_e32 v8, 0x43800000, v175
	v_mul_f32_e32 v3, 0x43800000, v3
	v_med3_f32 v8, v8, s79, v193
	v_med3_f32 v3, v3, s79, v193
	v_cvt_pk_fp8_f32 v57, v8, v3 op_sel:[0,0,1]
	v_add_u32_e32 v2, v13, v33
	ds_write_b128 v4, v[50:53] offset:16
	v_or_b32_e32 v8, s8, v162
	ds_write_b128 v2, v[54:57]
	s_waitcnt lgkmcnt(0)
; #define LAS __attribute__((address_space(3)))
; #define LDS_WAIT() asm volatile("s_waitcnt lgkmcnt(0)" ::: "memory")
; __device__ __forceinline__ void tr128_f8(const float* W, int ldw, int srccol, unsigned char* WT, size_t dstrow0, int K, int k0, LAS unsigned char* tile, int lane) {
;     ...
;     const int c = lane & 7;
; #pragma unroll
;     for (int j = 0; j < 16; ++j) { const int n = (lane >> 3) + 8 * j; const v4u o = *(const LAS v4u*)(tile + n * 128 + ((c ^ (n & 7)) << 4));
;         __builtin_nontemporal_store(o, (v4u*)(WT + (dstrow0 + n) * K + k0 + 16 * c)); }
;     LDS_WAIT(); asm volatile("" ::: "memory");
	v_add_u32_e32 v56, v35, v37
	ds_read_b128 v[56:59], v56
	v_add_u32_e32 v60, v35, v39
	ds_read_b128 v[60:63], v60
	v_add_u32_e32 v64, v35, v179
	ds_read_b128 v[64:67], v64
	v_add_u32_e32 v68, v35, v180
	ds_read_b128 v[68:71], v68
	v_add_u32_e32 v72, v35, v181
	ds_read_b128 v[72:75], v72
	v_add_u32_e32 v76, v35, v182
	ds_read_b128 v[76:79], v76
	v_add_u32_e32 v80, v35, v183
	ds_read_b128 v[80:83], v80
	v_add_u32_e32 v84, v35, v184
	ds_read_b128 v[84:87], v84
	v_add_u32_e32 v88, v35, v185
	ds_read_b128 v[88:91], v88
	v_add_u32_e32 v92, v35, v186
	ds_read_b128 v[92:95], v92
	v_add_u32_e32 v96, v35, v187
	ds_read_b128 v[96:99], v96
	v_add_u32_e32 v100, v35, v188
	ds_read_b128 v[100:103], v100
	v_add_u32_e32 v104, v35, v189
	ds_read_b128 v[104:107], v104
	v_add_u32_e32 v108, v35, v190
	ds_read_b128 v[108:111], v108
	v_add_u32_e32 v112, v35, v191
	ds_read_b128 v[112:115], v112
	v_add_u32_e32 v116, v35, v192
	ds_read_b128 v[116:119], v116
	v_lshl_add_u64 v[50:51], v[46:47], 0, s[6:7]
	v_lshlrev_b32_e32 v8, 11, v8
	v_lshl_add_u64 v[52:53], v[50:51], 0, v[8:9]
	v_or_b32_e32 v8, s8, v10
	s_waitcnt lgkmcnt(15)
	global_store_dwordx4 v[52:53], v[56:59], off nt
	v_lshlrev_b32_e32 v8, 11, v8
	v_lshl_add_u64 v[52:53], v[50:51], 0, v[8:9]
	v_or_b32_e32 v8, s8, v12
	v_lshlrev_b32_e32 v8, 11, v8
	v_readlane_b32 s37, v250, 61
	v_readlane_b32 s38, v250, 62
	s_waitcnt lgkmcnt(14)
	global_store_dwordx4 v[52:53], v[60:63], off nt
	v_lshl_add_u64 v[52:53], v[50:51], 0, v[8:9]
	v_or_b32_e32 v8, s8, v14
	v_lshlrev_b32_e32 v8, 11, v8
	v_readlane_b32 s39, v250, 63
	v_readlane_b32 s40, v251, 0
	v_readlane_b32 s41, v251, 1
	s_waitcnt lgkmcnt(13)
	global_store_dwordx4 v[52:53], v[64:67], off nt
	v_lshl_add_u64 v[52:53], v[50:51], 0, v[8:9]
	v_or_b32_e32 v8, s8, v16
	v_lshlrev_b32_e32 v8, 11, v8
	v_readlane_b32 s44, v251, 4
	v_readlane_b32 s45, v251, 5
	v_readlane_b32 s46, v251, 6
	s_waitcnt lgkmcnt(12)
	global_store_dwordx4 v[52:53], v[68:71], off nt
	v_lshl_add_u64 v[52:53], v[50:51], 0, v[8:9]
	v_or_b32_e32 v8, s8, v18
	v_lshlrev_b32_e32 v8, 11, v8
	v_readlane_b32 s47, v251, 7
	v_readlane_b32 s48, v251, 8
	v_readlane_b32 s49, v251, 9
	s_waitcnt lgkmcnt(11)
	global_store_dwordx4 v[52:53], v[72:75], off nt
	v_lshl_add_u64 v[52:53], v[50:51], 0, v[8:9]
	v_or_b32_e32 v8, s8, v20
	v_lshlrev_b32_e32 v8, 11, v8
	v_readlane_b32 s50, v251, 10
	v_readlane_b32 s51, v251, 11
	s_waitcnt lgkmcnt(10)
	global_store_dwordx4 v[52:53], v[76:79], off nt
	v_lshl_add_u64 v[52:53], v[50:51], 0, v[8:9]
	s_nop 0
	v_or_b32_e32 v8, s8, v22
	v_lshlrev_b32_e32 v8, 11, v8
	s_waitcnt lgkmcnt(9)
	global_store_dwordx4 v[52:53], v[80:83], off nt
	s_nop 1
	v_lshl_add_u64 v[52:53], v[50:51], 0, v[8:9]
	v_or_b32_e32 v8, s8, v24
	v_lshlrev_b32_e32 v8, 11, v8
	s_waitcnt lgkmcnt(8)
	global_store_dwordx4 v[52:53], v[84:87], off nt
	v_lshl_add_u64 v[52:53], v[50:51], 0, v[8:9]
	s_nop 0
	v_or_b32_e32 v8, s8, v26
	v_lshlrev_b32_e32 v8, 11, v8
	s_waitcnt lgkmcnt(7)
	global_store_dwordx4 v[52:53], v[88:91], off nt
	s_nop 1
	v_lshl_add_u64 v[52:53], v[50:51], 0, v[8:9]
	v_or_b32_e32 v8, s8, v28
	v_lshlrev_b32_e32 v8, 11, v8
	s_waitcnt lgkmcnt(6)
	global_store_dwordx4 v[52:53], v[92:95], off nt
	v_lshl_add_u64 v[52:53], v[50:51], 0, v[8:9]
	s_nop 0
	v_or_b32_e32 v8, s8, v30
	v_lshlrev_b32_e32 v8, 11, v8
	s_waitcnt lgkmcnt(5)
	global_store_dwordx4 v[52:53], v[96:99], off nt
	s_nop 1
	v_lshl_add_u64 v[52:53], v[50:51], 0, v[8:9]
	v_or_b32_e32 v8, s8, v32
	v_lshlrev_b32_e32 v8, 11, v8
	s_waitcnt lgkmcnt(4)
	global_store_dwordx4 v[52:53], v[100:103], off nt
	v_lshl_add_u64 v[52:53], v[50:51], 0, v[8:9]
	s_nop 0
	v_or_b32_e32 v8, s8, v34
	v_lshlrev_b32_e32 v8, 11, v8
	s_waitcnt lgkmcnt(3)
	global_store_dwordx4 v[52:53], v[104:107], off nt
	s_nop 1
	v_lshl_add_u64 v[52:53], v[50:51], 0, v[8:9]
	v_or_b32_e32 v8, s8, v36
	v_lshlrev_b32_e32 v8, 11, v8
	s_waitcnt lgkmcnt(2)
	global_store_dwordx4 v[52:53], v[108:111], off nt
	v_lshl_add_u64 v[52:53], v[50:51], 0, v[8:9]
	s_nop 0
	v_or_b32_e32 v8, s8, v38
	v_lshlrev_b32_e32 v8, 11, v8
	v_lshl_add_u64 v[50:51], v[50:51], 0, v[8:9]
	s_waitcnt lgkmcnt(1)
	global_store_dwordx4 v[52:53], v[112:115], off nt
	s_nop 1
	s_waitcnt lgkmcnt(0)
	global_store_dwordx4 v[50:51], v[116:119], off nt
	s_waitcnt lgkmcnt(0)

; #define CV_LOAD(v, kb) do { _Pragma("unroll") for (int j = 0; j < 16; ++j) v[j] = __builtin_nontemporal_load((const f32x2*)(src + (size_t)((kb) * 16 + j) * ldw)); } while (0)
; __device__ __forceinline__ void tr128_f8(const float* W, int ldw, int srccol, unsigned char* WT, size_t dstrow0, int K, int k0, LAS unsigned char* tile, int lane) {
;     const float* src = W + (size_t)k0 * ldw + srccol + 2 * lane;
;     f32x2 va[16], vb[16], vc[16], vd[16];
;     ...
;     CV_LOAD(va, 0); CV_LOAD(vb, 1); CV_LOAD(vc, 2);
;     CV_LOAD(vd, 3); CV_PUT(va, 0); CV_LOAD(va, 4); CV_PUT(vb, 1); CV_LOAD(vb, 5); CV_PUT(vc, 2); CV_LOAD(vc, 6); CV_PUT(vd, 3); CV_LOAD(vd, 7);
.LBB0_512:
	s_andn2_b64 vcc, exec, s[8:9]
	s_cbranch_vccnz .LBB0_491
	s_lshl_b32 s8, s10, 3
	s_and_b32 s8, s8, 0xffffff80
	s_lshl_b32 s6, s10, 7
	s_ashr_i32 s9, s8, 31
	v_readlane_b32 s36, v250, 60
	s_and_b32 s6, s6, 0x780
	s_lshl_b64 s[10:11], s[8:9], 13
	v_readlane_b32 s40, v251, 0
	v_readlane_b32 s41, v251, 1
	s_add_u32 s10, s40, s10
	s_addc_u32 s11, s41, s11
	s_lshl_b32 s12, s6, 2
	s_add_u32 s10, s10, s12
	s_addc_u32 s11, s11, 0
	v_lshlrev_b32_e32 v8, 2, v6
	v_lshl_add_u64 v[2:3], s[10:11], 0, v[8:9]
	v_add_co_u32_e32 v50, vcc, s20, v2
	global_load_dwordx2 v[4:5], v8, s[10:11] nt
	s_nop 0
	v_addc_co_u32_e32 v51, vcc, 0, v3, vcc
	v_add_co_u32_e32 v52, vcc, s21, v2
	global_load_dwordx2 v[50:51], v[50:51], off nt
	s_nop 0
	v_addc_co_u32_e32 v53, vcc, 0, v3, vcc
	v_add_co_u32_e32 v54, vcc, s22, v2
	global_load_dwordx2 v[52:53], v[52:53], off nt
	s_nop 0
	v_addc_co_u32_e32 v55, vcc, 0, v3, vcc
	v_add_co_u32_e32 v56, vcc, s23, v2
	global_load_dwordx2 v[54:55], v[54:55], off nt
	s_nop 0
	v_addc_co_u32_e32 v57, vcc, 0, v3, vcc
	v_add_co_u32_e32 v58, vcc, s24, v2
	s_mov_b32 s10, 0x16000
	s_nop 0
	v_addc_co_u32_e32 v59, vcc, 0, v3, vcc
	v_add_co_u32_e32 v60, vcc, s25, v2
	global_load_dwordx2 v[56:57], v[56:57], off nt
	s_nop 0
	v_addc_co_u32_e32 v61, vcc, 0, v3, vcc
	v_add_co_u32_e32 v62, vcc, s26, v2
	global_load_dwordx2 v[58:59], v[58:59], off nt
	s_nop 0
	v_addc_co_u32_e32 v63, vcc, 0, v3, vcc
	v_add_co_u32_e32 v64, vcc, s27, v2
	global_load_dwordx2 v[60:61], v[60:61], off nt
	s_nop 0
	v_addc_co_u32_e32 v65, vcc, 0, v3, vcc
	v_add_co_u32_e32 v66, vcc, s33, v2
	global_load_dwordx2 v[64:65], v[64:65], off nt
	s_nop 0
	v_addc_co_u32_e32 v67, vcc, 0, v3, vcc
	v_add_co_u32_e32 v68, vcc, s34, v2
	global_load_dwordx2 v[66:67], v[66:67], off nt
	s_nop 0
	v_addc_co_u32_e32 v69, vcc, 0, v3, vcc
	v_add_co_u32_e32 v70, vcc, s10, v2
	s_mov_b32 s10, 0x1a000
	s_nop 0
	v_addc_co_u32_e32 v71, vcc, 0, v3, vcc
	v_add_co_u32_e32 v72, vcc, s58, v2
	global_load_dwordx2 v[62:63], v[62:63], off nt
	s_nop 0
	v_addc_co_u32_e32 v73, vcc, 0, v3, vcc
	v_add_co_u32_e32 v74, vcc, s10, v2
	global_load_dwordx2 v[72:73], v[72:73], off nt
	s_nop 0
	v_addc_co_u32_e32 v75, vcc, 0, v3, vcc
	global_load_dwordx2 v[74:75], v[74:75], off nt
	v_add_co_u32_e32 v76, vcc, s62, v2
	s_mov_b32 s10, 0x1e000
	s_nop 0
	v_addc_co_u32_e32 v77, vcc, 0, v3, vcc
	global_load_dwordx2 v[68:69], v[68:69], off nt
	v_add_co_u32_e32 v78, vcc, s10, v2
	global_load_dwordx2 v[70:71], v[70:71], off nt
	s_nop 0
	v_addc_co_u32_e32 v79, vcc, 0, v3, vcc
	global_load_dwordx2 v[76:77], v[76:77], off nt
	v_add_co_u32_e32 v80, vcc, s29, v2
	global_load_dwordx2 v[78:79], v[78:79], off nt
	s_nop 0
	v_addc_co_u32_e32 v81, vcc, 0, v3, vcc
	s_mov_b32 s10, 0x22000
	v_add_co_u32_e32 v82, vcc, s10, v2
	s_mov_b32 s10, 0x26000
	s_nop 0
	v_addc_co_u32_e32 v83, vcc, 0, v3, vcc
	v_add_co_u32_e32 v84, vcc, s31, v2
	global_load_dwordx2 v[80:81], v[80:81], off nt
	s_nop 0
	v_addc_co_u32_e32 v85, vcc, 0, v3, vcc
	v_add_co_u32_e32 v86, vcc, s10, v2
	s_mov_b32 s10, 0x2a000
	s_nop 0
	v_addc_co_u32_e32 v87, vcc, 0, v3, vcc
	v_add_co_u32_e32 v88, vcc, s35, v2
	global_load_dwordx2 v[82:83], v[82:83], off nt
	s_nop 0
	v_addc_co_u32_e32 v89, vcc, 0, v3, vcc
	v_add_co_u32_e32 v90, vcc, s10, v2
	s_mov_b32 s10, 0x2e000
	s_nop 0
	v_addc_co_u32_e32 v91, vcc, 0, v3, vcc
	v_add_co_u32_e32 v92, vcc, s66, v2
	global_load_dwordx2 v[86:87], v[86:87], off nt
	s_nop 0
	v_addc_co_u32_e32 v93, vcc, 0, v3, vcc
	v_add_co_u32_e32 v94, vcc, s10, v2
	s_mov_b32 s10, 0x32000
	s_nop 0
	v_addc_co_u32_e32 v95, vcc, 0, v3, vcc
	v_add_co_u32_e32 v96, vcc, s70, v2
	global_load_dwordx2 v[88:89], v[88:89], off nt
	s_nop 0
	v_addc_co_u32_e32 v97, vcc, 0, v3, vcc
	v_add_co_u32_e32 v98, vcc, s10, v2
	s_mov_b32 s10, 0x36000
	s_nop 0
	v_addc_co_u32_e32 v99, vcc, 0, v3, vcc
	v_add_co_u32_e32 v100, vcc, s74, v2
	global_load_dwordx2 v[90:91], v[90:91], off nt
	s_nop 0
	v_addc_co_u32_e32 v101, vcc, 0, v3, vcc
	v_add_co_u32_e32 v102, vcc, s10, v2
	s_mov_b32 s10, 0x3a000
	s_nop 0
	v_addc_co_u32_e32 v103, vcc, 0, v3, vcc
	v_add_co_u32_e32 v104, vcc, s78, v2
	global_load_dwordx2 v[84:85], v[84:85], off nt
	s_nop 0
	v_addc_co_u32_e32 v105, vcc, 0, v3, vcc
	v_add_co_u32_e32 v106, vcc, s10, v2
	s_mov_b32 s10, 0x3e000
	s_nop 0
	v_addc_co_u32_e32 v107, vcc, 0, v3, vcc
	v_add_co_u32_e32 v108, vcc, s83, v2
	global_load_dwordx2 v[94:95], v[94:95], off nt
	s_nop 0
	v_addc_co_u32_e32 v109, vcc, 0, v3, vcc
	v_add_co_u32_e32 v110, vcc, s10, v2
	s_mov_b32 s10, 0x42000
	s_nop 0
	v_addc_co_u32_e32 v111, vcc, 0, v3, vcc
	v_add_co_u32_e32 v112, vcc, s87, v2
	global_load_dwordx2 v[96:97], v[96:97], off nt
	s_nop 0
	v_addc_co_u32_e32 v113, vcc, 0, v3, vcc
	v_add_co_u32_e32 v114, vcc, s10, v2
	s_mov_b32 s10, 0x46000
	s_nop 0
	v_addc_co_u32_e32 v115, vcc, 0, v3, vcc
	v_add_co_u32_e32 v116, vcc, s91, v2
	global_load_dwordx2 v[98:99], v[98:99], off nt
	s_nop 0
	v_addc_co_u32_e32 v117, vcc, 0, v3, vcc
	v_add_co_u32_e32 v118, vcc, s10, v2
	s_mov_b32 s10, 0x4a000
	s_nop 0
	v_addc_co_u32_e32 v119, vcc, 0, v3, vcc
	v_add_co_u32_e32 v120, vcc, s95, v2
	global_load_dwordx2 v[92:93], v[92:93], off nt
	s_nop 0
	v_addc_co_u32_e32 v121, vcc, 0, v3, vcc
	v_add_co_u32_e32 v122, vcc, s10, v2
	s_mov_b32 s10, 0x4e000
	s_nop 0
	v_addc_co_u32_e32 v123, vcc, 0, v3, vcc
	v_add_co_u32_e32 v124, vcc, s53, v2
	global_load_dwordx2 v[102:103], v[102:103], off nt
	s_nop 0
	v_addc_co_u32_e32 v125, vcc, 0, v3, vcc
	v_add_co_u32_e32 v126, vcc, s10, v2
	s_mov_b32 s10, 0x52000
	s_nop 0
	v_addc_co_u32_e32 v127, vcc, 0, v3, vcc
	v_add_co_u32_e32 v128, vcc, s55, v2
	global_load_dwordx2 v[104:105], v[104:105], off nt
	s_nop 0
	v_addc_co_u32_e32 v129, vcc, 0, v3, vcc
	v_add_co_u32_e32 v130, vcc, s10, v2
	s_mov_b32 s10, 0x56000
	s_nop 0
	v_addc_co_u32_e32 v131, vcc, 0, v3, vcc
	v_add_co_u32_e32 v132, vcc, s57, v2
	global_load_dwordx2 v[106:107], v[106:107], off nt
	s_nop 0
	v_addc_co_u32_e32 v133, vcc, 0, v3, vcc
	v_add_co_u32_e32 v134, vcc, s10, v2
	global_load_dwordx2 v[100:101], v[100:101], off nt
	s_nop 0
	v_addc_co_u32_e32 v135, vcc, 0, v3, vcc
	v_add_co_u32_e32 v136, vcc, s59, v2
	s_waitcnt vmcnt(29)
; #define CV_LOAD(v, kb) do { _Pragma("unroll") for (int j = 0; j < 16; ++j) v[j] = __builtin_nontemporal_load((const f32x2*)(src + (size_t)((kb) * 16 + j) * ldw)); } while (0)
; __device__ __forceinline__ void tr128_f8(const float* W, int ldw, int srccol, unsigned char* WT, size_t dstrow0, int K, int k0, LAS unsigned char* tile, int lane) {
;     ...
;     CV_LOAD(va, 0); CV_LOAD(vb, 1); CV_LOAD(vc, 2);
;     CV_LOAD(vd, 3); CV_PUT(va, 0); CV_LOAD(va, 4); CV_PUT(vb, 1); CV_LOAD(vb, 5); CV_PUT(vc, 2); CV_LOAD(vc, 6); CV_PUT(vd, 3); CV_LOAD(vd, 7);
	v_mul_f32_e32 v4, 0x43800000, v4
	s_waitcnt vmcnt(28)
	v_mul_f32_e32 v8, 0x43800000, v50
	v_addc_co_u32_e32 v137, vcc, 0, v3, vcc
	s_mov_b32 s10, 0x5a000
	v_med3_f32 v4, v4, s79, v193
	v_med3_f32 v8, v8, s79, v193
	v_mov_b32_e32 v194, v9
	global_load_dwordx2 v[108:109], v[108:109], off nt
	v_add_co_u32_e32 v138, vcc, s10, v2
	global_load_dwordx2 v[110:111], v[110:111], off nt
	v_cvt_pk_fp8_f32 v194, v4, v8
	s_waitcnt vmcnt(27)
	v_mul_f32_e32 v4, 0x43800000, v56
	s_waitcnt vmcnt(26)
	v_mul_f32_e32 v8, 0x43800000, v58
	v_addc_co_u32_e32 v139, vcc, 0, v3, vcc
	v_med3_f32 v4, v4, s79, v193
	v_med3_f32 v8, v8, s79, v193
	v_mov_b32_e32 v195, v9
	v_add_co_u32_e32 v140, vcc, s61, v2
	v_mul_f32_e32 v50, 0x43800000, v52
	v_mul_f32_e32 v52, 0x43800000, v54
	v_cvt_pk_fp8_f32 v195, v4, v8
	s_waitcnt vmcnt(24)
	v_mul_f32_e32 v4, 0x43800000, v64
	s_waitcnt vmcnt(23)
	v_mul_f32_e32 v8, 0x43800000, v66
	v_addc_co_u32_e32 v141, vcc, 0, v3, vcc
	s_mov_b32 s10, 0x5e000
	v_med3_f32 v50, v50, s79, v193
	v_med3_f32 v52, v52, s79, v193
	v_med3_f32 v4, v4, s79, v193
	v_med3_f32 v8, v8, s79, v193
	v_mov_b32_e32 v196, v9
	v_add_co_u32_e32 v142, vcc, s10, v2
	v_cvt_pk_fp8_f32 v194, v50, v52 op_sel:[0,0,1]
	v_mul_f32_e32 v50, 0x43800000, v60
	s_waitcnt vmcnt(22)
	v_mul_f32_e32 v52, 0x43800000, v62
	v_cvt_pk_fp8_f32 v196, v4, v8
	s_waitcnt vmcnt(21)
	v_mul_f32_e32 v4, 0x43800000, v72
	s_waitcnt vmcnt(20)
	v_mul_f32_e32 v8, 0x43800000, v74
	v_addc_co_u32_e32 v143, vcc, 0, v3, vcc
	v_med3_f32 v50, v50, s79, v193
	v_med3_f32 v52, v52, s79, v193
	v_med3_f32 v4, v4, s79, v193
	v_med3_f32 v8, v8, s79, v193
	v_mov_b32_e32 v197, v9
	v_add_co_u32_e32 v144, vcc, s63, v2
	v_cvt_pk_fp8_f32 v195, v50, v52 op_sel:[0,0,1]
	s_waitcnt vmcnt(19)
	v_mul_f32_e32 v50, 0x43800000, v68
	s_waitcnt vmcnt(18)
	v_mul_f32_e32 v52, 0x43800000, v70
	v_cvt_pk_fp8_f32 v197, v4, v8
	v_addc_co_u32_e32 v145, vcc, 0, v3, vcc
	s_mov_b32 s10, 0x62000
	v_med3_f32 v50, v50, s79, v193
	v_med3_f32 v52, v52, s79, v193
	v_add_co_u32_e32 v146, vcc, s10, v2
	v_cvt_pk_fp8_f32 v196, v50, v52 op_sel:[0,0,1]
	s_waitcnt vmcnt(17)
	v_mul_f32_e32 v50, 0x43800000, v76
	s_waitcnt vmcnt(16)
	v_mul_f32_e32 v52, 0x43800000, v78
	v_addc_co_u32_e32 v147, vcc, 0, v3, vcc
	v_med3_f32 v50, v50, s79, v193
	v_med3_f32 v52, v52, s79, v193
	v_add_co_u32_e32 v148, vcc, s65, v2
	v_cvt_pk_fp8_f32 v197, v50, v52 op_sel:[0,0,1]
	v_mul_f32_e32 v4, 0x43800000, v5
	v_mul_f32_e32 v5, 0x43800000, v51
	v_mul_f32_e32 v50, 0x43800000, v55
	v_addc_co_u32_e32 v149, vcc, 0, v3, vcc
	s_mov_b32 s10, 0x66000
	v_med3_f32 v4, v4, s79, v193
	v_med3_f32 v5, v5, s79, v193
	v_med3_f32 v51, v50, s79, v193
	v_mov_b32_e32 v50, v9
	v_add_co_u32_e32 v150, vcc, s10, v2
	v_cvt_pk_fp8_f32 v50, v4, v5
	s_nop 0
	v_addc_co_u32_e32 v151, vcc, 0, v3, vcc
	v_add_co_u32_e32 v152, vcc, s67, v2
	v_mul_f32_e32 v8, 0x43800000, v53
	s_nop 0
	v_addc_co_u32_e32 v153, vcc, 0, v3, vcc
	s_mov_b32 s10, 0x6a000
	v_med3_f32 v8, v8, s79, v193
	v_add_co_u32_e32 v154, vcc, s10, v2
	v_cvt_pk_fp8_f32 v50, v8, v51 op_sel:[0,0,1]
	v_mul_f32_e32 v4, 0x43800000, v57
	v_mul_f32_e32 v5, 0x43800000, v59
	v_mul_f32_e32 v51, 0x43800000, v63
	v_addc_co_u32_e32 v155, vcc, 0, v3, vcc
	v_med3_f32 v4, v4, s79, v193
	v_med3_f32 v5, v5, s79, v193
	v_med3_f32 v52, v51, s79, v193
	v_mov_b32_e32 v51, v9
	v_add_co_u32_e32 v156, vcc, s69, v2
	v_cvt_pk_fp8_f32 v51, v4, v5
	s_nop 0
	v_addc_co_u32_e32 v157, vcc, 0, v3, vcc
	s_mov_b32 s10, 0x6e000
	v_add_co_u32_e32 v158, vcc, s10, v2
	v_mul_f32_e32 v8, 0x43800000, v61
	s_nop 0
	v_addc_co_u32_e32 v159, vcc, 0, v3, vcc
	v_med3_f32 v8, v8, s79, v193
	v_add_co_u32_e32 v160, vcc, s71, v2
	v_cvt_pk_fp8_f32 v51, v8, v52 op_sel:[0,0,1]
	v_mul_f32_e32 v4, 0x43800000, v65
	v_mul_f32_e32 v5, 0x43800000, v67
	v_mul_f32_e32 v52, 0x43800000, v71
	v_addc_co_u32_e32 v161, vcc, 0, v3, vcc
	s_mov_b32 s10, 0x72000
	v_med3_f32 v4, v4, s79, v193
	v_med3_f32 v5, v5, s79, v193
	v_med3_f32 v53, v52, s79, v193
	v_mov_b32_e32 v52, v9
	v_add_co_u32_e32 v164, vcc, s10, v2
	v_cvt_pk_fp8_f32 v52, v4, v5
	s_nop 0
	v_addc_co_u32_e32 v165, vcc, 0, v3, vcc
	v_add_co_u32_e32 v166, vcc, s73, v2
	v_mul_f32_e32 v8, 0x43800000, v69
	s_nop 0
	v_addc_co_u32_e32 v167, vcc, 0, v3, vcc
	s_mov_b32 s10, 0x76000
	v_med3_f32 v8, v8, s79, v193
	v_add_co_u32_e32 v168, vcc, s10, v2
	v_cvt_pk_fp8_f32 v52, v8, v53 op_sel:[0,0,1]
	v_mul_f32_e32 v4, 0x43800000, v73
	v_mul_f32_e32 v5, 0x43800000, v75
	v_mul_f32_e32 v53, 0x43800000, v79
	v_addc_co_u32_e32 v169, vcc, 0, v3, vcc
	v_med3_f32 v4, v4, s79, v193
	v_med3_f32 v5, v5, s79, v193
	v_med3_f32 v54, v53, s79, v193
	v_mov_b32_e32 v53, v9
	v_add_co_u32_e32 v170, vcc, s75, v2
	v_cvt_pk_fp8_f32 v53, v4, v5
	s_nop 0
	v_addc_co_u32_e32 v171, vcc, 0, v3, vcc
	s_mov_b32 s10, 0x7a000
	v_add_co_u32_e32 v172, vcc, s10, v2
	v_mul_f32_e32 v8, 0x43800000, v77
	s_nop 0
	v_addc_co_u32_e32 v173, vcc, 0, v3, vcc
	v_med3_f32 v8, v8, s79, v193
	v_add_co_u32_e32 v174, vcc, s77, v2
	v_cvt_pk_fp8_f32 v53, v8, v54 op_sel:[0,0,1]
	s_nop 0
	v_addc_co_u32_e32 v175, vcc, 0, v3, vcc
	s_mov_b32 s10, 0x7e000
	v_add_co_u32_e32 v176, vcc, s10, v2
	v_add_u32_e32 v4, v13, v15
	s_nop 0
	v_addc_co_u32_e32 v177, vcc, 0, v3, vcc
	ds_write_b128 v4, v[50:53]
	v_add_co_u32_e32 v4, vcc, s80, v2
	s_mov_b32 s10, 0x82000
	s_nop 0
	v_addc_co_u32_e32 v5, vcc, 0, v3, vcc
	v_add_co_u32_e32 v50, vcc, s10, v2
	s_mov_b32 s10, 0x86000
	s_nop 0
	v_addc_co_u32_e32 v51, vcc, 0, v3, vcc
	v_add_co_u32_e32 v52, vcc, s82, v2
	global_load_dwordx2 v[112:113], v[112:113], off nt
	s_nop 0
	v_addc_co_u32_e32 v53, vcc, 0, v3, vcc
	v_add_co_u32_e32 v54, vcc, s10, v2
	s_mov_b32 s10, 0x8a000
	s_nop 0
	v_addc_co_u32_e32 v55, vcc, 0, v3, vcc
; #define CV_LOAD(v, kb) do { _Pragma("unroll") for (int j = 0; j < 16; ++j) v[j] = __builtin_nontemporal_load((const f32x2*)(src + (size_t)((kb) * 16 + j) * ldw)); } while (0)
; __device__ __forceinline__ void tr128_f8(const float* W, int ldw, int srccol, unsigned char* WT, size_t dstrow0, int K, int k0, LAS unsigned char* tile, int lane) {
;     ...
;     CV_LOAD(va, 0); CV_LOAD(vb, 1); CV_LOAD(vc, 2);
;     CV_LOAD(vd, 3); CV_PUT(va, 0); CV_LOAD(va, 4); CV_PUT(vb, 1); CV_LOAD(vb, 5); CV_PUT(vc, 2); CV_LOAD(vc, 6); CV_PUT(vd, 3); CV_LOAD(vd, 7);
	v_add_co_u32_e32 v56, vcc, s84, v2
	global_load_dwordx2 v[114:115], v[114:115], off nt
	s_nop 0
	v_addc_co_u32_e32 v57, vcc, 0, v3, vcc
	v_add_co_u32_e32 v58, vcc, s10, v2
	global_load_dwordx2 v[120:121], v[120:121], off nt
	s_nop 0
	v_addc_co_u32_e32 v59, vcc, 0, v3, vcc
	v_add_co_u32_e32 v60, vcc, s86, v2
	global_load_dwordx2 v[122:123], v[122:123], off nt
	s_nop 0
	v_addc_co_u32_e32 v61, vcc, 0, v3, vcc
	s_mov_b32 s10, 0x8e000
	v_add_co_u32_e32 v62, vcc, s10, v2
	global_load_dwordx2 v[116:117], v[116:117], off nt
	s_nop 0
	v_addc_co_u32_e32 v63, vcc, 0, v3, vcc
	global_load_dwordx2 v[118:119], v[118:119], off nt
	v_add_co_u32_e32 v64, vcc, s88, v2
	global_load_dwordx2 v[124:125], v[124:125], off nt
	s_nop 0
	v_addc_co_u32_e32 v65, vcc, 0, v3, vcc
	global_load_dwordx2 v[128:129], v[128:129], off nt
	s_mov_b32 s10, 0x92000
	global_load_dwordx2 v[130:131], v[130:131], off nt
	v_add_co_u32_e32 v66, vcc, s10, v2
	global_load_dwordx2 v[126:127], v[126:127], off nt
	s_nop 0
	v_addc_co_u32_e32 v67, vcc, 0, v3, vcc
	global_load_dwordx2 v[134:135], v[134:135], off nt
	v_add_co_u32_e32 v68, vcc, s90, v2
	global_load_dwordx2 v[136:137], v[136:137], off nt
	s_nop 0
	v_addc_co_u32_e32 v69, vcc, 0, v3, vcc
	global_load_dwordx2 v[138:139], v[138:139], off nt
	s_mov_b32 s10, 0x96000
	global_load_dwordx2 v[132:133], v[132:133], off nt
	v_add_co_u32_e32 v70, vcc, s10, v2
	global_load_dwordx2 v[140:141], v[140:141], off nt
	s_nop 0
	v_addc_co_u32_e32 v71, vcc, 0, v3, vcc
	global_load_dwordx2 v[142:143], v[142:143], off nt
	v_add_co_u32_e32 v72, vcc, s92, v2
	s_mov_b32 s10, 0x9a000
	s_nop 0
	v_addc_co_u32_e32 v73, vcc, 0, v3, vcc
	v_add_co_u32_e32 v74, vcc, s10, v2
	s_mov_b32 s10, 0x9e000
	s_nop 0
	v_addc_co_u32_e32 v75, vcc, 0, v3, vcc
	v_add_co_u32_e32 v76, vcc, s94, v2
	v_add_u32_e32 v8, v7, v11
	s_nop 0
	v_addc_co_u32_e32 v77, vcc, 0, v3, vcc
	v_add_co_u32_e32 v78, vcc, s10, v2
	s_waitcnt vmcnt(30)
	v_mul_f32_e32 v82, 0x43800000, v82
	v_addc_co_u32_e32 v79, vcc, 0, v3, vcc
	global_load_dwordx2 v[78:79], v[78:79], off nt
	v_mul_f32_e32 v80, 0x43800000, v80
	ds_write_b128 v8, v[194:197]
	v_med3_f32 v80, v80, s79, v193
	v_med3_f32 v82, v82, s79, v193
	v_mov_b32_e32 v194, v9
	v_cvt_pk_fp8_f32 v194, v80, v82
	s_waitcnt vmcnt(29)
	v_mul_f32_e32 v80, 0x43800000, v88
	s_waitcnt vmcnt(28)
	v_mul_f32_e32 v82, 0x43800000, v90
	v_med3_f32 v80, v80, s79, v193
	v_med3_f32 v82, v82, s79, v193
	v_mov_b32_e32 v195, v9
	s_waitcnt vmcnt(27)
	v_mul_f32_e32 v84, 0x43800000, v84
	v_mul_f32_e32 v86, 0x43800000, v86
	v_cvt_pk_fp8_f32 v195, v80, v82
	s_waitcnt vmcnt(25)
	v_mul_f32_e32 v80, 0x43800000, v96
	s_waitcnt vmcnt(24)
	v_mul_f32_e32 v82, 0x43800000, v98
	v_med3_f32 v84, v84, s79, v193
	v_med3_f32 v86, v86, s79, v193
	v_med3_f32 v80, v80, s79, v193
	v_med3_f32 v82, v82, s79, v193
	v_mov_b32_e32 v196, v9
	v_cvt_pk_fp8_f32 v194, v84, v86 op_sel:[0,0,1]
	s_waitcnt vmcnt(23)
	v_mul_f32_e32 v84, 0x43800000, v92
	v_mul_f32_e32 v86, 0x43800000, v94
	v_cvt_pk_fp8_f32 v196, v80, v82
	s_waitcnt vmcnt(21)
	v_mul_f32_e32 v80, 0x43800000, v104
	s_waitcnt vmcnt(20)
	v_mul_f32_e32 v82, 0x43800000, v106
	v_med3_f32 v84, v84, s79, v193
	v_med3_f32 v86, v86, s79, v193
	v_med3_f32 v80, v80, s79, v193
	v_med3_f32 v82, v82, s79, v193
	v_mov_b32_e32 v197, v9
	v_cvt_pk_fp8_f32 v195, v84, v86 op_sel:[0,0,1]
	s_waitcnt vmcnt(19)
	v_mul_f32_e32 v84, 0x43800000, v100
	v_mul_f32_e32 v86, 0x43800000, v102
	v_cvt_pk_fp8_f32 v197, v80, v82
	v_med3_f32 v84, v84, s79, v193
	v_med3_f32 v86, v86, s79, v193
	v_cvt_pk_fp8_f32 v196, v84, v86 op_sel:[0,0,1]
	s_waitcnt vmcnt(18)
	v_mul_f32_e32 v84, 0x43800000, v108
	s_waitcnt vmcnt(17)
	v_mul_f32_e32 v86, 0x43800000, v110
	v_med3_f32 v84, v84, s79, v193
	v_med3_f32 v86, v86, s79, v193
	v_mul_f32_e32 v80, 0x43800000, v81
	v_mul_f32_e32 v81, 0x43800000, v83
	v_cvt_pk_fp8_f32 v197, v84, v86 op_sel:[0,0,1]
	v_med3_f32 v84, v80, s79, v193
	v_med3_f32 v81, v81, s79, v193
	v_mov_b32_e32 v80, v9
	v_cvt_pk_fp8_f32 v80, v84, v81
	v_mul_f32_e32 v82, 0x43800000, v85
	v_mul_f32_e32 v83, 0x43800000, v87
	v_med3_f32 v82, v82, s79, v193
	v_med3_f32 v83, v83, s79, v193
	v_cvt_pk_fp8_f32 v80, v82, v83 op_sel:[0,0,1]
	v_mul_f32_e32 v81, 0x43800000, v89
	v_mul_f32_e32 v82, 0x43800000, v91
	v_med3_f32 v85, v81, s79, v193
	v_med3_f32 v82, v82, s79, v193
	v_mov_b32_e32 v81, v9
	v_cvt_pk_fp8_f32 v81, v85, v82
	v_mul_f32_e32 v83, 0x43800000, v93
	v_mul_f32_e32 v84, 0x43800000, v95
	v_med3_f32 v83, v83, s79, v193
	v_med3_f32 v84, v84, s79, v193
	v_cvt_pk_fp8_f32 v81, v83, v84 op_sel:[0,0,1]
	v_mul_f32_e32 v82, 0x43800000, v97
	v_mul_f32_e32 v83, 0x43800000, v99
	v_med3_f32 v86, v82, s79, v193
	v_med3_f32 v83, v83, s79, v193
	v_mov_b32_e32 v82, v9
	v_cvt_pk_fp8_f32 v82, v86, v83
	v_mul_f32_e32 v84, 0x43800000, v101
	v_mul_f32_e32 v85, 0x43800000, v103
	v_med3_f32 v84, v84, s79, v193
	v_med3_f32 v85, v85, s79, v193
	v_cvt_pk_fp8_f32 v82, v84, v85 op_sel:[0,0,1]
	v_mul_f32_e32 v83, 0x43800000, v105
	v_mul_f32_e32 v84, 0x43800000, v107
	v_med3_f32 v87, v83, s79, v193
	v_med3_f32 v84, v84, s79, v193
	v_mov_b32_e32 v83, v9
	v_cvt_pk_fp8_f32 v83, v87, v84
	v_mul_f32_e32 v85, 0x43800000, v109
	v_mul_f32_e32 v86, 0x43800000, v111
	v_med3_f32 v85, v85, s79, v193
	v_med3_f32 v86, v86, s79, v193
	v_cvt_pk_fp8_f32 v83, v85, v86 op_sel:[0,0,1]
	global_load_dwordx2 v[144:145], v[144:145], off nt
	ds_write_b128 v8, v[194:197] offset:16
	global_load_dwordx2 v[146:147], v[146:147], off nt
	v_add_u32_e32 v8, v13, v11
	global_load_dwordx2 v[152:153], v[152:153], off nt
	ds_write_b128 v8, v[80:83]
	global_load_dwordx2 v[154:155], v[154:155], off nt
	v_add_co_u32_e32 v80, vcc, s96, v2
	s_mov_b32 s10, 0xa2000
; #define CV_LOAD(v, kb) do { _Pragma("unroll") for (int j = 0; j < 16; ++j) v[j] = __builtin_nontemporal_load((const f32x2*)(src + (size_t)((kb) * 16 + j) * ldw)); } while (0)
; __device__ __forceinline__ void tr128_f8(const float* W, int ldw, int srccol, unsigned char* WT, size_t dstrow0, int K, int k0, LAS unsigned char* tile, int lane) {
;     ...
;     CV_LOAD(va, 0); CV_LOAD(vb, 1); CV_LOAD(vc, 2);
;     CV_LOAD(vd, 3); CV_PUT(va, 0); CV_LOAD(va, 4); CV_PUT(vb, 1); CV_LOAD(vb, 5); CV_PUT(vc, 2); CV_LOAD(vc, 6); CV_PUT(vd, 3); CV_LOAD(vd, 7);
	s_nop 0
	v_addc_co_u32_e32 v81, vcc, 0, v3, vcc
	global_load_dwordx2 v[148:149], v[148:149], off nt
	v_add_co_u32_e32 v82, vcc, s10, v2
	global_load_dwordx2 v[150:151], v[150:151], off nt
	s_nop 0
	v_addc_co_u32_e32 v83, vcc, 0, v3, vcc
	global_load_dwordx2 v[160:161], v[160:161], off nt
	v_add_co_u32_e32 v84, vcc, s4, v2
	global_load_dwordx2 v[164:165], v[164:165], off nt
	s_nop 0
	v_addc_co_u32_e32 v85, vcc, 0, v3, vcc
	global_load_dwordx2 v[156:157], v[156:157], off nt
	s_mov_b32 s10, 0xa6000
	global_load_dwordx2 v[158:159], v[158:159], off nt
	v_add_co_u32_e32 v86, vcc, s10, v2
	global_load_dwordx2 v[170:171], v[170:171], off nt
	s_nop 0
	v_addc_co_u32_e32 v87, vcc, 0, v3, vcc
	global_load_dwordx2 v[172:173], v[172:173], off nt
	v_add_co_u32_e32 v88, vcc, s14, v2
	global_load_dwordx2 v[166:167], v[166:167], off nt
	s_nop 0
	v_addc_co_u32_e32 v89, vcc, 0, v3, vcc
	global_load_dwordx2 v[168:169], v[168:169], off nt
	s_mov_b32 s10, 0xaa000
	global_load_dwordx2 v[174:175], v[174:175], off nt
	v_add_co_u32_e32 v90, vcc, s10, v2
	global_load_dwordx2 v[176:177], v[176:177], off nt
	s_nop 0
	v_addc_co_u32_e32 v91, vcc, 0, v3, vcc
	v_add_co_u32_e32 v92, vcc, s18, v2
	s_mov_b32 s10, 0xae000
	s_nop 0
	v_addc_co_u32_e32 v93, vcc, 0, v3, vcc
	global_load_dwordx2 v[88:89], v[88:89], off nt
	v_mov_b32_e32 v194, v9
	global_load_dwordx2 v[90:91], v[90:91], off nt
	v_mov_b32_e32 v195, v9
	global_load_dwordx2 v[94:95], v[92:93], off nt
	v_add_co_u32_e32 v92, vcc, s10, v2
	s_mov_b32 s10, 0xb2000
	s_nop 0
	v_addc_co_u32_e32 v93, vcc, 0, v3, vcc
	global_load_dwordx2 v[100:101], v[92:93], off nt
	v_add_co_u32_e32 v92, vcc, s5, v2
	s_waitcnt vmcnt(36)
	v_mul_f32_e32 v8, 0x43800000, v112
	v_addc_co_u32_e32 v93, vcc, 0, v3, vcc
	v_add_co_u32_e32 v96, vcc, s10, v2
	s_waitcnt vmcnt(35)
	v_mul_f32_e32 v112, 0x43800000, v114
	v_addc_co_u32_e32 v97, vcc, 0, v3, vcc
	v_add_co_u32_e32 v98, vcc, s54, v2
	s_mov_b32 s10, 0xb6000
	s_nop 0
	v_addc_co_u32_e32 v99, vcc, 0, v3, vcc
	v_med3_f32 v8, v8, s79, v193
	v_med3_f32 v112, v112, s79, v193
	global_load_dwordx2 v[92:93], v[92:93], off nt
	v_cvt_pk_fp8_f32 v194, v8, v112
	global_load_dwordx2 v[96:97], v[96:97], off nt
	s_waitcnt vmcnt(36)
	v_mul_f32_e32 v8, 0x43800000, v120
	global_load_dwordx2 v[102:103], v[98:99], off nt
	v_add_co_u32_e32 v98, vcc, s10, v2
	s_waitcnt vmcnt(36)
	v_mul_f32_e32 v112, 0x43800000, v122
	v_addc_co_u32_e32 v99, vcc, 0, v3, vcc
	v_med3_f32 v8, v8, s79, v193
	v_med3_f32 v112, v112, s79, v193
	global_load_dwordx2 v[106:107], v[98:99], off nt
	s_waitcnt vmcnt(36)
	v_mul_f32_e32 v114, 0x43800000, v116
	s_waitcnt vmcnt(35)
	v_mul_f32_e32 v116, 0x43800000, v118
	v_cvt_pk_fp8_f32 v195, v8, v112
	s_waitcnt vmcnt(33)
	v_mul_f32_e32 v8, 0x43800000, v128
	s_waitcnt vmcnt(32)
	v_mul_f32_e32 v112, 0x43800000, v130
	v_med3_f32 v114, v114, s79, v193
	v_med3_f32 v116, v116, s79, v193
	v_med3_f32 v8, v8, s79, v193
	v_med3_f32 v112, v112, s79, v193
	v_mov_b32_e32 v196, v9
	v_cvt_pk_fp8_f32 v194, v114, v116 op_sel:[0,0,1]
	v_mul_f32_e32 v114, 0x43800000, v124
	s_waitcnt vmcnt(31)
	v_mul_f32_e32 v116, 0x43800000, v126
	v_cvt_pk_fp8_f32 v196, v8, v112
	s_waitcnt vmcnt(29)
	v_mul_f32_e32 v8, 0x43800000, v136
	s_waitcnt vmcnt(28)
	v_mul_f32_e32 v112, 0x43800000, v138
	v_med3_f32 v114, v114, s79, v193
	v_med3_f32 v116, v116, s79, v193
	v_med3_f32 v8, v8, s79, v193
	v_med3_f32 v112, v112, s79, v193
	v_mov_b32_e32 v197, v9
	v_cvt_pk_fp8_f32 v195, v114, v116 op_sel:[0,0,1]
	s_waitcnt vmcnt(27)
	v_mul_f32_e32 v114, 0x43800000, v132
	v_mul_f32_e32 v116, 0x43800000, v134
	v_cvt_pk_fp8_f32 v197, v8, v112
	v_mul_f32_e32 v8, 0x43800000, v113
	v_mul_f32_e32 v112, 0x43800000, v115
	v_med3_f32 v114, v114, s79, v193
	v_med3_f32 v116, v116, s79, v193
	v_med3_f32 v8, v8, s79, v193
	v_med3_f32 v115, v112, s79, v193
	v_mov_b32_e32 v112, v9
	v_cvt_pk_fp8_f32 v196, v114, v116 op_sel:[0,0,1]
	s_waitcnt vmcnt(26)
	v_mul_f32_e32 v114, 0x43800000, v140
	s_waitcnt vmcnt(25)
	v_mul_f32_e32 v116, 0x43800000, v142
	v_cvt_pk_fp8_f32 v112, v8, v115
	v_med3_f32 v114, v114, s79, v193
	v_med3_f32 v116, v116, s79, v193
	v_cvt_pk_fp8_f32 v197, v114, v116 op_sel:[0,0,1]
	v_mul_f32_e32 v113, 0x43800000, v117
	v_mul_f32_e32 v114, 0x43800000, v119
	v_med3_f32 v113, v113, s79, v193
	v_med3_f32 v114, v114, s79, v193
	v_cvt_pk_fp8_f32 v112, v113, v114 op_sel:[0,0,1]
	v_mul_f32_e32 v8, 0x43800000, v121
	v_mul_f32_e32 v113, 0x43800000, v123
	v_med3_f32 v8, v8, s79, v193
	v_med3_f32 v116, v113, s79, v193
	v_mov_b32_e32 v113, v9
	v_cvt_pk_fp8_f32 v113, v8, v116
	v_mul_f32_e32 v114, 0x43800000, v125
	v_mul_f32_e32 v115, 0x43800000, v127
	v_med3_f32 v114, v114, s79, v193
	v_med3_f32 v115, v115, s79, v193
	v_cvt_pk_fp8_f32 v113, v114, v115 op_sel:[0,0,1]
	v_mul_f32_e32 v8, 0x43800000, v129
	v_mul_f32_e32 v114, 0x43800000, v131
	v_med3_f32 v8, v8, s79, v193
	v_med3_f32 v117, v114, s79, v193
	v_mov_b32_e32 v114, v9
	v_cvt_pk_fp8_f32 v114, v8, v117
	v_mul_f32_e32 v115, 0x43800000, v133
	v_mul_f32_e32 v116, 0x43800000, v135
	v_med3_f32 v115, v115, s79, v193
	v_med3_f32 v116, v116, s79, v193
	v_cvt_pk_fp8_f32 v114, v115, v116 op_sel:[0,0,1]
	v_mul_f32_e32 v8, 0x43800000, v137
	v_mul_f32_e32 v115, 0x43800000, v139
	v_med3_f32 v8, v8, s79, v193
	v_med3_f32 v118, v115, s79, v193
	v_mov_b32_e32 v115, v9
	v_add_co_u32_e32 v98, vcc, s30, v2
	v_cvt_pk_fp8_f32 v115, v8, v118
	s_nop 0
	v_addc_co_u32_e32 v99, vcc, 0, v3, vcc
	s_mov_b32 s10, 0xba000
	v_add_co_u32_e32 v104, vcc, s10, v2
	v_mul_f32_e32 v116, 0x43800000, v141
	v_mul_f32_e32 v117, 0x43800000, v143
	v_addc_co_u32_e32 v105, vcc, 0, v3, vcc
	v_med3_f32 v116, v116, s79, v193
	v_med3_f32 v117, v117, s79, v193
	v_add_co_u32_e32 v108, vcc, s15, v2
	v_cvt_pk_fp8_f32 v115, v116, v117 op_sel:[0,0,1]
	s_nop 0
	v_addc_co_u32_e32 v109, vcc, 0, v3, vcc
	s_mov_b32 s10, 0xbe000
	v_add_co_u32_e32 v110, vcc, s10, v2
	v_add_u32_e32 v116, v13, v19
	s_nop 0
	v_addc_co_u32_e32 v111, vcc, 0, v3, vcc
	ds_write_b128 v116, v[112:115]
	v_add_co_u32_e32 v112, vcc, s17, v2
	s_mov_b32 s10, 0xc2000
	s_nop 0
	v_addc_co_u32_e32 v113, vcc, 0, v3, vcc
	v_add_co_u32_e32 v114, vcc, s10, v2
	s_mov_b32 s10, 0xc6000
	s_nop 0
	v_addc_co_u32_e32 v115, vcc, 0, v3, vcc
	v_add_co_u32_e32 v116, vcc, s19, v2
	global_load_dwordx2 v[112:113], v[112:113], off nt
	s_nop 0
	v_addc_co_u32_e32 v117, vcc, 0, v3, vcc
	global_load_dwordx2 v[114:115], v[114:115], off nt
	v_add_u32_e32 v8, v7, v17
	global_load_dwordx2 v[118:119], v[116:117], off nt
	v_add_co_u32_e32 v116, vcc, s10, v2
	s_mov_b32 s10, 0xca000
	s_nop 0
	v_addc_co_u32_e32 v117, vcc, 0, v3, vcc
	global_load_dwordx2 v[124:125], v[116:117], off nt
	v_add_co_u32_e32 v116, vcc, s28, v2
	global_load_dwordx2 v[4:5], v[4:5], off nt
	s_nop 0
	v_addc_co_u32_e32 v117, vcc, 0, v3, vcc
	v_add_co_u32_e32 v120, vcc, s10, v2
	global_load_dwordx2 v[50:51], v[50:51], off nt
	s_nop 0
	v_addc_co_u32_e32 v121, vcc, 0, v3, vcc
	v_add_co_u32_e32 v122, vcc, s52, v2
	s_mov_b32 s10, 0xce000
	s_nop 0
	v_addc_co_u32_e32 v123, vcc, 0, v3, vcc
	global_load_dwordx2 v[116:117], v[116:117], off nt
	s_waitcnt vmcnt(30)
; #define CV_LOAD(v, kb) do { _Pragma("unroll") for (int j = 0; j < 16; ++j) v[j] = __builtin_nontemporal_load((const f32x2*)(src + (size_t)((kb) * 16 + j) * ldw)); } while (0)
; __device__ __forceinline__ void tr128_f8(const float* W, int ldw, int srccol, unsigned char* WT, size_t dstrow0, int K, int k0, LAS unsigned char* tile, int lane) {
;     ...
;     CV_LOAD(va, 0); CV_LOAD(vb, 1); CV_LOAD(vc, 2);
;     CV_LOAD(vd, 3); CV_PUT(va, 0); CV_LOAD(va, 4); CV_PUT(vb, 1); CV_LOAD(vb, 5); CV_PUT(vc, 2); CV_LOAD(vc, 6); CV_PUT(vd, 3); CV_LOAD(vd, 7);
	v_mul_f32_e32 v144, 0x43800000, v144
	global_load_dwordx2 v[120:121], v[120:121], off nt
	s_waitcnt vmcnt(30)
	v_mul_f32_e32 v146, 0x43800000, v146
	global_load_dwordx2 v[126:127], v[122:123], off nt
	v_add_co_u32_e32 v122, vcc, s10, v2
	global_load_dwordx2 v[54:55], v[54:55], off nt
	s_nop 0
	v_addc_co_u32_e32 v123, vcc, 0, v3, vcc
	global_load_dwordx2 v[56:57], v[56:57], off nt
	s_mov_b32 s10, 0xd2000
	global_load_dwordx2 v[58:59], v[58:59], off nt
	ds_write_b128 v8, v[194:197]
	global_load_dwordx2 v[132:133], v[122:123], off nt
	v_add_co_u32_e32 v122, vcc, s56, v2
	global_load_dwordx2 v[52:53], v[52:53], off nt
	s_nop 0
	v_addc_co_u32_e32 v123, vcc, 0, v3, vcc
	global_load_dwordx2 v[62:63], v[62:63], off nt
	v_add_co_u32_e32 v128, vcc, s10, v2
	global_load_dwordx2 v[64:65], v[64:65], off nt
	s_nop 0
	v_addc_co_u32_e32 v129, vcc, 0, v3, vcc
	global_load_dwordx2 v[66:67], v[66:67], off nt
	v_add_co_u32_e32 v130, vcc, s60, v2
	global_load_dwordx2 v[60:61], v[60:61], off nt
	s_nop 0
	v_addc_co_u32_e32 v131, vcc, 0, v3, vcc
	global_load_dwordx2 v[70:71], v[70:71], off nt
	s_mov_b32 s10, 0xd6000
	global_load_dwordx2 v[72:73], v[72:73], off nt
	v_med3_f32 v144, v144, s79, v193
	global_load_dwordx2 v[74:75], v[74:75], off nt
	v_med3_f32 v146, v146, s79, v193
	global_load_dwordx2 v[68:69], v[68:69], off nt
	v_mov_b32_e32 v194, v9
	global_load_dwordx2 v[122:123], v[122:123], off nt
	v_cvt_pk_fp8_f32 v194, v144, v146
	global_load_dwordx2 v[128:129], v[128:129], off nt
	v_mov_b32_e32 v195, v9
	global_load_dwordx2 v[134:135], v[130:131], off nt
	v_add_co_u32_e32 v130, vcc, s10, v2
	global_load_dwordx2 v[76:77], v[76:77], off nt
	s_nop 0
	v_addc_co_u32_e32 v131, vcc, 0, v3, vcc
	global_load_dwordx2 v[138:139], v[130:131], off nt
	s_waitcnt vmcnt(48)
	v_mul_f32_e32 v144, 0x43800000, v152
	s_waitcnt vmcnt(47)
	v_mul_f32_e32 v146, 0x43800000, v154
	v_med3_f32 v144, v144, s79, v193
	v_med3_f32 v146, v146, s79, v193
	s_waitcnt vmcnt(46)
	v_mul_f32_e32 v148, 0x43800000, v148
	s_waitcnt vmcnt(45)
	v_mul_f32_e32 v150, 0x43800000, v150
	v_cvt_pk_fp8_f32 v195, v144, v146
	s_waitcnt vmcnt(44)
	v_mul_f32_e32 v144, 0x43800000, v160
	s_waitcnt vmcnt(43)
	v_mul_f32_e32 v146, 0x43800000, v164
	v_med3_f32 v148, v148, s79, v193
	v_med3_f32 v150, v150, s79, v193
	v_med3_f32 v144, v144, s79, v193
	v_med3_f32 v146, v146, s79, v193
	v_mov_b32_e32 v196, v9
	v_cvt_pk_fp8_f32 v194, v148, v150 op_sel:[0,0,1]
	s_waitcnt vmcnt(42)
	v_mul_f32_e32 v148, 0x43800000, v156
	s_waitcnt vmcnt(41)
	v_mul_f32_e32 v150, 0x43800000, v158
	v_cvt_pk_fp8_f32 v196, v144, v146
	s_waitcnt vmcnt(40)
	v_mul_f32_e32 v144, 0x43800000, v170
	s_waitcnt vmcnt(39)
	v_mul_f32_e32 v146, 0x43800000, v172
	v_med3_f32 v148, v148, s79, v193
	v_med3_f32 v150, v150, s79, v193
	v_med3_f32 v144, v144, s79, v193
	v_med3_f32 v146, v146, s79, v193
	v_mov_b32_e32 v197, v9
	v_cvt_pk_fp8_f32 v195, v148, v150 op_sel:[0,0,1]
	s_waitcnt vmcnt(38)
	v_mul_f32_e32 v148, 0x43800000, v166
	s_waitcnt vmcnt(37)
	v_mul_f32_e32 v150, 0x43800000, v168
	v_cvt_pk_fp8_f32 v197, v144, v146
	v_med3_f32 v148, v148, s79, v193
	v_med3_f32 v150, v150, s79, v193
	v_cvt_pk_fp8_f32 v196, v148, v150 op_sel:[0,0,1]
	s_waitcnt vmcnt(36)
	v_mul_f32_e32 v148, 0x43800000, v174
	s_waitcnt vmcnt(35)
	v_mul_f32_e32 v150, 0x43800000, v176
	v_med3_f32 v148, v148, s79, v193
	v_med3_f32 v150, v150, s79, v193
	v_mul_f32_e32 v144, 0x43800000, v145
	v_mul_f32_e32 v145, 0x43800000, v147
	v_cvt_pk_fp8_f32 v197, v148, v150 op_sel:[0,0,1]
	v_med3_f32 v148, v144, s79, v193
	v_med3_f32 v145, v145, s79, v193
	v_mov_b32_e32 v144, v9
	v_cvt_pk_fp8_f32 v144, v148, v145
	v_mul_f32_e32 v146, 0x43800000, v149
	v_mul_f32_e32 v147, 0x43800000, v151
	v_med3_f32 v146, v146, s79, v193
	v_med3_f32 v147, v147, s79, v193
	v_cvt_pk_fp8_f32 v144, v146, v147 op_sel:[0,0,1]
	v_mul_f32_e32 v145, 0x43800000, v153
	v_mul_f32_e32 v146, 0x43800000, v155
	v_med3_f32 v149, v145, s79, v193
	v_med3_f32 v146, v146, s79, v193
	v_mov_b32_e32 v145, v9
	v_cvt_pk_fp8_f32 v145, v149, v146
	v_mul_f32_e32 v147, 0x43800000, v157
	v_mul_f32_e32 v148, 0x43800000, v159
	v_med3_f32 v147, v147, s79, v193
	v_med3_f32 v148, v148, s79, v193
	v_cvt_pk_fp8_f32 v145, v147, v148 op_sel:[0,0,1]
	v_mul_f32_e32 v146, 0x43800000, v161
	v_mul_f32_e32 v147, 0x43800000, v165
	v_med3_f32 v150, v146, s79, v193
	v_med3_f32 v147, v147, s79, v193
	v_mov_b32_e32 v146, v9
	v_cvt_pk_fp8_f32 v146, v150, v147
	v_mul_f32_e32 v148, 0x43800000, v167
	v_mul_f32_e32 v149, 0x43800000, v169
	v_med3_f32 v148, v148, s79, v193
	v_med3_f32 v149, v149, s79, v193
	v_cvt_pk_fp8_f32 v146, v148, v149 op_sel:[0,0,1]
	v_mul_f32_e32 v147, 0x43800000, v171
	v_mul_f32_e32 v148, 0x43800000, v173
	v_med3_f32 v151, v147, s79, v193
	v_med3_f32 v148, v148, s79, v193
	v_mov_b32_e32 v147, v9
	global_load_dwordx2 v[80:81], v[80:81], off nt
	v_add_co_u32_e32 v130, vcc, s64, v2
	global_load_dwordx2 v[82:83], v[82:83], off nt
	v_cvt_pk_fp8_f32 v147, v151, v148
	global_load_dwordx2 v[84:85], v[84:85], off nt
	v_addc_co_u32_e32 v131, vcc, 0, v3, vcc
	s_mov_b32 s10, 0xda000
	v_add_co_u32_e32 v136, vcc, s10, v2
	v_mul_f32_e32 v149, 0x43800000, v175
	v_mul_f32_e32 v150, 0x43800000, v177
	v_addc_co_u32_e32 v137, vcc, 0, v3, vcc
	v_med3_f32 v149, v149, s79, v193
	v_med3_f32 v150, v150, s79, v193
	global_load_dwordx2 v[86:87], v[86:87], off nt
	v_add_co_u32_e32 v140, vcc, s68, v2
	v_cvt_pk_fp8_f32 v147, v149, v150 op_sel:[0,0,1]
	s_nop 0
	v_addc_co_u32_e32 v141, vcc, 0, v3, vcc
	s_mov_b32 s10, 0xde000
	v_add_co_u32_e32 v142, vcc, s10, v2
	ds_write_b128 v8, v[194:197] offset:16
	s_nop 0
	v_addc_co_u32_e32 v143, vcc, 0, v3, vcc
	v_add_u32_e32 v8, v13, v21
	ds_write_b128 v8, v[144:147]
	v_add_co_u32_e32 v144, vcc, s72, v2
	s_mov_b32 s10, 0xe2000
	s_nop 0
	v_addc_co_u32_e32 v145, vcc, 0, v3, vcc
	v_add_co_u32_e32 v146, vcc, s10, v2
	s_mov_b32 s10, 0xe6000
	s_nop 0
	v_addc_co_u32_e32 v147, vcc, 0, v3, vcc
	v_add_co_u32_e32 v148, vcc, s76, v2
	global_load_dwordx2 v[144:145], v[144:145], off nt
	s_nop 0
	v_addc_co_u32_e32 v149, vcc, 0, v3, vcc
	global_load_dwordx2 v[146:147], v[146:147], off nt
	s_waitcnt vmcnt(27)
; #define CV_LOAD(v, kb) do { _Pragma("unroll") for (int j = 0; j < 16; ++j) v[j] = __builtin_nontemporal_load((const f32x2*)(src + (size_t)((kb) * 16 + j) * ldw)); } while (0)
; __device__ __forceinline__ void tr128_f8(const float* W, int ldw, int srccol, unsigned char* WT, size_t dstrow0, int K, int k0, LAS unsigned char* tile, int lane) {
;     ...
;     CV_LOAD(va, 0); CV_LOAD(vb, 1); CV_LOAD(vc, 2);
;     CV_LOAD(vd, 3); CV_PUT(va, 0); CV_LOAD(va, 4); CV_PUT(vb, 1); CV_LOAD(vb, 5); CV_PUT(vc, 2); CV_LOAD(vc, 6); CV_PUT(vd, 3); CV_LOAD(vd, 7);
	v_mul_f32_e32 v8, 0x43800000, v50
	global_load_dwordx2 v[150:151], v[148:149], off nt
	v_add_co_u32_e32 v148, vcc, s10, v2
	s_mov_b32 s10, 0xea000
	s_nop 0
	v_addc_co_u32_e32 v149, vcc, 0, v3, vcc
	global_load_dwordx2 v[156:157], v[148:149], off nt
	v_add_co_u32_e32 v148, vcc, s81, v2
	global_load_dwordx2 v[98:99], v[98:99], off nt
	s_nop 0
	v_addc_co_u32_e32 v149, vcc, 0, v3, vcc
	global_load_dwordx2 v[104:105], v[104:105], off nt
	v_add_co_u32_e32 v152, vcc, s10, v2
	global_load_dwordx2 v[108:109], v[108:109], off nt
	s_nop 0
	v_addc_co_u32_e32 v153, vcc, 0, v3, vcc
	v_add_co_u32_e32 v154, vcc, s85, v2
	s_mov_b32 s10, 0xee000
	s_nop 0
	v_addc_co_u32_e32 v155, vcc, 0, v3, vcc
	global_load_dwordx2 v[110:111], v[110:111], off nt
	v_med3_f32 v8, v8, s79, v193
	global_load_dwordx2 v[148:149], v[148:149], off nt
	v_mov_b32_e32 v194, v9
	global_load_dwordx2 v[152:153], v[152:153], off nt
	v_mov_b32_e32 v195, v9
	global_load_dwordx2 v[158:159], v[154:155], off nt
	v_add_co_u32_e32 v154, vcc, s10, v2
	s_mov_b32 s10, 0xf2000
	s_nop 0
	v_addc_co_u32_e32 v155, vcc, 0, v3, vcc
	global_load_dwordx2 v[166:167], v[154:155], off nt
	v_add_co_u32_e32 v154, vcc, s89, v2
	s_waitcnt vmcnt(29)
	v_mul_f32_e32 v50, 0x43800000, v52
	v_addc_co_u32_e32 v155, vcc, 0, v3, vcc
	v_add_co_u32_e32 v160, vcc, s10, v2
	s_mov_b32 s10, 0xf6000
	s_nop 0
	v_addc_co_u32_e32 v161, vcc, 0, v3, vcc
	v_add_co_u32_e32 v164, vcc, s93, v2
	global_load_dwordx2 v[154:155], v[154:155], off nt
	s_nop 0
	v_addc_co_u32_e32 v165, vcc, 0, v3, vcc
	global_load_dwordx2 v[160:161], v[160:161], off nt
	v_mul_f32_e32 v52, 0x43800000, v54
	global_load_dwordx2 v[168:169], v[164:165], off nt
	v_add_co_u32_e32 v164, vcc, s10, v2
	s_mov_b32 s10, 0xfa000
	s_nop 0
	v_addc_co_u32_e32 v165, vcc, 0, v3, vcc
	global_load_dwordx2 v[172:173], v[164:165], off nt
	v_add_co_u32_e32 v164, vcc, s97, v2
	v_med3_f32 v50, v50, s79, v193
	s_nop 0
	v_addc_co_u32_e32 v165, vcc, 0, v3, vcc
	v_add_co_u32_e32 v170, vcc, s10, v2
	s_mov_b32 s10, 0xfe000
	s_nop 0
	v_addc_co_u32_e32 v171, vcc, 0, v3, vcc
	v_add_co_u32_e32 v174, vcc, s16, v2
	v_med3_f32 v52, v52, s79, v193
	s_nop 0
	v_addc_co_u32_e32 v175, vcc, 0, v3, vcc
	v_add_co_u32_e32 v2, vcc, s10, v2
	v_mov_b32_e32 v196, v9
	s_nop 0
	v_addc_co_u32_e32 v3, vcc, 0, v3, vcc
	global_load_dwordx2 v[2:3], v[2:3], off nt
	v_mul_f32_e32 v4, 0x43800000, v4
	v_med3_f32 v4, v4, s79, v193
	v_cvt_pk_fp8_f32 v194, v4, v8
	v_mul_f32_e32 v4, 0x43800000, v56
	v_mul_f32_e32 v8, 0x43800000, v58
	v_med3_f32 v4, v4, s79, v193
	v_med3_f32 v8, v8, s79, v193
	v_cvt_pk_fp8_f32 v195, v4, v8
	s_waitcnt vmcnt(32)
	v_mul_f32_e32 v4, 0x43800000, v64
	s_waitcnt vmcnt(31)
	v_mul_f32_e32 v8, 0x43800000, v66
	v_med3_f32 v4, v4, s79, v193
	v_med3_f32 v8, v8, s79, v193
	v_cvt_pk_fp8_f32 v194, v50, v52 op_sel:[0,0,1]
	s_waitcnt vmcnt(30)
	v_mul_f32_e32 v50, 0x43800000, v60
	v_mul_f32_e32 v52, 0x43800000, v62
	v_cvt_pk_fp8_f32 v196, v4, v8
	s_waitcnt vmcnt(28)
	v_mul_f32_e32 v4, 0x43800000, v72
	s_waitcnt vmcnt(27)
	v_mul_f32_e32 v8, 0x43800000, v74
	v_med3_f32 v50, v50, s79, v193
	v_med3_f32 v52, v52, s79, v193
	v_med3_f32 v4, v4, s79, v193
	v_med3_f32 v8, v8, s79, v193
	v_mov_b32_e32 v197, v9
	v_cvt_pk_fp8_f32 v195, v50, v52 op_sel:[0,0,1]
	s_waitcnt vmcnt(26)
	v_mul_f32_e32 v50, 0x43800000, v68
	v_mul_f32_e32 v52, 0x43800000, v70
	v_cvt_pk_fp8_f32 v197, v4, v8
	v_med3_f32 v50, v50, s79, v193
	v_med3_f32 v52, v52, s79, v193
	v_cvt_pk_fp8_f32 v196, v50, v52 op_sel:[0,0,1]
	s_waitcnt vmcnt(22)
	v_mul_f32_e32 v50, 0x43800000, v76
	v_mul_f32_e32 v52, 0x43800000, v78
	v_med3_f32 v50, v50, s79, v193
	v_med3_f32 v52, v52, s79, v193
	v_cvt_pk_fp8_f32 v197, v50, v52 op_sel:[0,0,1]
	v_mul_f32_e32 v4, 0x43800000, v5
	v_mul_f32_e32 v5, 0x43800000, v51
	v_mul_f32_e32 v50, 0x43800000, v55
	v_med3_f32 v4, v4, s79, v193
	v_med3_f32 v5, v5, s79, v193
	v_med3_f32 v51, v50, s79, v193
	v_mov_b32_e32 v50, v9
	v_cvt_pk_fp8_f32 v50, v4, v5
	v_mul_f32_e32 v8, 0x43800000, v53
	v_med3_f32 v8, v8, s79, v193
	v_mul_f32_e32 v4, 0x43800000, v57
	v_cvt_pk_fp8_f32 v50, v8, v51 op_sel:[0,0,1]
	v_mul_f32_e32 v5, 0x43800000, v59
	v_mul_f32_e32 v51, 0x43800000, v63
	v_med3_f32 v4, v4, s79, v193
	v_med3_f32 v5, v5, s79, v193
	v_med3_f32 v52, v51, s79, v193
	v_mov_b32_e32 v51, v9
	v_cvt_pk_fp8_f32 v51, v4, v5
	v_mul_f32_e32 v8, 0x43800000, v61
	v_med3_f32 v8, v8, s79, v193
	v_mul_f32_e32 v4, 0x43800000, v65
	v_cvt_pk_fp8_f32 v51, v8, v52 op_sel:[0,0,1]
	v_mul_f32_e32 v5, 0x43800000, v67
	v_mul_f32_e32 v52, 0x43800000, v71
	v_med3_f32 v4, v4, s79, v193
	v_med3_f32 v5, v5, s79, v193
	v_med3_f32 v53, v52, s79, v193
	v_mov_b32_e32 v52, v9
	v_cvt_pk_fp8_f32 v52, v4, v5
	v_mul_f32_e32 v8, 0x43800000, v69
	v_med3_f32 v8, v8, s79, v193
	global_load_dwordx2 v[130:131], v[130:131], off nt
	v_cvt_pk_fp8_f32 v52, v8, v53 op_sel:[0,0,1]
	global_load_dwordx2 v[136:137], v[136:137], off nt
	v_mul_f32_e32 v4, 0x43800000, v73
	global_load_dwordx2 v[140:141], v[140:141], off nt
	v_mul_f32_e32 v5, 0x43800000, v75
	global_load_dwordx2 v[142:143], v[142:143], off nt
	v_mul_f32_e32 v53, 0x43800000, v79
	v_med3_f32 v4, v4, s79, v193
	v_med3_f32 v5, v5, s79, v193
	v_med3_f32 v54, v53, s79, v193
	v_mov_b32_e32 v53, v9
	v_cvt_pk_fp8_f32 v53, v4, v5
	v_mul_f32_e32 v8, 0x43800000, v77
	v_med3_f32 v8, v8, s79, v193
	v_add_u32_e32 v5, v13, v25
	v_cvt_pk_fp8_f32 v53, v8, v54 op_sel:[0,0,1]
	s_waitcnt vmcnt(23)
	v_mul_f32_e32 v8, 0x43800000, v82
	v_med3_f32 v8, v8, s79, v193
	global_load_dwordx2 v[164:165], v[164:165], off nt
	ds_write_b128 v5, v[50:53]
	v_mul_f32_e32 v5, 0x43800000, v80
	s_waitcnt vmcnt(23)
; #define CV_LOAD(v, kb) do { _Pragma("unroll") for (int j = 0; j < 16; ++j) v[j] = __builtin_nontemporal_load((const f32x2*)(src + (size_t)((kb) * 16 + j) * ldw)); } while (0)
; __device__ __forceinline__ void tr128_f8(const float* W, int ldw, int srccol, unsigned char* WT, size_t dstrow0, int K, int k0, LAS unsigned char* tile, int lane) {
;     ...
;     CV_LOAD(va, 0); CV_LOAD(vb, 1); CV_LOAD(vc, 2);
;     CV_LOAD(vd, 3); CV_PUT(va, 0); CV_LOAD(va, 4); CV_PUT(vb, 1); CV_LOAD(vb, 5); CV_PUT(vc, 2); CV_LOAD(vc, 6); CV_PUT(vd, 3); CV_LOAD(vd, 7);
;     CV_PUT(va, 4); CV_PUT(vb, 5); CV_PUT(vc, 6); CV_PUT(vd, 7);
	v_mul_f32_e32 v50, 0x43800000, v84
	v_med3_f32 v5, v5, s79, v193
	v_med3_f32 v52, v50, s79, v193
	v_mov_b32_e32 v50, v9
	v_cvt_pk_fp8_f32 v50, v5, v8
	s_waitcnt vmcnt(22)
	v_mul_f32_e32 v51, 0x43800000, v86
	v_med3_f32 v51, v51, s79, v193
	v_mul_f32_e32 v5, 0x43800000, v88
	v_cvt_pk_fp8_f32 v50, v52, v51 op_sel:[0,0,1]
	v_mul_f32_e32 v8, 0x43800000, v90
	v_mul_f32_e32 v51, 0x43800000, v94
	v_med3_f32 v5, v5, s79, v193
	v_med3_f32 v8, v8, s79, v193
	v_med3_f32 v53, v51, s79, v193
	v_mov_b32_e32 v51, v9
	v_cvt_pk_fp8_f32 v51, v5, v8
	v_mul_f32_e32 v52, 0x43800000, v100
	v_med3_f32 v52, v52, s79, v193
	v_mul_f32_e32 v5, 0x43800000, v92
	v_cvt_pk_fp8_f32 v51, v53, v52 op_sel:[0,0,1]
	v_mul_f32_e32 v8, 0x43800000, v96
	v_mul_f32_e32 v52, 0x43800000, v102
	v_med3_f32 v5, v5, s79, v193
	v_med3_f32 v8, v8, s79, v193
	v_med3_f32 v54, v52, s79, v193
	v_mov_b32_e32 v52, v9
	v_cvt_pk_fp8_f32 v52, v5, v8
	v_mul_f32_e32 v53, 0x43800000, v106
	v_med3_f32 v53, v53, s79, v193
	s_waitcnt vmcnt(17)
	v_mul_f32_e32 v5, 0x43800000, v98
	v_cvt_pk_fp8_f32 v52, v54, v53 op_sel:[0,0,1]
	s_waitcnt vmcnt(16)
	v_mul_f32_e32 v8, 0x43800000, v104
	s_waitcnt vmcnt(15)
	v_mul_f32_e32 v53, 0x43800000, v108
	v_med3_f32 v5, v5, s79, v193
	v_med3_f32 v8, v8, s79, v193
	v_med3_f32 v55, v53, s79, v193
	v_mov_b32_e32 v53, v9
	v_cvt_pk_fp8_f32 v53, v5, v8
	s_waitcnt vmcnt(14)
	v_mul_f32_e32 v54, 0x43800000, v110
	v_med3_f32 v54, v54, s79, v193
	v_mul_f32_e32 v5, 0x43800000, v81
	v_cvt_pk_fp8_f32 v53, v55, v54 op_sel:[0,0,1]
	v_mul_f32_e32 v8, 0x43800000, v83
	v_mul_f32_e32 v54, 0x43800000, v85
	v_med3_f32 v5, v5, s79, v193
	v_med3_f32 v8, v8, s79, v193
	v_med3_f32 v56, v54, s79, v193
	v_mov_b32_e32 v54, v9
	v_cvt_pk_fp8_f32 v54, v5, v8
	v_mul_f32_e32 v55, 0x43800000, v87
	v_med3_f32 v55, v55, s79, v193
	v_mul_f32_e32 v5, 0x43800000, v89
	v_cvt_pk_fp8_f32 v54, v56, v55 op_sel:[0,0,1]
	v_mul_f32_e32 v8, 0x43800000, v91
	v_mul_f32_e32 v55, 0x43800000, v95
	v_med3_f32 v5, v5, s79, v193
	v_med3_f32 v8, v8, s79, v193
	v_med3_f32 v57, v55, s79, v193
	v_mov_b32_e32 v55, v9
	v_cvt_pk_fp8_f32 v55, v5, v8
	v_mul_f32_e32 v56, 0x43800000, v101
	v_med3_f32 v56, v56, s79, v193
	v_mul_f32_e32 v5, 0x43800000, v93
	v_cvt_pk_fp8_f32 v55, v57, v56 op_sel:[0,0,1]
	v_mul_f32_e32 v8, 0x43800000, v97
	v_mul_f32_e32 v56, 0x43800000, v103
	v_med3_f32 v5, v5, s79, v193
	v_med3_f32 v8, v8, s79, v193
	v_med3_f32 v58, v56, s79, v193
	v_mov_b32_e32 v56, v9
	v_cvt_pk_fp8_f32 v56, v5, v8
	v_mul_f32_e32 v57, 0x43800000, v107
	v_med3_f32 v57, v57, s79, v193
	global_load_dwordx2 v[170:171], v[170:171], off nt
	v_cvt_pk_fp8_f32 v56, v58, v57 op_sel:[0,0,1]
	global_load_dwordx2 v[174:175], v[174:175], off nt
	v_mul_f32_e32 v5, 0x43800000, v99
	v_mul_f32_e32 v8, 0x43800000, v105
	v_mul_f32_e32 v57, 0x43800000, v109
	v_med3_f32 v5, v5, s79, v193
	v_med3_f32 v8, v8, s79, v193
	v_med3_f32 v59, v57, s79, v193
	v_mov_b32_e32 v57, v9
	v_cvt_pk_fp8_f32 v57, v5, v8
	v_mul_f32_e32 v58, 0x43800000, v111
	v_med3_f32 v58, v58, s79, v193
	v_add_u32_e32 v4, v7, v23
	v_cvt_pk_fp8_f32 v57, v59, v58 op_sel:[0,0,1]
	ds_write_b128 v4, v[194:197]
	ds_write_b128 v4, v[50:53] offset:16
	v_add_u32_e32 v4, v13, v27
	ds_write_b128 v4, v[54:57]
	v_mul_f32_e32 v4, 0x43800000, v112
	v_mul_f32_e32 v5, 0x43800000, v114
	v_mul_f32_e32 v50, 0x43800000, v124
	v_med3_f32 v4, v4, s79, v193
	v_med3_f32 v5, v5, s79, v193
	v_med3_f32 v51, v50, s79, v193
	v_mov_b32_e32 v50, v9
	v_cvt_pk_fp8_f32 v50, v4, v5
	v_mul_f32_e32 v8, 0x43800000, v118
	v_med3_f32 v8, v8, s79, v193
	v_mul_f32_e32 v4, 0x43800000, v116
	v_cvt_pk_fp8_f32 v50, v8, v51 op_sel:[0,0,1]
	v_mul_f32_e32 v5, 0x43800000, v120
	v_mul_f32_e32 v51, 0x43800000, v132
	v_med3_f32 v4, v4, s79, v193
	v_med3_f32 v5, v5, s79, v193
	v_med3_f32 v52, v51, s79, v193
	v_mov_b32_e32 v51, v9
	v_cvt_pk_fp8_f32 v51, v4, v5
	v_mul_f32_e32 v8, 0x43800000, v126
	v_med3_f32 v8, v8, s79, v193
	v_mul_f32_e32 v4, 0x43800000, v122
	v_cvt_pk_fp8_f32 v51, v8, v52 op_sel:[0,0,1]
	v_mul_f32_e32 v5, 0x43800000, v128
	v_mul_f32_e32 v52, 0x43800000, v138
	v_med3_f32 v4, v4, s79, v193
	v_med3_f32 v5, v5, s79, v193
	v_med3_f32 v53, v52, s79, v193
	v_mov_b32_e32 v52, v9
	v_cvt_pk_fp8_f32 v52, v4, v5
	v_mul_f32_e32 v8, 0x43800000, v134
	v_med3_f32 v8, v8, s79, v193
	s_waitcnt vmcnt(6)
	v_mul_f32_e32 v4, 0x43800000, v130
	v_cvt_pk_fp8_f32 v52, v8, v53 op_sel:[0,0,1]
	s_waitcnt vmcnt(5)
	v_mul_f32_e32 v5, 0x43800000, v136
	s_waitcnt vmcnt(3)
; #define LDS_WAIT() asm volatile("s_waitcnt lgkmcnt(0)" ::: "memory")
; #define CV_LOAD(v, kb) do { _Pragma("unroll") for (int j = 0; j < 16; ++j) v[j] = __builtin_nontemporal_load((const f32x2*)(src + (size_t)((kb) * 16 + j) * ldw)); } while (0)
; __device__ __forceinline__ void tr128_f8(const float* W, int ldw, int srccol, unsigned char* WT, size_t dstrow0, int K, int k0, LAS unsigned char* tile, int lane) {
;     ...
;     CV_LOAD(va, 0); CV_LOAD(vb, 1); CV_LOAD(vc, 2);
;     CV_LOAD(vd, 3); CV_PUT(va, 0); CV_LOAD(va, 4); CV_PUT(vb, 1); CV_LOAD(vb, 5); CV_PUT(vc, 2); CV_LOAD(vc, 6); CV_PUT(vd, 3); CV_LOAD(vd, 7);
;     CV_PUT(va, 4); CV_PUT(vb, 5); CV_PUT(vc, 6); CV_PUT(vd, 7);
;     ...
;     LDS_WAIT(); asm volatile("" ::: "memory");
	v_mul_f32_e32 v53, 0x43800000, v142
	v_med3_f32 v4, v4, s79, v193
	v_med3_f32 v5, v5, s79, v193
	v_med3_f32 v54, v53, s79, v193
	v_mov_b32_e32 v53, v9
	v_cvt_pk_fp8_f32 v53, v4, v5
	v_mul_f32_e32 v8, 0x43800000, v140
	v_med3_f32 v8, v8, s79, v193
	v_mul_f32_e32 v4, 0x43800000, v113
	v_cvt_pk_fp8_f32 v53, v8, v54 op_sel:[0,0,1]
	v_mul_f32_e32 v5, 0x43800000, v115
	v_mul_f32_e32 v54, 0x43800000, v125
	v_med3_f32 v4, v4, s79, v193
	v_med3_f32 v5, v5, s79, v193
	v_med3_f32 v55, v54, s79, v193
	v_mov_b32_e32 v54, v9
	v_cvt_pk_fp8_f32 v54, v4, v5
	v_mul_f32_e32 v8, 0x43800000, v119
	v_med3_f32 v8, v8, s79, v193
	v_mul_f32_e32 v4, 0x43800000, v117
	v_cvt_pk_fp8_f32 v54, v8, v55 op_sel:[0,0,1]
	v_mul_f32_e32 v5, 0x43800000, v121
	v_mul_f32_e32 v55, 0x43800000, v133
	v_med3_f32 v4, v4, s79, v193
	v_med3_f32 v5, v5, s79, v193
	v_med3_f32 v56, v55, s79, v193
	v_mov_b32_e32 v55, v9
	v_cvt_pk_fp8_f32 v55, v4, v5
	v_mul_f32_e32 v8, 0x43800000, v127
	v_med3_f32 v8, v8, s79, v193
	v_mul_f32_e32 v4, 0x43800000, v123
	v_cvt_pk_fp8_f32 v55, v8, v56 op_sel:[0,0,1]
	v_mul_f32_e32 v5, 0x43800000, v129
	v_mul_f32_e32 v56, 0x43800000, v139
	v_med3_f32 v4, v4, s79, v193
	v_med3_f32 v5, v5, s79, v193
	v_med3_f32 v57, v56, s79, v193
	v_mov_b32_e32 v56, v9
	v_cvt_pk_fp8_f32 v56, v4, v5
	v_mul_f32_e32 v8, 0x43800000, v135
	v_med3_f32 v8, v8, s79, v193
	v_mul_f32_e32 v4, 0x43800000, v131
	v_cvt_pk_fp8_f32 v56, v8, v57 op_sel:[0,0,1]
	v_mul_f32_e32 v5, 0x43800000, v137
	v_mul_f32_e32 v57, 0x43800000, v143
	v_med3_f32 v4, v4, s79, v193
	v_med3_f32 v5, v5, s79, v193
	v_med3_f32 v58, v57, s79, v193
	v_mov_b32_e32 v57, v9
	v_cvt_pk_fp8_f32 v57, v4, v5
	v_mul_f32_e32 v8, 0x43800000, v141
	v_med3_f32 v8, v8, s79, v193
	v_add_u32_e32 v4, v7, v29
	v_cvt_pk_fp8_f32 v57, v8, v58 op_sel:[0,0,1]
	v_add_u32_e32 v5, v13, v31
	ds_write_b128 v4, v[50:53]
	v_mul_f32_e32 v8, 0x43800000, v146
	ds_write_b128 v5, v[54:57]
	v_mul_f32_e32 v5, 0x43800000, v144
	v_mul_f32_e32 v50, 0x43800000, v150
	v_med3_f32 v5, v5, s79, v193
	v_med3_f32 v8, v8, s79, v193
	v_med3_f32 v52, v50, s79, v193
	v_mov_b32_e32 v50, v9
	v_cvt_pk_fp8_f32 v50, v5, v8
	v_mul_f32_e32 v51, 0x43800000, v156
	v_med3_f32 v51, v51, s79, v193
	v_mul_f32_e32 v5, 0x43800000, v148
	v_cvt_pk_fp8_f32 v50, v52, v51 op_sel:[0,0,1]
	v_mul_f32_e32 v8, 0x43800000, v152
	v_mul_f32_e32 v51, 0x43800000, v158
	v_med3_f32 v5, v5, s79, v193
	v_med3_f32 v8, v8, s79, v193
	v_med3_f32 v53, v51, s79, v193
	v_mov_b32_e32 v51, v9
	v_cvt_pk_fp8_f32 v51, v5, v8
	v_mul_f32_e32 v52, 0x43800000, v166
	v_med3_f32 v52, v52, s79, v193
	v_mul_f32_e32 v5, 0x43800000, v154
	v_cvt_pk_fp8_f32 v51, v53, v52 op_sel:[0,0,1]
	v_mul_f32_e32 v8, 0x43800000, v160
	v_mul_f32_e32 v52, 0x43800000, v168
	v_med3_f32 v5, v5, s79, v193
	v_med3_f32 v8, v8, s79, v193
	v_med3_f32 v54, v52, s79, v193
	v_mov_b32_e32 v52, v9
	v_cvt_pk_fp8_f32 v52, v5, v8
	v_mul_f32_e32 v53, 0x43800000, v172
	v_med3_f32 v53, v53, s79, v193
	s_waitcnt vmcnt(2)
	v_mul_f32_e32 v5, 0x43800000, v164
	v_cvt_pk_fp8_f32 v52, v54, v53 op_sel:[0,0,1]
	s_waitcnt vmcnt(1)
	v_mul_f32_e32 v8, 0x43800000, v170
	s_waitcnt vmcnt(0)
	v_mul_f32_e32 v53, 0x43800000, v174
	v_med3_f32 v5, v5, s79, v193
	v_med3_f32 v8, v8, s79, v193
	v_med3_f32 v54, v53, s79, v193
	v_mov_b32_e32 v53, v9
	v_cvt_pk_fp8_f32 v53, v5, v8
	v_mul_f32_e32 v2, 0x43800000, v2
	v_med3_f32 v2, v2, s79, v193
	v_mul_f32_e32 v5, 0x43800000, v147
	v_cvt_pk_fp8_f32 v53, v54, v2 op_sel:[0,0,1]
	v_mul_f32_e32 v2, 0x43800000, v145
	v_mul_f32_e32 v54, 0x43800000, v157
	v_med3_f32 v2, v2, s79, v193
	v_med3_f32 v5, v5, s79, v193
	v_med3_f32 v55, v54, s79, v193
	v_mov_b32_e32 v54, v9
	v_cvt_pk_fp8_f32 v54, v2, v5
	v_mul_f32_e32 v8, 0x43800000, v151
	v_med3_f32 v8, v8, s79, v193
	v_mul_f32_e32 v2, 0x43800000, v149
	v_cvt_pk_fp8_f32 v54, v8, v55 op_sel:[0,0,1]
	v_mul_f32_e32 v5, 0x43800000, v153
	v_mul_f32_e32 v55, 0x43800000, v167
	v_med3_f32 v2, v2, s79, v193
	v_med3_f32 v5, v5, s79, v193
	v_med3_f32 v56, v55, s79, v193
	v_mov_b32_e32 v55, v9
	v_cvt_pk_fp8_f32 v55, v2, v5
	v_mul_f32_e32 v8, 0x43800000, v159
	v_med3_f32 v8, v8, s79, v193
	v_mul_f32_e32 v2, 0x43800000, v155
	v_cvt_pk_fp8_f32 v55, v8, v56 op_sel:[0,0,1]
	v_mul_f32_e32 v5, 0x43800000, v161
	v_mul_f32_e32 v56, 0x43800000, v173
	v_med3_f32 v2, v2, s79, v193
	v_med3_f32 v5, v5, s79, v193
	v_med3_f32 v57, v56, s79, v193
	v_mov_b32_e32 v56, v9
	v_cvt_pk_fp8_f32 v56, v2, v5
	v_mul_f32_e32 v8, 0x43800000, v169
	v_med3_f32 v8, v8, s79, v193
	v_mul_f32_e32 v2, 0x43800000, v165
	v_mul_f32_e32 v5, 0x43800000, v171
	v_cvt_pk_fp8_f32 v56, v8, v57 op_sel:[0,0,1]
	v_med3_f32 v2, v2, s79, v193
	v_med3_f32 v5, v5, s79, v193
	v_mov_b32_e32 v57, v9
	v_cvt_pk_fp8_f32 v57, v2, v5
	v_mul_f32_e32 v8, 0x43800000, v175
	v_mul_f32_e32 v3, 0x43800000, v3
	v_med3_f32 v8, v8, s79, v193
	v_med3_f32 v3, v3, s79, v193
	v_cvt_pk_fp8_f32 v57, v8, v3 op_sel:[0,0,1]
	v_add_u32_e32 v2, v13, v33
	ds_write_b128 v4, v[50:53] offset:16
	v_or_b32_e32 v8, s6, v162
	ds_write_b128 v2, v[54:57]
	s_waitcnt lgkmcnt(0)
; #define LAS __attribute__((address_space(3)))
; #define LDS_WAIT() asm volatile("s_waitcnt lgkmcnt(0)" ::: "memory")
; __device__ __forceinline__ void tr128_f8(const float* W, int ldw, int srccol, unsigned char* WT, size_t dstrow0, int K, int k0, LAS unsigned char* tile, int lane) {
;     ...
;     const int c = lane & 7;
; #pragma unroll
;     for (int j = 0; j < 16; ++j) { const int n = (lane >> 3) + 8 * j; const v4u o = *(const LAS v4u*)(tile + n * 128 + ((c ^ (n & 7)) << 4));
;         __builtin_nontemporal_store(o, (v4u*)(WT + (dstrow0 + n) * K + k0 + 16 * c)); }
;     LDS_WAIT(); asm volatile("" ::: "memory");
	v_add_u32_e32 v56, v35, v37
	ds_read_b128 v[56:59], v56
	v_add_u32_e32 v60, v35, v39
	ds_read_b128 v[60:63], v60
	v_add_u32_e32 v64, v35, v179
	ds_read_b128 v[64:67], v64
	v_add_u32_e32 v68, v35, v180
	ds_read_b128 v[68:71], v68
	v_add_u32_e32 v72, v35, v181
	ds_read_b128 v[72:75], v72
	v_add_u32_e32 v76, v35, v182
	ds_read_b128 v[76:79], v76
	v_add_u32_e32 v80, v35, v183
	ds_read_b128 v[80:83], v80
	v_add_u32_e32 v84, v35, v184
	ds_read_b128 v[84:87], v84
	v_add_u32_e32 v88, v35, v185
	ds_read_b128 v[88:91], v88
	v_add_u32_e32 v92, v35, v186
	ds_read_b128 v[92:95], v92
	v_add_u32_e32 v96, v35, v187
	ds_read_b128 v[96:99], v96
	v_add_u32_e32 v100, v35, v188
	ds_read_b128 v[100:103], v100
	v_add_u32_e32 v104, v35, v189
	ds_read_b128 v[104:107], v104
	v_add_u32_e32 v108, v35, v190
	ds_read_b128 v[108:111], v108
	v_add_u32_e32 v112, v35, v191
	ds_read_b128 v[112:115], v112
	v_add_u32_e32 v116, v35, v192
	ds_read_b128 v[116:119], v116
	v_lshl_add_u64 v[50:51], v[48:49], 0, s[8:9]
	v_lshlrev_b32_e32 v8, 11, v8
	v_lshl_add_u64 v[52:53], v[50:51], 0, v[8:9]
	v_or_b32_e32 v8, s6, v10
	s_waitcnt lgkmcnt(15)
	global_store_dwordx4 v[52:53], v[56:59], off nt
	v_lshlrev_b32_e32 v8, 11, v8
	v_lshl_add_u64 v[52:53], v[50:51], 0, v[8:9]
	v_or_b32_e32 v8, s6, v12
	v_lshlrev_b32_e32 v8, 11, v8
	v_readlane_b32 s37, v250, 61
	v_readlane_b32 s38, v250, 62
	s_waitcnt lgkmcnt(14)
	global_store_dwordx4 v[52:53], v[60:63], off nt
	v_lshl_add_u64 v[52:53], v[50:51], 0, v[8:9]
	v_or_b32_e32 v8, s6, v14
	v_lshlrev_b32_e32 v8, 11, v8
	v_readlane_b32 s39, v250, 63
	v_readlane_b32 s42, v251, 2
	v_readlane_b32 s43, v251, 3
	s_waitcnt lgkmcnt(13)
	global_store_dwordx4 v[52:53], v[64:67], off nt
	v_lshl_add_u64 v[52:53], v[50:51], 0, v[8:9]
	v_or_b32_e32 v8, s6, v16
	v_lshlrev_b32_e32 v8, 11, v8
	v_readlane_b32 s44, v251, 4
	v_readlane_b32 s45, v251, 5
	v_readlane_b32 s46, v251, 6
	s_waitcnt lgkmcnt(12)
	global_store_dwordx4 v[52:53], v[68:71], off nt
	v_lshl_add_u64 v[52:53], v[50:51], 0, v[8:9]
	v_or_b32_e32 v8, s6, v18
	v_lshlrev_b32_e32 v8, 11, v8
	v_readlane_b32 s47, v251, 7
	v_readlane_b32 s48, v251, 8
	v_readlane_b32 s49, v251, 9
	s_waitcnt lgkmcnt(11)
	global_store_dwordx4 v[52:53], v[72:75], off nt
	v_lshl_add_u64 v[52:53], v[50:51], 0, v[8:9]
	v_or_b32_e32 v8, s6, v20
	v_lshlrev_b32_e32 v8, 11, v8
	v_readlane_b32 s50, v251, 10
	v_readlane_b32 s51, v251, 11
	s_waitcnt lgkmcnt(10)
	global_store_dwordx4 v[52:53], v[76:79], off nt
	v_lshl_add_u64 v[52:53], v[50:51], 0, v[8:9]
	s_nop 0
	v_or_b32_e32 v8, s6, v22
	v_lshlrev_b32_e32 v8, 11, v8
	s_waitcnt lgkmcnt(9)
	global_store_dwordx4 v[52:53], v[80:83], off nt
	s_nop 1
	v_lshl_add_u64 v[52:53], v[50:51], 0, v[8:9]
	v_or_b32_e32 v8, s6, v24
	v_lshlrev_b32_e32 v8, 11, v8
	s_waitcnt lgkmcnt(8)
	global_store_dwordx4 v[52:53], v[84:87], off nt
	v_lshl_add_u64 v[52:53], v[50:51], 0, v[8:9]
	s_nop 0
	v_or_b32_e32 v8, s6, v26
	v_lshlrev_b32_e32 v8, 11, v8
	s_waitcnt lgkmcnt(7)
	global_store_dwordx4 v[52:53], v[88:91], off nt
	s_nop 1
	v_lshl_add_u64 v[52:53], v[50:51], 0, v[8:9]
	v_or_b32_e32 v8, s6, v28
	v_lshlrev_b32_e32 v8, 11, v8
	s_waitcnt lgkmcnt(6)
	global_store_dwordx4 v[52:53], v[92:95], off nt
	v_lshl_add_u64 v[52:53], v[50:51], 0, v[8:9]
	s_nop 0
	v_or_b32_e32 v8, s6, v30
	v_lshlrev_b32_e32 v8, 11, v8
	s_waitcnt lgkmcnt(5)
	global_store_dwordx4 v[52:53], v[96:99], off nt
	s_nop 1
	v_lshl_add_u64 v[52:53], v[50:51], 0, v[8:9]
	v_or_b32_e32 v8, s6, v32
	v_lshlrev_b32_e32 v8, 11, v8
	s_waitcnt lgkmcnt(4)
	global_store_dwordx4 v[52:53], v[100:103], off nt
	v_lshl_add_u64 v[52:53], v[50:51], 0, v[8:9]
	s_nop 0
	v_or_b32_e32 v8, s6, v34
	v_lshlrev_b32_e32 v8, 11, v8
	s_waitcnt lgkmcnt(3)
	global_store_dwordx4 v[52:53], v[104:107], off nt
	s_nop 1
	v_lshl_add_u64 v[52:53], v[50:51], 0, v[8:9]
	v_or_b32_e32 v8, s6, v36
	v_lshlrev_b32_e32 v8, 11, v8
	s_waitcnt lgkmcnt(2)
	global_store_dwordx4 v[52:53], v[108:111], off nt
	v_lshl_add_u64 v[52:53], v[50:51], 0, v[8:9]
	s_nop 0
	v_or_b32_e32 v8, s6, v38
	v_lshlrev_b32_e32 v8, 11, v8
	v_lshl_add_u64 v[50:51], v[50:51], 0, v[8:9]
	s_waitcnt lgkmcnt(1)
	global_store_dwordx4 v[52:53], v[112:115], off nt
	s_nop 1
	s_waitcnt lgkmcnt(0)
	global_store_dwordx4 v[50:51], v[116:119], off nt
	s_waitcnt lgkmcnt(0)
	s_branch .LBB0_491

; #define LAS __attribute__((address_space(3)))
; __device__ __forceinline__ void ph4a_unit(const Args& a, LAS unsigned char* lds, int tid, int wave, int lane, int b, int ci, int p0, int np) {
;     ...
;     __syncthreads();
;     for (int i = tid; i < 64 * 128; i += NTHR) { const int q = i >> 7, ch = i & 127, head = ch >> 3, c8 = ch & 7;
;         const v4u v = *(const v4u*)(IQ + ((size_t)tok0 + q) * 1024 + ch * 8);
;         *(LAS v4u*)(lds + q * 2048 + ((head ^ ((q >> 3) & 1)) * 128) + ((c8 ^ (q & 7)) * 16)) = v; }
.LBB0_582:
	global_load_dwordx4 v[64:67], v[2:3], off
	v_lshl_add_u64 v[2:3], v[2:3], 0, s[8:9]
	global_load_dwordx4 v[68:71], v[2:3], off
	v_lshl_add_u64 v[2:3], v[2:3], 0, s[8:9]
	global_load_dwordx4 v[72:75], v[2:3], off
	v_lshl_add_u64 v[2:3], v[2:3], 0, s[8:9]
	global_load_dwordx4 v[76:79], v[2:3], off
	v_lshl_add_u64 v[2:3], v[2:3], 0, s[8:9]
	global_load_dwordx4 v[80:83], v[2:3], off
	v_lshl_add_u64 v[2:3], v[2:3], 0, s[8:9]
	global_load_dwordx4 v[84:87], v[2:3], off
	v_lshl_add_u64 v[2:3], v[2:3], 0, s[8:9]
	global_load_dwordx4 v[88:91], v[2:3], off
	v_lshl_add_u64 v[2:3], v[2:3], 0, s[8:9]
	global_load_dwordx4 v[92:95], v[2:3], off
	v_lshl_add_u64 v[2:3], v[2:3], 0, s[8:9]
	global_load_dwordx4 v[96:99], v[2:3], off
	v_lshl_add_u64 v[2:3], v[2:3], 0, s[8:9]
	global_load_dwordx4 v[100:103], v[2:3], off
	v_lshl_add_u64 v[2:3], v[2:3], 0, s[8:9]
	global_load_dwordx4 v[104:107], v[2:3], off
	v_lshl_add_u64 v[2:3], v[2:3], 0, s[8:9]
	global_load_dwordx4 v[108:111], v[2:3], off
	v_lshl_add_u64 v[2:3], v[2:3], 0, s[8:9]
	global_load_dwordx4 v[112:115], v[2:3], off
	v_lshl_add_u64 v[2:3], v[2:3], 0, s[8:9]
	global_load_dwordx4 v[116:119], v[2:3], off
	v_lshl_add_u64 v[2:3], v[2:3], 0, s[8:9]
	global_load_dwordx4 v[120:123], v[2:3], off
	v_lshl_add_u64 v[2:3], v[2:3], 0, s[8:9]
	global_load_dwordx4 v[124:127], v[2:3], off
	v_lshl_add_u64 v[2:3], v[2:3], 0, s[8:9]
	v_xor_b32_e32 v12, v5, v6
	v_lshrrev_b32_e32 v7, 10, v6
	v_lshlrev_b32_e32 v12, 4, v12
	v_bitop3_b32 v7, v7, v203, 1 bitop3:0x6c
	v_and_b32_e32 v12, 0x70, v12
	v_add_u32_e32 v6, 0x200, v6
	v_lshl_or_b32 v7, v7, 7, v12
	v_add_u32_e32 v5, 4, v5
	v_add_u32_e32 v7, v4, v7
	v_add_u32_e32 v4, 0x2000, v4
	s_waitcnt vmcnt(15)
	ds_write_b128 v7, v[64:67]
	v_xor_b32_e32 v12, v5, v6
	v_lshrrev_b32_e32 v7, 10, v6
	v_lshlrev_b32_e32 v12, 4, v12
	v_bitop3_b32 v7, v7, v203, 1 bitop3:0x6c
	v_and_b32_e32 v12, 0x70, v12
	v_add_u32_e32 v6, 0x200, v6
	v_lshl_or_b32 v7, v7, 7, v12
	v_add_u32_e32 v5, 4, v5
	v_add_u32_e32 v7, v4, v7
	v_add_u32_e32 v4, 0x2000, v4
	s_waitcnt vmcnt(14)
	ds_write_b128 v7, v[68:71]
	v_xor_b32_e32 v12, v5, v6
	v_lshrrev_b32_e32 v7, 10, v6
	v_lshlrev_b32_e32 v12, 4, v12
	v_bitop3_b32 v7, v7, v203, 1 bitop3:0x6c
	v_and_b32_e32 v12, 0x70, v12
	v_add_u32_e32 v6, 0x200, v6
	v_lshl_or_b32 v7, v7, 7, v12
	v_add_u32_e32 v5, 4, v5
	v_add_u32_e32 v7, v4, v7
	v_add_u32_e32 v4, 0x2000, v4
	s_waitcnt vmcnt(13)
	ds_write_b128 v7, v[72:75]
	v_xor_b32_e32 v12, v5, v6
	v_lshrrev_b32_e32 v7, 10, v6
	v_lshlrev_b32_e32 v12, 4, v12
	v_bitop3_b32 v7, v7, v203, 1 bitop3:0x6c
	v_and_b32_e32 v12, 0x70, v12
	v_add_u32_e32 v6, 0x200, v6
	v_lshl_or_b32 v7, v7, 7, v12
	v_add_u32_e32 v5, 4, v5
	v_add_u32_e32 v7, v4, v7
	v_add_u32_e32 v4, 0x2000, v4
	s_waitcnt vmcnt(12)
	ds_write_b128 v7, v[76:79]
	v_xor_b32_e32 v12, v5, v6
	v_lshrrev_b32_e32 v7, 10, v6
	v_lshlrev_b32_e32 v12, 4, v12
	v_bitop3_b32 v7, v7, v203, 1 bitop3:0x6c
	v_and_b32_e32 v12, 0x70, v12
	v_add_u32_e32 v6, 0x200, v6
	v_lshl_or_b32 v7, v7, 7, v12
	v_add_u32_e32 v5, 4, v5
	v_add_u32_e32 v7, v4, v7
	v_add_u32_e32 v4, 0x2000, v4
	s_waitcnt vmcnt(11)
	ds_write_b128 v7, v[80:83]
	v_xor_b32_e32 v12, v5, v6
	v_lshrrev_b32_e32 v7, 10, v6
	v_lshlrev_b32_e32 v12, 4, v12
	v_bitop3_b32 v7, v7, v203, 1 bitop3:0x6c
	v_and_b32_e32 v12, 0x70, v12
	v_add_u32_e32 v6, 0x200, v6
	v_lshl_or_b32 v7, v7, 7, v12
	v_add_u32_e32 v5, 4, v5
	v_add_u32_e32 v7, v4, v7
	v_add_u32_e32 v4, 0x2000, v4
	s_waitcnt vmcnt(10)
	ds_write_b128 v7, v[84:87]
	v_xor_b32_e32 v12, v5, v6
	v_lshrrev_b32_e32 v7, 10, v6
	v_lshlrev_b32_e32 v12, 4, v12
	v_bitop3_b32 v7, v7, v203, 1 bitop3:0x6c
	v_and_b32_e32 v12, 0x70, v12
	v_add_u32_e32 v6, 0x200, v6
	v_lshl_or_b32 v7, v7, 7, v12
	v_add_u32_e32 v5, 4, v5
	v_add_u32_e32 v7, v4, v7
	v_add_u32_e32 v4, 0x2000, v4
	s_waitcnt vmcnt(9)
	ds_write_b128 v7, v[88:91]
	v_xor_b32_e32 v12, v5, v6
	v_lshrrev_b32_e32 v7, 10, v6
	v_lshlrev_b32_e32 v12, 4, v12
	v_bitop3_b32 v7, v7, v203, 1 bitop3:0x6c
	v_and_b32_e32 v12, 0x70, v12
	v_add_u32_e32 v6, 0x200, v6
	v_lshl_or_b32 v7, v7, 7, v12
	v_add_u32_e32 v5, 4, v5
	v_add_u32_e32 v7, v4, v7
	v_add_u32_e32 v4, 0x2000, v4
	s_waitcnt vmcnt(8)
; #define LAS __attribute__((address_space(3)))
; __device__ __forceinline__ void ph4a_unit(const Args& a, LAS unsigned char* lds, int tid, int wave, int lane, int b, int ci, int p0, int np) {
;     ...
;     for (int i = tid; i < 64 * 128; i += NTHR) { const int q = i >> 7, ch = i & 127, head = ch >> 3, c8 = ch & 7;
;         const v4u v = *(const v4u*)(IQ + ((size_t)tok0 + q) * 1024 + ch * 8);
;         *(LAS v4u*)(lds + q * 2048 + ((head ^ ((q >> 3) & 1)) * 128) + ((c8 ^ (q & 7)) * 16)) = v; }
;     __syncthreads();
;     const int qt = wave & 1, q = qt * 32 + (lane & 31), hh = lane >> 5; const size_t tokq = (size_t)tok0 + q;
;     float wgt[16];
; #pragma unroll
;     for (int h4 = 0; h4 < 4; ++h4) { const f32x4 w4 = *(const f32x4*)(IW + tokq * 16 + 4 * h4); wgt[4 * h4] = w4[0]; wgt[4 * h4 + 1] = w4[1]; wgt[4 * h4 + 2] = w4[2]; wgt[4 * h4 + 3] = w4[3]; }
;     const LAS unsigned char* qb = lds + q * 2048; const int hx = ((q >> 3) & 1) * 128; int offk[4];
; #pragma unroll
;     for (int kk = 0; kk < 4; ++kk) offk[kk] = ((2 * kk + hh) ^ (q & 7)) * 16;
;     int it = wave >> 1;
;     bf16x8 ak[2][4];
;     if (it < np) { const bf16* kp = IK + ((size_t)b * SEQ + (p0 + it) * 64 + (lane & 31)) * 64 + hh * 8;
; #pragma unroll
;         for (int kk = 0; kk < 4; ++kk) { ak[0][kk] = *(const bf16x8*)(kp + kk * 16); ak[1][kk] = *(const bf16x8*)(kp + 32 * 64 + kk * 16); } }
	ds_write_b128 v7, v[92:95]
	v_xor_b32_e32 v12, v5, v6
	v_lshrrev_b32_e32 v7, 10, v6
	v_lshlrev_b32_e32 v12, 4, v12
	v_bitop3_b32 v7, v7, v203, 1 bitop3:0x6c
	v_and_b32_e32 v12, 0x70, v12
	v_add_u32_e32 v6, 0x200, v6
	v_lshl_or_b32 v7, v7, 7, v12
	v_add_u32_e32 v5, 4, v5
	v_add_u32_e32 v7, v4, v7
	v_add_u32_e32 v4, 0x2000, v4
	s_waitcnt vmcnt(7)
	ds_write_b128 v7, v[96:99]
	v_xor_b32_e32 v12, v5, v6
	v_lshrrev_b32_e32 v7, 10, v6
	v_lshlrev_b32_e32 v12, 4, v12
	v_bitop3_b32 v7, v7, v203, 1 bitop3:0x6c
	v_and_b32_e32 v12, 0x70, v12
	v_add_u32_e32 v6, 0x200, v6
	v_lshl_or_b32 v7, v7, 7, v12
	v_add_u32_e32 v5, 4, v5
	v_add_u32_e32 v7, v4, v7
	v_add_u32_e32 v4, 0x2000, v4
	s_waitcnt vmcnt(6)
	ds_write_b128 v7, v[100:103]
	v_xor_b32_e32 v12, v5, v6
	v_lshrrev_b32_e32 v7, 10, v6
	v_lshlrev_b32_e32 v12, 4, v12
	v_bitop3_b32 v7, v7, v203, 1 bitop3:0x6c
	v_and_b32_e32 v12, 0x70, v12
	v_add_u32_e32 v6, 0x200, v6
	v_lshl_or_b32 v7, v7, 7, v12
	v_add_u32_e32 v5, 4, v5
	v_add_u32_e32 v7, v4, v7
	v_add_u32_e32 v4, 0x2000, v4
	s_waitcnt vmcnt(5)
	ds_write_b128 v7, v[104:107]
	v_xor_b32_e32 v12, v5, v6
	v_lshrrev_b32_e32 v7, 10, v6
	v_lshlrev_b32_e32 v12, 4, v12
	v_bitop3_b32 v7, v7, v203, 1 bitop3:0x6c
	v_and_b32_e32 v12, 0x70, v12
	v_add_u32_e32 v6, 0x200, v6
	v_lshl_or_b32 v7, v7, 7, v12
	v_add_u32_e32 v5, 4, v5
	v_add_u32_e32 v7, v4, v7
	v_add_u32_e32 v4, 0x2000, v4
	s_waitcnt vmcnt(4)
	ds_write_b128 v7, v[108:111]
	v_xor_b32_e32 v12, v5, v6
	v_lshrrev_b32_e32 v7, 10, v6
	v_lshlrev_b32_e32 v12, 4, v12
	v_bitop3_b32 v7, v7, v203, 1 bitop3:0x6c
	v_and_b32_e32 v12, 0x70, v12
	v_add_u32_e32 v6, 0x200, v6
	v_lshl_or_b32 v7, v7, 7, v12
	v_add_u32_e32 v5, 4, v5
	v_add_u32_e32 v7, v4, v7
	v_add_u32_e32 v4, 0x2000, v4
	s_waitcnt vmcnt(3)
	ds_write_b128 v7, v[112:115]
	v_xor_b32_e32 v12, v5, v6
	v_lshrrev_b32_e32 v7, 10, v6
	v_lshlrev_b32_e32 v12, 4, v12
	v_bitop3_b32 v7, v7, v203, 1 bitop3:0x6c
	v_and_b32_e32 v12, 0x70, v12
	v_add_u32_e32 v6, 0x200, v6
	v_lshl_or_b32 v7, v7, 7, v12
	v_add_u32_e32 v5, 4, v5
	v_add_u32_e32 v7, v4, v7
	v_add_u32_e32 v4, 0x2000, v4
	s_waitcnt vmcnt(2)
	ds_write_b128 v7, v[116:119]
	v_xor_b32_e32 v12, v5, v6
	v_lshrrev_b32_e32 v7, 10, v6
	v_lshlrev_b32_e32 v12, 4, v12
	v_bitop3_b32 v7, v7, v203, 1 bitop3:0x6c
	v_and_b32_e32 v12, 0x70, v12
	v_add_u32_e32 v6, 0x200, v6
	v_lshl_or_b32 v7, v7, 7, v12
	v_add_u32_e32 v5, 4, v5
	v_add_u32_e32 v7, v4, v7
	v_add_u32_e32 v4, 0x2000, v4
	s_waitcnt vmcnt(1)
	ds_write_b128 v7, v[120:123]
	v_xor_b32_e32 v12, v5, v6
	v_lshrrev_b32_e32 v7, 10, v6
	v_lshlrev_b32_e32 v12, 4, v12
	v_bitop3_b32 v7, v7, v203, 1 bitop3:0x6c
	v_and_b32_e32 v12, 0x70, v12
	v_add_u32_e32 v6, 0x200, v6
	v_lshl_or_b32 v7, v7, 7, v12
	v_add_u32_e32 v5, 4, v5
	v_add_u32_e32 v7, v4, v7
	v_add_u32_e32 v4, 0x2000, v4
	s_waitcnt vmcnt(0)
	ds_write_b128 v7, v[124:127]
	s_or_b64 exec, exec, s[4:5]
	s_sub_i32 s8, 16, s13
	s_and_b64 s[4:5], s[0:1], exec
	s_cselect_b32 s8, 16, s8
	s_cmp_lt_i32 s12, s8
	s_waitcnt lgkmcnt(0)
	s_barrier
	s_cbranch_scc0 .LBB0_586
	s_and_b32 s4, s23, 0x3800
	s_add_i32 s11, s11, s4
	s_ashr_i32 s5, s11, 31
	v_mov_b32_e32 v3, s5
	s_lshl_b32 s5, s10, 1
	s_and_b64 s[0:1], s[0:1], exec
	v_or_b32_e32 v2, s11, v202
	s_cselect_b32 s9, 0, s5
	v_lshlrev_b64 v[4:5], 6, v[2:3]
	s_add_i32 s0, s9, s12
	v_lshl_add_u64 v[4:5], s[2:3], 0, v[4:5]
	v_mov_b32_e32 v183, 0
	v_or_b32_e32 v190, s4, v185
	s_lshl_b32 s0, s0, 6
	global_load_dwordx4 v[66:69], v[4:5], off
	global_load_dwordx4 v[70:73], v[4:5], off offset:16
	global_load_dwordx4 v[74:77], v[4:5], off offset:32
	global_load_dwordx4 v[78:81], v[4:5], off offset:48
	v_lshl_add_u64 v[4:5], s[82:83], 0, v[182:183]
	v_add_u32_e32 v182, s0, v190
	v_lshlrev_b64 v[6:7], 7, v[182:183]
	v_lshl_add_u64 v[6:7], v[180:181], 0, v[6:7]
	s_movk_i32 s10, 0x1000
	v_add_co_u32_e32 v8, vcc, s10, v6
	v_lshlrev_b64 v[2:3], 13, v[2:3]
	s_nop 0
	v_addc_co_u32_e32 v9, vcc, 0, v7, vcc
	global_load_dwordx4 v[146:149], v[6:7], off
	global_load_dwordx4 v[154:157], v[6:7], off offset:32
	global_load_dwordx4 v[174:177], v[8:9], off
	global_load_dwordx4 v[166:169], v[8:9], off offset:32
	global_load_dwordx4 v[158:161], v[6:7], off offset:64
	global_load_dwordx4 v[150:153], v[6:7], off offset:96
	global_load_dwordx4 v[170:173], v[8:9], off offset:64
	global_load_dwordx4 v[162:165], v[8:9], off offset:96
	v_lshl_add_u64 v[2:3], v[4:5], 0, v[2:3]
	s_mov_b64 s[4:5], 0x22800000
	s_mov_b32 s1, 0
	v_lshl_add_u64 v[188:189], v[2:3], 0, s[4:5]
	s_mov_b32 s13, s12

; #define LAS __attribute__((address_space(3)))
; __device__ __forceinline__ void ph4a_unit(const Args& a, LAS unsigned char* lds, int tid, int wave, int lane, int b, int ci, int p0, int np) {
;     ...
;     __syncthreads();
;     for (int i = tid; i < 64 * 128; i += NTHR) { const int q = i >> 7, ch = i & 127, head = ch >> 3, c8 = ch & 7;
;         const v4u v = *(const v4u*)(IQ + ((size_t)tok0 + q) * 1024 + ch * 8);
;         *(LAS v4u*)(lds + q * 2048 + ((head ^ ((q >> 3) & 1)) * 128) + ((c8 ^ (q & 7)) * 16)) = v; }
.LBB0_588:
	global_load_dwordx4 v[64:67], v[2:3], off
	v_lshl_add_u64 v[2:3], v[2:3], 0, s[8:9]
	global_load_dwordx4 v[68:71], v[2:3], off
	v_lshl_add_u64 v[2:3], v[2:3], 0, s[8:9]
	global_load_dwordx4 v[72:75], v[2:3], off
	v_lshl_add_u64 v[2:3], v[2:3], 0, s[8:9]
	global_load_dwordx4 v[76:79], v[2:3], off
	v_lshl_add_u64 v[2:3], v[2:3], 0, s[8:9]
	global_load_dwordx4 v[80:83], v[2:3], off
	v_lshl_add_u64 v[2:3], v[2:3], 0, s[8:9]
	global_load_dwordx4 v[84:87], v[2:3], off
	v_lshl_add_u64 v[2:3], v[2:3], 0, s[8:9]
	global_load_dwordx4 v[88:91], v[2:3], off
	v_lshl_add_u64 v[2:3], v[2:3], 0, s[8:9]
	global_load_dwordx4 v[92:95], v[2:3], off
	v_lshl_add_u64 v[2:3], v[2:3], 0, s[8:9]
	global_load_dwordx4 v[96:99], v[2:3], off
	v_lshl_add_u64 v[2:3], v[2:3], 0, s[8:9]
	global_load_dwordx4 v[100:103], v[2:3], off
	v_lshl_add_u64 v[2:3], v[2:3], 0, s[8:9]
	global_load_dwordx4 v[104:107], v[2:3], off
	v_lshl_add_u64 v[2:3], v[2:3], 0, s[8:9]
	global_load_dwordx4 v[108:111], v[2:3], off
	v_lshl_add_u64 v[2:3], v[2:3], 0, s[8:9]
	global_load_dwordx4 v[112:115], v[2:3], off
	v_lshl_add_u64 v[2:3], v[2:3], 0, s[8:9]
	global_load_dwordx4 v[116:119], v[2:3], off
	v_lshl_add_u64 v[2:3], v[2:3], 0, s[8:9]
	global_load_dwordx4 v[120:123], v[2:3], off
	v_lshl_add_u64 v[2:3], v[2:3], 0, s[8:9]
	global_load_dwordx4 v[124:127], v[2:3], off
	v_lshl_add_u64 v[2:3], v[2:3], 0, s[8:9]
	v_xor_b32_e32 v10, v184, v4
	v_lshrrev_b32_e32 v5, 10, v4
	v_lshlrev_b32_e32 v10, 4, v10
	v_bitop3_b32 v5, v5, v203, 1 bitop3:0x6c
	v_and_b32_e32 v10, 0x70, v10
	v_add_u32_e32 v4, 0x200, v4
	v_lshl_or_b32 v5, v5, 7, v10
	v_add_u32_e32 v184, 4, v184
	v_add_u32_e32 v5, v187, v5
	v_add_u32_e32 v187, 0x2000, v187
	s_waitcnt vmcnt(15)
	ds_write_b128 v5, v[64:67]
	v_xor_b32_e32 v10, v184, v4
	v_lshrrev_b32_e32 v5, 10, v4
	v_lshlrev_b32_e32 v10, 4, v10
	v_bitop3_b32 v5, v5, v203, 1 bitop3:0x6c
	v_and_b32_e32 v10, 0x70, v10
	v_add_u32_e32 v4, 0x200, v4
	v_lshl_or_b32 v5, v5, 7, v10
	v_add_u32_e32 v184, 4, v184
	v_add_u32_e32 v5, v187, v5
	v_add_u32_e32 v187, 0x2000, v187
	s_waitcnt vmcnt(14)
	ds_write_b128 v5, v[68:71]
	v_xor_b32_e32 v10, v184, v4
	v_lshrrev_b32_e32 v5, 10, v4
	v_lshlrev_b32_e32 v10, 4, v10
	v_bitop3_b32 v5, v5, v203, 1 bitop3:0x6c
	v_and_b32_e32 v10, 0x70, v10
	v_add_u32_e32 v4, 0x200, v4
	v_lshl_or_b32 v5, v5, 7, v10
	v_add_u32_e32 v184, 4, v184
	v_add_u32_e32 v5, v187, v5
	v_add_u32_e32 v187, 0x2000, v187
	s_waitcnt vmcnt(13)
	ds_write_b128 v5, v[72:75]
	v_xor_b32_e32 v10, v184, v4
	v_lshrrev_b32_e32 v5, 10, v4
	v_lshlrev_b32_e32 v10, 4, v10
	v_bitop3_b32 v5, v5, v203, 1 bitop3:0x6c
	v_and_b32_e32 v10, 0x70, v10
	v_add_u32_e32 v4, 0x200, v4
	v_lshl_or_b32 v5, v5, 7, v10
	v_add_u32_e32 v184, 4, v184
	v_add_u32_e32 v5, v187, v5
	v_add_u32_e32 v187, 0x2000, v187
	s_waitcnt vmcnt(12)
	ds_write_b128 v5, v[76:79]
	v_xor_b32_e32 v10, v184, v4
	v_lshrrev_b32_e32 v5, 10, v4
	v_lshlrev_b32_e32 v10, 4, v10
	v_bitop3_b32 v5, v5, v203, 1 bitop3:0x6c
	v_and_b32_e32 v10, 0x70, v10
	v_add_u32_e32 v4, 0x200, v4
	v_lshl_or_b32 v5, v5, 7, v10
	v_add_u32_e32 v184, 4, v184
	v_add_u32_e32 v5, v187, v5
	v_add_u32_e32 v187, 0x2000, v187
	s_waitcnt vmcnt(11)
	ds_write_b128 v5, v[80:83]
	v_xor_b32_e32 v10, v184, v4
	v_lshrrev_b32_e32 v5, 10, v4
	v_lshlrev_b32_e32 v10, 4, v10
	v_bitop3_b32 v5, v5, v203, 1 bitop3:0x6c
	v_and_b32_e32 v10, 0x70, v10
	v_add_u32_e32 v4, 0x200, v4
	v_lshl_or_b32 v5, v5, 7, v10
	v_add_u32_e32 v184, 4, v184
	v_add_u32_e32 v5, v187, v5
	v_add_u32_e32 v187, 0x2000, v187
	s_waitcnt vmcnt(10)
	ds_write_b128 v5, v[84:87]
	v_xor_b32_e32 v10, v184, v4
	v_lshrrev_b32_e32 v5, 10, v4
	v_lshlrev_b32_e32 v10, 4, v10
	v_bitop3_b32 v5, v5, v203, 1 bitop3:0x6c
	v_and_b32_e32 v10, 0x70, v10
	v_add_u32_e32 v4, 0x200, v4
	v_lshl_or_b32 v5, v5, 7, v10
	v_add_u32_e32 v184, 4, v184
	v_add_u32_e32 v5, v187, v5
	v_add_u32_e32 v187, 0x2000, v187
	s_waitcnt vmcnt(9)
	ds_write_b128 v5, v[88:91]
	v_xor_b32_e32 v10, v184, v4
	v_lshrrev_b32_e32 v5, 10, v4
	v_lshlrev_b32_e32 v10, 4, v10
	v_bitop3_b32 v5, v5, v203, 1 bitop3:0x6c
	v_and_b32_e32 v10, 0x70, v10
	v_add_u32_e32 v4, 0x200, v4
	v_lshl_or_b32 v5, v5, 7, v10
	v_add_u32_e32 v184, 4, v184
	v_add_u32_e32 v5, v187, v5
	v_add_u32_e32 v187, 0x2000, v187
	s_waitcnt vmcnt(8)
	ds_write_b128 v5, v[92:95]
	v_xor_b32_e32 v10, v184, v4
	v_lshrrev_b32_e32 v5, 10, v4
	v_lshlrev_b32_e32 v10, 4, v10
	v_bitop3_b32 v5, v5, v203, 1 bitop3:0x6c
	v_and_b32_e32 v10, 0x70, v10
	v_add_u32_e32 v4, 0x200, v4
	v_lshl_or_b32 v5, v5, 7, v10
	v_add_u32_e32 v184, 4, v184
	v_add_u32_e32 v5, v187, v5
	v_add_u32_e32 v187, 0x2000, v187
	s_waitcnt vmcnt(7)
; #define LAS __attribute__((address_space(3)))
; __device__ __forceinline__ void ph4a_unit(const Args& a, LAS unsigned char* lds, int tid, int wave, int lane, int b, int ci, int p0, int np) {
;     ...
;     for (int i = tid; i < 64 * 128; i += NTHR) { const int q = i >> 7, ch = i & 127, head = ch >> 3, c8 = ch & 7;
;         const v4u v = *(const v4u*)(IQ + ((size_t)tok0 + q) * 1024 + ch * 8);
;         *(LAS v4u*)(lds + q * 2048 + ((head ^ ((q >> 3) & 1)) * 128) + ((c8 ^ (q & 7)) * 16)) = v; }
;     __syncthreads();
;     const int qt = wave & 1, q = qt * 32 + (lane & 31), hh = lane >> 5; const size_t tokq = (size_t)tok0 + q;
;     float wgt[16];
; #pragma unroll
;     for (int h4 = 0; h4 < 4; ++h4) { const f32x4 w4 = *(const f32x4*)(IW + tokq * 16 + 4 * h4); wgt[4 * h4] = w4[0]; wgt[4 * h4 + 1] = w4[1]; wgt[4 * h4 + 2] = w4[2]; wgt[4 * h4 + 3] = w4[3]; }
;     const LAS unsigned char* qb = lds + q * 2048; const int hx = ((q >> 3) & 1) * 128; int offk[4];
; #pragma unroll
;     for (int kk = 0; kk < 4; ++kk) offk[kk] = ((2 * kk + hh) ^ (q & 7)) * 16;
;     int it = wave >> 1;
;     bf16x8 ak[2][4];
;     if (it < np) { const bf16* kp = IK + ((size_t)b * SEQ + (p0 + it) * 64 + (lane & 31)) * 64 + hh * 8;
; #pragma unroll
;         for (int kk = 0; kk < 4; ++kk) { ak[0][kk] = *(const bf16x8*)(kp + kk * 16); ak[1][kk] = *(const bf16x8*)(kp + 32 * 64 + kk * 16); } }
	ds_write_b128 v5, v[96:99]
	v_xor_b32_e32 v10, v184, v4
	v_lshrrev_b32_e32 v5, 10, v4
	v_lshlrev_b32_e32 v10, 4, v10
	v_bitop3_b32 v5, v5, v203, 1 bitop3:0x6c
	v_and_b32_e32 v10, 0x70, v10
	v_add_u32_e32 v4, 0x200, v4
	v_lshl_or_b32 v5, v5, 7, v10
	v_add_u32_e32 v184, 4, v184
	v_add_u32_e32 v5, v187, v5
	v_add_u32_e32 v187, 0x2000, v187
	s_waitcnt vmcnt(6)
	ds_write_b128 v5, v[100:103]
	v_xor_b32_e32 v10, v184, v4
	v_lshrrev_b32_e32 v5, 10, v4
	v_lshlrev_b32_e32 v10, 4, v10
	v_bitop3_b32 v5, v5, v203, 1 bitop3:0x6c
	v_and_b32_e32 v10, 0x70, v10
	v_add_u32_e32 v4, 0x200, v4
	v_lshl_or_b32 v5, v5, 7, v10
	v_add_u32_e32 v184, 4, v184
	v_add_u32_e32 v5, v187, v5
	v_add_u32_e32 v187, 0x2000, v187
	s_waitcnt vmcnt(5)
	ds_write_b128 v5, v[104:107]
	v_xor_b32_e32 v10, v184, v4
	v_lshrrev_b32_e32 v5, 10, v4
	v_lshlrev_b32_e32 v10, 4, v10
	v_bitop3_b32 v5, v5, v203, 1 bitop3:0x6c
	v_and_b32_e32 v10, 0x70, v10
	v_add_u32_e32 v4, 0x200, v4
	v_lshl_or_b32 v5, v5, 7, v10
	v_add_u32_e32 v184, 4, v184
	v_add_u32_e32 v5, v187, v5
	v_add_u32_e32 v187, 0x2000, v187
	s_waitcnt vmcnt(4)
	ds_write_b128 v5, v[108:111]
	v_xor_b32_e32 v10, v184, v4
	v_lshrrev_b32_e32 v5, 10, v4
	v_lshlrev_b32_e32 v10, 4, v10
	v_bitop3_b32 v5, v5, v203, 1 bitop3:0x6c
	v_and_b32_e32 v10, 0x70, v10
	v_add_u32_e32 v4, 0x200, v4
	v_lshl_or_b32 v5, v5, 7, v10
	v_add_u32_e32 v184, 4, v184
	v_add_u32_e32 v5, v187, v5
	v_add_u32_e32 v187, 0x2000, v187
	s_waitcnt vmcnt(3)
	ds_write_b128 v5, v[112:115]
	v_xor_b32_e32 v10, v184, v4
	v_lshrrev_b32_e32 v5, 10, v4
	v_lshlrev_b32_e32 v10, 4, v10
	v_bitop3_b32 v5, v5, v203, 1 bitop3:0x6c
	v_and_b32_e32 v10, 0x70, v10
	v_add_u32_e32 v4, 0x200, v4
	v_lshl_or_b32 v5, v5, 7, v10
	v_add_u32_e32 v184, 4, v184
	v_add_u32_e32 v5, v187, v5
	v_add_u32_e32 v187, 0x2000, v187
	s_waitcnt vmcnt(2)
	ds_write_b128 v5, v[116:119]
	v_xor_b32_e32 v10, v184, v4
	v_lshrrev_b32_e32 v5, 10, v4
	v_lshlrev_b32_e32 v10, 4, v10
	v_bitop3_b32 v5, v5, v203, 1 bitop3:0x6c
	v_and_b32_e32 v10, 0x70, v10
	v_add_u32_e32 v4, 0x200, v4
	v_lshl_or_b32 v5, v5, 7, v10
	v_add_u32_e32 v184, 4, v184
	v_add_u32_e32 v5, v187, v5
	v_add_u32_e32 v187, 0x2000, v187
	s_waitcnt vmcnt(1)
	ds_write_b128 v5, v[120:123]
	v_xor_b32_e32 v10, v184, v4
	v_lshrrev_b32_e32 v5, 10, v4
	v_lshlrev_b32_e32 v10, 4, v10
	v_bitop3_b32 v5, v5, v203, 1 bitop3:0x6c
	v_and_b32_e32 v10, 0x70, v10
	v_add_u32_e32 v4, 0x200, v4
	v_lshl_or_b32 v5, v5, 7, v10
	v_add_u32_e32 v184, 4, v184
	v_add_u32_e32 v5, v187, v5
	v_add_u32_e32 v187, 0x2000, v187
	s_waitcnt vmcnt(0)
	ds_write_b128 v5, v[124:127]
	s_or_b64 exec, exec, s[4:5]
	s_sub_i32 s4, 16, s14
	s_and_b64 s[0:1], vcc, exec
	s_cselect_b32 s4, 16, s4
	s_cmp_lt_u32 s12, s4
	s_waitcnt lgkmcnt(0)
	s_barrier
	s_cbranch_scc0 .LBB0_592
	s_and_b32 s5, s11, 0x3800
	s_add_i32 s13, s13, s5
	s_ashr_i32 s0, s13, 31
	v_mov_b32_e32 v3, s0
	v_or_b32_e32 v2, s13, v202
	v_lshlrev_b64 v[4:5], 6, v[2:3]
	v_lshl_add_u64 v[4:5], s[2:3], 0, v[4:5]
	s_lshl_b32 s2, s10, 1
	s_and_b64 s[0:1], vcc, exec
	s_cselect_b32 s2, 0, s2
	v_or_b32_e32 v186, s5, v185
	s_add_i32 s0, s2, s12
	v_lshl_add_u32 v182, s0, 6, v186
	v_mov_b32_e32 v183, 0
	global_load_dwordx4 v[66:69], v[4:5], off
	global_load_dwordx4 v[70:73], v[4:5], off offset:16
	global_load_dwordx4 v[74:77], v[4:5], off offset:32
	global_load_dwordx4 v[78:81], v[4:5], off offset:48
	v_lshlrev_b64 v[4:5], 7, v[182:183]
	v_lshl_add_u64 v[4:5], v[180:181], 0, v[4:5]
	s_movk_i32 s3, 0x1000
	v_add_co_u32_e32 v6, vcc, s3, v4
	s_mov_b32 s1, 0
	s_nop 0
	v_addc_co_u32_e32 v7, vcc, 0, v5, vcc
	global_load_dwordx4 v[146:149], v[4:5], off
	global_load_dwordx4 v[154:157], v[4:5], off offset:32
	global_load_dwordx4 v[174:177], v[6:7], off
	global_load_dwordx4 v[166:169], v[6:7], off offset:32
	global_load_dwordx4 v[158:161], v[4:5], off offset:64
	global_load_dwordx4 v[150:153], v[4:5], off offset:96
	global_load_dwordx4 v[170:173], v[6:7], off offset:64
	global_load_dwordx4 v[162:165], v[6:7], off offset:96
	v_lshlrev_b64 v[2:3], 13, v[2:3]
	s_lshl_b64 s[0:1], s[0:1], 8
	v_and_b32_e32 v4, 32, v0
	v_lshl_add_u64 v[2:3], v[2:3], 0, s[0:1]
	v_lshrrev_b32_e32 v4, 1, v4
	v_or_b32_e32 v2, v2, v4
	v_lshl_add_u64 v[2:3], s[82:83], 0, v[2:3]
	s_mov_b64 s[0:1], 0x22800080
	v_lshl_add_u64 v[184:185], v[2:3], 0, s[0:1]
	s_mov_b64 s[0:1], 0x400
